# SSM pass-2 epilogue (both layers): in-quad transpose, 8 dwordx2 loads + 8 dwordx2 stores per item instead of a 32-step serial ushort-load/short-store chain (1)
# speedup vs baseline: 1.0205x; 1.0050x over previous
; template <class T> __device__ __forceinline__ void est(T* p, T v) { if constexpr (MK_EPI_NT != 0) __builtin_nontemporal_store(v, p); else *p = v; }
; template <int DIR> ...
;     const int dg = DIR * 64 + g; const float ar = lamb_l[(dg * 64 + lane) * 2], ai = lamb_l[(dg * 64 + lane) * 2 + 1], tr = lamt_l[(dg * 64 + lane) * 2], ti = lamt_l[(dg * 64 + lane) * 2 + 1];
;     float sr = 0.f, si = 0.f;
;     { const float* e = est + ((((size_t)(DIR * 2 + b) * 64 + g) * 32) * 64 + lane) * 2; f32x2 ev[32];
; #pragma unroll
;       for (int m = 0; m < 32; ++m) ev[m] = *(const f32x2*)(e + (size_t)m * 128);
; #pragma unroll
;       for (int mm = 0; mm < 32; ++mm) { const int m = DIR ? 31 - mm : mm; const bool use = DIR ? (m > n) : (m < n);
;           const float nsr = fmaf(tr, sr, fmaf(-ti, si, ev[m].x)), nsi = fmaf(tr, si, fmaf(ti, sr, ev[m].y)); sr = use ? nsr : sr; si = use ? nsi : si; } }
.LBB0_648:
	s_bfe_u32 s31, s30, 0x60005
	v_lshl_or_b32 v2, s31, 9, v174
	global_load_dwordx2 v[142:143], v2, s[10:11]
	global_load_dwordx2 v[4:5], v2, s[8:9]
	s_ashr_i32 s14, s30, 11
	s_ashr_i32 s15, s14, 31
	s_lshl_b64 s[4:5], s[14:15], 17
	s_lshl_b32 s0, s31, 11
	s_or_b32 s4, s4, s0
	v_mov_b32_e32 v3, s5
	v_or_b32_e32 v2, s4, v194
	v_lshl_add_u64 v[2:3], v[2:3], 3, s[76:77]
	global_load_dwordx2 v[64:65], v[2:3], off
	global_load_dwordx2 v[62:63], v[2:3], off offset:512
	global_load_dwordx2 v[60:61], v[2:3], off offset:1024
	global_load_dwordx2 v[58:59], v[2:3], off offset:1536
	global_load_dwordx2 v[56:57], v[2:3], off offset:2048
	global_load_dwordx2 v[54:55], v[2:3], off offset:2560
	global_load_dwordx2 v[52:53], v[2:3], off offset:3072
	global_load_dwordx2 v[50:51], v[2:3], off offset:3584
	v_add_co_u32_e32 v6, vcc, s16, v2
	s_and_b32 s22, s30, 31
	s_nop 0
	v_addc_co_u32_e32 v7, vcc, 0, v3, vcc
	v_add_co_u32_e32 v8, vcc, s17, v2
	s_cmp_eq_u32 s22, 0
	s_nop 0
	v_addc_co_u32_e32 v9, vcc, 0, v3, vcc
	global_load_dwordx2 v[48:49], v[8:9], off offset:-4096
	global_load_dwordx2 v[46:47], v[6:7], off offset:512
	global_load_dwordx2 v[44:45], v[6:7], off offset:1024
	global_load_dwordx2 v[42:43], v[6:7], off offset:1536
	global_load_dwordx2 v[40:41], v[6:7], off offset:2048
	global_load_dwordx2 v[38:39], v[6:7], off offset:2560
	global_load_dwordx2 v[36:37], v[6:7], off offset:3072
	global_load_dwordx2 v[34:35], v[6:7], off offset:3584
	global_load_dwordx2 v[32:33], v[8:9], off
	global_load_dwordx2 v[30:31], v[8:9], off offset:512
	global_load_dwordx2 v[28:29], v[8:9], off offset:1024
	global_load_dwordx2 v[26:27], v[8:9], off offset:1536
	global_load_dwordx2 v[24:25], v[8:9], off offset:2048
	global_load_dwordx2 v[22:23], v[8:9], off offset:2560
	global_load_dwordx2 v[20:21], v[8:9], off offset:3072
	global_load_dwordx2 v[18:19], v[8:9], off offset:3584
	v_add_co_u32_e32 v2, vcc, s26, v2
	s_waitcnt vmcnt(23)
	v_fmamk_f32 v64, v5, 0x80000000, v64
	v_addc_co_u32_e32 v3, vcc, 0, v3, vcc
	global_load_dwordx2 v[16:17], v[2:3], off
	global_load_dwordx2 v[14:15], v[2:3], off offset:512
	global_load_dwordx2 v[12:13], v[2:3], off offset:1024
	global_load_dwordx2 v[10:11], v[2:3], off offset:1536
	global_load_dwordx2 v[8:9], v[2:3], off offset:2048
	global_load_dwordx2 v[6:7], v[2:3], off offset:2560
	s_nop 0
	global_load_dwordx2 v[2:3], v[2:3], off offset:3072
	v_fmac_f32_e32 v65, 0, v5
	s_cselect_b64 vcc, -1, 0
	v_fmac_f32_e32 v64, 0, v4
	v_fmac_f32_e32 v65, 0, v4
	v_cndmask_b32_e64 v64, v64, 0, vcc
	v_cndmask_b32_e64 v65, v65, 0, vcc
	s_cmp_gt_u32 s22, 1
	s_waitcnt vmcnt(29)
	v_fma_f32 v62, -v5, v65, v62
	v_fmac_f32_e32 v63, v5, v64
	s_cselect_b64 s[0:1], -1, 0
	v_fmac_f32_e32 v62, v4, v64
	v_fmac_f32_e32 v63, v4, v65
	v_cndmask_b32_e64 v62, v64, v62, s[0:1]
	v_cndmask_b32_e64 v63, v65, v63, s[0:1]
	s_cmp_gt_u32 s22, 2
	s_waitcnt vmcnt(28)
	v_fma_f32 v60, -v5, v63, v60
	v_fmac_f32_e32 v61, v5, v62
	s_cselect_b64 s[0:1], -1, 0
	v_fmac_f32_e32 v60, v4, v62
	v_fmac_f32_e32 v61, v4, v63
	v_cndmask_b32_e64 v60, v62, v60, s[0:1]
	v_cndmask_b32_e64 v61, v63, v61, s[0:1]
	s_cmp_gt_u32 s22, 3
	s_waitcnt vmcnt(27)
	v_fma_f32 v58, -v5, v61, v58
	v_fmac_f32_e32 v59, v5, v60
	s_cselect_b64 s[0:1], -1, 0
	v_fmac_f32_e32 v58, v4, v60
	v_fmac_f32_e32 v59, v4, v61
	v_cndmask_b32_e64 v58, v60, v58, s[0:1]
	v_cndmask_b32_e64 v59, v61, v59, s[0:1]
	s_cmp_gt_u32 s22, 4
	s_waitcnt vmcnt(26)
	v_fma_f32 v56, -v5, v59, v56
	v_fmac_f32_e32 v57, v5, v58
	s_cselect_b64 s[0:1], -1, 0
	v_fmac_f32_e32 v56, v4, v58
	v_fmac_f32_e32 v57, v4, v59
	v_cndmask_b32_e64 v56, v58, v56, s[0:1]
	v_cndmask_b32_e64 v57, v59, v57, s[0:1]
	s_cmp_gt_u32 s22, 5
	s_waitcnt vmcnt(25)
	v_fma_f32 v54, -v5, v57, v54
	v_fmac_f32_e32 v55, v5, v56
	s_cselect_b64 s[0:1], -1, 0
	v_fmac_f32_e32 v54, v4, v56
	v_fmac_f32_e32 v55, v4, v57
	v_cndmask_b32_e64 v54, v56, v54, s[0:1]
	v_cndmask_b32_e64 v55, v57, v55, s[0:1]
	s_cmp_gt_u32 s22, 6
	s_waitcnt vmcnt(24)
	v_fma_f32 v52, -v5, v55, v52
	v_fmac_f32_e32 v53, v5, v54
	s_cselect_b64 s[0:1], -1, 0
	v_fmac_f32_e32 v52, v4, v54
	v_fmac_f32_e32 v53, v4, v55
	v_cndmask_b32_e64 v52, v54, v52, s[0:1]
	v_cndmask_b32_e64 v53, v55, v53, s[0:1]
	s_cmp_gt_u32 s22, 7
	s_waitcnt vmcnt(23)
	v_fma_f32 v50, -v5, v53, v50
	v_fmac_f32_e32 v51, v5, v52
	s_cselect_b64 s[0:1], -1, 0
	v_fmac_f32_e32 v50, v4, v52
	v_fmac_f32_e32 v51, v4, v53
	v_cndmask_b32_e64 v50, v52, v50, s[0:1]
	v_cndmask_b32_e64 v51, v53, v51, s[0:1]
	s_cmp_gt_u32 s22, 8
	s_waitcnt vmcnt(22)
	v_fma_f32 v48, -v5, v51, v48
	v_fmac_f32_e32 v49, v5, v50
	s_cselect_b64 s[0:1], -1, 0
	v_fmac_f32_e32 v48, v4, v50
	v_fmac_f32_e32 v49, v4, v51
	v_cndmask_b32_e64 v48, v50, v48, s[0:1]
	v_cndmask_b32_e64 v49, v51, v49, s[0:1]
	s_cmp_gt_u32 s22, 9
	s_waitcnt vmcnt(21)
	v_fma_f32 v46, -v5, v49, v46
	v_fmac_f32_e32 v47, v5, v48
	s_cselect_b64 s[0:1], -1, 0
	v_fmac_f32_e32 v46, v4, v48
	v_fmac_f32_e32 v47, v4, v49
	v_cndmask_b32_e64 v46, v48, v46, s[0:1]
	v_cndmask_b32_e64 v47, v49, v47, s[0:1]
	s_cmp_gt_u32 s22, 10
	s_waitcnt vmcnt(20)
	v_fma_f32 v44, -v5, v47, v44
	v_fmac_f32_e32 v45, v5, v46
	s_cselect_b64 s[0:1], -1, 0
	v_fmac_f32_e32 v44, v4, v46
	v_fmac_f32_e32 v45, v4, v47
	v_cndmask_b32_e64 v44, v46, v44, s[0:1]
	v_cndmask_b32_e64 v45, v47, v45, s[0:1]
	s_cmp_gt_u32 s22, 11
	s_waitcnt vmcnt(19)
	v_fma_f32 v42, -v5, v45, v42
	v_fmac_f32_e32 v43, v5, v44
	s_cselect_b64 s[0:1], -1, 0
	v_fmac_f32_e32 v42, v4, v44
	v_fmac_f32_e32 v43, v4, v45
	v_cndmask_b32_e64 v42, v44, v42, s[0:1]
	v_cndmask_b32_e64 v43, v45, v43, s[0:1]
	s_cmp_gt_u32 s22, 12
	s_waitcnt vmcnt(18)
; template <int DIR> ...
;     ...
;       for (int mm = 0; mm < 32; ++mm) { const int m = DIR ? 31 - mm : mm; const bool use = DIR ? (m > n) : (m < n);
;           const float nsr = fmaf(tr, sr, fmaf(-ti, si, ev[m].x)), nsi = fmaf(tr, si, fmaf(ti, sr, ev[m].y)); sr = use ? nsr : sr; si = use ? nsi : si; } }
	v_fma_f32 v40, -v5, v43, v40
	v_fmac_f32_e32 v41, v5, v42
	s_cselect_b64 s[0:1], -1, 0
	v_fmac_f32_e32 v40, v4, v42
	v_fmac_f32_e32 v41, v4, v43
	v_cndmask_b32_e64 v40, v42, v40, s[0:1]
	v_cndmask_b32_e64 v41, v43, v41, s[0:1]
	s_cmp_gt_u32 s22, 13
	s_waitcnt vmcnt(17)
	v_fma_f32 v38, -v5, v41, v38
	v_fmac_f32_e32 v39, v5, v40
	s_cselect_b64 s[0:1], -1, 0
	v_fmac_f32_e32 v38, v4, v40
	v_fmac_f32_e32 v39, v4, v41
	v_cndmask_b32_e64 v38, v40, v38, s[0:1]
	v_cndmask_b32_e64 v39, v41, v39, s[0:1]
	s_cmp_gt_u32 s22, 14
	s_waitcnt vmcnt(16)
	v_fma_f32 v36, -v5, v39, v36
	v_fmac_f32_e32 v37, v5, v38
	s_cselect_b64 s[0:1], -1, 0
	v_fmac_f32_e32 v36, v4, v38
	v_fmac_f32_e32 v37, v4, v39
	v_cndmask_b32_e64 v36, v38, v36, s[0:1]
	v_cndmask_b32_e64 v37, v39, v37, s[0:1]
	s_cmp_gt_u32 s22, 15
	s_waitcnt vmcnt(15)
	v_fma_f32 v34, -v5, v37, v34
	v_fmac_f32_e32 v35, v5, v36
	s_cselect_b64 s[0:1], -1, 0
	v_fmac_f32_e32 v34, v4, v36
	v_fmac_f32_e32 v35, v4, v37
	v_cndmask_b32_e64 v34, v36, v34, s[0:1]
	v_cndmask_b32_e64 v35, v37, v35, s[0:1]
	s_cmp_gt_u32 s22, 16
	s_waitcnt vmcnt(14)
	v_fma_f32 v32, -v5, v35, v32
	v_fmac_f32_e32 v33, v5, v34
	s_cselect_b64 s[0:1], -1, 0
	v_fmac_f32_e32 v32, v4, v34
	v_fmac_f32_e32 v33, v4, v35
	v_cndmask_b32_e64 v32, v34, v32, s[0:1]
	v_cndmask_b32_e64 v33, v35, v33, s[0:1]
	s_cmp_gt_u32 s22, 17
	s_waitcnt vmcnt(13)
	v_fma_f32 v30, -v5, v33, v30
	v_fmac_f32_e32 v31, v5, v32
	s_cselect_b64 s[0:1], -1, 0
	v_fmac_f32_e32 v30, v4, v32
	v_fmac_f32_e32 v31, v4, v33
	v_cndmask_b32_e64 v30, v32, v30, s[0:1]
	v_cndmask_b32_e64 v31, v33, v31, s[0:1]
	s_cmp_gt_u32 s22, 18
	s_waitcnt vmcnt(12)
	v_fma_f32 v28, -v5, v31, v28
	v_fmac_f32_e32 v29, v5, v30
	s_cselect_b64 s[0:1], -1, 0
	v_fmac_f32_e32 v28, v4, v30
	v_fmac_f32_e32 v29, v4, v31
	v_cndmask_b32_e64 v28, v30, v28, s[0:1]
	v_cndmask_b32_e64 v29, v31, v29, s[0:1]
	s_cmp_gt_u32 s22, 19
	s_waitcnt vmcnt(11)
	v_fma_f32 v26, -v5, v29, v26
	v_fmac_f32_e32 v27, v5, v28
	s_cselect_b64 s[0:1], -1, 0
	v_fmac_f32_e32 v26, v4, v28
	v_fmac_f32_e32 v27, v4, v29
	v_cndmask_b32_e64 v26, v28, v26, s[0:1]
	v_cndmask_b32_e64 v27, v29, v27, s[0:1]
	s_cmp_gt_u32 s22, 20
	s_waitcnt vmcnt(10)
	v_fma_f32 v24, -v5, v27, v24
	v_fmac_f32_e32 v25, v5, v26
	s_cselect_b64 s[0:1], -1, 0
	v_fmac_f32_e32 v24, v4, v26
	v_fmac_f32_e32 v25, v4, v27
	v_cndmask_b32_e64 v24, v26, v24, s[0:1]
	v_cndmask_b32_e64 v25, v27, v25, s[0:1]
	s_cmp_gt_u32 s22, 21
	s_waitcnt vmcnt(9)
	v_fma_f32 v22, -v5, v25, v22
	v_fmac_f32_e32 v23, v5, v24
	s_cselect_b64 s[0:1], -1, 0
	v_fmac_f32_e32 v22, v4, v24
	v_fmac_f32_e32 v23, v4, v25
	v_cndmask_b32_e64 v22, v24, v22, s[0:1]
	v_cndmask_b32_e64 v23, v25, v23, s[0:1]
	s_cmp_gt_u32 s22, 22
	s_waitcnt vmcnt(8)
	v_fma_f32 v20, -v5, v23, v20
	v_fmac_f32_e32 v21, v5, v22
	s_cselect_b64 s[0:1], -1, 0
	v_fmac_f32_e32 v20, v4, v22
	v_fmac_f32_e32 v21, v4, v23
	v_cndmask_b32_e64 v20, v22, v20, s[0:1]
	v_cndmask_b32_e64 v21, v23, v21, s[0:1]
	s_cmp_gt_u32 s22, 23
	s_waitcnt vmcnt(7)
	v_fma_f32 v18, -v5, v21, v18
	v_fmac_f32_e32 v19, v5, v20
	s_cselect_b64 s[0:1], -1, 0
	v_fmac_f32_e32 v18, v4, v20
	v_fmac_f32_e32 v19, v4, v21
	v_cndmask_b32_e64 v18, v20, v18, s[0:1]
	v_cndmask_b32_e64 v19, v21, v19, s[0:1]
	s_cmp_gt_u32 s22, 24
	s_waitcnt vmcnt(6)
	v_fma_f32 v16, -v5, v19, v16
	v_fmac_f32_e32 v17, v5, v18
	s_cselect_b64 s[0:1], -1, 0
	v_fmac_f32_e32 v16, v4, v18
	v_fmac_f32_e32 v17, v4, v19
	v_cndmask_b32_e64 v16, v18, v16, s[0:1]
	v_cndmask_b32_e64 v17, v19, v17, s[0:1]
	s_cmp_gt_u32 s22, 25
	s_waitcnt vmcnt(5)
	v_fma_f32 v14, -v5, v17, v14
	v_fmac_f32_e32 v15, v5, v16
	s_cselect_b64 s[0:1], -1, 0
	v_fmac_f32_e32 v14, v4, v16
	v_fmac_f32_e32 v15, v4, v17
	v_cndmask_b32_e64 v14, v16, v14, s[0:1]
	v_cndmask_b32_e64 v15, v17, v15, s[0:1]
	s_cmp_gt_u32 s22, 26
	s_waitcnt vmcnt(4)
	v_fma_f32 v12, -v5, v15, v12
	v_fmac_f32_e32 v13, v5, v14
	s_cselect_b64 s[0:1], -1, 0
	v_fmac_f32_e32 v12, v4, v14
	v_fmac_f32_e32 v13, v4, v15
	v_cndmask_b32_e64 v12, v14, v12, s[0:1]
	v_cndmask_b32_e64 v13, v15, v13, s[0:1]
	s_cmp_gt_u32 s22, 27
	s_waitcnt vmcnt(3)
	v_fma_f32 v10, -v5, v13, v10
	v_fmac_f32_e32 v11, v5, v12
	s_cselect_b64 s[0:1], -1, 0
	v_fmac_f32_e32 v10, v4, v12
	v_fmac_f32_e32 v11, v4, v13
	v_cndmask_b32_e64 v10, v12, v10, s[0:1]
	v_cndmask_b32_e64 v11, v13, v11, s[0:1]
	s_cmp_gt_u32 s22, 28
	s_waitcnt vmcnt(2)
	v_fma_f32 v8, -v5, v11, v8
	v_fmac_f32_e32 v9, v5, v10
	s_cselect_b64 s[0:1], -1, 0
	v_fmac_f32_e32 v8, v4, v10
	v_fmac_f32_e32 v9, v4, v11
	v_cndmask_b32_e64 v8, v10, v8, s[0:1]
	v_cndmask_b32_e64 v9, v11, v9, s[0:1]
	s_cmp_gt_u32 s22, 29
	s_waitcnt vmcnt(1)
	v_fma_f32 v6, -v5, v9, v6
	v_fmac_f32_e32 v7, v5, v8
	s_cselect_b64 s[0:1], -1, 0
	v_fmac_f32_e32 v6, v4, v8
	v_fmac_f32_e32 v7, v4, v9
	s_cmp_eq_u32 s22, 31
	v_cndmask_b32_e64 v6, v8, v6, s[0:1]
	v_cndmask_b32_e64 v10, v9, v7, s[0:1]
	s_cselect_b64 s[0:1], -1, 0
	s_lshl_b32 s12, s31, 12
	s_waitcnt vmcnt(0)
; #define LAS __attribute__((address_space(3)))
; __device__ __forceinline__ unsigned cvt_pk_bf16(float lo, float hi) { unsigned r; asm volatile("v_cvt_pk_bf16_f32 %0, %1, %2" : "=v"(r) : "v"(lo), "v"(hi)); return r; }
; template <int DIR> ...
;     ...
;           const float nsr = fmaf(tr, sr, fmaf(-ti, si, ev[m].x)), nsi = fmaf(tr, si, fmaf(ti, sr, ev[m].y)); sr = use ? nsr : sr; si = use ? nsi : si; } }
;     const BuFrags f = load_bufrags(bbar_l + (size_t)dg * 2 * 64 * 16, lane);
;     bf16x8 cb[4];
; #pragma unroll
;     for (int ks = 0; ks < 4; ++ks) cb[ks] = *(const bf16x8*)(ctt_l + ((size_t)dg * 16 + (lane & 15)) * 128 + 32 * ks + 8 * (lane >> 4));
;     bf16x8 ua[4];
; #pragma unroll
;     for (int s = 0; s < 4; ++s) ua[s] = bu_load(proj, b * SEQ + n * 128 + (DIR ? 3 - s : s) * 32, g, lane);
; #pragma unroll
;     for (int s = 0; s < 4; ++s) { const int sb = DIR ? 3 - s : s; float BR[32], BI[32];
;         bu_block(ua[s], f, BR, BI);
; #pragma unroll
;         for (int tt = 0; tt < 32; ++tt) { const int t = DIR ? 31 - tt : tt; const float nsr = fmaf(ar, sr, fmaf(-ai, si, BR[t])), nsi = fmaf(ar, si, fmaf(ai, sr, BI[t])); sr = nsr; si = nsi;
;             *(LAS unsigned*)(sl + (t * 136 + 2 * lane) * 2) = cvt_pk_bf16(sr, si); }
	v_fma_f32 v2, -v5, v10, v2
	s_add_u32 s20, s3, s12
	v_fmac_f32_e32 v2, v4, v6
	s_addc_u32 s21, s34, 0
	v_fmac_f32_e32 v3, v5, v6
	v_cndmask_b32_e64 v66, v6, v2, s[0:1]
	v_lshl_add_u64 v[6:7], s[20:21], 0, v[158:159]
	v_lshl_add_u64 v[8:9], s[20:21], 0, v[162:163]
	v_lshl_add_u64 v[6:7], v[6:7], 0, v[160:161]
	v_lshl_add_u64 v[8:9], v[8:9], 0, v[160:161]
	global_load_dwordx4 v[122:125], v[6:7], off
	global_load_dwordx4 v[126:129], v[8:9], off
	global_load_dwordx4 v[130:133], v[6:7], off offset:2048
	v_lshl_add_u64 v[6:7], s[20:21], 0, v[164:165]
	v_lshl_add_u64 v[6:7], v[6:7], 0, v[160:161]
	global_load_dwordx4 v[134:137], v[6:7], off
	v_lshl_add_u64 v[6:7], v[156:157], 0, s[12:13]
	s_lshl_b32 s12, s14, 12
	s_lshl_b32 s14, s22, 7
	s_or_b32 s14, s14, s12
	v_or_b32_e32 v2, s14, v170
	v_fmac_f32_e32 v3, v4, v10
	v_mad_i64_i32 v[4:5], s[20:21], v2, s27, v[166:167]
	s_lshl_b32 s12, s31, 5
	v_lshl_add_u64 v[4:5], v[4:5], 0, s[12:13]
	v_lshl_add_u64 v[4:5], v[4:5], 0, v[160:161]
	global_load_dwordx4 v[118:121], v[6:7], off
	global_load_dwordx4 v[114:117], v[6:7], off offset:64
	global_load_dwordx4 v[110:113], v[6:7], off offset:128
	global_load_dwordx4 v[106:109], v[6:7], off offset:192
	v_or_b32_e32 v8, 32, v2
	global_load_dwordx4 v[4:7], v[4:5], off offset:3072
	v_mad_i64_i32 v[8:9], s[20:21], v8, s27, v[166:167]
	v_lshl_add_u64 v[8:9], v[8:9], 0, s[12:13]
	v_lshl_add_u64 v[8:9], v[8:9], 0, v[160:161]
	global_load_dwordx4 v[90:93], v[8:9], off offset:3072
	v_or_b32_e32 v8, 64, v2
	v_mad_i64_i32 v[8:9], s[20:21], v8, s27, v[166:167]
	v_lshl_add_u64 v[8:9], v[8:9], 0, s[12:13]
	v_lshl_add_u64 v[8:9], v[8:9], 0, v[160:161]
	v_or_b32_e32 v2, 0x60, v2
	global_load_dwordx4 v[98:101], v[8:9], off offset:3072
	v_mad_i64_i32 v[8:9], s[20:21], v2, s27, v[166:167]
	v_lshl_add_u64 v[8:9], v[8:9], 0, s[12:13]
	v_lshl_add_u64 v[8:9], v[8:9], 0, v[160:161]
	global_load_dwordx4 v[138:141], v[8:9], off offset:3072
	v_cndmask_b32_e64 v67, v10, v3, s[0:1]
	s_waitcnt vmcnt(3)
	v_mfma_f32_32x32x16_bf16 v[50:65], v[4:7], v[122:125], 0
	s_or_b32 s15, s31, 64
	s_add_u32 s4, s4, 0x40000
	s_addc_u32 s5, s5, 0
	s_cmp_lt_u32 s22, 30
	v_mfma_f32_32x32x16_bf16 v[18:33], v[4:7], v[126:129], 0
	v_mfma_f32_32x32x16_bf16 v[34:49], v[4:7], v[130:133], 0
	s_nop 10
	v_permlane32_swap_b32_e32 v50, v18
	v_fma_f32 v50, -v143, v67, v50
	v_permlane32_swap_b32_e32 v51, v19
	v_fmac_f32_e32 v50, v142, v66
	v_permlane32_swap_b32_e32 v52, v20
	v_mfma_f32_32x32x16_bf16 v[2:17], v[4:7], v[134:137], 0
	v_permlane32_swap_b32_e32 v53, v21
	v_permlane32_swap_b32_e32 v54, v22
	v_permlane32_swap_b32_e32 v55, v23
	v_permlane32_swap_b32_e32 v56, v24
	s_nop 7
	v_permlane32_swap_b32_e32 v34, v2
	v_fmac_f32_e32 v34, v143, v66
	v_permlane32_swap_b32_e32 v35, v3
	v_fmac_f32_e32 v34, v142, v67
	v_fma_f32 v51, -v143, v34, v51
	v_fmac_f32_e32 v35, v143, v50
	v_permlane32_swap_b32_e32 v36, v4
	v_cvt_pk_bf16_f32 v66, v50, v34
	ds_write_b32 v171, v66
	v_fmac_f32_e32 v51, v142, v50
	v_fmac_f32_e32 v35, v142, v34
	v_cvt_pk_bf16_f32 v34, v51, v35
	ds_write_b32 v171, v34 offset:272
	v_fma_f32 v34, -v143, v35, v52
	v_fmac_f32_e32 v36, v143, v51
	v_permlane32_swap_b32_e32 v37, v5
	v_fmac_f32_e32 v34, v142, v51
	v_fmac_f32_e32 v36, v142, v35
	v_cvt_pk_bf16_f32 v35, v34, v36
	ds_write_b32 v171, v35 offset:544
	v_fma_f32 v35, -v143, v36, v53
	v_fmac_f32_e32 v37, v143, v34
	v_fmac_f32_e32 v35, v142, v34
	v_fmac_f32_e32 v37, v142, v36
	v_fma_f32 v18, -v143, v37, v18
	v_fmac_f32_e32 v2, v143, v35
	v_fmac_f32_e32 v18, v142, v35
	v_fmac_f32_e32 v2, v142, v37
	v_cvt_pk_bf16_f32 v34, v35, v37
	v_fma_f32 v19, -v143, v2, v19
	v_fmac_f32_e32 v3, v143, v18
	ds_write_b32 v171, v34 offset:816
	v_cvt_pk_bf16_f32 v34, v18, v2
	ds_write_b32 v171, v34 offset:1088
	v_fmac_f32_e32 v19, v142, v18
	v_fmac_f32_e32 v3, v142, v2
	v_cvt_pk_bf16_f32 v2, v19, v3
	ds_write_b32 v171, v2 offset:1360
	v_fma_f32 v2, -v143, v3, v20
	v_fmac_f32_e32 v4, v143, v19
	v_fmac_f32_e32 v2, v142, v19
	v_fmac_f32_e32 v4, v142, v3
	v_cvt_pk_bf16_f32 v3, v2, v4
	ds_write_b32 v171, v3 offset:1632
	v_fma_f32 v3, -v143, v4, v21
	v_fmac_f32_e32 v5, v143, v2
	v_permlane32_swap_b32_e32 v38, v6
	v_fmac_f32_e32 v3, v142, v2
	v_fmac_f32_e32 v5, v142, v4
	v_cvt_pk_bf16_f32 v2, v3, v5
	ds_write_b32 v171, v2 offset:1904
	v_fma_f32 v2, -v143, v5, v54
	v_fmac_f32_e32 v38, v143, v3
	v_permlane32_swap_b32_e32 v39, v7
	v_fmac_f32_e32 v2, v142, v3
	v_fmac_f32_e32 v38, v142, v5
	v_cvt_pk_bf16_f32 v3, v2, v38
	ds_write_b32 v171, v3 offset:2176
	v_fma_f32 v3, -v143, v38, v55
	v_fmac_f32_e32 v39, v143, v2
	v_permlane32_swap_b32_e32 v40, v8
	v_fmac_f32_e32 v3, v142, v2
	v_fmac_f32_e32 v39, v142, v38
	v_cvt_pk_bf16_f32 v2, v3, v39
	ds_write_b32 v171, v2 offset:2448
	v_fma_f32 v2, -v143, v39, v56
	v_fmac_f32_e32 v40, v143, v3
	v_permlane32_swap_b32_e32 v57, v25
	v_permlane32_swap_b32_e32 v41, v9
	v_fmac_f32_e32 v2, v142, v3
	v_fmac_f32_e32 v40, v142, v39
	v_cvt_pk_bf16_f32 v3, v2, v40
	ds_write_b32 v171, v3 offset:2720
	v_fma_f32 v3, -v143, v40, v57
	v_fmac_f32_e32 v41, v143, v2
	v_fmac_f32_e32 v3, v142, v2
	v_fmac_f32_e32 v41, v142, v40
	v_cvt_pk_bf16_f32 v2, v3, v41
	ds_write_b32 v171, v2 offset:2992
	v_fma_f32 v2, -v143, v41, v22
	v_fmac_f32_e32 v6, v143, v3
	v_fmac_f32_e32 v2, v142, v3
	v_fmac_f32_e32 v6, v142, v41
	v_cvt_pk_bf16_f32 v3, v2, v6
	ds_write_b32 v171, v3 offset:3264
	v_fma_f32 v3, -v143, v6, v23
	v_fmac_f32_e32 v7, v143, v2
	v_fmac_f32_e32 v3, v142, v2
	v_fmac_f32_e32 v7, v142, v6
	v_cvt_pk_bf16_f32 v2, v3, v7
	ds_write_b32 v171, v2 offset:3536
	v_fma_f32 v2, -v143, v7, v24
	v_fmac_f32_e32 v8, v143, v3
	v_fmac_f32_e32 v2, v142, v3
	v_fmac_f32_e32 v8, v142, v7
; #define LAS __attribute__((address_space(3)))
; __device__ __forceinline__ unsigned cvt_pk_bf16(float lo, float hi) { unsigned r; asm volatile("v_cvt_pk_bf16_f32 %0, %1, %2" : "=v"(r) : "v"(lo), "v"(hi)); return r; }
; #define LDS_WAIT() asm volatile("s_waitcnt lgkmcnt(0)" ::: "memory")
; template <int DIR> ...
;     ...
;         for (int tt = 0; tt < 32; ++tt) { const int t = DIR ? 31 - tt : tt; const float nsr = fmaf(ar, sr, fmaf(-ai, si, BR[t])), nsi = fmaf(ar, si, fmaf(ai, sr, BI[t])); sr = nsr; si = nsi;
;             *(LAS unsigned*)(sl + (t * 136 + 2 * lane) * 2) = cvt_pk_bf16(sr, si); }
;         LDS_WAIT();
; #pragma unroll
;         for (int rb = 0; rb < 2; ++rb)
; #pragma unroll
;             for (int ks = 0; ks < 4; ++ks) { const bf16x8 a = *(const LAS bf16x8*)(sl + ((16 * rb + (lane & 15)) * 136 + 32 * ks + 8 * (lane >> 4)) * 2);
;                 yacc[2 * sb + rb] = __builtin_amdgcn_mfma_f32_16x16x32_bf16(a, cb[ks], yacc[2 * sb + rb], 0, 0, 0); }
;         LDS_WAIT(); }
	v_cvt_pk_bf16_f32 v3, v2, v8
	ds_write_b32 v171, v3 offset:3808
	v_fma_f32 v3, -v143, v8, v25
	v_fmac_f32_e32 v9, v143, v2
	v_permlane32_swap_b32_e32 v58, v26
	v_permlane32_swap_b32_e32 v42, v10
	v_fmac_f32_e32 v3, v142, v2
	v_fmac_f32_e32 v9, v142, v8
	v_cvt_pk_bf16_f32 v2, v3, v9
	ds_write_b32 v171, v2 offset:4080
	v_fma_f32 v2, -v143, v9, v58
	v_fmac_f32_e32 v42, v143, v3
	v_permlane32_swap_b32_e32 v59, v27
	v_permlane32_swap_b32_e32 v43, v11
	v_fmac_f32_e32 v2, v142, v3
	v_fmac_f32_e32 v42, v142, v9
	v_cvt_pk_bf16_f32 v3, v2, v42
	ds_write_b32 v171, v3 offset:4352
	v_fma_f32 v3, -v143, v42, v59
	v_fmac_f32_e32 v43, v143, v2
	v_permlane32_swap_b32_e32 v60, v28
	v_permlane32_swap_b32_e32 v44, v12
	v_fmac_f32_e32 v3, v142, v2
	v_fmac_f32_e32 v43, v142, v42
	v_cvt_pk_bf16_f32 v2, v3, v43
	ds_write_b32 v171, v2 offset:4624
	v_fma_f32 v2, -v143, v43, v60
	v_fmac_f32_e32 v44, v143, v3
	v_permlane32_swap_b32_e32 v61, v29
	v_permlane32_swap_b32_e32 v45, v13
	v_fmac_f32_e32 v2, v142, v3
	v_fmac_f32_e32 v44, v142, v43
	v_cvt_pk_bf16_f32 v3, v2, v44
	ds_write_b32 v171, v3 offset:4896
	v_fma_f32 v3, -v143, v44, v61
	v_fmac_f32_e32 v45, v143, v2
	v_fmac_f32_e32 v3, v142, v2
	v_fmac_f32_e32 v45, v142, v44
	v_cvt_pk_bf16_f32 v2, v3, v45
	ds_write_b32 v171, v2 offset:5168
	v_fma_f32 v2, -v143, v45, v26
	v_fmac_f32_e32 v10, v143, v3
	v_fmac_f32_e32 v2, v142, v3
	v_fmac_f32_e32 v10, v142, v45
	v_cvt_pk_bf16_f32 v3, v2, v10
	ds_write_b32 v171, v3 offset:5440
	v_fma_f32 v3, -v143, v10, v27
	v_fmac_f32_e32 v11, v143, v2
	v_fmac_f32_e32 v3, v142, v2
	v_fmac_f32_e32 v11, v142, v10
	v_cvt_pk_bf16_f32 v2, v3, v11
	ds_write_b32 v171, v2 offset:5712
	v_fma_f32 v2, -v143, v11, v28
	v_fmac_f32_e32 v12, v143, v3
	v_fmac_f32_e32 v2, v142, v3
	v_fmac_f32_e32 v12, v142, v11
	v_cvt_pk_bf16_f32 v3, v2, v12
	ds_write_b32 v171, v3 offset:5984
	v_fma_f32 v3, -v143, v12, v29
	v_fmac_f32_e32 v13, v143, v2
	v_permlane32_swap_b32_e32 v62, v30
	v_permlane32_swap_b32_e32 v46, v14
	v_fmac_f32_e32 v3, v142, v2
	v_fmac_f32_e32 v13, v142, v12
	v_cvt_pk_bf16_f32 v2, v3, v13
	ds_write_b32 v171, v2 offset:6256
	v_fma_f32 v2, -v143, v13, v62
	v_fmac_f32_e32 v46, v143, v3
	v_permlane32_swap_b32_e32 v63, v31
	v_permlane32_swap_b32_e32 v47, v15
	v_fmac_f32_e32 v2, v142, v3
	v_fmac_f32_e32 v46, v142, v13
	v_cvt_pk_bf16_f32 v3, v2, v46
	ds_write_b32 v171, v3 offset:6528
	v_fma_f32 v3, -v143, v46, v63
	v_fmac_f32_e32 v47, v143, v2
	v_permlane32_swap_b32_e32 v64, v32
	v_permlane32_swap_b32_e32 v48, v16
	v_fmac_f32_e32 v3, v142, v2
	v_fmac_f32_e32 v47, v142, v46
	v_cvt_pk_bf16_f32 v2, v3, v47
	ds_write_b32 v171, v2 offset:6800
	v_fma_f32 v2, -v143, v47, v64
	v_fmac_f32_e32 v48, v143, v3
	v_permlane32_swap_b32_e32 v65, v33
	v_permlane32_swap_b32_e32 v49, v17
	v_fmac_f32_e32 v2, v142, v3
	v_fmac_f32_e32 v48, v142, v47
	v_cvt_pk_bf16_f32 v3, v2, v48
	ds_write_b32 v171, v3 offset:7072
	v_fma_f32 v3, -v143, v48, v65
	v_fmac_f32_e32 v49, v143, v2
	v_fmac_f32_e32 v3, v142, v2
	v_fmac_f32_e32 v49, v142, v48
	v_cvt_pk_bf16_f32 v2, v3, v49
	ds_write_b32 v171, v2 offset:7344
	v_fma_f32 v2, -v143, v49, v30
	v_fmac_f32_e32 v14, v143, v3
	v_fmac_f32_e32 v2, v142, v3
	v_fmac_f32_e32 v14, v142, v49
	v_cvt_pk_bf16_f32 v3, v2, v14
	ds_write_b32 v171, v3 offset:7616
	v_fma_f32 v3, -v143, v14, v31
	v_fmac_f32_e32 v15, v143, v2
	v_fmac_f32_e32 v3, v142, v2
	v_fmac_f32_e32 v15, v142, v14
	v_cvt_pk_bf16_f32 v2, v3, v15
	ds_write_b32 v171, v2 offset:7888
	v_fma_f32 v2, -v143, v15, v32
	v_fmac_f32_e32 v16, v143, v3
	v_fmac_f32_e32 v2, v142, v3
	v_fmac_f32_e32 v16, v142, v15
	v_fma_f32 v10, -v143, v16, v33
	v_fmac_f32_e32 v17, v143, v2
	v_cvt_pk_bf16_f32 v3, v2, v16
	ds_write_b32 v171, v3 offset:8160
	v_fmac_f32_e32 v10, v142, v2
	v_fmac_f32_e32 v17, v142, v16
	v_cvt_pk_bf16_f32 v2, v10, v17
	ds_write_b32 v171, v2 offset:8432
	s_waitcnt lgkmcnt(0)
	ds_read_b128 v[2:5], v175
	ds_read_b128 v[6:9], v175 offset:64
	s_waitcnt lgkmcnt(1)
	v_mfma_f32_16x16x32_bf16 v[2:5], v[2:5], v[118:121], 0
	s_waitcnt lgkmcnt(0)
	v_mfma_f32_16x16x32_bf16 v[2:5], v[6:9], v[114:117], v[2:5]
	ds_read_b128 v[6:9], v175 offset:128
	s_waitcnt lgkmcnt(0)
	v_mfma_f32_16x16x32_bf16 v[2:5], v[6:9], v[110:113], v[2:5]
	ds_read_b128 v[6:9], v175 offset:192
	s_waitcnt lgkmcnt(0)
	v_mfma_f32_16x16x32_bf16 v[86:89], v[6:9], v[106:109], v[2:5]
	s_nop 4
	ds_read_b128 v[2:5], v175 offset:4352
	ds_read_b128 v[6:9], v175 offset:4416
	s_waitcnt lgkmcnt(1)
	v_mfma_f32_16x16x32_bf16 v[2:5], v[2:5], v[118:121], 0
	s_waitcnt lgkmcnt(0)
	v_mfma_f32_16x16x32_bf16 v[2:5], v[6:9], v[114:117], v[2:5]
	ds_read_b128 v[6:9], v175 offset:4480
	s_waitcnt lgkmcnt(0)
	v_mfma_f32_16x16x32_bf16 v[2:5], v[6:9], v[110:113], v[2:5]
	ds_read_b128 v[6:9], v175 offset:4544
	s_waitcnt lgkmcnt(0)
	s_waitcnt vmcnt(2)
	v_mfma_f32_32x32x16_bf16 v[66:81], v[90:93], v[122:125], 0
	v_mfma_f32_32x32x16_bf16 v[34:49], v[90:93], v[126:129], 0
	v_mfma_f32_32x32x16_bf16 v[50:65], v[90:93], v[130:133], 0
	s_nop 10
	v_permlane32_swap_b32_e32 v66, v34
	v_permlane32_swap_b32_e32 v67, v35
	v_permlane32_swap_b32_e32 v68, v36
	v_permlane32_swap_b32_e32 v69, v37
	v_mfma_f32_32x32x16_bf16 v[18:33], v[90:93], v[134:137], 0
	v_permlane32_swap_b32_e32 v70, v38
	v_permlane32_swap_b32_e32 v71, v39
	v_permlane32_swap_b32_e32 v72, v40
	v_permlane32_swap_b32_e32 v73, v41
	s_nop 7
	v_permlane32_swap_b32_e32 v50, v18
	s_waitcnt lgkmcnt(0)
; #define LAS __attribute__((address_space(3)))
; __device__ __forceinline__ unsigned cvt_pk_bf16(float lo, float hi) { unsigned r; asm volatile("v_cvt_pk_bf16_f32 %0, %1, %2" : "=v"(r) : "v"(lo), "v"(hi)); return r; }
; template <int DIR> ...
;     ...
;         for (int tt = 0; tt < 32; ++tt) { const int t = DIR ? 31 - tt : tt; const float nsr = fmaf(ar, sr, fmaf(-ai, si, BR[t])), nsi = fmaf(ar, si, fmaf(ai, sr, BI[t])); sr = nsr; si = nsi;
;             *(LAS unsigned*)(sl + (t * 136 + 2 * lane) * 2) = cvt_pk_bf16(sr, si); }
	v_mfma_f32_16x16x32_bf16 v[82:85], v[6:9], v[106:109], v[2:5]
	v_fmac_f32_e32 v50, v143, v10
	v_permlane32_swap_b32_e32 v51, v19
	s_nop 0
	v_fma_f32 v2, -v143, v17, v66
	v_fmac_f32_e32 v2, v142, v10
	v_fmac_f32_e32 v50, v142, v17
	v_cvt_pk_bf16_f32 v3, v2, v50
	ds_write_b32 v171, v3
	v_fma_f32 v3, -v143, v50, v67
	v_fmac_f32_e32 v51, v143, v2
	v_permlane32_swap_b32_e32 v52, v20
	v_fmac_f32_e32 v3, v142, v2
	v_fmac_f32_e32 v51, v142, v50
	v_cvt_pk_bf16_f32 v2, v3, v51
	ds_write_b32 v171, v2 offset:272
	v_fma_f32 v2, -v143, v51, v68
	v_fmac_f32_e32 v52, v143, v3
	v_permlane32_swap_b32_e32 v53, v21
	v_fmac_f32_e32 v2, v142, v3
	v_fmac_f32_e32 v52, v142, v51
	v_cvt_pk_bf16_f32 v3, v2, v52
	ds_write_b32 v171, v3 offset:544
	v_fma_f32 v3, -v143, v52, v69
	v_fmac_f32_e32 v53, v143, v2
	v_fmac_f32_e32 v3, v142, v2
	v_fmac_f32_e32 v53, v142, v52
	v_cvt_pk_bf16_f32 v2, v3, v53
	ds_write_b32 v171, v2 offset:816
	v_fma_f32 v2, -v143, v53, v34
	v_fmac_f32_e32 v18, v143, v3
	v_fmac_f32_e32 v2, v142, v3
	v_fmac_f32_e32 v18, v142, v53
	v_cvt_pk_bf16_f32 v3, v2, v18
	ds_write_b32 v171, v3 offset:1088
	v_fma_f32 v3, -v143, v18, v35
	v_fmac_f32_e32 v19, v143, v2
	v_fmac_f32_e32 v3, v142, v2
	v_fmac_f32_e32 v19, v142, v18
	v_cvt_pk_bf16_f32 v2, v3, v19
	ds_write_b32 v171, v2 offset:1360
	v_fma_f32 v2, -v143, v19, v36
	v_fmac_f32_e32 v20, v143, v3
	v_fmac_f32_e32 v2, v142, v3
	v_fmac_f32_e32 v20, v142, v19
	v_cvt_pk_bf16_f32 v3, v2, v20
	ds_write_b32 v171, v3 offset:1632
	v_fma_f32 v3, -v143, v20, v37
	v_fmac_f32_e32 v21, v143, v2
	v_permlane32_swap_b32_e32 v54, v22
	v_fmac_f32_e32 v3, v142, v2
	v_fmac_f32_e32 v21, v142, v20
	v_cvt_pk_bf16_f32 v2, v3, v21
	ds_write_b32 v171, v2 offset:1904
	v_fma_f32 v2, -v143, v21, v70
	v_fmac_f32_e32 v54, v143, v3
	v_permlane32_swap_b32_e32 v55, v23
	v_fmac_f32_e32 v2, v142, v3
	v_fmac_f32_e32 v54, v142, v21
	v_cvt_pk_bf16_f32 v3, v2, v54
	ds_write_b32 v171, v3 offset:2176
	v_fma_f32 v3, -v143, v54, v71
	v_fmac_f32_e32 v55, v143, v2
	v_permlane32_swap_b32_e32 v56, v24
	v_fmac_f32_e32 v3, v142, v2
	v_fmac_f32_e32 v55, v142, v54
	v_cvt_pk_bf16_f32 v2, v3, v55
	ds_write_b32 v171, v2 offset:2448
	v_fma_f32 v2, -v143, v55, v72
	v_fmac_f32_e32 v56, v143, v3
	v_permlane32_swap_b32_e32 v57, v25
	v_fmac_f32_e32 v2, v142, v3
	v_fmac_f32_e32 v56, v142, v55
	v_cvt_pk_bf16_f32 v3, v2, v56
	ds_write_b32 v171, v3 offset:2720
	v_fma_f32 v3, -v143, v56, v73
	v_fmac_f32_e32 v57, v143, v2
	v_fmac_f32_e32 v3, v142, v2
	v_fmac_f32_e32 v57, v142, v56
	v_cvt_pk_bf16_f32 v2, v3, v57
	ds_write_b32 v171, v2 offset:2992
	v_fma_f32 v2, -v143, v57, v38
	v_fmac_f32_e32 v22, v143, v3
	v_fmac_f32_e32 v2, v142, v3
	v_fmac_f32_e32 v22, v142, v57
	v_cvt_pk_bf16_f32 v3, v2, v22
	ds_write_b32 v171, v3 offset:3264
	v_fma_f32 v3, -v143, v22, v39
	v_fmac_f32_e32 v23, v143, v2
	v_fmac_f32_e32 v3, v142, v2
	v_fmac_f32_e32 v23, v142, v22
	v_cvt_pk_bf16_f32 v2, v3, v23
	ds_write_b32 v171, v2 offset:3536
	v_fma_f32 v2, -v143, v23, v40
	v_fmac_f32_e32 v24, v143, v3
	v_fmac_f32_e32 v2, v142, v3
	v_fmac_f32_e32 v24, v142, v23
	v_cvt_pk_bf16_f32 v3, v2, v24
	ds_write_b32 v171, v3 offset:3808
	v_fma_f32 v3, -v143, v24, v41
	v_fmac_f32_e32 v25, v143, v2
	v_permlane32_swap_b32_e32 v74, v42
	v_permlane32_swap_b32_e32 v58, v26
	v_fmac_f32_e32 v3, v142, v2
	v_fmac_f32_e32 v25, v142, v24
	v_cvt_pk_bf16_f32 v2, v3, v25
	ds_write_b32 v171, v2 offset:4080
	v_fma_f32 v2, -v143, v25, v74
	v_fmac_f32_e32 v58, v143, v3
	v_permlane32_swap_b32_e32 v75, v43
	v_permlane32_swap_b32_e32 v59, v27
	v_fmac_f32_e32 v2, v142, v3
	v_fmac_f32_e32 v58, v142, v25
	v_cvt_pk_bf16_f32 v3, v2, v58
	ds_write_b32 v171, v3 offset:4352
	v_fma_f32 v3, -v143, v58, v75
	v_fmac_f32_e32 v59, v143, v2
	v_permlane32_swap_b32_e32 v76, v44
	v_permlane32_swap_b32_e32 v60, v28
	v_fmac_f32_e32 v3, v142, v2
	v_fmac_f32_e32 v59, v142, v58
	v_cvt_pk_bf16_f32 v2, v3, v59
	ds_write_b32 v171, v2 offset:4624
	v_fma_f32 v2, -v143, v59, v76
	v_fmac_f32_e32 v60, v143, v3
	v_permlane32_swap_b32_e32 v77, v45
	v_permlane32_swap_b32_e32 v61, v29
	v_fmac_f32_e32 v2, v142, v3
	v_fmac_f32_e32 v60, v142, v59
	v_cvt_pk_bf16_f32 v3, v2, v60
	ds_write_b32 v171, v3 offset:4896
	v_fma_f32 v3, -v143, v60, v77
	v_fmac_f32_e32 v61, v143, v2
	v_fmac_f32_e32 v3, v142, v2
	v_fmac_f32_e32 v61, v142, v60
	v_cvt_pk_bf16_f32 v2, v3, v61
	ds_write_b32 v171, v2 offset:5168
	v_fma_f32 v2, -v143, v61, v42
	v_fmac_f32_e32 v26, v143, v3
	v_fmac_f32_e32 v2, v142, v3
	v_fmac_f32_e32 v26, v142, v61
	v_cvt_pk_bf16_f32 v3, v2, v26
	ds_write_b32 v171, v3 offset:5440
	v_fma_f32 v3, -v143, v26, v43
	v_fmac_f32_e32 v27, v143, v2
	v_fmac_f32_e32 v3, v142, v2
	v_fmac_f32_e32 v27, v142, v26
	v_cvt_pk_bf16_f32 v2, v3, v27
	ds_write_b32 v171, v2 offset:5712
	v_fma_f32 v2, -v143, v27, v44
	v_fmac_f32_e32 v28, v143, v3
	v_fmac_f32_e32 v2, v142, v3
	v_fmac_f32_e32 v28, v142, v27
	v_cvt_pk_bf16_f32 v3, v2, v28
	ds_write_b32 v171, v3 offset:5984
	v_fma_f32 v3, -v143, v28, v45
	v_fmac_f32_e32 v29, v143, v2
	v_permlane32_swap_b32_e32 v78, v46
	v_permlane32_swap_b32_e32 v62, v30
	v_fmac_f32_e32 v3, v142, v2
	v_fmac_f32_e32 v29, v142, v28
	v_cvt_pk_bf16_f32 v2, v3, v29
	ds_write_b32 v171, v2 offset:6256
	v_fma_f32 v2, -v143, v29, v78
	v_fmac_f32_e32 v62, v143, v3
	v_permlane32_swap_b32_e32 v79, v47
	v_permlane32_swap_b32_e32 v63, v31
	v_fmac_f32_e32 v2, v142, v3
	v_fmac_f32_e32 v62, v142, v29
	v_cvt_pk_bf16_f32 v3, v2, v62
	ds_write_b32 v171, v3 offset:6528
	v_fma_f32 v3, -v143, v62, v79
	v_fmac_f32_e32 v63, v143, v2
	v_permlane32_swap_b32_e32 v80, v48
	v_permlane32_swap_b32_e32 v64, v32
	v_fmac_f32_e32 v3, v142, v2
	v_fmac_f32_e32 v63, v142, v62
	v_cvt_pk_bf16_f32 v2, v3, v63
	ds_write_b32 v171, v2 offset:6800
	v_fma_f32 v2, -v143, v63, v80
	v_fmac_f32_e32 v64, v143, v3
	v_permlane32_swap_b32_e32 v81, v49
	v_permlane32_swap_b32_e32 v65, v33
	v_fmac_f32_e32 v2, v142, v3
	v_fmac_f32_e32 v64, v142, v63
	v_cvt_pk_bf16_f32 v3, v2, v64
	ds_write_b32 v171, v3 offset:7072
	v_fma_f32 v3, -v143, v64, v81
	v_fmac_f32_e32 v65, v143, v2
	v_fmac_f32_e32 v3, v142, v2
	v_fmac_f32_e32 v65, v142, v64
	v_cvt_pk_bf16_f32 v2, v3, v65
	ds_write_b32 v171, v2 offset:7344
	v_fma_f32 v2, -v143, v65, v46
	v_fmac_f32_e32 v30, v143, v3
	v_fmac_f32_e32 v2, v142, v3
	v_fmac_f32_e32 v30, v142, v65
	v_cvt_pk_bf16_f32 v3, v2, v30
	ds_write_b32 v171, v3 offset:7616
	v_fma_f32 v3, -v143, v30, v47
	v_fmac_f32_e32 v31, v143, v2
	v_fmac_f32_e32 v3, v142, v2
	v_fmac_f32_e32 v31, v142, v30
	v_cvt_pk_bf16_f32 v2, v3, v31
	ds_write_b32 v171, v2 offset:7888
	v_fma_f32 v2, -v143, v31, v48
	v_fmac_f32_e32 v32, v143, v3
	v_fmac_f32_e32 v2, v142, v3
	v_fmac_f32_e32 v32, v142, v31
	v_fma_f32 v18, -v143, v32, v49
	v_fmac_f32_e32 v33, v143, v2
	v_cvt_pk_bf16_f32 v3, v2, v32
	ds_write_b32 v171, v3 offset:8160
	v_fmac_f32_e32 v18, v142, v2
	v_fmac_f32_e32 v33, v142, v32
	v_cvt_pk_bf16_f32 v2, v18, v33
	ds_write_b32 v171, v2 offset:8432
	s_waitcnt lgkmcnt(0)
; #define LAS __attribute__((address_space(3)))
; __device__ __forceinline__ unsigned cvt_pk_bf16(float lo, float hi) { unsigned r; asm volatile("v_cvt_pk_bf16_f32 %0, %1, %2" : "=v"(r) : "v"(lo), "v"(hi)); return r; }
; #define LDS_WAIT() asm volatile("s_waitcnt lgkmcnt(0)" ::: "memory")
; template <int DIR> ...
;     ...
;     for (int s = 0; s < 4; ++s) { const int sb = DIR ? 3 - s : s; float BR[32], BI[32];
;         bu_block(ua[s], f, BR, BI);
; #pragma unroll
;         for (int tt = 0; tt < 32; ++tt) { const int t = DIR ? 31 - tt : tt; const float nsr = fmaf(ar, sr, fmaf(-ai, si, BR[t])), nsi = fmaf(ar, si, fmaf(ai, sr, BI[t])); sr = nsr; si = nsi;
;             *(LAS unsigned*)(sl + (t * 136 + 2 * lane) * 2) = cvt_pk_bf16(sr, si); }
;         LDS_WAIT();
; #pragma unroll
;         for (int rb = 0; rb < 2; ++rb)
; #pragma unroll
;             for (int ks = 0; ks < 4; ++ks) { const bf16x8 a = *(const LAS bf16x8*)(sl + ((16 * rb + (lane & 15)) * 136 + 32 * ks + 8 * (lane >> 4)) * 2);
;                 yacc[2 * sb + rb] = __builtin_amdgcn_mfma_f32_16x16x32_bf16(a, cb[ks], yacc[2 * sb + rb], 0, 0, 0); }
;         LDS_WAIT(); }
	ds_read_b128 v[2:5], v175
	ds_read_b128 v[6:9], v175 offset:64
	s_waitcnt lgkmcnt(1)
	v_mfma_f32_16x16x32_bf16 v[2:5], v[2:5], v[118:121], 0
	s_waitcnt lgkmcnt(0)
	v_mfma_f32_16x16x32_bf16 v[2:5], v[6:9], v[114:117], v[2:5]
	ds_read_b128 v[6:9], v175 offset:128
	s_waitcnt lgkmcnt(0)
	v_mfma_f32_16x16x32_bf16 v[2:5], v[6:9], v[110:113], v[2:5]
	ds_read_b128 v[6:9], v175 offset:192
	s_waitcnt lgkmcnt(0)
	v_mfma_f32_16x16x32_bf16 v[90:93], v[6:9], v[106:109], v[2:5]
	s_nop 4
	ds_read_b128 v[2:5], v175 offset:4352
	ds_read_b128 v[6:9], v175 offset:4416
	s_waitcnt lgkmcnt(1)
	v_mfma_f32_16x16x32_bf16 v[2:5], v[2:5], v[118:121], 0
	s_waitcnt lgkmcnt(0)
	v_mfma_f32_16x16x32_bf16 v[2:5], v[6:9], v[114:117], v[2:5]
	ds_read_b128 v[6:9], v175 offset:4480
	s_waitcnt lgkmcnt(0)
	v_mfma_f32_16x16x32_bf16 v[2:5], v[6:9], v[110:113], v[2:5]
	ds_read_b128 v[6:9], v175 offset:4544
	s_waitcnt lgkmcnt(0)
	s_waitcnt lgkmcnt(0)
	v_mfma_f32_16x16x32_bf16 v[94:97], v[6:9], v[106:109], v[2:5]
	s_waitcnt vmcnt(1)
	v_mfma_f32_32x32x16_bf16 v[66:81], v[98:101], v[122:125], 0
	v_mfma_f32_32x32x16_bf16 v[34:49], v[98:101], v[126:129], 0
	v_mfma_f32_32x32x16_bf16 v[50:65], v[98:101], v[130:133], 0
	s_nop 10
	v_permlane32_swap_b32_e32 v66, v34
	v_fma_f32 v19, -v143, v33, v66
	v_permlane32_swap_b32_e32 v67, v35
	v_fmac_f32_e32 v19, v142, v18
	v_permlane32_swap_b32_e32 v68, v36
	v_mfma_f32_32x32x16_bf16 v[2:17], v[98:101], v[134:137], 0
	v_permlane32_swap_b32_e32 v69, v37
	v_permlane32_swap_b32_e32 v70, v38
	v_permlane32_swap_b32_e32 v71, v39
	v_permlane32_swap_b32_e32 v72, v40
	s_nop 7
	v_permlane32_swap_b32_e32 v50, v2
	v_fmac_f32_e32 v50, v143, v18
	v_permlane32_swap_b32_e32 v51, v3
	v_fmac_f32_e32 v50, v142, v33
	v_cvt_pk_bf16_f32 v18, v19, v50
	ds_write_b32 v171, v18
	v_fma_f32 v18, -v143, v50, v67
	v_fmac_f32_e32 v51, v143, v19
	v_permlane32_swap_b32_e32 v52, v4
	v_fmac_f32_e32 v18, v142, v19
	v_fmac_f32_e32 v51, v142, v50
	v_cvt_pk_bf16_f32 v19, v18, v51
	ds_write_b32 v171, v19 offset:272
	v_fma_f32 v19, -v143, v51, v68
	v_fmac_f32_e32 v52, v143, v18
	v_permlane32_swap_b32_e32 v53, v5
	v_fmac_f32_e32 v19, v142, v18
	v_fmac_f32_e32 v52, v142, v51
	v_cvt_pk_bf16_f32 v18, v19, v52
	ds_write_b32 v171, v18 offset:544
	v_fma_f32 v18, -v143, v52, v69
	v_fmac_f32_e32 v53, v143, v19
	v_fmac_f32_e32 v18, v142, v19
	v_fmac_f32_e32 v53, v142, v52
	v_cvt_pk_bf16_f32 v19, v18, v53
	ds_write_b32 v171, v19 offset:816
	v_fma_f32 v19, -v143, v53, v34
	v_fmac_f32_e32 v2, v143, v18
	v_fmac_f32_e32 v19, v142, v18
	v_fmac_f32_e32 v2, v142, v53
	v_cvt_pk_bf16_f32 v18, v19, v2
	ds_write_b32 v171, v18 offset:1088
	v_fma_f32 v18, -v143, v2, v35
	v_fmac_f32_e32 v3, v143, v19
	v_fmac_f32_e32 v18, v142, v19
	v_fmac_f32_e32 v3, v142, v2
	v_cvt_pk_bf16_f32 v2, v18, v3
	ds_write_b32 v171, v2 offset:1360
	v_fma_f32 v2, -v143, v3, v36
	v_fmac_f32_e32 v4, v143, v18
	v_fmac_f32_e32 v2, v142, v18
	v_fmac_f32_e32 v4, v142, v3
	v_cvt_pk_bf16_f32 v3, v2, v4
	ds_write_b32 v171, v3 offset:1632
	v_fma_f32 v3, -v143, v4, v37
	v_fmac_f32_e32 v5, v143, v2
	v_permlane32_swap_b32_e32 v54, v6
	v_fmac_f32_e32 v3, v142, v2
	v_fmac_f32_e32 v5, v142, v4
	v_cvt_pk_bf16_f32 v2, v3, v5
	ds_write_b32 v171, v2 offset:1904
	v_fma_f32 v2, -v143, v5, v70
	v_fmac_f32_e32 v54, v143, v3
	v_permlane32_swap_b32_e32 v55, v7
	v_fmac_f32_e32 v2, v142, v3
	v_fmac_f32_e32 v54, v142, v5
	v_cvt_pk_bf16_f32 v3, v2, v54
	ds_write_b32 v171, v3 offset:2176
	v_fma_f32 v3, -v143, v54, v71
	v_fmac_f32_e32 v55, v143, v2
	v_permlane32_swap_b32_e32 v56, v8
	v_fmac_f32_e32 v3, v142, v2
	v_fmac_f32_e32 v55, v142, v54
	v_cvt_pk_bf16_f32 v2, v3, v55
	ds_write_b32 v171, v2 offset:2448
	v_fma_f32 v2, -v143, v55, v72
	v_fmac_f32_e32 v56, v143, v3
	v_permlane32_swap_b32_e32 v73, v41
	v_permlane32_swap_b32_e32 v57, v9
	v_fmac_f32_e32 v2, v142, v3
	v_fmac_f32_e32 v56, v142, v55
	v_cvt_pk_bf16_f32 v3, v2, v56
	ds_write_b32 v171, v3 offset:2720
	v_fma_f32 v3, -v143, v56, v73
	v_fmac_f32_e32 v57, v143, v2
	v_fmac_f32_e32 v3, v142, v2
	v_fmac_f32_e32 v57, v142, v56
	v_cvt_pk_bf16_f32 v2, v3, v57
	ds_write_b32 v171, v2 offset:2992
	v_fma_f32 v2, -v143, v57, v38
	v_fmac_f32_e32 v6, v143, v3
	v_fmac_f32_e32 v2, v142, v3
	v_fmac_f32_e32 v6, v142, v57
	v_cvt_pk_bf16_f32 v3, v2, v6
	ds_write_b32 v171, v3 offset:3264
	v_fma_f32 v3, -v143, v6, v39
	v_fmac_f32_e32 v7, v143, v2
	v_fmac_f32_e32 v3, v142, v2
	v_fmac_f32_e32 v7, v142, v6
	v_cvt_pk_bf16_f32 v2, v3, v7
	ds_write_b32 v171, v2 offset:3536
	v_fma_f32 v2, -v143, v7, v40
	v_fmac_f32_e32 v8, v143, v3
	v_fmac_f32_e32 v2, v142, v3
	v_fmac_f32_e32 v8, v142, v7
	v_cvt_pk_bf16_f32 v3, v2, v8
	ds_write_b32 v171, v3 offset:3808
	v_fma_f32 v3, -v143, v8, v41
	v_fmac_f32_e32 v9, v143, v2
	v_permlane32_swap_b32_e32 v74, v42
	v_permlane32_swap_b32_e32 v58, v10
	v_fmac_f32_e32 v3, v142, v2
	v_fmac_f32_e32 v9, v142, v8
	v_cvt_pk_bf16_f32 v2, v3, v9
	ds_write_b32 v171, v2 offset:4080
	v_fma_f32 v2, -v143, v9, v74
	v_fmac_f32_e32 v58, v143, v3
	v_permlane32_swap_b32_e32 v75, v43
	v_permlane32_swap_b32_e32 v59, v11
	v_fmac_f32_e32 v2, v142, v3
	v_fmac_f32_e32 v58, v142, v9
	v_cvt_pk_bf16_f32 v3, v2, v58
	ds_write_b32 v171, v3 offset:4352
	v_fma_f32 v3, -v143, v58, v75
	v_fmac_f32_e32 v59, v143, v2
	v_permlane32_swap_b32_e32 v76, v44
	v_permlane32_swap_b32_e32 v60, v12
	v_fmac_f32_e32 v3, v142, v2
	v_fmac_f32_e32 v59, v142, v58
	v_cvt_pk_bf16_f32 v2, v3, v59
	ds_write_b32 v171, v2 offset:4624
	v_fma_f32 v2, -v143, v59, v76
	v_fmac_f32_e32 v60, v143, v3
	v_permlane32_swap_b32_e32 v77, v45
	v_permlane32_swap_b32_e32 v61, v13
	v_fmac_f32_e32 v2, v142, v3
	v_fmac_f32_e32 v60, v142, v59
	v_cvt_pk_bf16_f32 v3, v2, v60
; #define LAS __attribute__((address_space(3)))
; __device__ __forceinline__ unsigned cvt_pk_bf16(float lo, float hi) { unsigned r; asm volatile("v_cvt_pk_bf16_f32 %0, %1, %2" : "=v"(r) : "v"(lo), "v"(hi)); return r; }
; #define LDS_WAIT() asm volatile("s_waitcnt lgkmcnt(0)" ::: "memory")
; template <int DIR> ...
;     ...
;     for (int s = 0; s < 4; ++s) { const int sb = DIR ? 3 - s : s; float BR[32], BI[32];
;         bu_block(ua[s], f, BR, BI);
; #pragma unroll
;         for (int tt = 0; tt < 32; ++tt) { const int t = DIR ? 31 - tt : tt; const float nsr = fmaf(ar, sr, fmaf(-ai, si, BR[t])), nsi = fmaf(ar, si, fmaf(ai, sr, BI[t])); sr = nsr; si = nsi;
;             *(LAS unsigned*)(sl + (t * 136 + 2 * lane) * 2) = cvt_pk_bf16(sr, si); }
;         LDS_WAIT();
; #pragma unroll
;         for (int rb = 0; rb < 2; ++rb)
; #pragma unroll
;             for (int ks = 0; ks < 4; ++ks) { const bf16x8 a = *(const LAS bf16x8*)(sl + ((16 * rb + (lane & 15)) * 136 + 32 * ks + 8 * (lane >> 4)) * 2);
;                 yacc[2 * sb + rb] = __builtin_amdgcn_mfma_f32_16x16x32_bf16(a, cb[ks], yacc[2 * sb + rb], 0, 0, 0); }
;         LDS_WAIT(); }
	ds_write_b32 v171, v3 offset:4896
	v_fma_f32 v3, -v143, v60, v77
	v_fmac_f32_e32 v61, v143, v2
	v_fmac_f32_e32 v3, v142, v2
	v_fmac_f32_e32 v61, v142, v60
	v_cvt_pk_bf16_f32 v2, v3, v61
	ds_write_b32 v171, v2 offset:5168
	v_fma_f32 v2, -v143, v61, v42
	v_fmac_f32_e32 v10, v143, v3
	v_fmac_f32_e32 v2, v142, v3
	v_fmac_f32_e32 v10, v142, v61
	v_cvt_pk_bf16_f32 v3, v2, v10
	ds_write_b32 v171, v3 offset:5440
	v_fma_f32 v3, -v143, v10, v43
	v_fmac_f32_e32 v11, v143, v2
	v_fmac_f32_e32 v3, v142, v2
	v_fmac_f32_e32 v11, v142, v10
	v_cvt_pk_bf16_f32 v2, v3, v11
	ds_write_b32 v171, v2 offset:5712
	v_fma_f32 v2, -v143, v11, v44
	v_fmac_f32_e32 v12, v143, v3
	v_fmac_f32_e32 v2, v142, v3
	v_fmac_f32_e32 v12, v142, v11
	v_cvt_pk_bf16_f32 v3, v2, v12
	ds_write_b32 v171, v3 offset:5984
	v_fma_f32 v3, -v143, v12, v45
	v_fmac_f32_e32 v13, v143, v2
	v_permlane32_swap_b32_e32 v78, v46
	v_permlane32_swap_b32_e32 v62, v14
	v_fmac_f32_e32 v3, v142, v2
	v_fmac_f32_e32 v13, v142, v12
	v_cvt_pk_bf16_f32 v2, v3, v13
	ds_write_b32 v171, v2 offset:6256
	v_fma_f32 v2, -v143, v13, v78
	v_fmac_f32_e32 v62, v143, v3
	v_permlane32_swap_b32_e32 v79, v47
	v_permlane32_swap_b32_e32 v63, v15
	v_fmac_f32_e32 v2, v142, v3
	v_fmac_f32_e32 v62, v142, v13
	v_cvt_pk_bf16_f32 v3, v2, v62
	ds_write_b32 v171, v3 offset:6528
	v_fma_f32 v3, -v143, v62, v79
	v_fmac_f32_e32 v63, v143, v2
	v_permlane32_swap_b32_e32 v80, v48
	v_permlane32_swap_b32_e32 v64, v16
	v_fmac_f32_e32 v3, v142, v2
	v_fmac_f32_e32 v63, v142, v62
	v_cvt_pk_bf16_f32 v2, v3, v63
	ds_write_b32 v171, v2 offset:6800
	v_fma_f32 v2, -v143, v63, v80
	v_fmac_f32_e32 v64, v143, v3
	v_permlane32_swap_b32_e32 v81, v49
	v_permlane32_swap_b32_e32 v65, v17
	v_fmac_f32_e32 v2, v142, v3
	v_fmac_f32_e32 v64, v142, v63
	v_cvt_pk_bf16_f32 v3, v2, v64
	ds_write_b32 v171, v3 offset:7072
	v_fma_f32 v3, -v143, v64, v81
	v_fmac_f32_e32 v65, v143, v2
	v_fmac_f32_e32 v3, v142, v2
	v_fmac_f32_e32 v65, v142, v64
	v_cvt_pk_bf16_f32 v2, v3, v65
	ds_write_b32 v171, v2 offset:7344
	v_fma_f32 v2, -v143, v65, v46
	v_fmac_f32_e32 v14, v143, v3
	v_fmac_f32_e32 v2, v142, v3
	v_fmac_f32_e32 v14, v142, v65
	v_cvt_pk_bf16_f32 v3, v2, v14
	ds_write_b32 v171, v3 offset:7616
	v_fma_f32 v3, -v143, v14, v47
	v_fmac_f32_e32 v15, v143, v2
	v_fmac_f32_e32 v3, v142, v2
	v_fmac_f32_e32 v15, v142, v14
	v_cvt_pk_bf16_f32 v2, v3, v15
	ds_write_b32 v171, v2 offset:7888
	v_fma_f32 v2, -v143, v15, v48
	v_fmac_f32_e32 v16, v143, v3
	v_fmac_f32_e32 v2, v142, v3
	v_fmac_f32_e32 v16, v142, v15
	v_fma_f32 v10, -v143, v16, v49
	v_fmac_f32_e32 v17, v143, v2
	v_cvt_pk_bf16_f32 v3, v2, v16
	ds_write_b32 v171, v3 offset:8160
	v_fmac_f32_e32 v10, v142, v2
	v_fmac_f32_e32 v17, v142, v16
	v_cvt_pk_bf16_f32 v2, v10, v17
	ds_write_b32 v171, v2 offset:8432
	s_waitcnt lgkmcnt(0)
	ds_read_b128 v[2:5], v175
	ds_read_b128 v[6:9], v175 offset:64
	s_waitcnt lgkmcnt(1)
	v_mfma_f32_16x16x32_bf16 v[2:5], v[2:5], v[118:121], 0
	s_waitcnt lgkmcnt(0)
	v_mfma_f32_16x16x32_bf16 v[2:5], v[6:9], v[114:117], v[2:5]
	ds_read_b128 v[6:9], v175 offset:128
	s_waitcnt lgkmcnt(0)
	v_mfma_f32_16x16x32_bf16 v[2:5], v[6:9], v[110:113], v[2:5]
	ds_read_b128 v[6:9], v175 offset:192
	s_waitcnt lgkmcnt(0)
	v_mfma_f32_16x16x32_bf16 v[98:101], v[6:9], v[106:109], v[2:5]
	s_nop 4
	ds_read_b128 v[2:5], v175 offset:4352
	ds_read_b128 v[6:9], v175 offset:4416
	s_waitcnt lgkmcnt(1)
	v_mfma_f32_16x16x32_bf16 v[2:5], v[2:5], v[118:121], 0
	s_waitcnt lgkmcnt(0)
	v_mfma_f32_16x16x32_bf16 v[2:5], v[6:9], v[114:117], v[2:5]
	ds_read_b128 v[6:9], v175 offset:4480
	s_waitcnt lgkmcnt(0)
	v_mfma_f32_16x16x32_bf16 v[2:5], v[6:9], v[110:113], v[2:5]
	ds_read_b128 v[6:9], v175 offset:4544
	s_waitcnt lgkmcnt(0)
	s_waitcnt vmcnt(0)
	v_mfma_f32_32x32x16_bf16 v[66:81], v[138:141], v[122:125], 0
	v_mfma_f32_32x32x16_bf16 v[34:49], v[138:141], v[126:129], 0
	v_mfma_f32_32x32x16_bf16 v[50:65], v[138:141], v[130:133], 0
	s_nop 10
	v_permlane32_swap_b32_e32 v66, v34
	v_permlane32_swap_b32_e32 v67, v35
	v_permlane32_swap_b32_e32 v68, v36
	v_permlane32_swap_b32_e32 v69, v37
	v_mfma_f32_32x32x16_bf16 v[18:33], v[138:141], v[134:137], 0
	v_permlane32_swap_b32_e32 v70, v38
	v_permlane32_swap_b32_e32 v71, v39
	v_permlane32_swap_b32_e32 v72, v40
	v_permlane32_swap_b32_e32 v73, v41
	s_nop 7
	v_permlane32_swap_b32_e32 v50, v18
	s_waitcnt lgkmcnt(0)
; #define LAS __attribute__((address_space(3)))
; __device__ __forceinline__ unsigned cvt_pk_bf16(float lo, float hi) { unsigned r; asm volatile("v_cvt_pk_bf16_f32 %0, %1, %2" : "=v"(r) : "v"(lo), "v"(hi)); return r; }
; template <int DIR> ...
;     ...
;         for (int tt = 0; tt < 32; ++tt) { const int t = DIR ? 31 - tt : tt; const float nsr = fmaf(ar, sr, fmaf(-ai, si, BR[t])), nsi = fmaf(ar, si, fmaf(ai, sr, BI[t])); sr = nsr; si = nsi;
;             *(LAS unsigned*)(sl + (t * 136 + 2 * lane) * 2) = cvt_pk_bf16(sr, si); }
	v_mfma_f32_16x16x32_bf16 v[102:105], v[6:9], v[106:109], v[2:5]
	v_fmac_f32_e32 v50, v143, v10
	v_permlane32_swap_b32_e32 v51, v19
	s_nop 0
	v_fma_f32 v2, -v143, v17, v66
	v_fmac_f32_e32 v2, v142, v10
	v_fmac_f32_e32 v50, v142, v17
	v_cvt_pk_bf16_f32 v3, v2, v50
	ds_write_b32 v171, v3
	v_fma_f32 v3, -v143, v50, v67
	v_fmac_f32_e32 v51, v143, v2
	v_permlane32_swap_b32_e32 v52, v20
	v_fmac_f32_e32 v3, v142, v2
	v_fmac_f32_e32 v51, v142, v50
	v_cvt_pk_bf16_f32 v2, v3, v51
	ds_write_b32 v171, v2 offset:272
	v_fma_f32 v2, -v143, v51, v68
	v_fmac_f32_e32 v52, v143, v3
	v_permlane32_swap_b32_e32 v53, v21
	v_fmac_f32_e32 v2, v142, v3
	v_fmac_f32_e32 v52, v142, v51
	v_cvt_pk_bf16_f32 v3, v2, v52
	ds_write_b32 v171, v3 offset:544
	v_fma_f32 v3, -v143, v52, v69
	v_fmac_f32_e32 v53, v143, v2
	v_fmac_f32_e32 v3, v142, v2
	v_fmac_f32_e32 v53, v142, v52
	v_cvt_pk_bf16_f32 v2, v3, v53
	ds_write_b32 v171, v2 offset:816
	v_fma_f32 v2, -v143, v53, v34
	v_fmac_f32_e32 v18, v143, v3
	v_fmac_f32_e32 v2, v142, v3
	v_fmac_f32_e32 v18, v142, v53
	v_cvt_pk_bf16_f32 v3, v2, v18
	ds_write_b32 v171, v3 offset:1088
	v_fma_f32 v3, -v143, v18, v35
	v_fmac_f32_e32 v19, v143, v2
	v_fmac_f32_e32 v3, v142, v2
	v_fmac_f32_e32 v19, v142, v18
	v_cvt_pk_bf16_f32 v2, v3, v19
	ds_write_b32 v171, v2 offset:1360
	v_fma_f32 v2, -v143, v19, v36
	v_fmac_f32_e32 v20, v143, v3
	v_fmac_f32_e32 v2, v142, v3
	v_fmac_f32_e32 v20, v142, v19
	v_cvt_pk_bf16_f32 v3, v2, v20
	ds_write_b32 v171, v3 offset:1632
	v_fma_f32 v3, -v143, v20, v37
	v_fmac_f32_e32 v21, v143, v2
	v_permlane32_swap_b32_e32 v54, v22
	v_fmac_f32_e32 v3, v142, v2
	v_fmac_f32_e32 v21, v142, v20
	v_cvt_pk_bf16_f32 v2, v3, v21
	ds_write_b32 v171, v2 offset:1904
	v_fma_f32 v2, -v143, v21, v70
	v_fmac_f32_e32 v54, v143, v3
	v_permlane32_swap_b32_e32 v55, v23
	v_fmac_f32_e32 v2, v142, v3
	v_fmac_f32_e32 v54, v142, v21
	v_cvt_pk_bf16_f32 v3, v2, v54
	ds_write_b32 v171, v3 offset:2176
	v_fma_f32 v3, -v143, v54, v71
	v_fmac_f32_e32 v55, v143, v2
	v_permlane32_swap_b32_e32 v56, v24
	v_fmac_f32_e32 v3, v142, v2
	v_fmac_f32_e32 v55, v142, v54
	v_cvt_pk_bf16_f32 v2, v3, v55
	ds_write_b32 v171, v2 offset:2448
	v_fma_f32 v2, -v143, v55, v72
	v_fmac_f32_e32 v56, v143, v3
	v_permlane32_swap_b32_e32 v57, v25
	v_fmac_f32_e32 v2, v142, v3
	v_fmac_f32_e32 v56, v142, v55
	v_cvt_pk_bf16_f32 v3, v2, v56
	ds_write_b32 v171, v3 offset:2720
	v_fma_f32 v3, -v143, v56, v73
	v_fmac_f32_e32 v57, v143, v2
	v_fmac_f32_e32 v3, v142, v2
	v_fmac_f32_e32 v57, v142, v56
	v_cvt_pk_bf16_f32 v2, v3, v57
	ds_write_b32 v171, v2 offset:2992
	v_fma_f32 v2, -v143, v57, v38
	v_fmac_f32_e32 v22, v143, v3
	v_fmac_f32_e32 v2, v142, v3
	v_fmac_f32_e32 v22, v142, v57
	v_cvt_pk_bf16_f32 v3, v2, v22
	ds_write_b32 v171, v3 offset:3264
	v_fma_f32 v3, -v143, v22, v39
	v_fmac_f32_e32 v23, v143, v2
	v_fmac_f32_e32 v3, v142, v2
	v_fmac_f32_e32 v23, v142, v22
	v_cvt_pk_bf16_f32 v2, v3, v23
	ds_write_b32 v171, v2 offset:3536
	v_fma_f32 v2, -v143, v23, v40
	v_fmac_f32_e32 v24, v143, v3
	v_fmac_f32_e32 v2, v142, v3
	v_fmac_f32_e32 v24, v142, v23
	v_cvt_pk_bf16_f32 v3, v2, v24
	ds_write_b32 v171, v3 offset:3808
	v_fma_f32 v3, -v143, v24, v41
	v_fmac_f32_e32 v25, v143, v2
	v_permlane32_swap_b32_e32 v74, v42
	v_permlane32_swap_b32_e32 v58, v26
	v_fmac_f32_e32 v3, v142, v2
	v_fmac_f32_e32 v25, v142, v24
	v_cvt_pk_bf16_f32 v2, v3, v25
	ds_write_b32 v171, v2 offset:4080
	v_fma_f32 v2, -v143, v25, v74
	v_fmac_f32_e32 v58, v143, v3
	v_permlane32_swap_b32_e32 v75, v43
	v_permlane32_swap_b32_e32 v59, v27
	v_fmac_f32_e32 v2, v142, v3
	v_fmac_f32_e32 v58, v142, v25
	v_cvt_pk_bf16_f32 v3, v2, v58
	ds_write_b32 v171, v3 offset:4352
	v_fma_f32 v3, -v143, v58, v75
	v_fmac_f32_e32 v59, v143, v2
	v_permlane32_swap_b32_e32 v76, v44
	v_permlane32_swap_b32_e32 v60, v28
	v_fmac_f32_e32 v3, v142, v2
	v_fmac_f32_e32 v59, v142, v58
	v_cvt_pk_bf16_f32 v2, v3, v59
	ds_write_b32 v171, v2 offset:4624
	v_fma_f32 v2, -v143, v59, v76
	v_fmac_f32_e32 v60, v143, v3
	v_permlane32_swap_b32_e32 v77, v45
	v_permlane32_swap_b32_e32 v61, v29
	v_fmac_f32_e32 v2, v142, v3
	v_fmac_f32_e32 v60, v142, v59
	v_cvt_pk_bf16_f32 v3, v2, v60
	ds_write_b32 v171, v3 offset:4896
	v_fma_f32 v3, -v143, v60, v77
	v_fmac_f32_e32 v61, v143, v2
	v_fmac_f32_e32 v3, v142, v2
	v_fmac_f32_e32 v61, v142, v60
	v_cvt_pk_bf16_f32 v2, v3, v61
	ds_write_b32 v171, v2 offset:5168
	v_fma_f32 v2, -v143, v61, v42
	v_fmac_f32_e32 v26, v143, v3
	v_fmac_f32_e32 v2, v142, v3
	v_fmac_f32_e32 v26, v142, v61
	v_cvt_pk_bf16_f32 v3, v2, v26
	ds_write_b32 v171, v3 offset:5440
	v_fma_f32 v3, -v143, v26, v43
	v_fmac_f32_e32 v27, v143, v2
	v_fmac_f32_e32 v3, v142, v2
	v_fmac_f32_e32 v27, v142, v26
	v_cvt_pk_bf16_f32 v2, v3, v27
	ds_write_b32 v171, v2 offset:5712
	v_fma_f32 v2, -v143, v27, v44
	v_fmac_f32_e32 v28, v143, v3
	v_fmac_f32_e32 v2, v142, v3
	v_fmac_f32_e32 v28, v142, v27
	v_cvt_pk_bf16_f32 v3, v2, v28
	ds_write_b32 v171, v3 offset:5984
	v_fma_f32 v3, -v143, v28, v45
	v_fmac_f32_e32 v29, v143, v2
	v_permlane32_swap_b32_e32 v78, v46
	v_permlane32_swap_b32_e32 v62, v30
	v_fmac_f32_e32 v3, v142, v2
	v_fmac_f32_e32 v29, v142, v28
	v_cvt_pk_bf16_f32 v2, v3, v29
	ds_write_b32 v171, v2 offset:6256
	v_fma_f32 v2, -v143, v29, v78
	v_fmac_f32_e32 v62, v143, v3
	v_permlane32_swap_b32_e32 v79, v47
	v_permlane32_swap_b32_e32 v63, v31
	v_fmac_f32_e32 v2, v142, v3
	v_fmac_f32_e32 v62, v142, v29
	v_cvt_pk_bf16_f32 v3, v2, v62
	ds_write_b32 v171, v3 offset:6528
	v_fma_f32 v3, -v143, v62, v79
	v_fmac_f32_e32 v63, v143, v2
	v_permlane32_swap_b32_e32 v80, v48
	v_permlane32_swap_b32_e32 v64, v32
	v_fmac_f32_e32 v3, v142, v2
	v_fmac_f32_e32 v63, v142, v62
	v_cvt_pk_bf16_f32 v2, v3, v63
	ds_write_b32 v171, v2 offset:6800
	v_fma_f32 v2, -v143, v63, v80
	v_fmac_f32_e32 v64, v143, v3
	v_permlane32_swap_b32_e32 v81, v49
	v_permlane32_swap_b32_e32 v65, v33
	v_fmac_f32_e32 v2, v142, v3
	v_fmac_f32_e32 v64, v142, v63
	v_cvt_pk_bf16_f32 v3, v2, v64
	ds_write_b32 v171, v3 offset:7072
	v_fma_f32 v3, -v143, v64, v81
	v_fmac_f32_e32 v65, v143, v2
	v_fmac_f32_e32 v3, v142, v2
	v_fmac_f32_e32 v65, v142, v64
	v_cvt_pk_bf16_f32 v2, v3, v65
	ds_write_b32 v171, v2 offset:7344
	v_fma_f32 v2, -v143, v65, v46
	v_fmac_f32_e32 v30, v143, v3
	v_fmac_f32_e32 v2, v142, v3
	v_fmac_f32_e32 v30, v142, v65
	v_cvt_pk_bf16_f32 v3, v2, v30
	ds_write_b32 v171, v3 offset:7616
	v_fma_f32 v3, -v143, v30, v47
	v_fmac_f32_e32 v31, v143, v2
	v_fmac_f32_e32 v3, v142, v2
	v_fmac_f32_e32 v31, v142, v30
	v_cvt_pk_bf16_f32 v2, v3, v31
	ds_write_b32 v171, v2 offset:7888
	v_fma_f32 v2, -v143, v31, v48
	v_fmac_f32_e32 v32, v143, v3
	v_fmac_f32_e32 v2, v142, v3
	v_fmac_f32_e32 v32, v142, v31
	v_cvt_pk_bf16_f32 v3, v2, v32
	ds_write_b32 v171, v3 offset:8160
	v_fma_f32 v3, -v143, v32, v49
	v_fmac_f32_e32 v33, v143, v2
	v_fmac_f32_e32 v3, v142, v2
	v_fmac_f32_e32 v33, v142, v32
	v_cvt_pk_bf16_f32 v2, v3, v33
	ds_write_b32 v171, v2 offset:8432
	s_waitcnt lgkmcnt(0)
; #define LAS __attribute__((address_space(3)))
; #define LDS_WAIT() asm volatile("s_waitcnt lgkmcnt(0)" ::: "memory")
; template <class T> __device__ __forceinline__ void est(T* p, T v) { if constexpr (MK_EPI_NT != 0) __builtin_nontemporal_store(v, p); else *p = v; }
; template <int DIR> ...
;     const int dg = DIR * 64 + g; const float ar = lamb_l[(dg * 64 + lane) * 2], ai = lamb_l[(dg * 64 + lane) * 2 + 1], tr = lamt_l[(dg * 64 + lane) * 2], ti = lamt_l[(dg * 64 + lane) * 2 + 1];
;     float sr = 0.f, si = 0.f;
;     { const float* e = est + ((((size_t)(DIR * 2 + b) * 64 + g) * 32) * 64 + lane) * 2; f32x2 ev[32];
; #pragma unroll
;       for (int m = 0; m < 32; ++m) ev[m] = *(const f32x2*)(e + (size_t)m * 128);
; #pragma unroll
;       for (int mm = 0; mm < 32; ++mm) { const int m = DIR ? 31 - mm : mm; const bool use = DIR ? (m > n) : (m < n);
;           const float nsr = fmaf(tr, sr, fmaf(-ti, si, ev[m].x)), nsi = fmaf(tr, si, fmaf(ti, sr, ev[m].y)); sr = use ? nsr : sr; si = use ? nsi : si; } }
;     ...
;         for (int rb = 0; rb < 2; ++rb)
; #pragma unroll
;             for (int ks = 0; ks < 4; ++ks) { const bf16x8 a = *(const LAS bf16x8*)(sl + ((16 * rb + (lane & 15)) * 136 + 32 * ks + 8 * (lane >> 4)) * 2);
;                 yacc[2 * sb + rb] = __builtin_amdgcn_mfma_f32_16x16x32_bf16(a, cb[ks], yacc[2 * sb + rb], 0, 0, 0); }
;         LDS_WAIT(); }
	ds_read_b128 v[2:5], v175
	ds_read_b128 v[6:9], v175 offset:64
	s_waitcnt lgkmcnt(1)
	v_mfma_f32_16x16x32_bf16 v[2:5], v[2:5], v[118:121], 0
	s_waitcnt lgkmcnt(0)
	v_mfma_f32_16x16x32_bf16 v[2:5], v[6:9], v[114:117], v[2:5]
	ds_read_b128 v[6:9], v175 offset:128
	s_waitcnt lgkmcnt(0)
	v_mfma_f32_16x16x32_bf16 v[2:5], v[6:9], v[110:113], v[2:5]
	ds_read_b128 v[6:9], v175 offset:192
	s_waitcnt lgkmcnt(0)
	v_mfma_f32_16x16x32_bf16 v[66:69], v[6:9], v[106:109], v[2:5]
	s_nop 4
	ds_read_b128 v[2:5], v175 offset:4352
	ds_read_b128 v[6:9], v175 offset:4416
	s_waitcnt lgkmcnt(1)
	v_mfma_f32_16x16x32_bf16 v[2:5], v[2:5], v[118:121], 0
	s_waitcnt lgkmcnt(0)
	v_mfma_f32_16x16x32_bf16 v[2:5], v[6:9], v[114:117], v[2:5]
	ds_read_b128 v[6:9], v175 offset:4480
	s_waitcnt lgkmcnt(0)
	v_mfma_f32_16x16x32_bf16 v[2:5], v[6:9], v[110:113], v[2:5]
	ds_read_b128 v[6:9], v175 offset:4544
	s_waitcnt lgkmcnt(0)
	s_waitcnt lgkmcnt(0)
	v_mfma_f32_16x16x32_bf16 v[70:73], v[6:9], v[106:109], v[2:5]
	s_nop 4
	v_lshl_or_b32 v2, s15, 9, v174
	global_load_dwordx2 v[168:169], v2, s[10:11]
	global_load_dwordx2 v[4:5], v2, s[8:9]
	v_mov_b32_e32 v3, s5
	v_or_b32_e32 v2, s4, v194
	v_lshl_add_u64 v[12:13], v[2:3], 3, s[76:77]
	v_add_co_u32_e64 v20, s[4:5], s16, v12
	global_load_dwordx2 v[2:3], v[12:13], off offset:512
	global_load_dwordx2 v[6:7], v[12:13], off offset:1024
	global_load_dwordx2 v[8:9], v[12:13], off offset:1536
	global_load_dwordx2 v[10:11], v[12:13], off offset:2048
	global_load_dwordx2 v[14:15], v[12:13], off offset:2560
	global_load_dwordx2 v[16:17], v[12:13], off offset:3072
	global_load_dwordx2 v[18:19], v[12:13], off offset:3584
	v_addc_co_u32_e64 v21, s[4:5], 0, v13, s[4:5]
	v_add_co_u32_e64 v22, s[4:5], s17, v12
	s_nop 1
	v_addc_co_u32_e64 v23, s[4:5], 0, v13, s[4:5]
	v_add_co_u32_e64 v12, s[4:5], s26, v12
	global_load_dwordx2 v[24:25], v[22:23], off offset:-4096
	global_load_dwordx2 v[26:27], v[20:21], off offset:512
	global_load_dwordx2 v[28:29], v[20:21], off offset:1024
	global_load_dwordx2 v[30:31], v[20:21], off offset:1536
	global_load_dwordx2 v[32:33], v[20:21], off offset:2048
	global_load_dwordx2 v[34:35], v[20:21], off offset:2560
	global_load_dwordx2 v[36:37], v[20:21], off offset:3072
	s_nop 0
	global_load_dwordx2 v[20:21], v[20:21], off offset:3584
	s_nop 0
	global_load_dwordx2 v[38:39], v[22:23], off
	global_load_dwordx2 v[40:41], v[22:23], off offset:512
	global_load_dwordx2 v[42:43], v[22:23], off offset:1024
	global_load_dwordx2 v[44:45], v[22:23], off offset:1536
	global_load_dwordx2 v[46:47], v[22:23], off offset:2048
	global_load_dwordx2 v[48:49], v[22:23], off offset:2560
	global_load_dwordx2 v[50:51], v[22:23], off offset:3072
	s_nop 0
	global_load_dwordx2 v[22:23], v[22:23], off offset:3584
	v_addc_co_u32_e64 v13, s[4:5], 0, v13, s[4:5]
	global_load_dwordx2 v[52:53], v[12:13], off
	global_load_dwordx2 v[54:55], v[12:13], off offset:512
	global_load_dwordx2 v[56:57], v[12:13], off offset:1024
	global_load_dwordx2 v[58:59], v[12:13], off offset:1536
	global_load_dwordx2 v[60:61], v[12:13], off offset:2048
	global_load_dwordx2 v[62:63], v[12:13], off offset:2560
	global_load_dwordx2 v[64:65], v[12:13], off offset:3072
	s_nop 0
	global_load_dwordx2 v[12:13], v[12:13], off offset:3584
	s_waitcnt vmcnt(0)
	v_fmamk_f32 v12, v5, 0x80000000, v12
	v_fmac_f32_e32 v13, 0, v5
	v_fmac_f32_e32 v12, 0, v4
	v_fmac_f32_e32 v13, 0, v4
	v_cndmask_b32_e64 v12, v12, 0, s[0:1]
	v_cndmask_b32_e64 v13, v13, 0, s[0:1]
	v_fma_f32 v64, -v5, v13, v64
	v_fmac_f32_e32 v65, v5, v12
	s_cselect_b64 s[0:1], -1, 0
	v_fmac_f32_e32 v64, v4, v12
	v_fmac_f32_e32 v65, v4, v13
	v_cndmask_b32_e64 v12, v12, v64, s[0:1]
	v_cndmask_b32_e64 v13, v13, v65, s[0:1]
	s_cmp_lt_u32 s22, 29
	v_fma_f32 v62, -v5, v13, v62
	v_fmac_f32_e32 v63, v5, v12
	s_cselect_b64 s[0:1], -1, 0
	v_fmac_f32_e32 v62, v4, v12
	v_fmac_f32_e32 v63, v4, v13
	v_cndmask_b32_e64 v12, v12, v62, s[0:1]
	v_cndmask_b32_e64 v13, v13, v63, s[0:1]
	s_cmp_lt_u32 s22, 28
	v_fma_f32 v60, -v5, v13, v60
	v_fmac_f32_e32 v61, v5, v12
	s_cselect_b64 s[0:1], -1, 0
	v_fmac_f32_e32 v60, v4, v12
	v_fmac_f32_e32 v61, v4, v13
	v_cndmask_b32_e64 v12, v12, v60, s[0:1]
	v_cndmask_b32_e64 v13, v13, v61, s[0:1]
	s_cmp_lt_u32 s22, 27
	v_fma_f32 v58, -v5, v13, v58
	v_fmac_f32_e32 v59, v5, v12
	s_cselect_b64 s[0:1], -1, 0
	v_fmac_f32_e32 v58, v4, v12
	v_fmac_f32_e32 v59, v4, v13
	v_cndmask_b32_e64 v12, v12, v58, s[0:1]
	v_cndmask_b32_e64 v13, v13, v59, s[0:1]
	s_cmp_lt_u32 s22, 26
	v_fma_f32 v56, -v5, v13, v56
	v_fmac_f32_e32 v57, v5, v12
	s_cselect_b64 s[0:1], -1, 0
	v_fmac_f32_e32 v56, v4, v12
	v_fmac_f32_e32 v57, v4, v13
	v_cndmask_b32_e64 v12, v12, v56, s[0:1]
	v_cndmask_b32_e64 v13, v13, v57, s[0:1]
	s_cmp_lt_u32 s22, 25
	v_fma_f32 v54, -v5, v13, v54
	v_fmac_f32_e32 v55, v5, v12
	s_cselect_b64 s[0:1], -1, 0
	v_fmac_f32_e32 v54, v4, v12
	v_fmac_f32_e32 v55, v4, v13
	v_cndmask_b32_e64 v12, v12, v54, s[0:1]
	v_cndmask_b32_e64 v13, v13, v55, s[0:1]
	s_cmp_lt_u32 s22, 24
	v_fma_f32 v52, -v5, v13, v52
	v_fmac_f32_e32 v53, v5, v12
	s_cselect_b64 s[0:1], -1, 0
	v_fmac_f32_e32 v52, v4, v12
	v_fmac_f32_e32 v53, v4, v13
	v_cndmask_b32_e64 v12, v12, v52, s[0:1]
	v_cndmask_b32_e64 v13, v13, v53, s[0:1]
	s_cmp_lt_u32 s22, 23
	v_fma_f32 v22, -v5, v13, v22
	v_fmac_f32_e32 v23, v5, v12
	s_cselect_b64 s[0:1], -1, 0
	v_fmac_f32_e32 v22, v4, v12
	v_fmac_f32_e32 v23, v4, v13
	v_cndmask_b32_e64 v12, v12, v22, s[0:1]
	v_cndmask_b32_e64 v13, v13, v23, s[0:1]
	s_cmp_lt_u32 s22, 22
	v_fma_f32 v22, -v5, v13, v50
	v_fmac_f32_e32 v51, v5, v12
	s_cselect_b64 s[0:1], -1, 0
	v_fmac_f32_e32 v22, v4, v12
	v_fmac_f32_e32 v51, v4, v13
	v_cndmask_b32_e64 v12, v12, v22, s[0:1]
; template <class T> __device__ __forceinline__ void est(T* p, T v) { if constexpr (MK_EPI_NT != 0) __builtin_nontemporal_store(v, p); else *p = v; }
; template <int DIR> ...
;     const int dg = DIR * 64 + g; const float ar = lamb_l[(dg * 64 + lane) * 2], ai = lamb_l[(dg * 64 + lane) * 2 + 1], tr = lamt_l[(dg * 64 + lane) * 2], ti = lamt_l[(dg * 64 + lane) * 2 + 1];
;     float sr = 0.f, si = 0.f;
;     { const float* e = est + ((((size_t)(DIR * 2 + b) * 64 + g) * 32) * 64 + lane) * 2; f32x2 ev[32];
; #pragma unroll
;       for (int m = 0; m < 32; ++m) ev[m] = *(const f32x2*)(e + (size_t)m * 128);
; #pragma unroll
;       for (int mm = 0; mm < 32; ++mm) { const int m = DIR ? 31 - mm : mm; const bool use = DIR ? (m > n) : (m < n);
;           const float nsr = fmaf(tr, sr, fmaf(-ti, si, ev[m].x)), nsi = fmaf(tr, si, fmaf(ti, sr, ev[m].y)); sr = use ? nsr : sr; si = use ? nsi : si; } }
;     const BuFrags f = load_bufrags(bbar_l + (size_t)dg * 2 * 64 * 16, lane);
;     bf16x8 cb[4];
; #pragma unroll
;     for (int ks = 0; ks < 4; ++ks) cb[ks] = *(const bf16x8*)(ctt_l + ((size_t)dg * 16 + (lane & 15)) * 128 + 32 * ks + 8 * (lane >> 4));
;     bf16x8 ua[4];
; #pragma unroll
;     for (int s = 0; s < 4; ++s) ua[s] = bu_load(proj, b * SEQ + n * 128 + (DIR ? 3 - s : s) * 32, g, lane);
	v_cndmask_b32_e64 v13, v13, v51, s[0:1]
	s_cmp_lt_u32 s22, 21
	v_fma_f32 v22, -v5, v13, v48
	v_fmac_f32_e32 v49, v5, v12
	s_cselect_b64 s[0:1], -1, 0
	v_fmac_f32_e32 v22, v4, v12
	v_fmac_f32_e32 v49, v4, v13
	v_cndmask_b32_e64 v12, v12, v22, s[0:1]
	v_cndmask_b32_e64 v13, v13, v49, s[0:1]
	s_cmp_lt_u32 s22, 20
	v_fma_f32 v22, -v5, v13, v46
	v_fmac_f32_e32 v47, v5, v12
	s_cselect_b64 s[0:1], -1, 0
	v_fmac_f32_e32 v22, v4, v12
	v_fmac_f32_e32 v47, v4, v13
	v_cndmask_b32_e64 v12, v12, v22, s[0:1]
	v_cndmask_b32_e64 v13, v13, v47, s[0:1]
	s_cmp_lt_u32 s22, 19
	v_fma_f32 v22, -v5, v13, v44
	v_fmac_f32_e32 v45, v5, v12
	s_cselect_b64 s[0:1], -1, 0
	v_fmac_f32_e32 v22, v4, v12
	v_fmac_f32_e32 v45, v4, v13
	v_cndmask_b32_e64 v12, v12, v22, s[0:1]
	v_cndmask_b32_e64 v13, v13, v45, s[0:1]
	s_cmp_lt_u32 s22, 18
	v_fma_f32 v22, -v5, v13, v42
	v_fmac_f32_e32 v43, v5, v12
	s_cselect_b64 s[0:1], -1, 0
	v_fmac_f32_e32 v22, v4, v12
	v_fmac_f32_e32 v43, v4, v13
	v_cndmask_b32_e64 v12, v12, v22, s[0:1]
	v_cndmask_b32_e64 v13, v13, v43, s[0:1]
	s_cmp_lt_u32 s22, 17
	v_fma_f32 v22, -v5, v13, v40
	v_fmac_f32_e32 v41, v5, v12
	s_cselect_b64 s[0:1], -1, 0
	v_fmac_f32_e32 v22, v4, v12
	v_fmac_f32_e32 v41, v4, v13
	v_cndmask_b32_e64 v12, v12, v22, s[0:1]
	v_cndmask_b32_e64 v13, v13, v41, s[0:1]
	s_cmp_lt_u32 s22, 16
	v_fma_f32 v22, -v5, v13, v38
	v_fmac_f32_e32 v39, v5, v12
	s_cselect_b64 s[0:1], -1, 0
	v_fmac_f32_e32 v22, v4, v12
	v_fmac_f32_e32 v39, v4, v13
	v_cndmask_b32_e64 v12, v12, v22, s[0:1]
	v_cndmask_b32_e64 v13, v13, v39, s[0:1]
	s_cmp_lt_u32 s22, 15
	v_fma_f32 v20, -v5, v13, v20
	v_fmac_f32_e32 v21, v5, v12
	s_cselect_b64 s[0:1], -1, 0
	v_fmac_f32_e32 v20, v4, v12
	v_fmac_f32_e32 v21, v4, v13
	v_cndmask_b32_e64 v12, v12, v20, s[0:1]
	v_cndmask_b32_e64 v13, v13, v21, s[0:1]
	s_cmp_lt_u32 s22, 14
	v_fma_f32 v20, -v5, v13, v36
	v_fmac_f32_e32 v37, v5, v12
	s_cselect_b64 s[0:1], -1, 0
	v_fmac_f32_e32 v20, v4, v12
	v_fmac_f32_e32 v37, v4, v13
	v_cndmask_b32_e64 v12, v12, v20, s[0:1]
	v_cndmask_b32_e64 v13, v13, v37, s[0:1]
	s_cmp_lt_u32 s22, 13
	v_fma_f32 v20, -v5, v13, v34
	v_fmac_f32_e32 v35, v5, v12
	s_cselect_b64 s[0:1], -1, 0
	v_fmac_f32_e32 v20, v4, v12
	v_fmac_f32_e32 v35, v4, v13
	v_cndmask_b32_e64 v12, v12, v20, s[0:1]
	v_cndmask_b32_e64 v13, v13, v35, s[0:1]
	s_cmp_lt_u32 s22, 12
	v_fma_f32 v20, -v5, v13, v32
	v_fmac_f32_e32 v33, v5, v12
	s_cselect_b64 s[0:1], -1, 0
	v_fmac_f32_e32 v20, v4, v12
	v_fmac_f32_e32 v33, v4, v13
	v_cndmask_b32_e64 v12, v12, v20, s[0:1]
	v_cndmask_b32_e64 v13, v13, v33, s[0:1]
	s_cmp_lt_u32 s22, 11
	v_fma_f32 v20, -v5, v13, v30
	v_fmac_f32_e32 v31, v5, v12
	s_cselect_b64 s[0:1], -1, 0
	v_fmac_f32_e32 v20, v4, v12
	v_fmac_f32_e32 v31, v4, v13
	v_cndmask_b32_e64 v12, v12, v20, s[0:1]
	v_cndmask_b32_e64 v13, v13, v31, s[0:1]
	s_cmp_lt_u32 s22, 10
	v_fma_f32 v20, -v5, v13, v28
	v_fmac_f32_e32 v29, v5, v12
	s_cselect_b64 s[0:1], -1, 0
	v_fmac_f32_e32 v20, v4, v12
	v_fmac_f32_e32 v29, v4, v13
	v_cndmask_b32_e64 v12, v12, v20, s[0:1]
	v_cndmask_b32_e64 v13, v13, v29, s[0:1]
	s_cmp_lt_u32 s22, 9
	v_fma_f32 v20, -v5, v13, v26
	v_fmac_f32_e32 v27, v5, v12
	s_cselect_b64 s[0:1], -1, 0
	v_fmac_f32_e32 v20, v4, v12
	v_fmac_f32_e32 v27, v4, v13
	v_cndmask_b32_e64 v12, v12, v20, s[0:1]
	v_cndmask_b32_e64 v13, v13, v27, s[0:1]
	s_cmp_lt_u32 s22, 8
	v_fma_f32 v20, -v5, v13, v24
	v_fmac_f32_e32 v25, v5, v12
	s_cselect_b64 s[0:1], -1, 0
	v_fmac_f32_e32 v20, v4, v12
	v_fmac_f32_e32 v25, v4, v13
	v_cndmask_b32_e64 v12, v12, v20, s[0:1]
	v_cndmask_b32_e64 v13, v13, v25, s[0:1]
	s_cmp_lt_u32 s22, 7
	v_fma_f32 v18, -v5, v13, v18
	v_fmac_f32_e32 v19, v5, v12
	s_cselect_b64 s[0:1], -1, 0
	v_fmac_f32_e32 v18, v4, v12
	v_fmac_f32_e32 v19, v4, v13
	v_cndmask_b32_e64 v12, v12, v18, s[0:1]
	v_cndmask_b32_e64 v13, v13, v19, s[0:1]
	s_cmp_lt_u32 s22, 6
	v_fma_f32 v16, -v5, v13, v16
	v_fmac_f32_e32 v17, v5, v12
	s_cselect_b64 s[0:1], -1, 0
	v_fmac_f32_e32 v16, v4, v12
	v_fmac_f32_e32 v17, v4, v13
	v_cndmask_b32_e64 v12, v12, v16, s[0:1]
	v_cndmask_b32_e64 v13, v13, v17, s[0:1]
	s_cmp_lt_u32 s22, 5
	v_fma_f32 v14, -v5, v13, v14
	v_fmac_f32_e32 v15, v5, v12
	s_cselect_b64 s[0:1], -1, 0
	v_fmac_f32_e32 v14, v4, v12
	v_fmac_f32_e32 v15, v4, v13
	v_cndmask_b32_e64 v12, v12, v14, s[0:1]
	v_cndmask_b32_e64 v13, v13, v15, s[0:1]
	s_cmp_lt_u32 s22, 4
	v_fma_f32 v10, -v5, v13, v10
	v_fmac_f32_e32 v11, v5, v12
	s_cselect_b64 s[0:1], -1, 0
	v_fmac_f32_e32 v10, v4, v12
	v_fmac_f32_e32 v11, v4, v13
	v_cndmask_b32_e64 v10, v12, v10, s[0:1]
	v_cndmask_b32_e64 v11, v13, v11, s[0:1]
	s_cmp_lt_u32 s22, 3
	v_fma_f32 v8, -v5, v11, v8
	v_fmac_f32_e32 v9, v5, v10
	s_cselect_b64 s[0:1], -1, 0
	v_fmac_f32_e32 v8, v4, v10
	v_fmac_f32_e32 v9, v4, v11
	v_cndmask_b32_e64 v8, v10, v8, s[0:1]
	v_cndmask_b32_e64 v9, v11, v9, s[0:1]
	s_cmp_lt_u32 s22, 2
	v_fma_f32 v6, -v5, v9, v6
	v_fmac_f32_e32 v7, v5, v8
	s_cselect_b64 s[0:1], -1, 0
	v_fmac_f32_e32 v6, v4, v8
	v_fmac_f32_e32 v7, v4, v9
	v_cndmask_b32_e64 v8, v8, v6, s[0:1]
	v_cndmask_b32_e64 v6, v9, v7, s[0:1]
	s_lshl_b32 s0, s15, 12
	v_fma_f32 v2, -v5, v6, v2
	s_add_u32 s4, s3, s0
	v_fmac_f32_e32 v2, v4, v8
	s_addc_u32 s5, s34, 0
	v_fmac_f32_e32 v3, v5, v8
	v_cndmask_b32_e32 v78, v8, v2, vcc
	v_lshl_add_u64 v[8:9], s[4:5], 0, v[158:159]
	v_lshl_add_u64 v[10:11], s[4:5], 0, v[162:163]
	v_lshl_add_u64 v[8:9], v[8:9], 0, v[160:161]
	v_lshl_add_u64 v[10:11], v[10:11], 0, v[160:161]
	global_load_dwordx4 v[134:137], v[8:9], off
	global_load_dwordx4 v[130:133], v[10:11], off
	global_load_dwordx4 v[122:125], v[8:9], off offset:2048
	v_lshl_add_u64 v[8:9], s[4:5], 0, v[164:165]
	v_or_b32_e32 v2, s14, v194
	s_mov_b32 s1, s13
	v_lshl_add_u64 v[8:9], v[8:9], 0, v[160:161]
	v_or_b32_e32 v2, 0x60, v2
	global_load_dwordx4 v[126:129], v[8:9], off
	v_lshl_add_u64 v[8:9], v[156:157], 0, s[0:1]
	v_fmac_f32_e32 v3, v4, v6
	v_mad_i64_i32 v[4:5], s[0:1], v2, s27, v[166:167]
	v_lshl_add_u64 v[4:5], v[4:5], 0, s[12:13]
	v_lshl_add_u64 v[4:5], v[4:5], 0, v[160:161]
	global_load_dwordx4 v[118:121], v[8:9], off
	global_load_dwordx4 v[114:117], v[8:9], off offset:64
	global_load_dwordx4 v[110:113], v[8:9], off offset:128
	global_load_dwordx4 v[106:109], v[8:9], off offset:192
	global_load_dwordx4 v[34:37], v[4:5], off offset:3072
	v_subrev_u32_e32 v4, 32, v2
	v_mad_i64_i32 v[4:5], s[0:1], v4, s27, v[166:167]
	v_lshl_add_u64 v[4:5], v[4:5], 0, s[12:13]
	v_lshl_add_u64 v[4:5], v[4:5], 0, v[160:161]
	v_subrev_u32_e32 v2, 64, v2
	global_load_dwordx4 v[74:77], v[4:5], off offset:3072
	v_mad_i64_i32 v[4:5], s[0:1], v2, s27, v[166:167]
	v_lshl_add_u64 v[4:5], v[4:5], 0, s[12:13]
	v_lshl_add_u64 v[4:5], v[4:5], 0, v[160:161]
	v_bitop3_b32 v2, s14, v176, v194 bitop3:0xc8
	global_load_dwordx4 v[150:153], v[4:5], off offset:3072
	v_mad_i64_i32 v[4:5], s[0:1], v2, s27, v[166:167]
	v_lshl_add_u64 v[4:5], v[4:5], 0, s[12:13]
	v_lshl_add_u64 v[4:5], v[4:5], 0, v[160:161]
	global_load_dwordx4 v[146:149], v[4:5], off offset:3072
	v_cndmask_b32_e32 v79, v6, v3, vcc
	s_waitcnt vmcnt(3)
; #define LAS __attribute__((address_space(3)))
; __device__ __forceinline__ unsigned cvt_pk_bf16(float lo, float hi) { unsigned r; asm volatile("v_cvt_pk_bf16_f32 %0, %1, %2" : "=v"(r) : "v"(lo), "v"(hi)); return r; }
; __device__ __forceinline__ void bu_block(const bf16x8 ua, const BuFrags& f, float (&BR)[32], float (&BI)[32]) {
;     const f32x16 z = {};
;     const f32x16 R0 = __builtin_amdgcn_mfma_f32_32x32x16_bf16(ua, f.r0, z, 0, 0, 0), R1 = __builtin_amdgcn_mfma_f32_32x32x16_bf16(ua, f.r1, z, 0, 0, 0);
;     const f32x16 I0 = __builtin_amdgcn_mfma_f32_32x32x16_bf16(ua, f.i0, z, 0, 0, 0), I1 = __builtin_amdgcn_mfma_f32_32x32x16_bf16(ua, f.i1, z, 0, 0, 0);
; #pragma unroll
;     for (int r = 0; r < 16; ++r) {
;         auto s = __builtin_amdgcn_permlane32_swap(__float_as_uint(R0[r]), __float_as_uint(R1[r]), false, false);
;         BR[8 * (r >> 2) + (r & 3)] = __uint_as_float(s[0]); BR[8 * (r >> 2) + 4 + (r & 3)] = __uint_as_float(s[1]);
;         auto q = __builtin_amdgcn_permlane32_swap(__float_as_uint(I0[r]), __float_as_uint(I1[r]), false, false);
;         BI[8 * (r >> 2) + (r & 3)] = __uint_as_float(q[0]); BI[8 * (r >> 2) + 4 + (r & 3)] = __uint_as_float(q[1]);
;     }
; template <int DIR> ...
;     ...
;     for (int s = 0; s < 4; ++s) { const int sb = DIR ? 3 - s : s; float BR[32], BI[32];
;         bu_block(ua[s], f, BR, BI);
; #pragma unroll
;         for (int tt = 0; tt < 32; ++tt) { const int t = DIR ? 31 - tt : tt; const float nsr = fmaf(ar, sr, fmaf(-ai, si, BR[t])), nsi = fmaf(ar, si, fmaf(ai, sr, BI[t])); sr = nsr; si = nsi;
;             *(LAS unsigned*)(sl + (t * 136 + 2 * lane) * 2) = cvt_pk_bf16(sr, si); }
	v_mfma_f32_32x32x16_bf16 v[18:33], v[34:37], v[134:137], 0
	s_add_i32 s30, s30, s58
	s_cmpk_gt_i32 s30, 0xfff
	v_mfma_f32_32x32x16_bf16 v[50:65], v[34:37], v[130:133], 0
	v_mfma_f32_32x32x16_bf16 v[2:17], v[34:37], v[122:125], 0
	s_nop 10
	v_permlane32_swap_b32_e32 v33, v65
	v_fma_f32 v65, -v169, v79, v65
	v_permlane32_swap_b32_e32 v32, v64
	v_fmac_f32_e32 v65, v168, v78
	v_permlane32_swap_b32_e32 v31, v63
	v_mfma_f32_32x32x16_bf16 v[34:49], v[34:37], v[126:129], 0
	v_permlane32_swap_b32_e32 v30, v62
	v_permlane32_swap_b32_e32 v29, v61
	v_permlane32_swap_b32_e32 v28, v60
	v_permlane32_swap_b32_e32 v27, v59
	s_nop 7
	v_permlane32_swap_b32_e32 v17, v49
	v_fmac_f32_e32 v49, v169, v78
	v_permlane32_swap_b32_e32 v16, v48
	v_fmac_f32_e32 v49, v168, v79
	v_fma_f32 v64, -v169, v49, v64
	v_fmac_f32_e32 v48, v169, v65
	v_permlane32_swap_b32_e32 v15, v47
	v_cvt_pk_bf16_f32 v78, v65, v49
	ds_write_b32 v171, v78 offset:8432
	v_fmac_f32_e32 v64, v168, v65
	v_fmac_f32_e32 v48, v168, v49
	v_cvt_pk_bf16_f32 v49, v64, v48
	ds_write_b32 v171, v49 offset:8160
	v_fma_f32 v49, -v169, v48, v63
	v_fmac_f32_e32 v47, v169, v64
	v_permlane32_swap_b32_e32 v14, v46
	v_fmac_f32_e32 v49, v168, v64
	v_fmac_f32_e32 v47, v168, v48
	v_cvt_pk_bf16_f32 v48, v49, v47
	ds_write_b32 v171, v48 offset:7888
	v_fma_f32 v48, -v169, v47, v62
	v_fmac_f32_e32 v46, v169, v49
	v_fmac_f32_e32 v48, v168, v49
	v_fmac_f32_e32 v46, v168, v47
	v_fma_f32 v33, -v169, v46, v33
	v_fmac_f32_e32 v17, v169, v48
	v_fmac_f32_e32 v33, v168, v48
	v_fmac_f32_e32 v17, v168, v46
	v_fma_f32 v32, -v169, v17, v32
	v_fmac_f32_e32 v16, v169, v33
	v_cvt_pk_bf16_f32 v47, v48, v46
	ds_write_b32 v171, v47 offset:7616
	v_cvt_pk_bf16_f32 v46, v33, v17
	ds_write_b32 v171, v46 offset:7344
	v_fmac_f32_e32 v32, v168, v33
	v_fmac_f32_e32 v16, v168, v17
	v_cvt_pk_bf16_f32 v17, v32, v16
	ds_write_b32 v171, v17 offset:7072
	v_fma_f32 v17, -v169, v16, v31
	v_fmac_f32_e32 v15, v169, v32
	v_fmac_f32_e32 v17, v168, v32
	v_fmac_f32_e32 v15, v168, v16
	v_cvt_pk_bf16_f32 v16, v17, v15
	ds_write_b32 v171, v16 offset:6800
	v_fma_f32 v16, -v169, v15, v30
	v_fmac_f32_e32 v14, v169, v17
	v_permlane32_swap_b32_e32 v13, v45
	v_fmac_f32_e32 v16, v168, v17
	v_fmac_f32_e32 v14, v168, v15
	v_cvt_pk_bf16_f32 v15, v16, v14
	ds_write_b32 v171, v15 offset:6528
	v_fma_f32 v15, -v169, v14, v61
	v_fmac_f32_e32 v45, v169, v16
	v_permlane32_swap_b32_e32 v12, v44
	v_fmac_f32_e32 v15, v168, v16
	v_fmac_f32_e32 v45, v168, v14
	v_cvt_pk_bf16_f32 v14, v15, v45
	ds_write_b32 v171, v14 offset:6256
	v_fma_f32 v14, -v169, v45, v60
	v_fmac_f32_e32 v44, v169, v15
	v_permlane32_swap_b32_e32 v11, v43
	v_fmac_f32_e32 v14, v168, v15
	v_fmac_f32_e32 v44, v168, v45
	v_cvt_pk_bf16_f32 v15, v14, v44
	ds_write_b32 v171, v15 offset:5984
	v_fma_f32 v15, -v169, v44, v59
	v_fmac_f32_e32 v43, v169, v14
	v_permlane32_swap_b32_e32 v26, v58
	v_permlane32_swap_b32_e32 v10, v42
	v_fmac_f32_e32 v15, v168, v14
	v_fmac_f32_e32 v43, v168, v44
	v_cvt_pk_bf16_f32 v14, v15, v43
	ds_write_b32 v171, v14 offset:5712
	v_fma_f32 v14, -v169, v43, v58
	v_fmac_f32_e32 v42, v169, v15
	v_fmac_f32_e32 v14, v168, v15
	v_fmac_f32_e32 v42, v168, v43
	v_cvt_pk_bf16_f32 v15, v14, v42
	ds_write_b32 v171, v15 offset:5440
	v_fma_f32 v15, -v169, v42, v29
	v_fmac_f32_e32 v13, v169, v14
	v_fmac_f32_e32 v15, v168, v14
	v_fmac_f32_e32 v13, v168, v42
	v_cvt_pk_bf16_f32 v14, v15, v13
	ds_write_b32 v171, v14 offset:5168
	v_fma_f32 v14, -v169, v13, v28
	v_fmac_f32_e32 v12, v169, v15
	v_fmac_f32_e32 v14, v168, v15
	v_fmac_f32_e32 v12, v168, v13
	v_cvt_pk_bf16_f32 v13, v14, v12
	ds_write_b32 v171, v13 offset:4896
	v_fma_f32 v13, -v169, v12, v27
	v_fmac_f32_e32 v11, v169, v14
	v_fmac_f32_e32 v13, v168, v14
	v_fmac_f32_e32 v11, v168, v12
	v_cvt_pk_bf16_f32 v12, v13, v11
	ds_write_b32 v171, v12 offset:4624
	v_fma_f32 v12, -v169, v11, v26
	v_fmac_f32_e32 v10, v169, v13
	v_permlane32_swap_b32_e32 v25, v57
	v_permlane32_swap_b32_e32 v9, v41
	v_fmac_f32_e32 v12, v168, v13
	v_fmac_f32_e32 v10, v168, v11
	v_cvt_pk_bf16_f32 v11, v12, v10
	ds_write_b32 v171, v11 offset:4352
	v_fma_f32 v11, -v169, v10, v57
	v_fmac_f32_e32 v41, v169, v12
	v_permlane32_swap_b32_e32 v24, v56
	v_permlane32_swap_b32_e32 v8, v40
	v_fmac_f32_e32 v11, v168, v12
	v_fmac_f32_e32 v41, v168, v10
	v_cvt_pk_bf16_f32 v10, v11, v41
	ds_write_b32 v171, v10 offset:4080
	v_fma_f32 v10, -v169, v41, v56
	v_fmac_f32_e32 v40, v169, v11
	v_permlane32_swap_b32_e32 v23, v55
	v_permlane32_swap_b32_e32 v7, v39
	v_fmac_f32_e32 v10, v168, v11
	v_fmac_f32_e32 v40, v168, v41
	v_cvt_pk_bf16_f32 v11, v10, v40
	ds_write_b32 v171, v11 offset:3808
	v_fma_f32 v11, -v169, v40, v55
	v_fmac_f32_e32 v39, v169, v10
	v_permlane32_swap_b32_e32 v22, v54
	v_permlane32_swap_b32_e32 v6, v38
	v_fmac_f32_e32 v11, v168, v10
	v_fmac_f32_e32 v39, v168, v40
	v_cvt_pk_bf16_f32 v10, v11, v39
	ds_write_b32 v171, v10 offset:3536
	v_fma_f32 v10, -v169, v39, v54
	v_fmac_f32_e32 v38, v169, v11
	v_fmac_f32_e32 v10, v168, v11
	v_fmac_f32_e32 v38, v168, v39
	v_cvt_pk_bf16_f32 v11, v10, v38
	ds_write_b32 v171, v11 offset:3264
	v_fma_f32 v11, -v169, v38, v25
	v_fmac_f32_e32 v9, v169, v10
	v_fmac_f32_e32 v11, v168, v10
	v_fmac_f32_e32 v9, v168, v38
	v_cvt_pk_bf16_f32 v10, v11, v9
	ds_write_b32 v171, v10 offset:2992
	v_fma_f32 v10, -v169, v9, v24
	v_fmac_f32_e32 v8, v169, v11
	v_fmac_f32_e32 v10, v168, v11
	v_fmac_f32_e32 v8, v168, v9
	v_cvt_pk_bf16_f32 v9, v10, v8
	ds_write_b32 v171, v9 offset:2720
	v_fma_f32 v9, -v169, v8, v23
	v_fmac_f32_e32 v7, v169, v10
	v_fmac_f32_e32 v9, v168, v10
	v_fmac_f32_e32 v7, v168, v8
	v_cvt_pk_bf16_f32 v8, v9, v7
	ds_write_b32 v171, v8 offset:2448
	v_fma_f32 v8, -v169, v7, v22
; #define LAS __attribute__((address_space(3)))
; __device__ __forceinline__ unsigned cvt_pk_bf16(float lo, float hi) { unsigned r; asm volatile("v_cvt_pk_bf16_f32 %0, %1, %2" : "=v"(r) : "v"(lo), "v"(hi)); return r; }
; #define LDS_WAIT() asm volatile("s_waitcnt lgkmcnt(0)" ::: "memory")
; template <int DIR> ...
;     ...
;     for (int s = 0; s < 4; ++s) { const int sb = DIR ? 3 - s : s; float BR[32], BI[32];
;         bu_block(ua[s], f, BR, BI);
; #pragma unroll
;         for (int tt = 0; tt < 32; ++tt) { const int t = DIR ? 31 - tt : tt; const float nsr = fmaf(ar, sr, fmaf(-ai, si, BR[t])), nsi = fmaf(ar, si, fmaf(ai, sr, BI[t])); sr = nsr; si = nsi;
;             *(LAS unsigned*)(sl + (t * 136 + 2 * lane) * 2) = cvt_pk_bf16(sr, si); }
;         LDS_WAIT();
; #pragma unroll
;         for (int rb = 0; rb < 2; ++rb)
; #pragma unroll
;             for (int ks = 0; ks < 4; ++ks) { const bf16x8 a = *(const LAS bf16x8*)(sl + ((16 * rb + (lane & 15)) * 136 + 32 * ks + 8 * (lane >> 4)) * 2);
;                 yacc[2 * sb + rb] = __builtin_amdgcn_mfma_f32_16x16x32_bf16(a, cb[ks], yacc[2 * sb + rb], 0, 0, 0); }
;         LDS_WAIT(); }
	v_fmac_f32_e32 v6, v169, v9
	v_permlane32_swap_b32_e32 v21, v53
	v_permlane32_swap_b32_e32 v5, v37
	v_fmac_f32_e32 v8, v168, v9
	v_fmac_f32_e32 v6, v168, v7
	v_cvt_pk_bf16_f32 v7, v8, v6
	ds_write_b32 v171, v7 offset:2176
	v_fma_f32 v7, -v169, v6, v53
	v_fmac_f32_e32 v37, v169, v8
	v_permlane32_swap_b32_e32 v20, v52
	v_permlane32_swap_b32_e32 v4, v36
	v_fmac_f32_e32 v7, v168, v8
	v_fmac_f32_e32 v37, v168, v6
	v_cvt_pk_bf16_f32 v6, v7, v37
	ds_write_b32 v171, v6 offset:1904
	v_fma_f32 v6, -v169, v37, v52
	v_fmac_f32_e32 v36, v169, v7
	v_permlane32_swap_b32_e32 v19, v51
	v_permlane32_swap_b32_e32 v3, v35
	v_fmac_f32_e32 v6, v168, v7
	v_fmac_f32_e32 v36, v168, v37
	v_cvt_pk_bf16_f32 v7, v6, v36
	ds_write_b32 v171, v7 offset:1632
	v_fma_f32 v7, -v169, v36, v51
	v_fmac_f32_e32 v35, v169, v6
	v_permlane32_swap_b32_e32 v18, v50
	v_permlane32_swap_b32_e32 v2, v34
	v_fmac_f32_e32 v7, v168, v6
	v_fmac_f32_e32 v35, v168, v36
	v_cvt_pk_bf16_f32 v6, v7, v35
	ds_write_b32 v171, v6 offset:1360
	v_fma_f32 v6, -v169, v35, v50
	v_fmac_f32_e32 v34, v169, v7
	v_fmac_f32_e32 v6, v168, v7
	v_fmac_f32_e32 v34, v168, v35
	v_cvt_pk_bf16_f32 v7, v6, v34
	ds_write_b32 v171, v7 offset:1088
	v_fma_f32 v7, -v169, v34, v21
	v_fmac_f32_e32 v5, v169, v6
	v_fmac_f32_e32 v7, v168, v6
	v_fmac_f32_e32 v5, v168, v34
	v_cvt_pk_bf16_f32 v6, v7, v5
	ds_write_b32 v171, v6 offset:816
	v_fma_f32 v6, -v169, v5, v20
	v_fmac_f32_e32 v4, v169, v7
	v_fmac_f32_e32 v6, v168, v7
	v_fmac_f32_e32 v4, v168, v5
	v_cvt_pk_bf16_f32 v5, v6, v4
	ds_write_b32 v171, v5 offset:544
	v_fma_f32 v5, -v169, v4, v19
	v_fmac_f32_e32 v3, v169, v6
	v_fmac_f32_e32 v5, v168, v6
	v_fmac_f32_e32 v3, v168, v4
	v_fma_f32 v12, -v169, v3, v18
	v_fmac_f32_e32 v2, v169, v5
	v_cvt_pk_bf16_f32 v4, v5, v3
	ds_write_b32 v171, v4 offset:272
	v_fmac_f32_e32 v12, v168, v5
	v_fmac_f32_e32 v2, v168, v3
	v_cvt_pk_bf16_f32 v3, v12, v2
	ds_write_b32 v171, v3
	s_waitcnt lgkmcnt(0)
	ds_read_b128 v[4:7], v175
	ds_read_b128 v[8:11], v175 offset:64
	s_waitcnt lgkmcnt(1)
	v_mfma_f32_16x16x32_bf16 v[4:7], v[4:7], v[118:121], v[66:69]
	s_waitcnt lgkmcnt(0)
	v_mfma_f32_16x16x32_bf16 v[4:7], v[8:11], v[114:117], v[4:7]
	ds_read_b128 v[8:11], v175 offset:128
	s_waitcnt lgkmcnt(0)
	v_mfma_f32_16x16x32_bf16 v[4:7], v[8:11], v[110:113], v[4:7]
	ds_read_b128 v[8:11], v175 offset:192
	s_waitcnt lgkmcnt(0)
	v_mfma_f32_16x16x32_bf16 v[142:145], v[8:11], v[106:109], v[4:7]
	s_nop 4
	ds_read_b128 v[4:7], v175 offset:4352
	ds_read_b128 v[8:11], v175 offset:4416
	s_waitcnt lgkmcnt(1)
	v_mfma_f32_16x16x32_bf16 v[4:7], v[4:7], v[118:121], v[70:73]
	s_waitcnt vmcnt(2)
	v_mfma_f32_32x32x16_bf16 v[34:49], v[74:77], v[134:137], 0
	v_mfma_f32_32x32x16_bf16 v[50:65], v[74:77], v[130:133], 0
	v_mfma_f32_32x32x16_bf16 v[18:33], v[74:77], v[122:125], 0
	s_nop 10
	v_permlane32_swap_b32_e32 v49, v65
	v_fma_f32 v3, -v169, v2, v65
	v_permlane32_swap_b32_e32 v48, v64
	v_fmac_f32_e32 v3, v168, v12
	v_permlane32_swap_b32_e32 v47, v63
	v_mfma_f32_32x32x16_bf16 v[66:81], v[74:77], v[126:129], 0
	v_permlane32_swap_b32_e32 v46, v62
	v_permlane32_swap_b32_e32 v45, v61
	v_permlane32_swap_b32_e32 v44, v60
	v_permlane32_swap_b32_e32 v43, v59
	s_waitcnt lgkmcnt(0)
	v_mfma_f32_16x16x32_bf16 v[4:7], v[8:11], v[114:117], v[4:7]
	ds_read_b128 v[8:11], v175 offset:4480
	s_nop 4
	v_permlane32_swap_b32_e32 v33, v81
	v_fmac_f32_e32 v81, v169, v12
	s_waitcnt lgkmcnt(0)
	v_mfma_f32_16x16x32_bf16 v[4:7], v[8:11], v[110:113], v[4:7]
	ds_read_b128 v[8:11], v175 offset:4544
	s_waitcnt lgkmcnt(0)
	v_permlane32_swap_b32_e32 v32, v80
	v_fmac_f32_e32 v81, v168, v2
	v_cvt_pk_bf16_f32 v2, v3, v81
	ds_write_b32 v171, v2 offset:8432
	v_fma_f32 v2, -v169, v81, v64
	v_fmac_f32_e32 v80, v169, v3
	v_permlane32_swap_b32_e32 v31, v79
	v_fmac_f32_e32 v2, v168, v3
	v_fmac_f32_e32 v80, v168, v81
	v_cvt_pk_bf16_f32 v3, v2, v80
	ds_write_b32 v171, v3 offset:8160
	v_fma_f32 v3, -v169, v80, v63
	v_fmac_f32_e32 v79, v169, v2
	v_permlane32_swap_b32_e32 v30, v78
	v_fmac_f32_e32 v3, v168, v2
	v_fmac_f32_e32 v79, v168, v80
	v_cvt_pk_bf16_f32 v2, v3, v79
	ds_write_b32 v171, v2 offset:7888
	v_fma_f32 v2, -v169, v79, v62
	v_fmac_f32_e32 v78, v169, v3
	v_fmac_f32_e32 v2, v168, v3
	v_fmac_f32_e32 v78, v168, v79
	v_cvt_pk_bf16_f32 v3, v2, v78
	ds_write_b32 v171, v3 offset:7616
	v_fma_f32 v3, -v169, v78, v49
	v_fmac_f32_e32 v33, v169, v2
	v_fmac_f32_e32 v3, v168, v2
	v_fmac_f32_e32 v33, v168, v78
	v_cvt_pk_bf16_f32 v2, v3, v33
	ds_write_b32 v171, v2 offset:7344
	v_fma_f32 v2, -v169, v33, v48
	v_fmac_f32_e32 v32, v169, v3
	v_fmac_f32_e32 v2, v168, v3
	v_fmac_f32_e32 v32, v168, v33
	v_cvt_pk_bf16_f32 v3, v2, v32
	ds_write_b32 v171, v3 offset:7072
	v_fma_f32 v3, -v169, v32, v47
	v_fmac_f32_e32 v31, v169, v2
	v_fmac_f32_e32 v3, v168, v2
	v_fmac_f32_e32 v31, v168, v32
	v_cvt_pk_bf16_f32 v2, v3, v31
	ds_write_b32 v171, v2 offset:6800
	v_fma_f32 v2, -v169, v31, v46
	v_fmac_f32_e32 v30, v169, v3
	v_permlane32_swap_b32_e32 v29, v77
	v_fmac_f32_e32 v2, v168, v3
	v_fmac_f32_e32 v30, v168, v31
	v_cvt_pk_bf16_f32 v3, v2, v30
	ds_write_b32 v171, v3 offset:6528
	v_fma_f32 v3, -v169, v30, v61
	v_fmac_f32_e32 v77, v169, v2
	v_permlane32_swap_b32_e32 v28, v76
	v_fmac_f32_e32 v3, v168, v2
	v_fmac_f32_e32 v77, v168, v30
	v_cvt_pk_bf16_f32 v2, v3, v77
	ds_write_b32 v171, v2 offset:6256
	v_fma_f32 v2, -v169, v77, v60
	v_fmac_f32_e32 v76, v169, v3
	v_permlane32_swap_b32_e32 v27, v75
	v_fmac_f32_e32 v2, v168, v3
	v_fmac_f32_e32 v76, v168, v77
	v_cvt_pk_bf16_f32 v3, v2, v76
	ds_write_b32 v171, v3 offset:5984
	v_fma_f32 v3, -v169, v76, v59
	v_fmac_f32_e32 v75, v169, v2
	v_permlane32_swap_b32_e32 v42, v58
	v_permlane32_swap_b32_e32 v26, v74
; #define LAS __attribute__((address_space(3)))
; __device__ __forceinline__ unsigned cvt_pk_bf16(float lo, float hi) { unsigned r; asm volatile("v_cvt_pk_bf16_f32 %0, %1, %2" : "=v"(r) : "v"(lo), "v"(hi)); return r; }
; #define LDS_WAIT() asm volatile("s_waitcnt lgkmcnt(0)" ::: "memory")
; template <int DIR> ...
;     ...
;     for (int s = 0; s < 4; ++s) { const int sb = DIR ? 3 - s : s; float BR[32], BI[32];
;         bu_block(ua[s], f, BR, BI);
; #pragma unroll
;         for (int tt = 0; tt < 32; ++tt) { const int t = DIR ? 31 - tt : tt; const float nsr = fmaf(ar, sr, fmaf(-ai, si, BR[t])), nsi = fmaf(ar, si, fmaf(ai, sr, BI[t])); sr = nsr; si = nsi;
;             *(LAS unsigned*)(sl + (t * 136 + 2 * lane) * 2) = cvt_pk_bf16(sr, si); }
;         LDS_WAIT();
; #pragma unroll
;         for (int rb = 0; rb < 2; ++rb)
; #pragma unroll
;             for (int ks = 0; ks < 4; ++ks) { const bf16x8 a = *(const LAS bf16x8*)(sl + ((16 * rb + (lane & 15)) * 136 + 32 * ks + 8 * (lane >> 4)) * 2);
;                 yacc[2 * sb + rb] = __builtin_amdgcn_mfma_f32_16x16x32_bf16(a, cb[ks], yacc[2 * sb + rb], 0, 0, 0); }
;         LDS_WAIT(); }
	v_fmac_f32_e32 v3, v168, v2
	v_fmac_f32_e32 v75, v168, v76
	v_cvt_pk_bf16_f32 v2, v3, v75
	ds_write_b32 v171, v2 offset:5712
	v_fma_f32 v2, -v169, v75, v58
	v_fmac_f32_e32 v74, v169, v3
	v_fmac_f32_e32 v2, v168, v3
	v_fmac_f32_e32 v74, v168, v75
	v_cvt_pk_bf16_f32 v3, v2, v74
	ds_write_b32 v171, v3 offset:5440
	v_fma_f32 v3, -v169, v74, v45
	v_fmac_f32_e32 v29, v169, v2
	v_fmac_f32_e32 v3, v168, v2
	v_fmac_f32_e32 v29, v168, v74
	v_cvt_pk_bf16_f32 v2, v3, v29
	ds_write_b32 v171, v2 offset:5168
	v_fma_f32 v2, -v169, v29, v44
	v_fmac_f32_e32 v28, v169, v3
	v_fmac_f32_e32 v2, v168, v3
	v_fmac_f32_e32 v28, v168, v29
	v_cvt_pk_bf16_f32 v3, v2, v28
	ds_write_b32 v171, v3 offset:4896
	v_fma_f32 v3, -v169, v28, v43
	v_fmac_f32_e32 v27, v169, v2
	v_fmac_f32_e32 v3, v168, v2
	v_fmac_f32_e32 v27, v168, v28
	v_cvt_pk_bf16_f32 v2, v3, v27
	ds_write_b32 v171, v2 offset:4624
	v_fma_f32 v2, -v169, v27, v42
	v_fmac_f32_e32 v26, v169, v3
	v_permlane32_swap_b32_e32 v41, v57
	v_permlane32_swap_b32_e32 v25, v73
	v_fmac_f32_e32 v2, v168, v3
	v_fmac_f32_e32 v26, v168, v27
	v_cvt_pk_bf16_f32 v3, v2, v26
	ds_write_b32 v171, v3 offset:4352
	v_fma_f32 v3, -v169, v26, v57
	v_fmac_f32_e32 v73, v169, v2
	v_permlane32_swap_b32_e32 v40, v56
	v_permlane32_swap_b32_e32 v24, v72
	v_fmac_f32_e32 v3, v168, v2
	v_fmac_f32_e32 v73, v168, v26
	v_cvt_pk_bf16_f32 v2, v3, v73
	ds_write_b32 v171, v2 offset:4080
	v_fma_f32 v2, -v169, v73, v56
	v_fmac_f32_e32 v72, v169, v3
	v_permlane32_swap_b32_e32 v39, v55
	v_permlane32_swap_b32_e32 v23, v71
	v_fmac_f32_e32 v2, v168, v3
	v_fmac_f32_e32 v72, v168, v73
	v_cvt_pk_bf16_f32 v3, v2, v72
	ds_write_b32 v171, v3 offset:3808
	v_fma_f32 v3, -v169, v72, v55
	v_fmac_f32_e32 v71, v169, v2
	v_permlane32_swap_b32_e32 v38, v54
	v_permlane32_swap_b32_e32 v22, v70
	v_fmac_f32_e32 v3, v168, v2
	v_fmac_f32_e32 v71, v168, v72
	v_cvt_pk_bf16_f32 v2, v3, v71
	ds_write_b32 v171, v2 offset:3536
	v_fma_f32 v2, -v169, v71, v54
	v_fmac_f32_e32 v70, v169, v3
	v_fmac_f32_e32 v2, v168, v3
	v_fmac_f32_e32 v70, v168, v71
	v_cvt_pk_bf16_f32 v3, v2, v70
	ds_write_b32 v171, v3 offset:3264
	v_fma_f32 v3, -v169, v70, v41
	v_fmac_f32_e32 v25, v169, v2
	v_fmac_f32_e32 v3, v168, v2
	v_fmac_f32_e32 v25, v168, v70
	v_cvt_pk_bf16_f32 v2, v3, v25
	ds_write_b32 v171, v2 offset:2992
	v_fma_f32 v2, -v169, v25, v40
	v_fmac_f32_e32 v24, v169, v3
	v_fmac_f32_e32 v2, v168, v3
	v_fmac_f32_e32 v24, v168, v25
	v_cvt_pk_bf16_f32 v3, v2, v24
	ds_write_b32 v171, v3 offset:2720
	v_fma_f32 v3, -v169, v24, v39
	v_fmac_f32_e32 v23, v169, v2
	v_fmac_f32_e32 v3, v168, v2
	v_fmac_f32_e32 v23, v168, v24
	v_cvt_pk_bf16_f32 v2, v3, v23
	ds_write_b32 v171, v2 offset:2448
	v_fma_f32 v2, -v169, v23, v38
	v_fmac_f32_e32 v22, v169, v3
	v_permlane32_swap_b32_e32 v37, v53
	v_permlane32_swap_b32_e32 v21, v69
	v_fmac_f32_e32 v2, v168, v3
	v_fmac_f32_e32 v22, v168, v23
	v_cvt_pk_bf16_f32 v3, v2, v22
	ds_write_b32 v171, v3 offset:2176
	v_fma_f32 v3, -v169, v22, v53
	v_fmac_f32_e32 v69, v169, v2
	v_permlane32_swap_b32_e32 v36, v52
	v_permlane32_swap_b32_e32 v20, v68
	v_fmac_f32_e32 v3, v168, v2
	v_fmac_f32_e32 v69, v168, v22
	v_cvt_pk_bf16_f32 v2, v3, v69
	ds_write_b32 v171, v2 offset:1904
	v_fma_f32 v2, -v169, v69, v52
	v_fmac_f32_e32 v68, v169, v3
	v_permlane32_swap_b32_e32 v35, v51
	v_permlane32_swap_b32_e32 v19, v67
	v_fmac_f32_e32 v2, v168, v3
	v_fmac_f32_e32 v68, v168, v69
	v_cvt_pk_bf16_f32 v3, v2, v68
	ds_write_b32 v171, v3 offset:1632
	v_fma_f32 v3, -v169, v68, v51
	v_fmac_f32_e32 v67, v169, v2
	v_permlane32_swap_b32_e32 v34, v50
	v_permlane32_swap_b32_e32 v18, v66
	v_fmac_f32_e32 v3, v168, v2
	v_fmac_f32_e32 v67, v168, v68
	v_cvt_pk_bf16_f32 v2, v3, v67
	ds_write_b32 v171, v2 offset:1360
	v_fma_f32 v2, -v169, v67, v50
	v_fmac_f32_e32 v66, v169, v3
	v_fmac_f32_e32 v2, v168, v3
	v_fmac_f32_e32 v66, v168, v67
	v_cvt_pk_bf16_f32 v3, v2, v66
	ds_write_b32 v171, v3 offset:1088
	v_fma_f32 v3, -v169, v66, v37
	v_fmac_f32_e32 v21, v169, v2
	v_fmac_f32_e32 v3, v168, v2
	v_fmac_f32_e32 v21, v168, v66
	v_cvt_pk_bf16_f32 v2, v3, v21
	ds_write_b32 v171, v2 offset:816
	v_fma_f32 v2, -v169, v21, v36
	v_fmac_f32_e32 v20, v169, v3
	v_fmac_f32_e32 v2, v168, v3
	v_fmac_f32_e32 v20, v168, v21
	v_cvt_pk_bf16_f32 v3, v2, v20
	ds_write_b32 v171, v3 offset:544
	v_fma_f32 v3, -v169, v20, v35
	v_fmac_f32_e32 v19, v169, v2
	v_fmac_f32_e32 v3, v168, v2
	v_fmac_f32_e32 v19, v168, v20
	v_cvt_pk_bf16_f32 v2, v3, v19
	v_fma_f32 v76, -v169, v19, v34
	v_fmac_f32_e32 v18, v169, v3
	ds_write_b32 v171, v2 offset:272
	v_fmac_f32_e32 v76, v168, v3
	v_fmac_f32_e32 v18, v168, v19
	v_cvt_pk_bf16_f32 v2, v76, v18
	ds_write_b32 v171, v2
	s_waitcnt lgkmcnt(0)
	s_waitcnt lgkmcnt(14)
	v_mfma_f32_16x16x32_bf16 v[138:141], v[8:11], v[106:109], v[4:7]
	s_nop 2
	ds_read_b128 v[2:5], v175
	ds_read_b128 v[6:9], v175 offset:64
	s_waitcnt lgkmcnt(1)
	v_mfma_f32_16x16x32_bf16 v[2:5], v[2:5], v[118:121], v[98:101]
	s_waitcnt lgkmcnt(0)
	v_mfma_f32_16x16x32_bf16 v[2:5], v[6:9], v[114:117], v[2:5]
	ds_read_b128 v[6:9], v175 offset:128
	s_waitcnt lgkmcnt(0)
	v_mfma_f32_16x16x32_bf16 v[2:5], v[6:9], v[110:113], v[2:5]
	ds_read_b128 v[6:9], v175 offset:192
	s_waitcnt lgkmcnt(0)
	v_mfma_f32_16x16x32_bf16 v[72:75], v[6:9], v[106:109], v[2:5]
	s_nop 4
	ds_read_b128 v[2:5], v175 offset:4352
	ds_read_b128 v[6:9], v175 offset:4416
	s_waitcnt lgkmcnt(1)
	v_mfma_f32_16x16x32_bf16 v[2:5], v[2:5], v[118:121], v[102:105]
	s_waitcnt lgkmcnt(0)
	v_mfma_f32_16x16x32_bf16 v[2:5], v[6:9], v[114:117], v[2:5]
	ds_read_b128 v[6:9], v175 offset:4480
	s_waitcnt lgkmcnt(0)
	v_mfma_f32_16x16x32_bf16 v[2:5], v[6:9], v[110:113], v[2:5]
	ds_read_b128 v[6:9], v175 offset:4544
	s_waitcnt lgkmcnt(0)
; #define LAS __attribute__((address_space(3)))
; __device__ __forceinline__ unsigned cvt_pk_bf16(float lo, float hi) { unsigned r; asm volatile("v_cvt_pk_bf16_f32 %0, %1, %2" : "=v"(r) : "v"(lo), "v"(hi)); return r; }
; #define LDS_WAIT() asm volatile("s_waitcnt lgkmcnt(0)" ::: "memory")
; template <int DIR> ...
;     ...
;     for (int s = 0; s < 4; ++s) { const int sb = DIR ? 3 - s : s; float BR[32], BI[32];
;         bu_block(ua[s], f, BR, BI);
; #pragma unroll
;         for (int tt = 0; tt < 32; ++tt) { const int t = DIR ? 31 - tt : tt; const float nsr = fmaf(ar, sr, fmaf(-ai, si, BR[t])), nsi = fmaf(ar, si, fmaf(ai, sr, BI[t])); sr = nsr; si = nsi;
;             *(LAS unsigned*)(sl + (t * 136 + 2 * lane) * 2) = cvt_pk_bf16(sr, si); }
;         LDS_WAIT();
; #pragma unroll
;         for (int rb = 0; rb < 2; ++rb)
; #pragma unroll
;             for (int ks = 0; ks < 4; ++ks) { const bf16x8 a = *(const LAS bf16x8*)(sl + ((16 * rb + (lane & 15)) * 136 + 32 * ks + 8 * (lane >> 4)) * 2);
;                 yacc[2 * sb + rb] = __builtin_amdgcn_mfma_f32_16x16x32_bf16(a, cb[ks], yacc[2 * sb + rb], 0, 0, 0); }
;         LDS_WAIT(); }
	s_waitcnt lgkmcnt(0)
	v_mfma_f32_16x16x32_bf16 v[68:71], v[6:9], v[106:109], v[2:5]
	s_waitcnt vmcnt(1)
	v_mfma_f32_32x32x16_bf16 v[20:35], v[150:153], v[134:137], 0
	v_mfma_f32_32x32x16_bf16 v[52:67], v[150:153], v[130:133], 0
	v_mfma_f32_32x32x16_bf16 v[2:17], v[150:153], v[122:125], 0
	s_nop 10
	v_permlane32_swap_b32_e32 v35, v67
	v_fma_f32 v19, -v169, v18, v67
	v_permlane32_swap_b32_e32 v34, v66
	v_fmac_f32_e32 v19, v168, v76
	v_permlane32_swap_b32_e32 v33, v65
	v_mfma_f32_32x32x16_bf16 v[36:51], v[150:153], v[126:129], 0
	v_permlane32_swap_b32_e32 v32, v64
	v_permlane32_swap_b32_e32 v31, v63
	v_permlane32_swap_b32_e32 v30, v62
	v_permlane32_swap_b32_e32 v29, v61
	s_nop 7
	v_permlane32_swap_b32_e32 v17, v51
	v_fmac_f32_e32 v51, v169, v76
	v_permlane32_swap_b32_e32 v16, v50
	v_fmac_f32_e32 v51, v168, v18
	v_cvt_pk_bf16_f32 v18, v19, v51
	ds_write_b32 v171, v18 offset:8432
	v_fma_f32 v18, -v169, v51, v66
	v_fmac_f32_e32 v50, v169, v19
	v_permlane32_swap_b32_e32 v15, v49
	v_fmac_f32_e32 v18, v168, v19
	v_fmac_f32_e32 v50, v168, v51
	v_cvt_pk_bf16_f32 v19, v18, v50
	ds_write_b32 v171, v19 offset:8160
	v_fma_f32 v19, -v169, v50, v65
	v_fmac_f32_e32 v49, v169, v18
	v_permlane32_swap_b32_e32 v14, v48
	v_fmac_f32_e32 v19, v168, v18
	v_fmac_f32_e32 v49, v168, v50
	v_cvt_pk_bf16_f32 v18, v19, v49
	ds_write_b32 v171, v18 offset:7888
	v_fma_f32 v18, -v169, v49, v64
	v_fmac_f32_e32 v48, v169, v19
	v_fmac_f32_e32 v18, v168, v19
	v_fmac_f32_e32 v48, v168, v49
	v_cvt_pk_bf16_f32 v19, v18, v48
	ds_write_b32 v171, v19 offset:7616
	v_fma_f32 v19, -v169, v48, v35
	v_fmac_f32_e32 v17, v169, v18
	v_fmac_f32_e32 v19, v168, v18
	v_fmac_f32_e32 v17, v168, v48
	v_cvt_pk_bf16_f32 v18, v19, v17
	ds_write_b32 v171, v18 offset:7344
	v_fma_f32 v18, -v169, v17, v34
	v_fmac_f32_e32 v16, v169, v19
	v_fmac_f32_e32 v18, v168, v19
	v_fmac_f32_e32 v16, v168, v17
	v_cvt_pk_bf16_f32 v17, v18, v16
	ds_write_b32 v171, v17 offset:7072
	v_fma_f32 v17, -v169, v16, v33
	v_fmac_f32_e32 v15, v169, v18
	v_fmac_f32_e32 v17, v168, v18
	v_fmac_f32_e32 v15, v168, v16
	v_cvt_pk_bf16_f32 v16, v17, v15
	ds_write_b32 v171, v16 offset:6800
	v_fma_f32 v16, -v169, v15, v32
	v_fmac_f32_e32 v14, v169, v17
	v_permlane32_swap_b32_e32 v13, v47
	v_fmac_f32_e32 v16, v168, v17
	v_fmac_f32_e32 v14, v168, v15
	v_cvt_pk_bf16_f32 v15, v16, v14
	ds_write_b32 v171, v15 offset:6528
	v_fma_f32 v15, -v169, v14, v63
	v_fmac_f32_e32 v47, v169, v16
	v_permlane32_swap_b32_e32 v12, v46
	v_fmac_f32_e32 v15, v168, v16
	v_fmac_f32_e32 v47, v168, v14
	v_cvt_pk_bf16_f32 v14, v15, v47
	ds_write_b32 v171, v14 offset:6256
	v_fma_f32 v14, -v169, v47, v62
	v_fmac_f32_e32 v46, v169, v15
	v_permlane32_swap_b32_e32 v11, v45
	v_fmac_f32_e32 v14, v168, v15
	v_fmac_f32_e32 v46, v168, v47
	v_cvt_pk_bf16_f32 v15, v14, v46
	ds_write_b32 v171, v15 offset:5984
	v_fma_f32 v15, -v169, v46, v61
	v_fmac_f32_e32 v45, v169, v14
	v_permlane32_swap_b32_e32 v28, v60
	v_permlane32_swap_b32_e32 v10, v44
	v_fmac_f32_e32 v15, v168, v14
	v_fmac_f32_e32 v45, v168, v46
	v_cvt_pk_bf16_f32 v14, v15, v45
	ds_write_b32 v171, v14 offset:5712
	v_fma_f32 v14, -v169, v45, v60
	v_fmac_f32_e32 v44, v169, v15
	v_fmac_f32_e32 v14, v168, v15
	v_fmac_f32_e32 v44, v168, v45
	v_cvt_pk_bf16_f32 v15, v14, v44
	ds_write_b32 v171, v15 offset:5440
	v_fma_f32 v15, -v169, v44, v31
	v_fmac_f32_e32 v13, v169, v14
	v_fmac_f32_e32 v15, v168, v14
	v_fmac_f32_e32 v13, v168, v44
	v_cvt_pk_bf16_f32 v14, v15, v13
	ds_write_b32 v171, v14 offset:5168
	v_fma_f32 v14, -v169, v13, v30
	v_fmac_f32_e32 v12, v169, v15
	v_fmac_f32_e32 v14, v168, v15
	v_fmac_f32_e32 v12, v168, v13
	v_cvt_pk_bf16_f32 v13, v14, v12
	ds_write_b32 v171, v13 offset:4896
	v_fma_f32 v13, -v169, v12, v29
	v_fmac_f32_e32 v11, v169, v14
	v_fmac_f32_e32 v13, v168, v14
	v_fmac_f32_e32 v11, v168, v12
	v_cvt_pk_bf16_f32 v12, v13, v11
	ds_write_b32 v171, v12 offset:4624
	v_fma_f32 v12, -v169, v11, v28
	v_fmac_f32_e32 v10, v169, v13
	v_permlane32_swap_b32_e32 v27, v59
	v_permlane32_swap_b32_e32 v9, v43
	v_fmac_f32_e32 v12, v168, v13
	v_fmac_f32_e32 v10, v168, v11
	v_cvt_pk_bf16_f32 v11, v12, v10
	ds_write_b32 v171, v11 offset:4352
	v_fma_f32 v11, -v169, v10, v59
	v_fmac_f32_e32 v43, v169, v12
	v_permlane32_swap_b32_e32 v26, v58
	v_permlane32_swap_b32_e32 v8, v42
	v_fmac_f32_e32 v11, v168, v12
	v_fmac_f32_e32 v43, v168, v10
	v_cvt_pk_bf16_f32 v10, v11, v43
	ds_write_b32 v171, v10 offset:4080
	v_fma_f32 v10, -v169, v43, v58
	v_fmac_f32_e32 v42, v169, v11
	v_permlane32_swap_b32_e32 v25, v57
	v_permlane32_swap_b32_e32 v7, v41
	v_fmac_f32_e32 v10, v168, v11
	v_fmac_f32_e32 v42, v168, v43
	v_cvt_pk_bf16_f32 v11, v10, v42
	ds_write_b32 v171, v11 offset:3808
	v_fma_f32 v11, -v169, v42, v57
	v_fmac_f32_e32 v41, v169, v10
	v_permlane32_swap_b32_e32 v24, v56
	v_permlane32_swap_b32_e32 v6, v40
	v_fmac_f32_e32 v11, v168, v10
	v_fmac_f32_e32 v41, v168, v42
	v_cvt_pk_bf16_f32 v10, v11, v41
	ds_write_b32 v171, v10 offset:3536
	v_fma_f32 v10, -v169, v41, v56
	v_fmac_f32_e32 v40, v169, v11
	v_fmac_f32_e32 v10, v168, v11
	v_fmac_f32_e32 v40, v168, v41
	v_cvt_pk_bf16_f32 v11, v10, v40
	ds_write_b32 v171, v11 offset:3264
	v_fma_f32 v11, -v169, v40, v27
	v_fmac_f32_e32 v9, v169, v10
	v_fmac_f32_e32 v11, v168, v10
	v_fmac_f32_e32 v9, v168, v40
	v_cvt_pk_bf16_f32 v10, v11, v9
	ds_write_b32 v171, v10 offset:2992
	v_fma_f32 v10, -v169, v9, v26
	v_fmac_f32_e32 v8, v169, v11
	v_fmac_f32_e32 v10, v168, v11
	v_fmac_f32_e32 v8, v168, v9
	v_cvt_pk_bf16_f32 v9, v10, v8
	ds_write_b32 v171, v9 offset:2720
	v_fma_f32 v9, -v169, v8, v25
	v_fmac_f32_e32 v7, v169, v10
	v_fmac_f32_e32 v9, v168, v10
	v_fmac_f32_e32 v7, v168, v8
	v_cvt_pk_bf16_f32 v8, v9, v7
; #define LAS __attribute__((address_space(3)))
; __device__ __forceinline__ unsigned cvt_pk_bf16(float lo, float hi) { unsigned r; asm volatile("v_cvt_pk_bf16_f32 %0, %1, %2" : "=v"(r) : "v"(lo), "v"(hi)); return r; }
; #define LDS_WAIT() asm volatile("s_waitcnt lgkmcnt(0)" ::: "memory")
; template <int DIR> ...
;     ...
;     for (int s = 0; s < 4; ++s) { const int sb = DIR ? 3 - s : s; float BR[32], BI[32];
;         bu_block(ua[s], f, BR, BI);
; #pragma unroll
;         for (int tt = 0; tt < 32; ++tt) { const int t = DIR ? 31 - tt : tt; const float nsr = fmaf(ar, sr, fmaf(-ai, si, BR[t])), nsi = fmaf(ar, si, fmaf(ai, sr, BI[t])); sr = nsr; si = nsi;
;             *(LAS unsigned*)(sl + (t * 136 + 2 * lane) * 2) = cvt_pk_bf16(sr, si); }
;         LDS_WAIT();
; #pragma unroll
;         for (int rb = 0; rb < 2; ++rb)
; #pragma unroll
;             for (int ks = 0; ks < 4; ++ks) { const bf16x8 a = *(const LAS bf16x8*)(sl + ((16 * rb + (lane & 15)) * 136 + 32 * ks + 8 * (lane >> 4)) * 2);
;                 yacc[2 * sb + rb] = __builtin_amdgcn_mfma_f32_16x16x32_bf16(a, cb[ks], yacc[2 * sb + rb], 0, 0, 0); }
;         LDS_WAIT(); }
	ds_write_b32 v171, v8 offset:2448
	v_fma_f32 v8, -v169, v7, v24
	v_fmac_f32_e32 v6, v169, v9
	v_permlane32_swap_b32_e32 v23, v55
	v_permlane32_swap_b32_e32 v5, v39
	v_fmac_f32_e32 v8, v168, v9
	v_fmac_f32_e32 v6, v168, v7
	v_cvt_pk_bf16_f32 v7, v8, v6
	ds_write_b32 v171, v7 offset:2176
	v_fma_f32 v7, -v169, v6, v55
	v_fmac_f32_e32 v39, v169, v8
	v_permlane32_swap_b32_e32 v22, v54
	v_permlane32_swap_b32_e32 v4, v38
	v_fmac_f32_e32 v7, v168, v8
	v_fmac_f32_e32 v39, v168, v6
	v_cvt_pk_bf16_f32 v6, v7, v39
	ds_write_b32 v171, v6 offset:1904
	v_fma_f32 v6, -v169, v39, v54
	v_fmac_f32_e32 v38, v169, v7
	v_permlane32_swap_b32_e32 v21, v53
	v_permlane32_swap_b32_e32 v3, v37
	v_fmac_f32_e32 v6, v168, v7
	v_fmac_f32_e32 v38, v168, v39
	v_cvt_pk_bf16_f32 v7, v6, v38
	ds_write_b32 v171, v7 offset:1632
	v_fma_f32 v7, -v169, v38, v53
	v_fmac_f32_e32 v37, v169, v6
	v_permlane32_swap_b32_e32 v20, v52
	v_permlane32_swap_b32_e32 v2, v36
	v_fmac_f32_e32 v7, v168, v6
	v_fmac_f32_e32 v37, v168, v38
	v_cvt_pk_bf16_f32 v6, v7, v37
	ds_write_b32 v171, v6 offset:1360
	v_fma_f32 v6, -v169, v37, v52
	v_fmac_f32_e32 v36, v169, v7
	v_fmac_f32_e32 v6, v168, v7
	v_fmac_f32_e32 v36, v168, v37
	v_cvt_pk_bf16_f32 v7, v6, v36
	ds_write_b32 v171, v7 offset:1088
	v_fma_f32 v7, -v169, v36, v23
	v_fmac_f32_e32 v5, v169, v6
	v_fmac_f32_e32 v7, v168, v6
	v_fmac_f32_e32 v5, v168, v36
	v_cvt_pk_bf16_f32 v6, v7, v5
	ds_write_b32 v171, v6 offset:816
	v_fma_f32 v6, -v169, v5, v22
	v_fmac_f32_e32 v4, v169, v7
	v_fmac_f32_e32 v6, v168, v7
	v_fmac_f32_e32 v4, v168, v5
	v_cvt_pk_bf16_f32 v5, v6, v4
	ds_write_b32 v171, v5 offset:544
	v_fma_f32 v5, -v169, v4, v21
	v_fmac_f32_e32 v3, v169, v6
	v_fmac_f32_e32 v5, v168, v6
	v_fmac_f32_e32 v3, v168, v4
	v_fma_f32 v80, -v169, v3, v20
	v_fmac_f32_e32 v2, v169, v5
	v_cvt_pk_bf16_f32 v4, v5, v3
	ds_write_b32 v171, v4 offset:272
	v_fmac_f32_e32 v80, v168, v5
	v_fmac_f32_e32 v2, v168, v3
	v_cvt_pk_bf16_f32 v3, v80, v2
	ds_write_b32 v171, v3
	s_waitcnt lgkmcnt(0)
	ds_read_b128 v[4:7], v175
	ds_read_b128 v[8:11], v175 offset:64
	s_waitcnt lgkmcnt(1)
	v_mfma_f32_16x16x32_bf16 v[4:7], v[4:7], v[118:121], v[90:93]
	s_waitcnt lgkmcnt(0)
	v_mfma_f32_16x16x32_bf16 v[4:7], v[8:11], v[114:117], v[4:7]
	ds_read_b128 v[8:11], v175 offset:128
	s_waitcnt lgkmcnt(0)
	v_mfma_f32_16x16x32_bf16 v[4:7], v[8:11], v[110:113], v[4:7]
	ds_read_b128 v[8:11], v175 offset:192
	s_waitcnt lgkmcnt(0)
	v_mfma_f32_16x16x32_bf16 v[90:93], v[8:11], v[106:109], v[4:7]
	s_nop 4
	ds_read_b128 v[4:7], v175 offset:4352
	ds_read_b128 v[8:11], v175 offset:4416
	s_waitcnt lgkmcnt(1)
	v_mfma_f32_16x16x32_bf16 v[4:7], v[4:7], v[118:121], v[94:97]
	s_waitcnt lgkmcnt(0)
	v_mfma_f32_16x16x32_bf16 v[4:7], v[8:11], v[114:117], v[4:7]
	ds_read_b128 v[8:11], v175 offset:4480
	s_waitcnt lgkmcnt(0)
	v_mfma_f32_16x16x32_bf16 v[4:7], v[8:11], v[110:113], v[4:7]
	ds_read_b128 v[8:11], v175 offset:4544
	s_waitcnt lgkmcnt(0)
	s_waitcnt lgkmcnt(0)
	v_mfma_f32_16x16x32_bf16 v[76:79], v[8:11], v[106:109], v[4:7]
	s_waitcnt vmcnt(0)
	v_mfma_f32_32x32x16_bf16 v[4:19], v[146:149], v[134:137], 0
	v_mfma_f32_32x32x16_bf16 v[52:67], v[146:149], v[130:133], 0
	v_mfma_f32_32x32x16_bf16 v[20:35], v[146:149], v[122:125], 0
	s_nop 10
	v_permlane32_swap_b32_e32 v19, v67
	v_fma_f32 v3, -v169, v2, v67
	v_permlane32_swap_b32_e32 v18, v66
	v_fmac_f32_e32 v3, v168, v80
	v_permlane32_swap_b32_e32 v17, v65
	v_mfma_f32_32x32x16_bf16 v[36:51], v[146:149], v[126:129], 0
	v_permlane32_swap_b32_e32 v16, v64
	v_permlane32_swap_b32_e32 v15, v63
	v_permlane32_swap_b32_e32 v14, v62
	v_permlane32_swap_b32_e32 v13, v61
	s_nop 7
	v_permlane32_swap_b32_e32 v35, v51
	v_fmac_f32_e32 v51, v169, v80
	v_permlane32_swap_b32_e32 v34, v50
	v_fmac_f32_e32 v51, v168, v2
	v_cvt_pk_bf16_f32 v2, v3, v51
	ds_write_b32 v171, v2 offset:8432
	v_fma_f32 v2, -v169, v51, v66
	v_fmac_f32_e32 v50, v169, v3
	v_permlane32_swap_b32_e32 v33, v49
	v_fmac_f32_e32 v2, v168, v3
	v_fmac_f32_e32 v50, v168, v51
	v_cvt_pk_bf16_f32 v3, v2, v50
	ds_write_b32 v171, v3 offset:8160
	v_fma_f32 v3, -v169, v50, v65
	v_fmac_f32_e32 v49, v169, v2
	v_permlane32_swap_b32_e32 v32, v48
	v_fmac_f32_e32 v3, v168, v2
	v_fmac_f32_e32 v49, v168, v50
	v_cvt_pk_bf16_f32 v2, v3, v49
	ds_write_b32 v171, v2 offset:7888
	v_fma_f32 v2, -v169, v49, v64
	v_fmac_f32_e32 v48, v169, v3
	v_fmac_f32_e32 v2, v168, v3
	v_fmac_f32_e32 v48, v168, v49
	v_cvt_pk_bf16_f32 v3, v2, v48
	ds_write_b32 v171, v3 offset:7616
	v_fma_f32 v3, -v169, v48, v19
	v_fmac_f32_e32 v35, v169, v2
	v_fmac_f32_e32 v3, v168, v2
	v_fmac_f32_e32 v35, v168, v48
	v_cvt_pk_bf16_f32 v2, v3, v35
	ds_write_b32 v171, v2 offset:7344
	v_fma_f32 v2, -v169, v35, v18
	v_fmac_f32_e32 v34, v169, v3
	v_fmac_f32_e32 v2, v168, v3
	v_fmac_f32_e32 v34, v168, v35
	v_cvt_pk_bf16_f32 v3, v2, v34
	ds_write_b32 v171, v3 offset:7072
	v_fma_f32 v3, -v169, v34, v17
	v_fmac_f32_e32 v33, v169, v2
	v_fmac_f32_e32 v3, v168, v2
	v_fmac_f32_e32 v33, v168, v34
	v_cvt_pk_bf16_f32 v2, v3, v33
	ds_write_b32 v171, v2 offset:6800
	v_fma_f32 v2, -v169, v33, v16
	v_fmac_f32_e32 v32, v169, v3
	v_permlane32_swap_b32_e32 v31, v47
	v_fmac_f32_e32 v2, v168, v3
	v_fmac_f32_e32 v32, v168, v33
	v_cvt_pk_bf16_f32 v3, v2, v32
	ds_write_b32 v171, v3 offset:6528
	v_fma_f32 v3, -v169, v32, v63
	v_fmac_f32_e32 v47, v169, v2
	v_permlane32_swap_b32_e32 v30, v46
	v_fmac_f32_e32 v3, v168, v2
	v_fmac_f32_e32 v47, v168, v32
	v_cvt_pk_bf16_f32 v2, v3, v47
	ds_write_b32 v171, v2 offset:6256
	v_fma_f32 v2, -v169, v47, v62
	v_fmac_f32_e32 v46, v169, v3
	v_permlane32_swap_b32_e32 v29, v45
	v_fmac_f32_e32 v2, v168, v3
	v_fmac_f32_e32 v46, v168, v47
	v_cvt_pk_bf16_f32 v3, v2, v46
; #define LAS __attribute__((address_space(3)))
; __device__ __forceinline__ unsigned cvt_pk_bf16(float lo, float hi) { unsigned r; asm volatile("v_cvt_pk_bf16_f32 %0, %1, %2" : "=v"(r) : "v"(lo), "v"(hi)); return r; }
; #define LDS_WAIT() asm volatile("s_waitcnt lgkmcnt(0)" ::: "memory")
; template <int DIR> ...
;     ...
;     for (int s = 0; s < 4; ++s) { const int sb = DIR ? 3 - s : s; float BR[32], BI[32];
;         bu_block(ua[s], f, BR, BI);
; #pragma unroll
;         for (int tt = 0; tt < 32; ++tt) { const int t = DIR ? 31 - tt : tt; const float nsr = fmaf(ar, sr, fmaf(-ai, si, BR[t])), nsi = fmaf(ar, si, fmaf(ai, sr, BI[t])); sr = nsr; si = nsi;
;             *(LAS unsigned*)(sl + (t * 136 + 2 * lane) * 2) = cvt_pk_bf16(sr, si); }
;         LDS_WAIT();
; #pragma unroll
;         for (int rb = 0; rb < 2; ++rb)
; #pragma unroll
;             for (int ks = 0; ks < 4; ++ks) { const bf16x8 a = *(const LAS bf16x8*)(sl + ((16 * rb + (lane & 15)) * 136 + 32 * ks + 8 * (lane >> 4)) * 2);
;                 yacc[2 * sb + rb] = __builtin_amdgcn_mfma_f32_16x16x32_bf16(a, cb[ks], yacc[2 * sb + rb], 0, 0, 0); }
;         LDS_WAIT(); }
	ds_write_b32 v171, v3 offset:5984
	v_fma_f32 v3, -v169, v46, v61
	v_fmac_f32_e32 v45, v169, v2
	v_permlane32_swap_b32_e32 v12, v60
	v_permlane32_swap_b32_e32 v28, v44
	v_fmac_f32_e32 v3, v168, v2
	v_fmac_f32_e32 v45, v168, v46
	v_cvt_pk_bf16_f32 v2, v3, v45
	ds_write_b32 v171, v2 offset:5712
	v_fma_f32 v2, -v169, v45, v60
	v_fmac_f32_e32 v44, v169, v3
	v_fmac_f32_e32 v2, v168, v3
	v_fmac_f32_e32 v44, v168, v45
	v_cvt_pk_bf16_f32 v3, v2, v44
	ds_write_b32 v171, v3 offset:5440
	v_fma_f32 v3, -v169, v44, v15
	v_fmac_f32_e32 v31, v169, v2
	v_fmac_f32_e32 v3, v168, v2
	v_fmac_f32_e32 v31, v168, v44
	v_cvt_pk_bf16_f32 v2, v3, v31
	ds_write_b32 v171, v2 offset:5168
	v_fma_f32 v2, -v169, v31, v14
	v_fmac_f32_e32 v30, v169, v3
	v_fmac_f32_e32 v2, v168, v3
	v_fmac_f32_e32 v30, v168, v31
	v_cvt_pk_bf16_f32 v3, v2, v30
	ds_write_b32 v171, v3 offset:4896
	v_fma_f32 v3, -v169, v30, v13
	v_fmac_f32_e32 v29, v169, v2
	v_fmac_f32_e32 v3, v168, v2
	v_fmac_f32_e32 v29, v168, v30
	v_cvt_pk_bf16_f32 v2, v3, v29
	ds_write_b32 v171, v2 offset:4624
	v_fma_f32 v2, -v169, v29, v12
	v_fmac_f32_e32 v28, v169, v3
	v_permlane32_swap_b32_e32 v11, v59
	v_permlane32_swap_b32_e32 v27, v43
	v_fmac_f32_e32 v2, v168, v3
	v_fmac_f32_e32 v28, v168, v29
	v_cvt_pk_bf16_f32 v3, v2, v28
	ds_write_b32 v171, v3 offset:4352
	v_fma_f32 v3, -v169, v28, v59
	v_fmac_f32_e32 v43, v169, v2
	v_permlane32_swap_b32_e32 v10, v58
	v_permlane32_swap_b32_e32 v26, v42
	v_fmac_f32_e32 v3, v168, v2
	v_fmac_f32_e32 v43, v168, v28
	v_cvt_pk_bf16_f32 v2, v3, v43
	ds_write_b32 v171, v2 offset:4080
	v_fma_f32 v2, -v169, v43, v58
	v_fmac_f32_e32 v42, v169, v3
	v_permlane32_swap_b32_e32 v9, v57
	v_permlane32_swap_b32_e32 v25, v41
	v_fmac_f32_e32 v2, v168, v3
	v_fmac_f32_e32 v42, v168, v43
	v_cvt_pk_bf16_f32 v3, v2, v42
	ds_write_b32 v171, v3 offset:3808
	v_fma_f32 v3, -v169, v42, v57
	v_fmac_f32_e32 v41, v169, v2
	v_permlane32_swap_b32_e32 v8, v56
	v_permlane32_swap_b32_e32 v24, v40
	v_fmac_f32_e32 v3, v168, v2
	v_fmac_f32_e32 v41, v168, v42
	v_cvt_pk_bf16_f32 v2, v3, v41
	ds_write_b32 v171, v2 offset:3536
	v_fma_f32 v2, -v169, v41, v56
	v_fmac_f32_e32 v40, v169, v3
	v_fmac_f32_e32 v2, v168, v3
	v_fmac_f32_e32 v40, v168, v41
	v_cvt_pk_bf16_f32 v3, v2, v40
	ds_write_b32 v171, v3 offset:3264
	v_fma_f32 v3, -v169, v40, v11
	v_fmac_f32_e32 v27, v169, v2
	v_fmac_f32_e32 v3, v168, v2
	v_fmac_f32_e32 v27, v168, v40
	v_cvt_pk_bf16_f32 v2, v3, v27
	ds_write_b32 v171, v2 offset:2992
	v_fma_f32 v2, -v169, v27, v10
	v_fmac_f32_e32 v26, v169, v3
	v_fmac_f32_e32 v2, v168, v3
	v_fmac_f32_e32 v26, v168, v27
	v_cvt_pk_bf16_f32 v3, v2, v26
	ds_write_b32 v171, v3 offset:2720
	v_fma_f32 v3, -v169, v26, v9
	v_fmac_f32_e32 v25, v169, v2
	v_fmac_f32_e32 v3, v168, v2
	v_fmac_f32_e32 v25, v168, v26
	v_cvt_pk_bf16_f32 v2, v3, v25
	ds_write_b32 v171, v2 offset:2448
	v_fma_f32 v2, -v169, v25, v8
	v_fmac_f32_e32 v24, v169, v3
	v_permlane32_swap_b32_e32 v7, v55
	v_permlane32_swap_b32_e32 v23, v39
	v_fmac_f32_e32 v2, v168, v3
	v_fmac_f32_e32 v24, v168, v25
	v_cvt_pk_bf16_f32 v3, v2, v24
	ds_write_b32 v171, v3 offset:2176
	v_fma_f32 v3, -v169, v24, v55
	v_fmac_f32_e32 v39, v169, v2
	v_permlane32_swap_b32_e32 v6, v54
	v_permlane32_swap_b32_e32 v22, v38
	v_fmac_f32_e32 v3, v168, v2
	v_fmac_f32_e32 v39, v168, v24
	v_cvt_pk_bf16_f32 v2, v3, v39
	ds_write_b32 v171, v2 offset:1904
	v_fma_f32 v2, -v169, v39, v54
	v_fmac_f32_e32 v38, v169, v3
	v_permlane32_swap_b32_e32 v5, v53
	v_permlane32_swap_b32_e32 v21, v37
	v_fmac_f32_e32 v2, v168, v3
	v_fmac_f32_e32 v38, v168, v39
	v_cvt_pk_bf16_f32 v3, v2, v38
	ds_write_b32 v171, v3 offset:1632
	v_fma_f32 v3, -v169, v38, v53
	v_fmac_f32_e32 v37, v169, v2
	v_permlane32_swap_b32_e32 v4, v52
	v_permlane32_swap_b32_e32 v20, v36
	v_fmac_f32_e32 v3, v168, v2
	v_fmac_f32_e32 v37, v168, v38
	v_cvt_pk_bf16_f32 v2, v3, v37
	ds_write_b32 v171, v2 offset:1360
	v_fma_f32 v2, -v169, v37, v52
	v_fmac_f32_e32 v36, v169, v3
	v_fmac_f32_e32 v2, v168, v3
	v_fmac_f32_e32 v36, v168, v37
	v_cvt_pk_bf16_f32 v3, v2, v36
	ds_write_b32 v171, v3 offset:1088
	v_fma_f32 v3, -v169, v36, v7
	v_fmac_f32_e32 v23, v169, v2
	v_fmac_f32_e32 v3, v168, v2
	v_fmac_f32_e32 v23, v168, v36
	v_cvt_pk_bf16_f32 v2, v3, v23
	ds_write_b32 v171, v2 offset:816
	v_fma_f32 v2, -v169, v23, v6
	v_fmac_f32_e32 v22, v169, v3
	v_fmac_f32_e32 v2, v168, v3
	v_fmac_f32_e32 v22, v168, v23
	v_cvt_pk_bf16_f32 v3, v2, v22
	ds_write_b32 v171, v3 offset:544
	v_fma_f32 v3, -v169, v22, v5
	v_fmac_f32_e32 v21, v169, v2
	v_fmac_f32_e32 v3, v168, v2
	v_fmac_f32_e32 v21, v168, v22
	v_cvt_pk_bf16_f32 v2, v3, v21
	ds_write_b32 v171, v2 offset:272
	v_fma_f32 v2, -v169, v21, v4
	v_fmac_f32_e32 v2, v168, v3
	v_fmac_f32_e32 v20, v169, v3
	v_fmac_f32_e32 v20, v168, v21
	v_cvt_pk_bf16_f32 v2, v2, v20
	ds_write_b32 v171, v2
	s_waitcnt lgkmcnt(0)
	ds_read_b128 v[2:5], v175
	ds_read_b128 v[6:9], v175 offset:64
	s_waitcnt lgkmcnt(1)
	v_mfma_f32_16x16x32_bf16 v[2:5], v[2:5], v[118:121], v[86:89]
	ds_read_b128 v[10:13], v175 offset:4416
	s_waitcnt lgkmcnt(1)
	v_mfma_f32_16x16x32_bf16 v[2:5], v[6:9], v[114:117], v[2:5]
	ds_read_b128 v[6:9], v175 offset:128
	s_waitcnt lgkmcnt(0)
	v_mfma_f32_16x16x32_bf16 v[2:5], v[6:9], v[110:113], v[2:5]
	ds_read_b128 v[6:9], v175 offset:192
	s_waitcnt lgkmcnt(0)
	v_mfma_f32_16x16x32_bf16 v[6:9], v[6:9], v[106:109], v[2:5]
	s_nop 4
	ds_read_b128 v[2:5], v175 offset:4352
	s_waitcnt lgkmcnt(0)
	v_mfma_f32_16x16x32_bf16 v[2:5], v[2:5], v[118:121], v[82:85]
	v_mfma_f32_16x16x32_bf16 v[2:5], v[10:13], v[114:117], v[2:5]
	ds_read_b128 v[10:13], v175 offset:4480
	s_waitcnt lgkmcnt(0)
	v_mfma_f32_16x16x32_bf16 v[2:5], v[10:13], v[110:113], v[2:5]
	ds_read_b128 v[10:13], v175 offset:4544
	s_waitcnt lgkmcnt(0)
; #define LAS __attribute__((address_space(3)))
; __device__ __forceinline__ float bf2f(bf16_t b) { return __uint_as_float((unsigned)b << 16); }
; __device__ __forceinline__ bf16_t f2bf(float f) { return (bf16_t)(cvt_pk_bf16(f, 0.f) & 0xffffu); }
; __device__ __forceinline__ float gelu_t(float x) { const float u = 0.7978845608028654f * (x + 0.044715f * x * x * x); return x * sigm(2.f * u); }
; #define LDS_WAIT() asm volatile("s_waitcnt lgkmcnt(0)" ::: "memory")
; template <int DIR> ...
;     ...
;         for (int rb = 0; rb < 2; ++rb)
; #pragma unroll
;             for (int ks = 0; ks < 4; ++ks) { const bf16x8 a = *(const LAS bf16x8*)(sl + ((16 * rb + (lane & 15)) * 136 + 32 * ks + 8 * (lane >> 4)) * 2);
;                 yacc[2 * sb + rb] = __builtin_amdgcn_mfma_f32_16x16x32_bf16(a, cb[ks], yacc[2 * sb + rb], 0, 0, 0); }
;         LDS_WAIT(); }
; __device__ __forceinline__ void ssm_pass2_item(const bf16_t* __restrict__ proj, const float* lamb_l, const float* lamt_l, const bf16_t* bbar_l, const bf16_t* ctt_l, const float* est, const float* __restrict__ dskip, ...
;     ...
;     const int c = lane & 15, ch = g * 16 + c; const float dk = dskip[ch];
; #pragma unroll
;     for (int blk = 0; blk < 8; ++blk)
; #pragma unroll
;         for (int r = 0; r < 4; ++r) { const int tok = b * SEQ + n * 128 + 16 * blk + 4 * (lane >> 4) + r;
;             const float y = yacc[blk][r] + dk * bf2f(proj[(size_t)tok * NIN + C_U + ch]); ssmy[(size_t)tok * 1024 + ch] = f2bf(gelu_t(y)); }
	s_waitcnt lgkmcnt(0)
	v_mfma_f32_16x16x32_bf16 v[2:5], v[10:13], v[106:109], v[2:5]
	v_lshl_or_b32 v10, s31, 4, v172
	v_or_b32_e32 v12, s14, v173
	v_and_b32_e32 v248, 3, v0
	v_sub_u32_e32 v249, v10, v248
	v_add_u32_e32 v12, v12, v248
	v_lshlrev_b32_e32 v13, 2, v249
	global_load_dwordx4 v[82:85], v13, s[46:47]
	v_lshlrev_b32_e32 v250, 1, v249
	v_mov_b32_e32 v251, 0
	v_mad_i64_i32 v[252:253], s[0:1], v12, s27, v[166:167]
	v_ashrrev_i32_e32 v13, 31, v12
	v_lshl_add_u64 v[252:253], v[252:253], 0, v[250:251]
	v_lshlrev_b64 v[14:15], 11, v[12:13]
	v_lshl_add_u64 v[254:255], s[28:29], 0, v[250:251]
	s_mov_b32 s101, 0
	v_lshl_add_u64 v[254:255], v[254:255], 0, v[14:15]
	global_load_dwordx2 v[106:107], v[252:253], off offset:3072
	s_mov_b32 s100, 0x54000
	v_lshl_add_u64 v[14:15], v[252:253], 0, s[100:101]
	global_load_dwordx2 v[108:109], v[14:15], off offset:3072
	s_mov_b32 s100, 0xa8000
	v_lshl_add_u64 v[14:15], v[252:253], 0, s[100:101]
	global_load_dwordx2 v[110:111], v[14:15], off offset:3072
	s_mov_b32 s100, 0xfc000
	v_lshl_add_u64 v[14:15], v[252:253], 0, s[100:101]
	global_load_dwordx2 v[112:113], v[14:15], off offset:3072
	s_mov_b32 s100, 0x150000
	v_lshl_add_u64 v[14:15], v[252:253], 0, s[100:101]
	global_load_dwordx2 v[114:115], v[14:15], off offset:3072
	s_mov_b32 s100, 0x1a4000
	v_lshl_add_u64 v[14:15], v[252:253], 0, s[100:101]
	global_load_dwordx2 v[116:117], v[14:15], off offset:3072
	s_mov_b32 s100, 0x1f8000
	v_lshl_add_u64 v[14:15], v[252:253], 0, s[100:101]
	global_load_dwordx2 v[118:119], v[14:15], off offset:3072
	s_mov_b32 s100, 0x24c000
	v_lshl_add_u64 v[14:15], v[252:253], 0, s[100:101]
	global_load_dwordx2 v[120:121], v[14:15], off offset:3072
	s_mov_b32 vcc_lo, 0xaaaaaaaa
	s_mov_b32 vcc_hi, 0xaaaaaaaa
	s_nop 1
	v_mov_b32_e32 v86, v7
	v_mov_b32_e32 v87, v9
	v_mov_b32_e32 v88, v3
	v_mov_b32_e32 v89, v5
	v_cndmask_b32_dpp v7, v6, v7, vcc quad_perm:[1,0,3,2] row_mask:0xf bank_mask:0xf
	v_cndmask_b32_dpp v9, v8, v9, vcc quad_perm:[1,0,3,2] row_mask:0xf bank_mask:0xf
	v_cndmask_b32_dpp v3, v2, v3, vcc quad_perm:[1,0,3,2] row_mask:0xf bank_mask:0xf
	v_cndmask_b32_dpp v5, v4, v5, vcc quad_perm:[1,0,3,2] row_mask:0xf bank_mask:0xf
	s_mov_b32 vcc_lo, 0x55555555
	s_mov_b32 vcc_hi, 0x55555555
	s_nop 1
	v_cndmask_b32_dpp v6, v86, v6, vcc quad_perm:[1,0,3,2] row_mask:0xf bank_mask:0xf
	v_cndmask_b32_dpp v8, v87, v8, vcc quad_perm:[1,0,3,2] row_mask:0xf bank_mask:0xf
	v_cndmask_b32_dpp v2, v88, v2, vcc quad_perm:[1,0,3,2] row_mask:0xf bank_mask:0xf
	v_cndmask_b32_dpp v4, v89, v4, vcc quad_perm:[1,0,3,2] row_mask:0xf bank_mask:0xf
	s_mov_b32 vcc_lo, 0xcccccccc
	s_mov_b32 vcc_hi, 0xcccccccc
	s_nop 1
	v_mov_b32_e32 v86, v8
	v_mov_b32_e32 v87, v9
	v_mov_b32_e32 v88, v4
	v_mov_b32_e32 v89, v5
	v_cndmask_b32_dpp v8, v6, v8, vcc quad_perm:[2,3,0,1] row_mask:0xf bank_mask:0xf
	v_cndmask_b32_dpp v9, v7, v9, vcc quad_perm:[2,3,0,1] row_mask:0xf bank_mask:0xf
	v_cndmask_b32_dpp v4, v2, v4, vcc quad_perm:[2,3,0,1] row_mask:0xf bank_mask:0xf
	v_cndmask_b32_dpp v5, v3, v5, vcc quad_perm:[2,3,0,1] row_mask:0xf bank_mask:0xf
	s_mov_b32 vcc_lo, 0x33333333
	s_mov_b32 vcc_hi, 0x33333333
	s_nop 1
	v_cndmask_b32_dpp v6, v86, v6, vcc quad_perm:[2,3,0,1] row_mask:0xf bank_mask:0xf
	v_cndmask_b32_dpp v7, v87, v7, vcc quad_perm:[2,3,0,1] row_mask:0xf bank_mask:0xf
	v_cndmask_b32_dpp v2, v88, v2, vcc quad_perm:[2,3,0,1] row_mask:0xf bank_mask:0xf
	v_cndmask_b32_dpp v3, v89, v3, vcc quad_perm:[2,3,0,1] row_mask:0xf bank_mask:0xf
	s_mov_b32 vcc_lo, 0xaaaaaaaa
	s_mov_b32 vcc_hi, 0xaaaaaaaa
	s_nop 1
	v_mov_b32_e32 v86, v91
	v_mov_b32_e32 v87, v93
	v_mov_b32_e32 v88, v77
	v_mov_b32_e32 v89, v79
	v_cndmask_b32_dpp v91, v90, v91, vcc quad_perm:[1,0,3,2] row_mask:0xf bank_mask:0xf
	v_cndmask_b32_dpp v93, v92, v93, vcc quad_perm:[1,0,3,2] row_mask:0xf bank_mask:0xf
	v_cndmask_b32_dpp v77, v76, v77, vcc quad_perm:[1,0,3,2] row_mask:0xf bank_mask:0xf
	v_cndmask_b32_dpp v79, v78, v79, vcc quad_perm:[1,0,3,2] row_mask:0xf bank_mask:0xf
	s_mov_b32 vcc_lo, 0x55555555
	s_mov_b32 vcc_hi, 0x55555555
	s_nop 1
	v_cndmask_b32_dpp v90, v86, v90, vcc quad_perm:[1,0,3,2] row_mask:0xf bank_mask:0xf
	v_cndmask_b32_dpp v92, v87, v92, vcc quad_perm:[1,0,3,2] row_mask:0xf bank_mask:0xf
	v_cndmask_b32_dpp v76, v88, v76, vcc quad_perm:[1,0,3,2] row_mask:0xf bank_mask:0xf
	v_cndmask_b32_dpp v78, v89, v78, vcc quad_perm:[1,0,3,2] row_mask:0xf bank_mask:0xf
	s_mov_b32 vcc_lo, 0xcccccccc
	s_mov_b32 vcc_hi, 0xcccccccc
	s_nop 1
	v_mov_b32_e32 v86, v92
	v_mov_b32_e32 v87, v93
	v_mov_b32_e32 v88, v78
	v_mov_b32_e32 v89, v79
	v_cndmask_b32_dpp v92, v90, v92, vcc quad_perm:[2,3,0,1] row_mask:0xf bank_mask:0xf
	v_cndmask_b32_dpp v93, v91, v93, vcc quad_perm:[2,3,0,1] row_mask:0xf bank_mask:0xf
	v_cndmask_b32_dpp v78, v76, v78, vcc quad_perm:[2,3,0,1] row_mask:0xf bank_mask:0xf
	v_cndmask_b32_dpp v79, v77, v79, vcc quad_perm:[2,3,0,1] row_mask:0xf bank_mask:0xf
	s_mov_b32 vcc_lo, 0x33333333
	s_mov_b32 vcc_hi, 0x33333333
	s_nop 1
	v_cndmask_b32_dpp v90, v86, v90, vcc quad_perm:[2,3,0,1] row_mask:0xf bank_mask:0xf
	v_cndmask_b32_dpp v91, v87, v91, vcc quad_perm:[2,3,0,1] row_mask:0xf bank_mask:0xf
	v_cndmask_b32_dpp v76, v88, v76, vcc quad_perm:[2,3,0,1] row_mask:0xf bank_mask:0xf
	v_cndmask_b32_dpp v77, v89, v77, vcc quad_perm:[2,3,0,1] row_mask:0xf bank_mask:0xf
	s_mov_b32 vcc_lo, 0xaaaaaaaa
	s_mov_b32 vcc_hi, 0xaaaaaaaa
	s_nop 1
	v_mov_b32_e32 v86, v73
	v_mov_b32_e32 v87, v75
	v_mov_b32_e32 v88, v69
	v_mov_b32_e32 v89, v71
	v_cndmask_b32_dpp v73, v72, v73, vcc quad_perm:[1,0,3,2] row_mask:0xf bank_mask:0xf
	v_cndmask_b32_dpp v75, v74, v75, vcc quad_perm:[1,0,3,2] row_mask:0xf bank_mask:0xf
; __device__ __forceinline__ float bf2f(bf16_t b) { return __uint_as_float((unsigned)b << 16); }
; __device__ __forceinline__ bf16_t f2bf(float f) { return (bf16_t)(cvt_pk_bf16(f, 0.f) & 0xffffu); }
; __device__ __forceinline__ float gelu_t(float x) { const float u = 0.7978845608028654f * (x + 0.044715f * x * x * x); return x * sigm(2.f * u); }
; __device__ __forceinline__ void ssm_pass2_item(const bf16_t* __restrict__ proj, const float* lamb_l, const float* lamt_l, const bf16_t* bbar_l, const bf16_t* ctt_l, const float* est, const float* __restrict__ dskip, ...
;     ...
;     const int c = lane & 15, ch = g * 16 + c; const float dk = dskip[ch];
; #pragma unroll
;     for (int blk = 0; blk < 8; ++blk)
; #pragma unroll
;         for (int r = 0; r < 4; ++r) { const int tok = b * SEQ + n * 128 + 16 * blk + 4 * (lane >> 4) + r;
;             const float y = yacc[blk][r] + dk * bf2f(proj[(size_t)tok * NIN + C_U + ch]); ssmy[(size_t)tok * 1024 + ch] = f2bf(gelu_t(y)); }
	v_cndmask_b32_dpp v69, v68, v69, vcc quad_perm:[1,0,3,2] row_mask:0xf bank_mask:0xf
	v_cndmask_b32_dpp v71, v70, v71, vcc quad_perm:[1,0,3,2] row_mask:0xf bank_mask:0xf
	s_mov_b32 vcc_lo, 0x55555555
	s_mov_b32 vcc_hi, 0x55555555
	s_nop 1
	v_cndmask_b32_dpp v72, v86, v72, vcc quad_perm:[1,0,3,2] row_mask:0xf bank_mask:0xf
	v_cndmask_b32_dpp v74, v87, v74, vcc quad_perm:[1,0,3,2] row_mask:0xf bank_mask:0xf
	v_cndmask_b32_dpp v68, v88, v68, vcc quad_perm:[1,0,3,2] row_mask:0xf bank_mask:0xf
	v_cndmask_b32_dpp v70, v89, v70, vcc quad_perm:[1,0,3,2] row_mask:0xf bank_mask:0xf
	s_mov_b32 vcc_lo, 0xcccccccc
	s_mov_b32 vcc_hi, 0xcccccccc
	s_nop 1
	v_mov_b32_e32 v86, v74
	v_mov_b32_e32 v87, v75
	v_mov_b32_e32 v88, v70
	v_mov_b32_e32 v89, v71
	v_cndmask_b32_dpp v74, v72, v74, vcc quad_perm:[2,3,0,1] row_mask:0xf bank_mask:0xf
	v_cndmask_b32_dpp v75, v73, v75, vcc quad_perm:[2,3,0,1] row_mask:0xf bank_mask:0xf
	v_cndmask_b32_dpp v70, v68, v70, vcc quad_perm:[2,3,0,1] row_mask:0xf bank_mask:0xf
	v_cndmask_b32_dpp v71, v69, v71, vcc quad_perm:[2,3,0,1] row_mask:0xf bank_mask:0xf
	s_mov_b32 vcc_lo, 0x33333333
	s_mov_b32 vcc_hi, 0x33333333
	s_nop 1
	v_cndmask_b32_dpp v72, v86, v72, vcc quad_perm:[2,3,0,1] row_mask:0xf bank_mask:0xf
	v_cndmask_b32_dpp v73, v87, v73, vcc quad_perm:[2,3,0,1] row_mask:0xf bank_mask:0xf
	v_cndmask_b32_dpp v68, v88, v68, vcc quad_perm:[2,3,0,1] row_mask:0xf bank_mask:0xf
	v_cndmask_b32_dpp v69, v89, v69, vcc quad_perm:[2,3,0,1] row_mask:0xf bank_mask:0xf
	s_mov_b32 vcc_lo, 0xaaaaaaaa
	s_mov_b32 vcc_hi, 0xaaaaaaaa
	s_nop 1
	v_mov_b32_e32 v86, v143
	v_mov_b32_e32 v87, v145
	v_mov_b32_e32 v88, v139
	v_mov_b32_e32 v89, v141
	v_cndmask_b32_dpp v143, v142, v143, vcc quad_perm:[1,0,3,2] row_mask:0xf bank_mask:0xf
	v_cndmask_b32_dpp v145, v144, v145, vcc quad_perm:[1,0,3,2] row_mask:0xf bank_mask:0xf
	v_cndmask_b32_dpp v139, v138, v139, vcc quad_perm:[1,0,3,2] row_mask:0xf bank_mask:0xf
	v_cndmask_b32_dpp v141, v140, v141, vcc quad_perm:[1,0,3,2] row_mask:0xf bank_mask:0xf
	s_mov_b32 vcc_lo, 0x55555555
	s_mov_b32 vcc_hi, 0x55555555
	s_nop 1
	v_cndmask_b32_dpp v142, v86, v142, vcc quad_perm:[1,0,3,2] row_mask:0xf bank_mask:0xf
	v_cndmask_b32_dpp v144, v87, v144, vcc quad_perm:[1,0,3,2] row_mask:0xf bank_mask:0xf
	v_cndmask_b32_dpp v138, v88, v138, vcc quad_perm:[1,0,3,2] row_mask:0xf bank_mask:0xf
	v_cndmask_b32_dpp v140, v89, v140, vcc quad_perm:[1,0,3,2] row_mask:0xf bank_mask:0xf
	s_mov_b32 vcc_lo, 0xcccccccc
	s_mov_b32 vcc_hi, 0xcccccccc
	s_nop 1
	v_mov_b32_e32 v86, v144
	v_mov_b32_e32 v87, v145
	v_mov_b32_e32 v88, v140
	v_mov_b32_e32 v89, v141
	v_cndmask_b32_dpp v144, v142, v144, vcc quad_perm:[2,3,0,1] row_mask:0xf bank_mask:0xf
	v_cndmask_b32_dpp v145, v143, v145, vcc quad_perm:[2,3,0,1] row_mask:0xf bank_mask:0xf
	v_cndmask_b32_dpp v140, v138, v140, vcc quad_perm:[2,3,0,1] row_mask:0xf bank_mask:0xf
	v_cndmask_b32_dpp v141, v139, v141, vcc quad_perm:[2,3,0,1] row_mask:0xf bank_mask:0xf
	s_mov_b32 vcc_lo, 0x33333333
	s_mov_b32 vcc_hi, 0x33333333
	s_nop 1
	v_cndmask_b32_dpp v142, v86, v142, vcc quad_perm:[2,3,0,1] row_mask:0xf bank_mask:0xf
	v_cndmask_b32_dpp v143, v87, v143, vcc quad_perm:[2,3,0,1] row_mask:0xf bank_mask:0xf
	v_cndmask_b32_dpp v138, v88, v138, vcc quad_perm:[2,3,0,1] row_mask:0xf bank_mask:0xf
	v_cndmask_b32_dpp v139, v89, v139, vcc quad_perm:[2,3,0,1] row_mask:0xf bank_mask:0xf
	s_waitcnt vmcnt(0)
	v_lshlrev_b32_e32 v86, 16, v106
	v_and_b32_e32 v87, 0xffff0000, v106
	v_lshlrev_b32_e32 v88, 16, v107
	v_and_b32_e32 v89, 0xffff0000, v107
	v_fma_f32 v6, v82, v86, v6
	v_fma_f32 v7, v83, v87, v7
	v_fma_f32 v8, v84, v88, v8
	v_fma_f32 v9, v85, v89, v9
	v_mul_f32_e32 v86, 0x3d372713, v6
	v_mul_f32_e32 v87, 0x3d372713, v7
	v_mul_f32_e32 v88, 0x3d372713, v8
	v_mul_f32_e32 v89, 0x3d372713, v9
	v_mul_f32_e32 v86, v6, v86
	v_mul_f32_e32 v87, v7, v87
	v_mul_f32_e32 v88, v8, v88
	v_mul_f32_e32 v89, v9, v89
	v_fma_f32 v86, v6, v86, v6
	v_fma_f32 v87, v7, v87, v7
	v_fma_f32 v88, v8, v88, v8
	v_fma_f32 v89, v9, v89, v9
	v_mul_f32_e32 v86, 0x3f4c422a, v86
	v_mul_f32_e32 v87, 0x3f4c422a, v87
	v_mul_f32_e32 v88, 0x3f4c422a, v88
	v_mul_f32_e32 v89, 0x3f4c422a, v89
	v_add_f32_e32 v86, v86, v86
	v_add_f32_e32 v87, v87, v87
	v_add_f32_e32 v88, v88, v88
	v_add_f32_e32 v89, v89, v89
	v_mul_f32_e32 v86, 0xbfb8aa3b, v86
	v_mul_f32_e32 v87, 0xbfb8aa3b, v87
	v_mul_f32_e32 v88, 0xbfb8aa3b, v88
	v_mul_f32_e32 v89, 0xbfb8aa3b, v89
	v_exp_f32_e32 v86, v86
	v_exp_f32_e32 v87, v87
	v_exp_f32_e32 v88, v88
	v_exp_f32_e32 v89, v89
	v_add_f32_e32 v86, 1.0, v86
	v_add_f32_e32 v87, 1.0, v87
	v_add_f32_e32 v88, 1.0, v88
	v_add_f32_e32 v89, 1.0, v89
	v_rcp_f32_e32 v86, v86
	v_rcp_f32_e32 v87, v87
	v_rcp_f32_e32 v88, v88
	v_rcp_f32_e32 v89, v89
	v_mul_f32_e32 v6, v6, v86
	v_mul_f32_e32 v7, v7, v87
	v_mul_f32_e32 v8, v8, v88
	v_mul_f32_e32 v9, v9, v89
	v_cvt_pk_bf16_f32 v6, v6, v7
	v_cvt_pk_bf16_f32 v7, v8, v9
	global_store_dwordx2 v[254:255], v[6:7], off
	v_lshlrev_b32_e32 v86, 16, v108
	v_and_b32_e32 v87, 0xffff0000, v108
	v_lshlrev_b32_e32 v88, 16, v109
	v_and_b32_e32 v89, 0xffff0000, v109
	v_fma_f32 v2, v82, v86, v2
	v_fma_f32 v3, v83, v87, v3
	v_fma_f32 v4, v84, v88, v4
	v_fma_f32 v5, v85, v89, v5
	v_mul_f32_e32 v86, 0x3d372713, v2
	v_mul_f32_e32 v87, 0x3d372713, v3
	v_mul_f32_e32 v88, 0x3d372713, v4
	v_mul_f32_e32 v89, 0x3d372713, v5
	v_mul_f32_e32 v86, v2, v86
	v_mul_f32_e32 v87, v3, v87
	v_mul_f32_e32 v88, v4, v88
	v_mul_f32_e32 v89, v5, v89
	v_fma_f32 v86, v2, v86, v2
	v_fma_f32 v87, v3, v87, v3
	v_fma_f32 v88, v4, v88, v4
	v_fma_f32 v89, v5, v89, v5
	v_mul_f32_e32 v86, 0x3f4c422a, v86
	v_mul_f32_e32 v87, 0x3f4c422a, v87
	v_mul_f32_e32 v88, 0x3f4c422a, v88
; __device__ __forceinline__ float bf2f(bf16_t b) { return __uint_as_float((unsigned)b << 16); }
; __device__ __forceinline__ bf16_t f2bf(float f) { return (bf16_t)(cvt_pk_bf16(f, 0.f) & 0xffffu); }
; __device__ __forceinline__ float gelu_t(float x) { const float u = 0.7978845608028654f * (x + 0.044715f * x * x * x); return x * sigm(2.f * u); }
; __device__ __forceinline__ void ssm_pass2_item(const bf16_t* __restrict__ proj, const float* lamb_l, const float* lamt_l, const bf16_t* bbar_l, const bf16_t* ctt_l, const float* est, const float* __restrict__ dskip, ...
;     ...
;     const int c = lane & 15, ch = g * 16 + c; const float dk = dskip[ch];
; #pragma unroll
;     for (int blk = 0; blk < 8; ++blk)
; #pragma unroll
;         for (int r = 0; r < 4; ++r) { const int tok = b * SEQ + n * 128 + 16 * blk + 4 * (lane >> 4) + r;
;             const float y = yacc[blk][r] + dk * bf2f(proj[(size_t)tok * NIN + C_U + ch]); ssmy[(size_t)tok * 1024 + ch] = f2bf(gelu_t(y)); }
	v_mul_f32_e32 v89, 0x3f4c422a, v89
	v_add_f32_e32 v86, v86, v86
	v_add_f32_e32 v87, v87, v87
	v_add_f32_e32 v88, v88, v88
	v_add_f32_e32 v89, v89, v89
	v_mul_f32_e32 v86, 0xbfb8aa3b, v86
	v_mul_f32_e32 v87, 0xbfb8aa3b, v87
	v_mul_f32_e32 v88, 0xbfb8aa3b, v88
	v_mul_f32_e32 v89, 0xbfb8aa3b, v89
	v_exp_f32_e32 v86, v86
	v_exp_f32_e32 v87, v87
	v_exp_f32_e32 v88, v88
	v_exp_f32_e32 v89, v89
	v_add_f32_e32 v86, 1.0, v86
	v_add_f32_e32 v87, 1.0, v87
	v_add_f32_e32 v88, 1.0, v88
	v_add_f32_e32 v89, 1.0, v89
	v_rcp_f32_e32 v86, v86
	v_rcp_f32_e32 v87, v87
	v_rcp_f32_e32 v88, v88
	v_rcp_f32_e32 v89, v89
	v_mul_f32_e32 v2, v2, v86
	v_mul_f32_e32 v3, v3, v87
	v_mul_f32_e32 v4, v4, v88
	v_mul_f32_e32 v5, v5, v89
	v_cvt_pk_bf16_f32 v2, v2, v3
	v_cvt_pk_bf16_f32 v3, v4, v5
	s_mov_b32 s100, 0x8000
	v_lshl_add_u64 v[14:15], v[254:255], 0, s[100:101]
	global_store_dwordx2 v[14:15], v[2:3], off
	v_lshlrev_b32_e32 v86, 16, v110
	v_and_b32_e32 v87, 0xffff0000, v110
	v_lshlrev_b32_e32 v88, 16, v111
	v_and_b32_e32 v89, 0xffff0000, v111
	v_fma_f32 v90, v82, v86, v90
	v_fma_f32 v91, v83, v87, v91
	v_fma_f32 v92, v84, v88, v92
	v_fma_f32 v93, v85, v89, v93
	v_mul_f32_e32 v86, 0x3d372713, v90
	v_mul_f32_e32 v87, 0x3d372713, v91
	v_mul_f32_e32 v88, 0x3d372713, v92
	v_mul_f32_e32 v89, 0x3d372713, v93
	v_mul_f32_e32 v86, v90, v86
	v_mul_f32_e32 v87, v91, v87
	v_mul_f32_e32 v88, v92, v88
	v_mul_f32_e32 v89, v93, v89
	v_fma_f32 v86, v90, v86, v90
	v_fma_f32 v87, v91, v87, v91
	v_fma_f32 v88, v92, v88, v92
	v_fma_f32 v89, v93, v89, v93
	v_mul_f32_e32 v86, 0x3f4c422a, v86
	v_mul_f32_e32 v87, 0x3f4c422a, v87
	v_mul_f32_e32 v88, 0x3f4c422a, v88
	v_mul_f32_e32 v89, 0x3f4c422a, v89
	v_add_f32_e32 v86, v86, v86
	v_add_f32_e32 v87, v87, v87
	v_add_f32_e32 v88, v88, v88
	v_add_f32_e32 v89, v89, v89
	v_mul_f32_e32 v86, 0xbfb8aa3b, v86
	v_mul_f32_e32 v87, 0xbfb8aa3b, v87
	v_mul_f32_e32 v88, 0xbfb8aa3b, v88
	v_mul_f32_e32 v89, 0xbfb8aa3b, v89
	v_exp_f32_e32 v86, v86
	v_exp_f32_e32 v87, v87
	v_exp_f32_e32 v88, v88
	v_exp_f32_e32 v89, v89
	v_add_f32_e32 v86, 1.0, v86
	v_add_f32_e32 v87, 1.0, v87
	v_add_f32_e32 v88, 1.0, v88
	v_add_f32_e32 v89, 1.0, v89
	v_rcp_f32_e32 v86, v86
	v_rcp_f32_e32 v87, v87
	v_rcp_f32_e32 v88, v88
	v_rcp_f32_e32 v89, v89
	v_mul_f32_e32 v90, v90, v86
	v_mul_f32_e32 v91, v91, v87
	v_mul_f32_e32 v92, v92, v88
	v_mul_f32_e32 v93, v93, v89
	v_cvt_pk_bf16_f32 v90, v90, v91
	v_cvt_pk_bf16_f32 v91, v92, v93
	s_mov_b32 s100, 0x10000
	v_lshl_add_u64 v[14:15], v[254:255], 0, s[100:101]
	global_store_dwordx2 v[14:15], v[90:91], off
	v_lshlrev_b32_e32 v86, 16, v112
	v_and_b32_e32 v87, 0xffff0000, v112
	v_lshlrev_b32_e32 v88, 16, v113
	v_and_b32_e32 v89, 0xffff0000, v113
	v_fma_f32 v76, v82, v86, v76
	v_fma_f32 v77, v83, v87, v77
	v_fma_f32 v78, v84, v88, v78
	v_fma_f32 v79, v85, v89, v79
	v_mul_f32_e32 v86, 0x3d372713, v76
	v_mul_f32_e32 v87, 0x3d372713, v77
	v_mul_f32_e32 v88, 0x3d372713, v78
	v_mul_f32_e32 v89, 0x3d372713, v79
	v_mul_f32_e32 v86, v76, v86
	v_mul_f32_e32 v87, v77, v87
	v_mul_f32_e32 v88, v78, v88
	v_mul_f32_e32 v89, v79, v89
	v_fma_f32 v86, v76, v86, v76
	v_fma_f32 v87, v77, v87, v77
	v_fma_f32 v88, v78, v88, v78
	v_fma_f32 v89, v79, v89, v79
	v_mul_f32_e32 v86, 0x3f4c422a, v86
	v_mul_f32_e32 v87, 0x3f4c422a, v87
	v_mul_f32_e32 v88, 0x3f4c422a, v88
	v_mul_f32_e32 v89, 0x3f4c422a, v89
	v_add_f32_e32 v86, v86, v86
	v_add_f32_e32 v87, v87, v87
	v_add_f32_e32 v88, v88, v88
	v_add_f32_e32 v89, v89, v89
	v_mul_f32_e32 v86, 0xbfb8aa3b, v86
	v_mul_f32_e32 v87, 0xbfb8aa3b, v87
	v_mul_f32_e32 v88, 0xbfb8aa3b, v88
	v_mul_f32_e32 v89, 0xbfb8aa3b, v89
	v_exp_f32_e32 v86, v86
	v_exp_f32_e32 v87, v87
	v_exp_f32_e32 v88, v88
	v_exp_f32_e32 v89, v89
	v_add_f32_e32 v86, 1.0, v86
	v_add_f32_e32 v87, 1.0, v87
	v_add_f32_e32 v88, 1.0, v88
	v_add_f32_e32 v89, 1.0, v89
	v_rcp_f32_e32 v86, v86
	v_rcp_f32_e32 v87, v87
	v_rcp_f32_e32 v88, v88
	v_rcp_f32_e32 v89, v89
	v_mul_f32_e32 v76, v76, v86
	v_mul_f32_e32 v77, v77, v87
	v_mul_f32_e32 v78, v78, v88
	v_mul_f32_e32 v79, v79, v89
	v_cvt_pk_bf16_f32 v76, v76, v77
	v_cvt_pk_bf16_f32 v77, v78, v79
	s_mov_b32 s100, 0x18000
	v_lshl_add_u64 v[14:15], v[254:255], 0, s[100:101]
	global_store_dwordx2 v[14:15], v[76:77], off
	v_lshlrev_b32_e32 v86, 16, v114
	v_and_b32_e32 v87, 0xffff0000, v114
	v_lshlrev_b32_e32 v88, 16, v115
	v_and_b32_e32 v89, 0xffff0000, v115
	v_fma_f32 v72, v82, v86, v72
	v_fma_f32 v73, v83, v87, v73
	v_fma_f32 v74, v84, v88, v74
	v_fma_f32 v75, v85, v89, v75
	v_mul_f32_e32 v86, 0x3d372713, v72
	v_mul_f32_e32 v87, 0x3d372713, v73
	v_mul_f32_e32 v88, 0x3d372713, v74
	v_mul_f32_e32 v89, 0x3d372713, v75
	v_mul_f32_e32 v86, v72, v86
	v_mul_f32_e32 v87, v73, v87
	v_mul_f32_e32 v88, v74, v88
	v_mul_f32_e32 v89, v75, v89
	v_fma_f32 v86, v72, v86, v72
	v_fma_f32 v87, v73, v87, v73
	v_fma_f32 v88, v74, v88, v74
	v_fma_f32 v89, v75, v89, v75
	v_mul_f32_e32 v86, 0x3f4c422a, v86
	v_mul_f32_e32 v87, 0x3f4c422a, v87
	v_mul_f32_e32 v88, 0x3f4c422a, v88
	v_mul_f32_e32 v89, 0x3f4c422a, v89
	v_add_f32_e32 v86, v86, v86
	v_add_f32_e32 v87, v87, v87
	v_add_f32_e32 v88, v88, v88
	v_add_f32_e32 v89, v89, v89
	v_mul_f32_e32 v86, 0xbfb8aa3b, v86
	v_mul_f32_e32 v87, 0xbfb8aa3b, v87
	v_mul_f32_e32 v88, 0xbfb8aa3b, v88
	v_mul_f32_e32 v89, 0xbfb8aa3b, v89
	v_exp_f32_e32 v86, v86
	v_exp_f32_e32 v87, v87
	v_exp_f32_e32 v88, v88
	v_exp_f32_e32 v89, v89
	v_add_f32_e32 v86, 1.0, v86
	v_add_f32_e32 v87, 1.0, v87
	v_add_f32_e32 v88, 1.0, v88
	v_add_f32_e32 v89, 1.0, v89
; __device__ __forceinline__ float bf2f(bf16_t b) { return __uint_as_float((unsigned)b << 16); }
; __device__ __forceinline__ bf16_t f2bf(float f) { return (bf16_t)(cvt_pk_bf16(f, 0.f) & 0xffffu); }
; __device__ __forceinline__ float gelu_t(float x) { const float u = 0.7978845608028654f * (x + 0.044715f * x * x * x); return x * sigm(2.f * u); }
; __device__ __forceinline__ void ssm_pass2_item(const bf16_t* __restrict__ proj, const float* lamb_l, const float* lamt_l, const bf16_t* bbar_l, const bf16_t* ctt_l, const float* est, const float* __restrict__ dskip, ...
;     ...
;     const int c = lane & 15, ch = g * 16 + c; const float dk = dskip[ch];
; #pragma unroll
;     for (int blk = 0; blk < 8; ++blk)
; #pragma unroll
;         for (int r = 0; r < 4; ++r) { const int tok = b * SEQ + n * 128 + 16 * blk + 4 * (lane >> 4) + r;
;             const float y = yacc[blk][r] + dk * bf2f(proj[(size_t)tok * NIN + C_U + ch]); ssmy[(size_t)tok * 1024 + ch] = f2bf(gelu_t(y)); }
	v_rcp_f32_e32 v86, v86
	v_rcp_f32_e32 v87, v87
	v_rcp_f32_e32 v88, v88
	v_rcp_f32_e32 v89, v89
	v_mul_f32_e32 v72, v72, v86
	v_mul_f32_e32 v73, v73, v87
	v_mul_f32_e32 v74, v74, v88
	v_mul_f32_e32 v75, v75, v89
	v_cvt_pk_bf16_f32 v72, v72, v73
	v_cvt_pk_bf16_f32 v73, v74, v75
	s_mov_b32 s100, 0x20000
	v_lshl_add_u64 v[14:15], v[254:255], 0, s[100:101]
	global_store_dwordx2 v[14:15], v[72:73], off
	v_lshlrev_b32_e32 v86, 16, v116
	v_and_b32_e32 v87, 0xffff0000, v116
	v_lshlrev_b32_e32 v88, 16, v117
	v_and_b32_e32 v89, 0xffff0000, v117
	v_fma_f32 v68, v82, v86, v68
	v_fma_f32 v69, v83, v87, v69
	v_fma_f32 v70, v84, v88, v70
	v_fma_f32 v71, v85, v89, v71
	v_mul_f32_e32 v86, 0x3d372713, v68
	v_mul_f32_e32 v87, 0x3d372713, v69
	v_mul_f32_e32 v88, 0x3d372713, v70
	v_mul_f32_e32 v89, 0x3d372713, v71
	v_mul_f32_e32 v86, v68, v86
	v_mul_f32_e32 v87, v69, v87
	v_mul_f32_e32 v88, v70, v88
	v_mul_f32_e32 v89, v71, v89
	v_fma_f32 v86, v68, v86, v68
	v_fma_f32 v87, v69, v87, v69
	v_fma_f32 v88, v70, v88, v70
	v_fma_f32 v89, v71, v89, v71
	v_mul_f32_e32 v86, 0x3f4c422a, v86
	v_mul_f32_e32 v87, 0x3f4c422a, v87
	v_mul_f32_e32 v88, 0x3f4c422a, v88
	v_mul_f32_e32 v89, 0x3f4c422a, v89
	v_add_f32_e32 v86, v86, v86
	v_add_f32_e32 v87, v87, v87
	v_add_f32_e32 v88, v88, v88
	v_add_f32_e32 v89, v89, v89
	v_mul_f32_e32 v86, 0xbfb8aa3b, v86
	v_mul_f32_e32 v87, 0xbfb8aa3b, v87
	v_mul_f32_e32 v88, 0xbfb8aa3b, v88
	v_mul_f32_e32 v89, 0xbfb8aa3b, v89
	v_exp_f32_e32 v86, v86
	v_exp_f32_e32 v87, v87
	v_exp_f32_e32 v88, v88
	v_exp_f32_e32 v89, v89
	v_add_f32_e32 v86, 1.0, v86
	v_add_f32_e32 v87, 1.0, v87
	v_add_f32_e32 v88, 1.0, v88
	v_add_f32_e32 v89, 1.0, v89
	v_rcp_f32_e32 v86, v86
	v_rcp_f32_e32 v87, v87
	v_rcp_f32_e32 v88, v88
	v_rcp_f32_e32 v89, v89
	v_mul_f32_e32 v68, v68, v86
	v_mul_f32_e32 v69, v69, v87
	v_mul_f32_e32 v70, v70, v88
	v_mul_f32_e32 v71, v71, v89
	v_cvt_pk_bf16_f32 v68, v68, v69
	v_cvt_pk_bf16_f32 v69, v70, v71
	s_mov_b32 s100, 0x28000
	v_lshl_add_u64 v[14:15], v[254:255], 0, s[100:101]
	global_store_dwordx2 v[14:15], v[68:69], off
	v_lshlrev_b32_e32 v86, 16, v118
	v_and_b32_e32 v87, 0xffff0000, v118
	v_lshlrev_b32_e32 v88, 16, v119
	v_and_b32_e32 v89, 0xffff0000, v119
	v_fma_f32 v142, v82, v86, v142
	v_fma_f32 v143, v83, v87, v143
	v_fma_f32 v144, v84, v88, v144
	v_fma_f32 v145, v85, v89, v145
	v_mul_f32_e32 v86, 0x3d372713, v142
	v_mul_f32_e32 v87, 0x3d372713, v143
	v_mul_f32_e32 v88, 0x3d372713, v144
	v_mul_f32_e32 v89, 0x3d372713, v145
	v_mul_f32_e32 v86, v142, v86
	v_mul_f32_e32 v87, v143, v87
	v_mul_f32_e32 v88, v144, v88
	v_mul_f32_e32 v89, v145, v89
	v_fma_f32 v86, v142, v86, v142
	v_fma_f32 v87, v143, v87, v143
	v_fma_f32 v88, v144, v88, v144
	v_fma_f32 v89, v145, v89, v145
	v_mul_f32_e32 v86, 0x3f4c422a, v86
	v_mul_f32_e32 v87, 0x3f4c422a, v87
	v_mul_f32_e32 v88, 0x3f4c422a, v88
	v_mul_f32_e32 v89, 0x3f4c422a, v89
	v_add_f32_e32 v86, v86, v86
	v_add_f32_e32 v87, v87, v87
	v_add_f32_e32 v88, v88, v88
	v_add_f32_e32 v89, v89, v89
	v_mul_f32_e32 v86, 0xbfb8aa3b, v86
	v_mul_f32_e32 v87, 0xbfb8aa3b, v87
	v_mul_f32_e32 v88, 0xbfb8aa3b, v88
	v_mul_f32_e32 v89, 0xbfb8aa3b, v89
	v_exp_f32_e32 v86, v86
	v_exp_f32_e32 v87, v87
	v_exp_f32_e32 v88, v88
	v_exp_f32_e32 v89, v89
	v_add_f32_e32 v86, 1.0, v86
	v_add_f32_e32 v87, 1.0, v87
	v_add_f32_e32 v88, 1.0, v88
	v_add_f32_e32 v89, 1.0, v89
	v_rcp_f32_e32 v86, v86
	v_rcp_f32_e32 v87, v87
	v_rcp_f32_e32 v88, v88
	v_rcp_f32_e32 v89, v89
	v_mul_f32_e32 v142, v142, v86
	v_mul_f32_e32 v143, v143, v87
	v_mul_f32_e32 v144, v144, v88
	v_mul_f32_e32 v145, v145, v89
	v_cvt_pk_bf16_f32 v142, v142, v143
	v_cvt_pk_bf16_f32 v143, v144, v145
	s_mov_b32 s100, 0x30000
	v_lshl_add_u64 v[14:15], v[254:255], 0, s[100:101]
	global_store_dwordx2 v[14:15], v[142:143], off
	v_lshlrev_b32_e32 v86, 16, v120
	v_and_b32_e32 v87, 0xffff0000, v120
	v_lshlrev_b32_e32 v88, 16, v121
	v_and_b32_e32 v89, 0xffff0000, v121
	v_fma_f32 v138, v82, v86, v138
	v_fma_f32 v139, v83, v87, v139
	v_fma_f32 v140, v84, v88, v140
	v_fma_f32 v141, v85, v89, v141
	v_mul_f32_e32 v86, 0x3d372713, v138
	v_mul_f32_e32 v87, 0x3d372713, v139
	v_mul_f32_e32 v88, 0x3d372713, v140
	v_mul_f32_e32 v89, 0x3d372713, v141
	v_mul_f32_e32 v86, v138, v86
	v_mul_f32_e32 v87, v139, v87
	v_mul_f32_e32 v88, v140, v88
	v_mul_f32_e32 v89, v141, v89
	v_fma_f32 v86, v138, v86, v138
	v_fma_f32 v87, v139, v87, v139
	v_fma_f32 v88, v140, v88, v140
	v_fma_f32 v89, v141, v89, v141
	v_mul_f32_e32 v86, 0x3f4c422a, v86
	v_mul_f32_e32 v87, 0x3f4c422a, v87
	v_mul_f32_e32 v88, 0x3f4c422a, v88
	v_mul_f32_e32 v89, 0x3f4c422a, v89
	v_add_f32_e32 v86, v86, v86
	v_add_f32_e32 v87, v87, v87
	v_add_f32_e32 v88, v88, v88
	v_add_f32_e32 v89, v89, v89
	v_mul_f32_e32 v86, 0xbfb8aa3b, v86
	v_mul_f32_e32 v87, 0xbfb8aa3b, v87
	v_mul_f32_e32 v88, 0xbfb8aa3b, v88
	v_mul_f32_e32 v89, 0xbfb8aa3b, v89
	v_exp_f32_e32 v86, v86
	v_exp_f32_e32 v87, v87
	v_exp_f32_e32 v88, v88
	v_exp_f32_e32 v89, v89
	v_add_f32_e32 v86, 1.0, v86
	v_add_f32_e32 v87, 1.0, v87
	v_add_f32_e32 v88, 1.0, v88
	v_add_f32_e32 v89, 1.0, v89
	v_rcp_f32_e32 v86, v86
	v_rcp_f32_e32 v87, v87
	v_rcp_f32_e32 v88, v88
	v_rcp_f32_e32 v89, v89
	v_mul_f32_e32 v138, v138, v86
	v_mul_f32_e32 v139, v139, v87
	v_mul_f32_e32 v140, v140, v88
	v_mul_f32_e32 v141, v141, v89
	v_cvt_pk_bf16_f32 v138, v138, v139
	v_cvt_pk_bf16_f32 v139, v140, v141
	s_mov_b32 s100, 0x38000
	v_lshl_add_u64 v[14:15], v[254:255], 0, s[100:101]
	global_store_dwordx2 v[14:15], v[138:139], off
	s_cbranch_scc0 .LBB0_648

; template <class T> __device__ __forceinline__ void est(T* p, T v) { if constexpr (MK_EPI_NT != 0) __builtin_nontemporal_store(v, p); else *p = v; }
; template <int DIR> ...
;     const int dg = DIR * 64 + g; const float ar = lamb_l[(dg * 64 + lane) * 2], ai = lamb_l[(dg * 64 + lane) * 2 + 1], tr = lamt_l[(dg * 64 + lane) * 2], ti = lamt_l[(dg * 64 + lane) * 2 + 1];
;     float sr = 0.f, si = 0.f;
;     { const float* e = est + ((((size_t)(DIR * 2 + b) * 64 + g) * 32) * 64 + lane) * 2; f32x2 ev[32];
; #pragma unroll
;       for (int m = 0; m < 32; ++m) ev[m] = *(const f32x2*)(e + (size_t)m * 128);
; #pragma unroll
;       for (int mm = 0; mm < 32; ++mm) { const int m = DIR ? 31 - mm : mm; const bool use = DIR ? (m > n) : (m < n);
;           const float nsr = fmaf(tr, sr, fmaf(-ti, si, ev[m].x)), nsi = fmaf(tr, si, fmaf(ti, sr, ev[m].y)); sr = use ? nsr : sr; si = use ? nsi : si; } }
.LBB0_1626:
	s_bfe_u32 s59, s57, 0x60005
	v_lshl_or_b32 v2, s59, 9, v174
	global_load_dwordx2 v[142:143], v2, s[10:11]
	global_load_dwordx2 v[4:5], v2, s[8:9]
	s_ashr_i32 s16, s57, 11
	s_ashr_i32 s17, s16, 31
	s_lshl_b64 s[4:5], s[16:17], 17
	s_lshl_b32 s0, s59, 11
	s_or_b32 s4, s4, s0
	v_mov_b32_e32 v3, s5
	v_or_b32_e32 v2, s4, v194
	v_lshl_add_u64 v[2:3], v[2:3], 3, s[76:77]
	global_load_dwordx2 v[64:65], v[2:3], off
	global_load_dwordx2 v[62:63], v[2:3], off offset:512
	global_load_dwordx2 v[60:61], v[2:3], off offset:1024
	global_load_dwordx2 v[58:59], v[2:3], off offset:1536
	global_load_dwordx2 v[56:57], v[2:3], off offset:2048
	global_load_dwordx2 v[54:55], v[2:3], off offset:2560
	global_load_dwordx2 v[52:53], v[2:3], off offset:3072
	global_load_dwordx2 v[50:51], v[2:3], off offset:3584
	v_add_co_u32_e32 v6, vcc, s38, v2
	s_and_b32 s3, s57, 31
	s_nop 0
	v_addc_co_u32_e32 v7, vcc, 0, v3, vcc
	v_add_co_u32_e32 v8, vcc, s39, v2
	s_cmp_eq_u32 s3, 0
	s_nop 0
	v_addc_co_u32_e32 v9, vcc, 0, v3, vcc
	global_load_dwordx2 v[48:49], v[8:9], off offset:-4096
	global_load_dwordx2 v[46:47], v[6:7], off offset:512
	global_load_dwordx2 v[44:45], v[6:7], off offset:1024
	global_load_dwordx2 v[42:43], v[6:7], off offset:1536
	global_load_dwordx2 v[40:41], v[6:7], off offset:2048
	global_load_dwordx2 v[38:39], v[6:7], off offset:2560
	global_load_dwordx2 v[36:37], v[6:7], off offset:3072
	global_load_dwordx2 v[34:35], v[6:7], off offset:3584
	global_load_dwordx2 v[32:33], v[8:9], off
	global_load_dwordx2 v[30:31], v[8:9], off offset:512
	global_load_dwordx2 v[28:29], v[8:9], off offset:1024
	global_load_dwordx2 v[26:27], v[8:9], off offset:1536
	global_load_dwordx2 v[24:25], v[8:9], off offset:2048
	global_load_dwordx2 v[22:23], v[8:9], off offset:2560
	global_load_dwordx2 v[20:21], v[8:9], off offset:3072
	global_load_dwordx2 v[18:19], v[8:9], off offset:3584
	v_add_co_u32_e32 v2, vcc, s40, v2
	s_waitcnt vmcnt(23)
	v_fmamk_f32 v64, v5, 0x80000000, v64
	v_addc_co_u32_e32 v3, vcc, 0, v3, vcc
	global_load_dwordx2 v[16:17], v[2:3], off
	global_load_dwordx2 v[14:15], v[2:3], off offset:512
	global_load_dwordx2 v[12:13], v[2:3], off offset:1024
	global_load_dwordx2 v[10:11], v[2:3], off offset:1536
	global_load_dwordx2 v[8:9], v[2:3], off offset:2048
	global_load_dwordx2 v[6:7], v[2:3], off offset:2560
	s_nop 0
	global_load_dwordx2 v[2:3], v[2:3], off offset:3072
	v_fmac_f32_e32 v65, 0, v5
	s_cselect_b64 vcc, -1, 0
	v_fmac_f32_e32 v64, 0, v4
	v_fmac_f32_e32 v65, 0, v4
	v_cndmask_b32_e64 v64, v64, 0, vcc
	v_cndmask_b32_e64 v65, v65, 0, vcc
	s_cmp_gt_u32 s3, 1
	s_waitcnt vmcnt(29)
	v_fma_f32 v62, -v5, v65, v62
	v_fmac_f32_e32 v63, v5, v64
	s_cselect_b64 s[0:1], -1, 0
	v_fmac_f32_e32 v62, v4, v64
	v_fmac_f32_e32 v63, v4, v65
	v_cndmask_b32_e64 v62, v64, v62, s[0:1]
	v_cndmask_b32_e64 v63, v65, v63, s[0:1]
	s_cmp_gt_u32 s3, 2
	s_waitcnt vmcnt(28)
	v_fma_f32 v60, -v5, v63, v60
	v_fmac_f32_e32 v61, v5, v62
	s_cselect_b64 s[0:1], -1, 0
	v_fmac_f32_e32 v60, v4, v62
	v_fmac_f32_e32 v61, v4, v63
	v_cndmask_b32_e64 v60, v62, v60, s[0:1]
	v_cndmask_b32_e64 v61, v63, v61, s[0:1]
	s_cmp_gt_u32 s3, 3
	s_waitcnt vmcnt(27)
	v_fma_f32 v58, -v5, v61, v58
	v_fmac_f32_e32 v59, v5, v60
	s_cselect_b64 s[0:1], -1, 0
	v_fmac_f32_e32 v58, v4, v60
	v_fmac_f32_e32 v59, v4, v61
	v_cndmask_b32_e64 v58, v60, v58, s[0:1]
	v_cndmask_b32_e64 v59, v61, v59, s[0:1]
	s_cmp_gt_u32 s3, 4
	s_waitcnt vmcnt(26)
	v_fma_f32 v56, -v5, v59, v56
	v_fmac_f32_e32 v57, v5, v58
	s_cselect_b64 s[0:1], -1, 0
	v_fmac_f32_e32 v56, v4, v58
	v_fmac_f32_e32 v57, v4, v59
	v_cndmask_b32_e64 v56, v58, v56, s[0:1]
	v_cndmask_b32_e64 v57, v59, v57, s[0:1]
	s_cmp_gt_u32 s3, 5
	s_waitcnt vmcnt(25)
	v_fma_f32 v54, -v5, v57, v54
	v_fmac_f32_e32 v55, v5, v56
	s_cselect_b64 s[0:1], -1, 0
	v_fmac_f32_e32 v54, v4, v56
	v_fmac_f32_e32 v55, v4, v57
	v_cndmask_b32_e64 v54, v56, v54, s[0:1]
	v_cndmask_b32_e64 v55, v57, v55, s[0:1]
	s_cmp_gt_u32 s3, 6
	s_waitcnt vmcnt(24)
	v_fma_f32 v52, -v5, v55, v52
	v_fmac_f32_e32 v53, v5, v54
	s_cselect_b64 s[0:1], -1, 0
	v_fmac_f32_e32 v52, v4, v54
	v_fmac_f32_e32 v53, v4, v55
	v_cndmask_b32_e64 v52, v54, v52, s[0:1]
	v_cndmask_b32_e64 v53, v55, v53, s[0:1]
	s_cmp_gt_u32 s3, 7
	s_waitcnt vmcnt(23)
	v_fma_f32 v50, -v5, v53, v50
	v_fmac_f32_e32 v51, v5, v52
	s_cselect_b64 s[0:1], -1, 0
	v_fmac_f32_e32 v50, v4, v52
	v_fmac_f32_e32 v51, v4, v53
	v_cndmask_b32_e64 v50, v52, v50, s[0:1]
	v_cndmask_b32_e64 v51, v53, v51, s[0:1]
	s_cmp_gt_u32 s3, 8
	s_waitcnt vmcnt(22)
	v_fma_f32 v48, -v5, v51, v48
	v_fmac_f32_e32 v49, v5, v50
	s_cselect_b64 s[0:1], -1, 0
	v_fmac_f32_e32 v48, v4, v50
	v_fmac_f32_e32 v49, v4, v51
	v_cndmask_b32_e64 v48, v50, v48, s[0:1]
	v_cndmask_b32_e64 v49, v51, v49, s[0:1]
	s_cmp_gt_u32 s3, 9
	s_waitcnt vmcnt(21)
	v_fma_f32 v46, -v5, v49, v46
	v_fmac_f32_e32 v47, v5, v48
	s_cselect_b64 s[0:1], -1, 0
	v_fmac_f32_e32 v46, v4, v48
	v_fmac_f32_e32 v47, v4, v49
	v_cndmask_b32_e64 v46, v48, v46, s[0:1]
	v_cndmask_b32_e64 v47, v49, v47, s[0:1]
	s_cmp_gt_u32 s3, 10
	s_waitcnt vmcnt(20)
	v_fma_f32 v44, -v5, v47, v44
	v_fmac_f32_e32 v45, v5, v46
	s_cselect_b64 s[0:1], -1, 0
	v_fmac_f32_e32 v44, v4, v46
	v_fmac_f32_e32 v45, v4, v47
	v_cndmask_b32_e64 v44, v46, v44, s[0:1]
	v_cndmask_b32_e64 v45, v47, v45, s[0:1]
	s_cmp_gt_u32 s3, 11
	s_waitcnt vmcnt(19)
	v_fma_f32 v42, -v5, v45, v42
	v_fmac_f32_e32 v43, v5, v44
	s_cselect_b64 s[0:1], -1, 0
	v_fmac_f32_e32 v42, v4, v44
	v_fmac_f32_e32 v43, v4, v45
	v_cndmask_b32_e64 v42, v44, v42, s[0:1]
	v_cndmask_b32_e64 v43, v45, v43, s[0:1]
	s_cmp_gt_u32 s3, 12
	s_waitcnt vmcnt(18)
; template <class T> __device__ __forceinline__ void est(T* p, T v) { if constexpr (MK_EPI_NT != 0) __builtin_nontemporal_store(v, p); else *p = v; }
; template <int DIR> ...
;     ...
;     { const float* e = est + ((((size_t)(DIR * 2 + b) * 64 + g) * 32) * 64 + lane) * 2; f32x2 ev[32];
; #pragma unroll
;       for (int m = 0; m < 32; ++m) ev[m] = *(const f32x2*)(e + (size_t)m * 128);
; #pragma unroll
;       for (int mm = 0; mm < 32; ++mm) { const int m = DIR ? 31 - mm : mm; const bool use = DIR ? (m > n) : (m < n);
;           const float nsr = fmaf(tr, sr, fmaf(-ti, si, ev[m].x)), nsi = fmaf(tr, si, fmaf(ti, sr, ev[m].y)); sr = use ? nsr : sr; si = use ? nsi : si; } }
	v_fma_f32 v40, -v5, v43, v40
	v_fmac_f32_e32 v41, v5, v42
	s_cselect_b64 s[0:1], -1, 0
	v_fmac_f32_e32 v40, v4, v42
	v_fmac_f32_e32 v41, v4, v43
	v_cndmask_b32_e64 v40, v42, v40, s[0:1]
	v_cndmask_b32_e64 v41, v43, v41, s[0:1]
	s_cmp_gt_u32 s3, 13
	s_waitcnt vmcnt(17)
	v_fma_f32 v38, -v5, v41, v38
	v_fmac_f32_e32 v39, v5, v40
	s_cselect_b64 s[0:1], -1, 0
	v_fmac_f32_e32 v38, v4, v40
	v_fmac_f32_e32 v39, v4, v41
	v_cndmask_b32_e64 v38, v40, v38, s[0:1]
	v_cndmask_b32_e64 v39, v41, v39, s[0:1]
	s_cmp_gt_u32 s3, 14
	s_waitcnt vmcnt(16)
	v_fma_f32 v36, -v5, v39, v36
	v_fmac_f32_e32 v37, v5, v38
	s_cselect_b64 s[0:1], -1, 0
	v_fmac_f32_e32 v36, v4, v38
	v_fmac_f32_e32 v37, v4, v39
	v_cndmask_b32_e64 v36, v38, v36, s[0:1]
	v_cndmask_b32_e64 v37, v39, v37, s[0:1]
	s_cmp_gt_u32 s3, 15
	s_waitcnt vmcnt(15)
	v_fma_f32 v34, -v5, v37, v34
	v_fmac_f32_e32 v35, v5, v36
	s_cselect_b64 s[0:1], -1, 0
	v_fmac_f32_e32 v34, v4, v36
	v_fmac_f32_e32 v35, v4, v37
	v_cndmask_b32_e64 v34, v36, v34, s[0:1]
	v_cndmask_b32_e64 v35, v37, v35, s[0:1]
	s_cmp_gt_u32 s3, 16
	s_waitcnt vmcnt(14)
	v_fma_f32 v32, -v5, v35, v32
	v_fmac_f32_e32 v33, v5, v34
	s_cselect_b64 s[0:1], -1, 0
	v_fmac_f32_e32 v32, v4, v34
	v_fmac_f32_e32 v33, v4, v35
	v_cndmask_b32_e64 v32, v34, v32, s[0:1]
	v_cndmask_b32_e64 v33, v35, v33, s[0:1]
	s_cmp_gt_u32 s3, 17
	s_waitcnt vmcnt(13)
	v_fma_f32 v30, -v5, v33, v30
	v_fmac_f32_e32 v31, v5, v32
	s_cselect_b64 s[0:1], -1, 0
	v_fmac_f32_e32 v30, v4, v32
	v_fmac_f32_e32 v31, v4, v33
	v_cndmask_b32_e64 v30, v32, v30, s[0:1]
	v_cndmask_b32_e64 v31, v33, v31, s[0:1]
	s_cmp_gt_u32 s3, 18
	s_waitcnt vmcnt(12)
	v_fma_f32 v28, -v5, v31, v28
	v_fmac_f32_e32 v29, v5, v30
	s_cselect_b64 s[0:1], -1, 0
	v_fmac_f32_e32 v28, v4, v30
	v_fmac_f32_e32 v29, v4, v31
	v_cndmask_b32_e64 v28, v30, v28, s[0:1]
	v_cndmask_b32_e64 v29, v31, v29, s[0:1]
	s_cmp_gt_u32 s3, 19
	s_waitcnt vmcnt(11)
	v_fma_f32 v26, -v5, v29, v26
	v_fmac_f32_e32 v27, v5, v28
	s_cselect_b64 s[0:1], -1, 0
	v_fmac_f32_e32 v26, v4, v28
	v_fmac_f32_e32 v27, v4, v29
	v_cndmask_b32_e64 v26, v28, v26, s[0:1]
	v_cndmask_b32_e64 v27, v29, v27, s[0:1]
	s_cmp_gt_u32 s3, 20
	s_waitcnt vmcnt(10)
	v_fma_f32 v24, -v5, v27, v24
	v_fmac_f32_e32 v25, v5, v26
	s_cselect_b64 s[0:1], -1, 0
	v_fmac_f32_e32 v24, v4, v26
	v_fmac_f32_e32 v25, v4, v27
	v_cndmask_b32_e64 v24, v26, v24, s[0:1]
	v_cndmask_b32_e64 v25, v27, v25, s[0:1]
	s_cmp_gt_u32 s3, 21
	s_waitcnt vmcnt(9)
	v_fma_f32 v22, -v5, v25, v22
	v_fmac_f32_e32 v23, v5, v24
	s_cselect_b64 s[0:1], -1, 0
	v_fmac_f32_e32 v22, v4, v24
	v_fmac_f32_e32 v23, v4, v25
	v_cndmask_b32_e64 v22, v24, v22, s[0:1]
	v_cndmask_b32_e64 v23, v25, v23, s[0:1]
	s_cmp_gt_u32 s3, 22
	s_waitcnt vmcnt(8)
	v_fma_f32 v20, -v5, v23, v20
	v_fmac_f32_e32 v21, v5, v22
	s_cselect_b64 s[0:1], -1, 0
	v_fmac_f32_e32 v20, v4, v22
	v_fmac_f32_e32 v21, v4, v23
	v_cndmask_b32_e64 v20, v22, v20, s[0:1]
	v_cndmask_b32_e64 v21, v23, v21, s[0:1]
	s_cmp_gt_u32 s3, 23
	s_waitcnt vmcnt(7)
	v_fma_f32 v18, -v5, v21, v18
	v_fmac_f32_e32 v19, v5, v20
	s_cselect_b64 s[0:1], -1, 0
	v_fmac_f32_e32 v18, v4, v20
	v_fmac_f32_e32 v19, v4, v21
	v_cndmask_b32_e64 v18, v20, v18, s[0:1]
	v_cndmask_b32_e64 v19, v21, v19, s[0:1]
	s_cmp_gt_u32 s3, 24
	s_waitcnt vmcnt(6)
	v_fma_f32 v16, -v5, v19, v16
	v_fmac_f32_e32 v17, v5, v18
	s_cselect_b64 s[0:1], -1, 0
	v_fmac_f32_e32 v16, v4, v18
	v_fmac_f32_e32 v17, v4, v19
	v_cndmask_b32_e64 v16, v18, v16, s[0:1]
	v_cndmask_b32_e64 v17, v19, v17, s[0:1]
	s_cmp_gt_u32 s3, 25
	s_waitcnt vmcnt(5)
	v_fma_f32 v14, -v5, v17, v14
	v_fmac_f32_e32 v15, v5, v16
	s_cselect_b64 s[0:1], -1, 0
	v_fmac_f32_e32 v14, v4, v16
	v_fmac_f32_e32 v15, v4, v17
	v_cndmask_b32_e64 v14, v16, v14, s[0:1]
	v_cndmask_b32_e64 v15, v17, v15, s[0:1]
	s_cmp_gt_u32 s3, 26
	s_waitcnt vmcnt(4)
	v_fma_f32 v12, -v5, v15, v12
	v_fmac_f32_e32 v13, v5, v14
	s_cselect_b64 s[0:1], -1, 0
	v_fmac_f32_e32 v12, v4, v14
	v_fmac_f32_e32 v13, v4, v15
	v_cndmask_b32_e64 v12, v14, v12, s[0:1]
	v_cndmask_b32_e64 v13, v15, v13, s[0:1]
	s_cmp_gt_u32 s3, 27
	s_waitcnt vmcnt(3)
	v_fma_f32 v10, -v5, v13, v10
	v_fmac_f32_e32 v11, v5, v12
	s_cselect_b64 s[0:1], -1, 0
	v_fmac_f32_e32 v10, v4, v12
	v_fmac_f32_e32 v11, v4, v13
	v_cndmask_b32_e64 v10, v12, v10, s[0:1]
	v_cndmask_b32_e64 v11, v13, v11, s[0:1]
	s_cmp_gt_u32 s3, 28
	s_waitcnt vmcnt(2)
	v_fma_f32 v8, -v5, v11, v8
	v_fmac_f32_e32 v9, v5, v10
	s_cselect_b64 s[0:1], -1, 0
	v_fmac_f32_e32 v8, v4, v10
	v_fmac_f32_e32 v9, v4, v11
	v_cndmask_b32_e64 v8, v10, v8, s[0:1]
	v_cndmask_b32_e64 v9, v11, v9, s[0:1]
	s_cmp_gt_u32 s3, 29
	s_waitcnt vmcnt(1)
	v_fma_f32 v6, -v5, v9, v6
	v_fmac_f32_e32 v7, v5, v8
	s_cselect_b64 s[0:1], -1, 0
	v_fmac_f32_e32 v6, v4, v8
	v_fmac_f32_e32 v7, v4, v9
	s_cmp_eq_u32 s3, 31
	v_cndmask_b32_e64 v6, v8, v6, s[0:1]
	v_cndmask_b32_e64 v10, v9, v7, s[0:1]
	s_cselect_b64 s[0:1], -1, 0
	s_lshl_b32 s12, s59, 12
	s_waitcnt vmcnt(0)
; #define LAS __attribute__((address_space(3)))
; __device__ __forceinline__ unsigned cvt_pk_bf16(float lo, float hi) { unsigned r; asm volatile("v_cvt_pk_bf16_f32 %0, %1, %2" : "=v"(r) : "v"(lo), "v"(hi)); return r; }
; template <int DIR> ...
;     ...
;     const BuFrags f = load_bufrags(bbar_l + (size_t)dg * 2 * 64 * 16, lane);
;     bf16x8 cb[4];
; #pragma unroll
;     for (int ks = 0; ks < 4; ++ks) cb[ks] = *(const bf16x8*)(ctt_l + ((size_t)dg * 16 + (lane & 15)) * 128 + 32 * ks + 8 * (lane >> 4));
;     bf16x8 ua[4];
; #pragma unroll
;     for (int s = 0; s < 4; ++s) ua[s] = bu_load(proj, b * SEQ + n * 128 + (DIR ? 3 - s : s) * 32, g, lane);
; #pragma unroll
;     for (int s = 0; s < 4; ++s) { const int sb = DIR ? 3 - s : s; float BR[32], BI[32];
;         bu_block(ua[s], f, BR, BI);
; #pragma unroll
;         for (int tt = 0; tt < 32; ++tt) { const int t = DIR ? 31 - tt : tt; const float nsr = fmaf(ar, sr, fmaf(-ai, si, BR[t])), nsi = fmaf(ar, si, fmaf(ai, sr, BI[t])); sr = nsr; si = nsi;
;             *(LAS unsigned*)(sl + (t * 136 + 2 * lane) * 2) = cvt_pk_bf16(sr, si); }
	v_fma_f32 v2, -v5, v10, v2
	s_add_u32 s20, s82, s12
	v_fmac_f32_e32 v2, v4, v6
	s_addc_u32 s21, s83, 0
	v_fmac_f32_e32 v3, v5, v6
	v_cndmask_b32_e64 v66, v6, v2, s[0:1]
	v_lshl_add_u64 v[6:7], s[20:21], 0, v[158:159]
	v_lshl_add_u64 v[8:9], s[20:21], 0, v[162:163]
	v_lshl_add_u64 v[6:7], v[6:7], 0, v[160:161]
	v_lshl_add_u64 v[8:9], v[8:9], 0, v[160:161]
	global_load_dwordx4 v[122:125], v[6:7], off
	global_load_dwordx4 v[126:129], v[8:9], off
	global_load_dwordx4 v[130:133], v[6:7], off offset:2048
	v_lshl_add_u64 v[6:7], s[20:21], 0, v[164:165]
	v_lshl_add_u64 v[6:7], v[6:7], 0, v[160:161]
	global_load_dwordx4 v[134:137], v[6:7], off
	v_lshl_add_u64 v[6:7], v[156:157], 0, s[12:13]
	s_lshl_b32 s12, s16, 12
	s_lshl_b32 s16, s3, 7
	s_or_b32 s16, s16, s12
	v_or_b32_e32 v2, s16, v170
	v_fmac_f32_e32 v3, v4, v10
	v_mad_i64_i32 v[4:5], s[20:21], v2, s41, v[166:167]
	s_lshl_b32 s12, s59, 5
	v_lshl_add_u64 v[4:5], v[4:5], 0, s[12:13]
	v_lshl_add_u64 v[4:5], v[4:5], 0, v[160:161]
	global_load_dwordx4 v[118:121], v[6:7], off
	global_load_dwordx4 v[114:117], v[6:7], off offset:64
	global_load_dwordx4 v[110:113], v[6:7], off offset:128
	global_load_dwordx4 v[106:109], v[6:7], off offset:192
	v_or_b32_e32 v8, 32, v2
	global_load_dwordx4 v[4:7], v[4:5], off offset:3072
	v_mad_i64_i32 v[8:9], s[20:21], v8, s41, v[166:167]
	v_lshl_add_u64 v[8:9], v[8:9], 0, s[12:13]
	v_lshl_add_u64 v[8:9], v[8:9], 0, v[160:161]
	global_load_dwordx4 v[90:93], v[8:9], off offset:3072
	v_or_b32_e32 v8, 64, v2
	v_mad_i64_i32 v[8:9], s[20:21], v8, s41, v[166:167]
	v_lshl_add_u64 v[8:9], v[8:9], 0, s[12:13]
	v_lshl_add_u64 v[8:9], v[8:9], 0, v[160:161]
	v_or_b32_e32 v2, 0x60, v2
	global_load_dwordx4 v[98:101], v[8:9], off offset:3072
	v_mad_i64_i32 v[8:9], s[20:21], v2, s41, v[166:167]
	v_lshl_add_u64 v[8:9], v[8:9], 0, s[12:13]
	v_lshl_add_u64 v[8:9], v[8:9], 0, v[160:161]
	global_load_dwordx4 v[138:141], v[8:9], off offset:3072
	v_cndmask_b32_e64 v67, v10, v3, s[0:1]
	s_waitcnt vmcnt(3)
	v_mfma_f32_32x32x16_bf16 v[50:65], v[4:7], v[122:125], 0
	s_or_b32 s17, s59, 64
	s_add_u32 s4, s4, 0x40000
	s_addc_u32 s5, s5, 0
	s_cmp_lt_u32 s3, 30
	v_mfma_f32_32x32x16_bf16 v[18:33], v[4:7], v[126:129], 0
	v_mfma_f32_32x32x16_bf16 v[34:49], v[4:7], v[130:133], 0
	s_nop 10
	v_permlane32_swap_b32_e32 v50, v18
	v_fma_f32 v50, -v143, v67, v50
	v_permlane32_swap_b32_e32 v51, v19
	v_fmac_f32_e32 v50, v142, v66
	v_permlane32_swap_b32_e32 v52, v20
	v_mfma_f32_32x32x16_bf16 v[2:17], v[4:7], v[134:137], 0
	v_permlane32_swap_b32_e32 v53, v21
	v_permlane32_swap_b32_e32 v54, v22
	v_permlane32_swap_b32_e32 v55, v23
	v_permlane32_swap_b32_e32 v56, v24
	s_nop 7
	v_permlane32_swap_b32_e32 v34, v2
	v_fmac_f32_e32 v34, v143, v66
	v_permlane32_swap_b32_e32 v35, v3
	v_fmac_f32_e32 v34, v142, v67
	v_fma_f32 v51, -v143, v34, v51
	v_fmac_f32_e32 v35, v143, v50
	v_permlane32_swap_b32_e32 v36, v4
	v_cvt_pk_bf16_f32 v66, v50, v34
	ds_write_b32 v171, v66
	v_fmac_f32_e32 v51, v142, v50
	v_fmac_f32_e32 v35, v142, v34
	v_cvt_pk_bf16_f32 v34, v51, v35
	ds_write_b32 v171, v34 offset:272
	v_fma_f32 v34, -v143, v35, v52
	v_fmac_f32_e32 v36, v143, v51
	v_permlane32_swap_b32_e32 v37, v5
	v_fmac_f32_e32 v34, v142, v51
	v_fmac_f32_e32 v36, v142, v35
	v_cvt_pk_bf16_f32 v35, v34, v36
	ds_write_b32 v171, v35 offset:544
	v_fma_f32 v35, -v143, v36, v53
	v_fmac_f32_e32 v37, v143, v34
	v_fmac_f32_e32 v35, v142, v34
	v_fmac_f32_e32 v37, v142, v36
	v_fma_f32 v18, -v143, v37, v18
	v_fmac_f32_e32 v2, v143, v35
	v_fmac_f32_e32 v18, v142, v35
	v_fmac_f32_e32 v2, v142, v37
	v_cvt_pk_bf16_f32 v34, v35, v37
	v_fma_f32 v19, -v143, v2, v19
	v_fmac_f32_e32 v3, v143, v18
	ds_write_b32 v171, v34 offset:816
	v_cvt_pk_bf16_f32 v34, v18, v2
	ds_write_b32 v171, v34 offset:1088
	v_fmac_f32_e32 v19, v142, v18
	v_fmac_f32_e32 v3, v142, v2
	v_cvt_pk_bf16_f32 v2, v19, v3
	ds_write_b32 v171, v2 offset:1360
	v_fma_f32 v2, -v143, v3, v20
	v_fmac_f32_e32 v4, v143, v19
	v_fmac_f32_e32 v2, v142, v19
	v_fmac_f32_e32 v4, v142, v3
	v_cvt_pk_bf16_f32 v3, v2, v4
	ds_write_b32 v171, v3 offset:1632
	v_fma_f32 v3, -v143, v4, v21
	v_fmac_f32_e32 v5, v143, v2
	v_permlane32_swap_b32_e32 v38, v6
	v_fmac_f32_e32 v3, v142, v2
	v_fmac_f32_e32 v5, v142, v4
	v_cvt_pk_bf16_f32 v2, v3, v5
	ds_write_b32 v171, v2 offset:1904
	v_fma_f32 v2, -v143, v5, v54
	v_fmac_f32_e32 v38, v143, v3
	v_permlane32_swap_b32_e32 v39, v7
	v_fmac_f32_e32 v2, v142, v3
	v_fmac_f32_e32 v38, v142, v5
	v_cvt_pk_bf16_f32 v3, v2, v38
	ds_write_b32 v171, v3 offset:2176
	v_fma_f32 v3, -v143, v38, v55
	v_fmac_f32_e32 v39, v143, v2
	v_permlane32_swap_b32_e32 v40, v8
	v_fmac_f32_e32 v3, v142, v2
	v_fmac_f32_e32 v39, v142, v38
	v_cvt_pk_bf16_f32 v2, v3, v39
	ds_write_b32 v171, v2 offset:2448
	v_fma_f32 v2, -v143, v39, v56
	v_fmac_f32_e32 v40, v143, v3
	v_permlane32_swap_b32_e32 v57, v25
	v_permlane32_swap_b32_e32 v41, v9
	v_fmac_f32_e32 v2, v142, v3
	v_fmac_f32_e32 v40, v142, v39
	v_cvt_pk_bf16_f32 v3, v2, v40
	ds_write_b32 v171, v3 offset:2720
	v_fma_f32 v3, -v143, v40, v57
	v_fmac_f32_e32 v41, v143, v2
	v_fmac_f32_e32 v3, v142, v2
	v_fmac_f32_e32 v41, v142, v40
	v_cvt_pk_bf16_f32 v2, v3, v41
	ds_write_b32 v171, v2 offset:2992
	v_fma_f32 v2, -v143, v41, v22
	v_fmac_f32_e32 v6, v143, v3
	v_fmac_f32_e32 v2, v142, v3
	v_fmac_f32_e32 v6, v142, v41
	v_cvt_pk_bf16_f32 v3, v2, v6
	ds_write_b32 v171, v3 offset:3264
	v_fma_f32 v3, -v143, v6, v23
	v_fmac_f32_e32 v7, v143, v2
	v_fmac_f32_e32 v3, v142, v2
	v_fmac_f32_e32 v7, v142, v6
	v_cvt_pk_bf16_f32 v2, v3, v7
	ds_write_b32 v171, v2 offset:3536
	v_fma_f32 v2, -v143, v7, v24
	v_fmac_f32_e32 v8, v143, v3
	v_fmac_f32_e32 v2, v142, v3
	v_fmac_f32_e32 v8, v142, v7
; #define LAS __attribute__((address_space(3)))
; __device__ __forceinline__ unsigned cvt_pk_bf16(float lo, float hi) { unsigned r; asm volatile("v_cvt_pk_bf16_f32 %0, %1, %2" : "=v"(r) : "v"(lo), "v"(hi)); return r; }
; #define LDS_WAIT() asm volatile("s_waitcnt lgkmcnt(0)" ::: "memory")
; template <int DIR> ...
;     ...
;     for (int s = 0; s < 4; ++s) { const int sb = DIR ? 3 - s : s; float BR[32], BI[32];
;         bu_block(ua[s], f, BR, BI);
; #pragma unroll
;         for (int tt = 0; tt < 32; ++tt) { const int t = DIR ? 31 - tt : tt; const float nsr = fmaf(ar, sr, fmaf(-ai, si, BR[t])), nsi = fmaf(ar, si, fmaf(ai, sr, BI[t])); sr = nsr; si = nsi;
;             *(LAS unsigned*)(sl + (t * 136 + 2 * lane) * 2) = cvt_pk_bf16(sr, si); }
;         LDS_WAIT();
; #pragma unroll
;         for (int rb = 0; rb < 2; ++rb)
; #pragma unroll
;             for (int ks = 0; ks < 4; ++ks) { const bf16x8 a = *(const LAS bf16x8*)(sl + ((16 * rb + (lane & 15)) * 136 + 32 * ks + 8 * (lane >> 4)) * 2);
;                 yacc[2 * sb + rb] = __builtin_amdgcn_mfma_f32_16x16x32_bf16(a, cb[ks], yacc[2 * sb + rb], 0, 0, 0); }
;         LDS_WAIT(); }
	v_cvt_pk_bf16_f32 v3, v2, v8
	ds_write_b32 v171, v3 offset:3808
	v_fma_f32 v3, -v143, v8, v25
	v_fmac_f32_e32 v9, v143, v2
	v_permlane32_swap_b32_e32 v58, v26
	v_permlane32_swap_b32_e32 v42, v10
	v_fmac_f32_e32 v3, v142, v2
	v_fmac_f32_e32 v9, v142, v8
	v_cvt_pk_bf16_f32 v2, v3, v9
	ds_write_b32 v171, v2 offset:4080
	v_fma_f32 v2, -v143, v9, v58
	v_fmac_f32_e32 v42, v143, v3
	v_permlane32_swap_b32_e32 v59, v27
	v_permlane32_swap_b32_e32 v43, v11
	v_fmac_f32_e32 v2, v142, v3
	v_fmac_f32_e32 v42, v142, v9
	v_cvt_pk_bf16_f32 v3, v2, v42
	ds_write_b32 v171, v3 offset:4352
	v_fma_f32 v3, -v143, v42, v59
	v_fmac_f32_e32 v43, v143, v2
	v_permlane32_swap_b32_e32 v60, v28
	v_permlane32_swap_b32_e32 v44, v12
	v_fmac_f32_e32 v3, v142, v2
	v_fmac_f32_e32 v43, v142, v42
	v_cvt_pk_bf16_f32 v2, v3, v43
	ds_write_b32 v171, v2 offset:4624
	v_fma_f32 v2, -v143, v43, v60
	v_fmac_f32_e32 v44, v143, v3
	v_permlane32_swap_b32_e32 v61, v29
	v_permlane32_swap_b32_e32 v45, v13
	v_fmac_f32_e32 v2, v142, v3
	v_fmac_f32_e32 v44, v142, v43
	v_cvt_pk_bf16_f32 v3, v2, v44
	ds_write_b32 v171, v3 offset:4896
	v_fma_f32 v3, -v143, v44, v61
	v_fmac_f32_e32 v45, v143, v2
	v_fmac_f32_e32 v3, v142, v2
	v_fmac_f32_e32 v45, v142, v44
	v_cvt_pk_bf16_f32 v2, v3, v45
	ds_write_b32 v171, v2 offset:5168
	v_fma_f32 v2, -v143, v45, v26
	v_fmac_f32_e32 v10, v143, v3
	v_fmac_f32_e32 v2, v142, v3
	v_fmac_f32_e32 v10, v142, v45
	v_cvt_pk_bf16_f32 v3, v2, v10
	ds_write_b32 v171, v3 offset:5440
	v_fma_f32 v3, -v143, v10, v27
	v_fmac_f32_e32 v11, v143, v2
	v_fmac_f32_e32 v3, v142, v2
	v_fmac_f32_e32 v11, v142, v10
	v_cvt_pk_bf16_f32 v2, v3, v11
	ds_write_b32 v171, v2 offset:5712
	v_fma_f32 v2, -v143, v11, v28
	v_fmac_f32_e32 v12, v143, v3
	v_fmac_f32_e32 v2, v142, v3
	v_fmac_f32_e32 v12, v142, v11
	v_cvt_pk_bf16_f32 v3, v2, v12
	ds_write_b32 v171, v3 offset:5984
	v_fma_f32 v3, -v143, v12, v29
	v_fmac_f32_e32 v13, v143, v2
	v_permlane32_swap_b32_e32 v62, v30
	v_permlane32_swap_b32_e32 v46, v14
	v_fmac_f32_e32 v3, v142, v2
	v_fmac_f32_e32 v13, v142, v12
	v_cvt_pk_bf16_f32 v2, v3, v13
	ds_write_b32 v171, v2 offset:6256
	v_fma_f32 v2, -v143, v13, v62
	v_fmac_f32_e32 v46, v143, v3
	v_permlane32_swap_b32_e32 v63, v31
	v_permlane32_swap_b32_e32 v47, v15
	v_fmac_f32_e32 v2, v142, v3
	v_fmac_f32_e32 v46, v142, v13
	v_cvt_pk_bf16_f32 v3, v2, v46
	ds_write_b32 v171, v3 offset:6528
	v_fma_f32 v3, -v143, v46, v63
	v_fmac_f32_e32 v47, v143, v2
	v_permlane32_swap_b32_e32 v64, v32
	v_permlane32_swap_b32_e32 v48, v16
	v_fmac_f32_e32 v3, v142, v2
	v_fmac_f32_e32 v47, v142, v46
	v_cvt_pk_bf16_f32 v2, v3, v47
	ds_write_b32 v171, v2 offset:6800
	v_fma_f32 v2, -v143, v47, v64
	v_fmac_f32_e32 v48, v143, v3
	v_permlane32_swap_b32_e32 v65, v33
	v_permlane32_swap_b32_e32 v49, v17
	v_fmac_f32_e32 v2, v142, v3
	v_fmac_f32_e32 v48, v142, v47
	v_cvt_pk_bf16_f32 v3, v2, v48
	ds_write_b32 v171, v3 offset:7072
	v_fma_f32 v3, -v143, v48, v65
	v_fmac_f32_e32 v49, v143, v2
	v_fmac_f32_e32 v3, v142, v2
	v_fmac_f32_e32 v49, v142, v48
	v_cvt_pk_bf16_f32 v2, v3, v49
	ds_write_b32 v171, v2 offset:7344
	v_fma_f32 v2, -v143, v49, v30
	v_fmac_f32_e32 v14, v143, v3
	v_fmac_f32_e32 v2, v142, v3
	v_fmac_f32_e32 v14, v142, v49
	v_cvt_pk_bf16_f32 v3, v2, v14
	ds_write_b32 v171, v3 offset:7616
	v_fma_f32 v3, -v143, v14, v31
	v_fmac_f32_e32 v15, v143, v2
	v_fmac_f32_e32 v3, v142, v2
	v_fmac_f32_e32 v15, v142, v14
	v_cvt_pk_bf16_f32 v2, v3, v15
	ds_write_b32 v171, v2 offset:7888
	v_fma_f32 v2, -v143, v15, v32
	v_fmac_f32_e32 v16, v143, v3
	v_fmac_f32_e32 v2, v142, v3
	v_fmac_f32_e32 v16, v142, v15
	v_fma_f32 v10, -v143, v16, v33
	v_fmac_f32_e32 v17, v143, v2
	v_cvt_pk_bf16_f32 v3, v2, v16
	ds_write_b32 v171, v3 offset:8160
	v_fmac_f32_e32 v10, v142, v2
	v_fmac_f32_e32 v17, v142, v16
	v_cvt_pk_bf16_f32 v2, v10, v17
	ds_write_b32 v171, v2 offset:8432
	s_waitcnt lgkmcnt(0)
	ds_read_b128 v[2:5], v175
	ds_read_b128 v[6:9], v175 offset:64
	s_waitcnt lgkmcnt(1)
	v_mfma_f32_16x16x32_bf16 v[2:5], v[2:5], v[118:121], 0
	s_waitcnt lgkmcnt(0)
	v_mfma_f32_16x16x32_bf16 v[2:5], v[6:9], v[114:117], v[2:5]
	ds_read_b128 v[6:9], v175 offset:128
	s_waitcnt lgkmcnt(0)
	v_mfma_f32_16x16x32_bf16 v[2:5], v[6:9], v[110:113], v[2:5]
	ds_read_b128 v[6:9], v175 offset:192
	s_waitcnt lgkmcnt(0)
	v_mfma_f32_16x16x32_bf16 v[86:89], v[6:9], v[106:109], v[2:5]
	s_nop 4
	ds_read_b128 v[2:5], v175 offset:4352
	ds_read_b128 v[6:9], v175 offset:4416
	s_waitcnt lgkmcnt(1)
	v_mfma_f32_16x16x32_bf16 v[2:5], v[2:5], v[118:121], 0
	s_waitcnt lgkmcnt(0)
	v_mfma_f32_16x16x32_bf16 v[2:5], v[6:9], v[114:117], v[2:5]
	ds_read_b128 v[6:9], v175 offset:4480
	s_waitcnt lgkmcnt(0)
	v_mfma_f32_16x16x32_bf16 v[2:5], v[6:9], v[110:113], v[2:5]
	ds_read_b128 v[6:9], v175 offset:4544
	s_waitcnt lgkmcnt(0)
	s_waitcnt vmcnt(2)
	v_mfma_f32_32x32x16_bf16 v[66:81], v[90:93], v[122:125], 0
	v_mfma_f32_32x32x16_bf16 v[34:49], v[90:93], v[126:129], 0
	v_mfma_f32_32x32x16_bf16 v[50:65], v[90:93], v[130:133], 0
	s_nop 10
	v_permlane32_swap_b32_e32 v66, v34
	v_permlane32_swap_b32_e32 v67, v35
	v_permlane32_swap_b32_e32 v68, v36
	v_permlane32_swap_b32_e32 v69, v37
	v_mfma_f32_32x32x16_bf16 v[18:33], v[90:93], v[134:137], 0
	v_permlane32_swap_b32_e32 v70, v38
	v_permlane32_swap_b32_e32 v71, v39
	v_permlane32_swap_b32_e32 v72, v40
	v_permlane32_swap_b32_e32 v73, v41
	s_nop 7
	v_permlane32_swap_b32_e32 v50, v18
	s_waitcnt lgkmcnt(0)
; #define LAS __attribute__((address_space(3)))
; __device__ __forceinline__ unsigned cvt_pk_bf16(float lo, float hi) { unsigned r; asm volatile("v_cvt_pk_bf16_f32 %0, %1, %2" : "=v"(r) : "v"(lo), "v"(hi)); return r; }
; #define LDS_WAIT() asm volatile("s_waitcnt lgkmcnt(0)" ::: "memory")
; template <int DIR> ...
;     ...
;     for (int s = 0; s < 4; ++s) { const int sb = DIR ? 3 - s : s; float BR[32], BI[32];
;         bu_block(ua[s], f, BR, BI);
; #pragma unroll
;         for (int tt = 0; tt < 32; ++tt) { const int t = DIR ? 31 - tt : tt; const float nsr = fmaf(ar, sr, fmaf(-ai, si, BR[t])), nsi = fmaf(ar, si, fmaf(ai, sr, BI[t])); sr = nsr; si = nsi;
;             *(LAS unsigned*)(sl + (t * 136 + 2 * lane) * 2) = cvt_pk_bf16(sr, si); }
;         LDS_WAIT();
; #pragma unroll
;         for (int rb = 0; rb < 2; ++rb)
; #pragma unroll
;             for (int ks = 0; ks < 4; ++ks) { const bf16x8 a = *(const LAS bf16x8*)(sl + ((16 * rb + (lane & 15)) * 136 + 32 * ks + 8 * (lane >> 4)) * 2);
;                 yacc[2 * sb + rb] = __builtin_amdgcn_mfma_f32_16x16x32_bf16(a, cb[ks], yacc[2 * sb + rb], 0, 0, 0); }
;         LDS_WAIT(); }
	v_mfma_f32_16x16x32_bf16 v[82:85], v[6:9], v[106:109], v[2:5]
	v_fmac_f32_e32 v50, v143, v10
	v_permlane32_swap_b32_e32 v51, v19
	s_nop 0
	v_fma_f32 v2, -v143, v17, v66
	v_fmac_f32_e32 v2, v142, v10
	v_fmac_f32_e32 v50, v142, v17
	v_cvt_pk_bf16_f32 v3, v2, v50
	ds_write_b32 v171, v3
	v_fma_f32 v3, -v143, v50, v67
	v_fmac_f32_e32 v51, v143, v2
	v_permlane32_swap_b32_e32 v52, v20
	v_fmac_f32_e32 v3, v142, v2
	v_fmac_f32_e32 v51, v142, v50
	v_cvt_pk_bf16_f32 v2, v3, v51
	ds_write_b32 v171, v2 offset:272
	v_fma_f32 v2, -v143, v51, v68
	v_fmac_f32_e32 v52, v143, v3
	v_permlane32_swap_b32_e32 v53, v21
	v_fmac_f32_e32 v2, v142, v3
	v_fmac_f32_e32 v52, v142, v51
	v_cvt_pk_bf16_f32 v3, v2, v52
	ds_write_b32 v171, v3 offset:544
	v_fma_f32 v3, -v143, v52, v69
	v_fmac_f32_e32 v53, v143, v2
	v_fmac_f32_e32 v3, v142, v2
	v_fmac_f32_e32 v53, v142, v52
	v_cvt_pk_bf16_f32 v2, v3, v53
	ds_write_b32 v171, v2 offset:816
	v_fma_f32 v2, -v143, v53, v34
	v_fmac_f32_e32 v18, v143, v3
	v_fmac_f32_e32 v2, v142, v3
	v_fmac_f32_e32 v18, v142, v53
	v_cvt_pk_bf16_f32 v3, v2, v18
	ds_write_b32 v171, v3 offset:1088
	v_fma_f32 v3, -v143, v18, v35
	v_fmac_f32_e32 v19, v143, v2
	v_fmac_f32_e32 v3, v142, v2
	v_fmac_f32_e32 v19, v142, v18
	v_cvt_pk_bf16_f32 v2, v3, v19
	ds_write_b32 v171, v2 offset:1360
	v_fma_f32 v2, -v143, v19, v36
	v_fmac_f32_e32 v20, v143, v3
	v_fmac_f32_e32 v2, v142, v3
	v_fmac_f32_e32 v20, v142, v19
	v_cvt_pk_bf16_f32 v3, v2, v20
	ds_write_b32 v171, v3 offset:1632
	v_fma_f32 v3, -v143, v20, v37
	v_fmac_f32_e32 v21, v143, v2
	v_permlane32_swap_b32_e32 v54, v22
	v_fmac_f32_e32 v3, v142, v2
	v_fmac_f32_e32 v21, v142, v20
	v_cvt_pk_bf16_f32 v2, v3, v21
	ds_write_b32 v171, v2 offset:1904
	v_fma_f32 v2, -v143, v21, v70
	v_fmac_f32_e32 v54, v143, v3
	v_permlane32_swap_b32_e32 v55, v23
	v_fmac_f32_e32 v2, v142, v3
	v_fmac_f32_e32 v54, v142, v21
	v_cvt_pk_bf16_f32 v3, v2, v54
	ds_write_b32 v171, v3 offset:2176
	v_fma_f32 v3, -v143, v54, v71
	v_fmac_f32_e32 v55, v143, v2
	v_permlane32_swap_b32_e32 v56, v24
	v_fmac_f32_e32 v3, v142, v2
	v_fmac_f32_e32 v55, v142, v54
	v_cvt_pk_bf16_f32 v2, v3, v55
	ds_write_b32 v171, v2 offset:2448
	v_fma_f32 v2, -v143, v55, v72
	v_fmac_f32_e32 v56, v143, v3
	v_permlane32_swap_b32_e32 v57, v25
	v_fmac_f32_e32 v2, v142, v3
	v_fmac_f32_e32 v56, v142, v55
	v_cvt_pk_bf16_f32 v3, v2, v56
	ds_write_b32 v171, v3 offset:2720
	v_fma_f32 v3, -v143, v56, v73
	v_fmac_f32_e32 v57, v143, v2
	v_fmac_f32_e32 v3, v142, v2
	v_fmac_f32_e32 v57, v142, v56
	v_cvt_pk_bf16_f32 v2, v3, v57
	ds_write_b32 v171, v2 offset:2992
	v_fma_f32 v2, -v143, v57, v38
	v_fmac_f32_e32 v22, v143, v3
	v_fmac_f32_e32 v2, v142, v3
	v_fmac_f32_e32 v22, v142, v57
	v_cvt_pk_bf16_f32 v3, v2, v22
	ds_write_b32 v171, v3 offset:3264
	v_fma_f32 v3, -v143, v22, v39
	v_fmac_f32_e32 v23, v143, v2
	v_fmac_f32_e32 v3, v142, v2
	v_fmac_f32_e32 v23, v142, v22
	v_cvt_pk_bf16_f32 v2, v3, v23
	ds_write_b32 v171, v2 offset:3536
	v_fma_f32 v2, -v143, v23, v40
	v_fmac_f32_e32 v24, v143, v3
	v_fmac_f32_e32 v2, v142, v3
	v_fmac_f32_e32 v24, v142, v23
	v_cvt_pk_bf16_f32 v3, v2, v24
	ds_write_b32 v171, v3 offset:3808
	v_fma_f32 v3, -v143, v24, v41
	v_fmac_f32_e32 v25, v143, v2
	v_permlane32_swap_b32_e32 v74, v42
	v_permlane32_swap_b32_e32 v58, v26
	v_fmac_f32_e32 v3, v142, v2
	v_fmac_f32_e32 v25, v142, v24
	v_cvt_pk_bf16_f32 v2, v3, v25
	ds_write_b32 v171, v2 offset:4080
	v_fma_f32 v2, -v143, v25, v74
	v_fmac_f32_e32 v58, v143, v3
	v_permlane32_swap_b32_e32 v75, v43
	v_permlane32_swap_b32_e32 v59, v27
	v_fmac_f32_e32 v2, v142, v3
	v_fmac_f32_e32 v58, v142, v25
	v_cvt_pk_bf16_f32 v3, v2, v58
	ds_write_b32 v171, v3 offset:4352
	v_fma_f32 v3, -v143, v58, v75
	v_fmac_f32_e32 v59, v143, v2
	v_permlane32_swap_b32_e32 v76, v44
	v_permlane32_swap_b32_e32 v60, v28
	v_fmac_f32_e32 v3, v142, v2
	v_fmac_f32_e32 v59, v142, v58
	v_cvt_pk_bf16_f32 v2, v3, v59
	ds_write_b32 v171, v2 offset:4624
	v_fma_f32 v2, -v143, v59, v76
	v_fmac_f32_e32 v60, v143, v3
	v_permlane32_swap_b32_e32 v77, v45
	v_permlane32_swap_b32_e32 v61, v29
	v_fmac_f32_e32 v2, v142, v3
	v_fmac_f32_e32 v60, v142, v59
	v_cvt_pk_bf16_f32 v3, v2, v60
	ds_write_b32 v171, v3 offset:4896
	v_fma_f32 v3, -v143, v60, v77
	v_fmac_f32_e32 v61, v143, v2
	v_fmac_f32_e32 v3, v142, v2
	v_fmac_f32_e32 v61, v142, v60
	v_cvt_pk_bf16_f32 v2, v3, v61
	ds_write_b32 v171, v2 offset:5168
	v_fma_f32 v2, -v143, v61, v42
	v_fmac_f32_e32 v26, v143, v3
	v_fmac_f32_e32 v2, v142, v3
	v_fmac_f32_e32 v26, v142, v61
	v_cvt_pk_bf16_f32 v3, v2, v26
	ds_write_b32 v171, v3 offset:5440
	v_fma_f32 v3, -v143, v26, v43
	v_fmac_f32_e32 v27, v143, v2
	v_fmac_f32_e32 v3, v142, v2
	v_fmac_f32_e32 v27, v142, v26
	v_cvt_pk_bf16_f32 v2, v3, v27
	ds_write_b32 v171, v2 offset:5712
	v_fma_f32 v2, -v143, v27, v44
	v_fmac_f32_e32 v28, v143, v3
	v_fmac_f32_e32 v2, v142, v3
	v_fmac_f32_e32 v28, v142, v27
	v_cvt_pk_bf16_f32 v3, v2, v28
	ds_write_b32 v171, v3 offset:5984
	v_fma_f32 v3, -v143, v28, v45
	v_fmac_f32_e32 v29, v143, v2
	v_permlane32_swap_b32_e32 v78, v46
	v_permlane32_swap_b32_e32 v62, v30
	v_fmac_f32_e32 v3, v142, v2
	v_fmac_f32_e32 v29, v142, v28
	v_cvt_pk_bf16_f32 v2, v3, v29
	ds_write_b32 v171, v2 offset:6256
	v_fma_f32 v2, -v143, v29, v78
	v_fmac_f32_e32 v62, v143, v3
	v_permlane32_swap_b32_e32 v79, v47
	v_permlane32_swap_b32_e32 v63, v31
	v_fmac_f32_e32 v2, v142, v3
	v_fmac_f32_e32 v62, v142, v29
	v_cvt_pk_bf16_f32 v3, v2, v62
	ds_write_b32 v171, v3 offset:6528
	v_fma_f32 v3, -v143, v62, v79
	v_fmac_f32_e32 v63, v143, v2
	v_permlane32_swap_b32_e32 v80, v48
	v_permlane32_swap_b32_e32 v64, v32
	v_fmac_f32_e32 v3, v142, v2
	v_fmac_f32_e32 v63, v142, v62
	v_cvt_pk_bf16_f32 v2, v3, v63
	ds_write_b32 v171, v2 offset:6800
	v_fma_f32 v2, -v143, v63, v80
	v_fmac_f32_e32 v64, v143, v3
	v_permlane32_swap_b32_e32 v81, v49
	v_permlane32_swap_b32_e32 v65, v33
	v_fmac_f32_e32 v2, v142, v3
	v_fmac_f32_e32 v64, v142, v63
	v_cvt_pk_bf16_f32 v3, v2, v64
	ds_write_b32 v171, v3 offset:7072
	v_fma_f32 v3, -v143, v64, v81
	v_fmac_f32_e32 v65, v143, v2
	v_fmac_f32_e32 v3, v142, v2
	v_fmac_f32_e32 v65, v142, v64
	v_cvt_pk_bf16_f32 v2, v3, v65
	ds_write_b32 v171, v2 offset:7344
	v_fma_f32 v2, -v143, v65, v46
	v_fmac_f32_e32 v30, v143, v3
	v_fmac_f32_e32 v2, v142, v3
	v_fmac_f32_e32 v30, v142, v65
	v_cvt_pk_bf16_f32 v3, v2, v30
	ds_write_b32 v171, v3 offset:7616
	v_fma_f32 v3, -v143, v30, v47
	v_fmac_f32_e32 v31, v143, v2
	v_fmac_f32_e32 v3, v142, v2
	v_fmac_f32_e32 v31, v142, v30
	v_cvt_pk_bf16_f32 v2, v3, v31
	ds_write_b32 v171, v2 offset:7888
	v_fma_f32 v2, -v143, v31, v48
	v_fmac_f32_e32 v32, v143, v3
	v_fmac_f32_e32 v2, v142, v3
	v_fmac_f32_e32 v32, v142, v31
	v_fma_f32 v18, -v143, v32, v49
	v_fmac_f32_e32 v33, v143, v2
	v_cvt_pk_bf16_f32 v3, v2, v32
	ds_write_b32 v171, v3 offset:8160
	v_fmac_f32_e32 v18, v142, v2
	v_fmac_f32_e32 v33, v142, v32
	v_cvt_pk_bf16_f32 v2, v18, v33
	ds_write_b32 v171, v2 offset:8432
	s_waitcnt lgkmcnt(0)
; #define LAS __attribute__((address_space(3)))
; __device__ __forceinline__ unsigned cvt_pk_bf16(float lo, float hi) { unsigned r; asm volatile("v_cvt_pk_bf16_f32 %0, %1, %2" : "=v"(r) : "v"(lo), "v"(hi)); return r; }
; #define LDS_WAIT() asm volatile("s_waitcnt lgkmcnt(0)" ::: "memory")
; template <int DIR> ...
;     ...
;     for (int s = 0; s < 4; ++s) { const int sb = DIR ? 3 - s : s; float BR[32], BI[32];
;         bu_block(ua[s], f, BR, BI);
; #pragma unroll
;         for (int tt = 0; tt < 32; ++tt) { const int t = DIR ? 31 - tt : tt; const float nsr = fmaf(ar, sr, fmaf(-ai, si, BR[t])), nsi = fmaf(ar, si, fmaf(ai, sr, BI[t])); sr = nsr; si = nsi;
;             *(LAS unsigned*)(sl + (t * 136 + 2 * lane) * 2) = cvt_pk_bf16(sr, si); }
;         LDS_WAIT();
; #pragma unroll
;         for (int rb = 0; rb < 2; ++rb)
; #pragma unroll
;             for (int ks = 0; ks < 4; ++ks) { const bf16x8 a = *(const LAS bf16x8*)(sl + ((16 * rb + (lane & 15)) * 136 + 32 * ks + 8 * (lane >> 4)) * 2);
;                 yacc[2 * sb + rb] = __builtin_amdgcn_mfma_f32_16x16x32_bf16(a, cb[ks], yacc[2 * sb + rb], 0, 0, 0); }
;         LDS_WAIT(); }
	ds_read_b128 v[2:5], v175
	ds_read_b128 v[6:9], v175 offset:64
	s_waitcnt lgkmcnt(1)
	v_mfma_f32_16x16x32_bf16 v[2:5], v[2:5], v[118:121], 0
	s_waitcnt lgkmcnt(0)
	v_mfma_f32_16x16x32_bf16 v[2:5], v[6:9], v[114:117], v[2:5]
	ds_read_b128 v[6:9], v175 offset:128
	s_waitcnt lgkmcnt(0)
	v_mfma_f32_16x16x32_bf16 v[2:5], v[6:9], v[110:113], v[2:5]
	ds_read_b128 v[6:9], v175 offset:192
	s_waitcnt lgkmcnt(0)
	v_mfma_f32_16x16x32_bf16 v[90:93], v[6:9], v[106:109], v[2:5]
	s_nop 4
	ds_read_b128 v[2:5], v175 offset:4352
	ds_read_b128 v[6:9], v175 offset:4416
	s_waitcnt lgkmcnt(1)
	v_mfma_f32_16x16x32_bf16 v[2:5], v[2:5], v[118:121], 0
	s_waitcnt lgkmcnt(0)
	v_mfma_f32_16x16x32_bf16 v[2:5], v[6:9], v[114:117], v[2:5]
	ds_read_b128 v[6:9], v175 offset:4480
	s_waitcnt lgkmcnt(0)
	v_mfma_f32_16x16x32_bf16 v[2:5], v[6:9], v[110:113], v[2:5]
	ds_read_b128 v[6:9], v175 offset:4544
	s_waitcnt lgkmcnt(0)
	s_waitcnt lgkmcnt(0)
	v_mfma_f32_16x16x32_bf16 v[94:97], v[6:9], v[106:109], v[2:5]
	s_waitcnt vmcnt(1)
	v_mfma_f32_32x32x16_bf16 v[66:81], v[98:101], v[122:125], 0
	v_mfma_f32_32x32x16_bf16 v[34:49], v[98:101], v[126:129], 0
	v_mfma_f32_32x32x16_bf16 v[50:65], v[98:101], v[130:133], 0
	s_nop 10
	v_permlane32_swap_b32_e32 v66, v34
	v_fma_f32 v19, -v143, v33, v66
	v_permlane32_swap_b32_e32 v67, v35
	v_fmac_f32_e32 v19, v142, v18
	v_permlane32_swap_b32_e32 v68, v36
	v_mfma_f32_32x32x16_bf16 v[2:17], v[98:101], v[134:137], 0
	v_permlane32_swap_b32_e32 v69, v37
	v_permlane32_swap_b32_e32 v70, v38
	v_permlane32_swap_b32_e32 v71, v39
	v_permlane32_swap_b32_e32 v72, v40
	s_nop 7
	v_permlane32_swap_b32_e32 v50, v2
	v_fmac_f32_e32 v50, v143, v18
	v_permlane32_swap_b32_e32 v51, v3
	v_fmac_f32_e32 v50, v142, v33
	v_cvt_pk_bf16_f32 v18, v19, v50
	ds_write_b32 v171, v18
	v_fma_f32 v18, -v143, v50, v67
	v_fmac_f32_e32 v51, v143, v19
	v_permlane32_swap_b32_e32 v52, v4
	v_fmac_f32_e32 v18, v142, v19
	v_fmac_f32_e32 v51, v142, v50
	v_cvt_pk_bf16_f32 v19, v18, v51
	ds_write_b32 v171, v19 offset:272
	v_fma_f32 v19, -v143, v51, v68
	v_fmac_f32_e32 v52, v143, v18
	v_permlane32_swap_b32_e32 v53, v5
	v_fmac_f32_e32 v19, v142, v18
	v_fmac_f32_e32 v52, v142, v51
	v_cvt_pk_bf16_f32 v18, v19, v52
	ds_write_b32 v171, v18 offset:544
	v_fma_f32 v18, -v143, v52, v69
	v_fmac_f32_e32 v53, v143, v19
	v_fmac_f32_e32 v18, v142, v19
	v_fmac_f32_e32 v53, v142, v52
	v_cvt_pk_bf16_f32 v19, v18, v53
	ds_write_b32 v171, v19 offset:816
	v_fma_f32 v19, -v143, v53, v34
	v_fmac_f32_e32 v2, v143, v18
	v_fmac_f32_e32 v19, v142, v18
	v_fmac_f32_e32 v2, v142, v53
	v_cvt_pk_bf16_f32 v18, v19, v2
	ds_write_b32 v171, v18 offset:1088
	v_fma_f32 v18, -v143, v2, v35
	v_fmac_f32_e32 v3, v143, v19
	v_fmac_f32_e32 v18, v142, v19
	v_fmac_f32_e32 v3, v142, v2
	v_cvt_pk_bf16_f32 v2, v18, v3
	ds_write_b32 v171, v2 offset:1360
	v_fma_f32 v2, -v143, v3, v36
	v_fmac_f32_e32 v4, v143, v18
	v_fmac_f32_e32 v2, v142, v18
	v_fmac_f32_e32 v4, v142, v3
	v_cvt_pk_bf16_f32 v3, v2, v4
	ds_write_b32 v171, v3 offset:1632
	v_fma_f32 v3, -v143, v4, v37
	v_fmac_f32_e32 v5, v143, v2
	v_permlane32_swap_b32_e32 v54, v6
	v_fmac_f32_e32 v3, v142, v2
	v_fmac_f32_e32 v5, v142, v4
	v_cvt_pk_bf16_f32 v2, v3, v5
	ds_write_b32 v171, v2 offset:1904
	v_fma_f32 v2, -v143, v5, v70
	v_fmac_f32_e32 v54, v143, v3
	v_permlane32_swap_b32_e32 v55, v7
	v_fmac_f32_e32 v2, v142, v3
	v_fmac_f32_e32 v54, v142, v5
	v_cvt_pk_bf16_f32 v3, v2, v54
	ds_write_b32 v171, v3 offset:2176
	v_fma_f32 v3, -v143, v54, v71
	v_fmac_f32_e32 v55, v143, v2
	v_permlane32_swap_b32_e32 v56, v8
	v_fmac_f32_e32 v3, v142, v2
	v_fmac_f32_e32 v55, v142, v54
	v_cvt_pk_bf16_f32 v2, v3, v55
	ds_write_b32 v171, v2 offset:2448
	v_fma_f32 v2, -v143, v55, v72
	v_fmac_f32_e32 v56, v143, v3
	v_permlane32_swap_b32_e32 v73, v41
	v_permlane32_swap_b32_e32 v57, v9
	v_fmac_f32_e32 v2, v142, v3
	v_fmac_f32_e32 v56, v142, v55
	v_cvt_pk_bf16_f32 v3, v2, v56
	ds_write_b32 v171, v3 offset:2720
	v_fma_f32 v3, -v143, v56, v73
	v_fmac_f32_e32 v57, v143, v2
	v_fmac_f32_e32 v3, v142, v2
	v_fmac_f32_e32 v57, v142, v56
	v_cvt_pk_bf16_f32 v2, v3, v57
	ds_write_b32 v171, v2 offset:2992
	v_fma_f32 v2, -v143, v57, v38
	v_fmac_f32_e32 v6, v143, v3
	v_fmac_f32_e32 v2, v142, v3
	v_fmac_f32_e32 v6, v142, v57
	v_cvt_pk_bf16_f32 v3, v2, v6
	ds_write_b32 v171, v3 offset:3264
	v_fma_f32 v3, -v143, v6, v39
	v_fmac_f32_e32 v7, v143, v2
	v_fmac_f32_e32 v3, v142, v2
	v_fmac_f32_e32 v7, v142, v6
	v_cvt_pk_bf16_f32 v2, v3, v7
	ds_write_b32 v171, v2 offset:3536
	v_fma_f32 v2, -v143, v7, v40
	v_fmac_f32_e32 v8, v143, v3
	v_fmac_f32_e32 v2, v142, v3
	v_fmac_f32_e32 v8, v142, v7
	v_cvt_pk_bf16_f32 v3, v2, v8
	ds_write_b32 v171, v3 offset:3808
	v_fma_f32 v3, -v143, v8, v41
	v_fmac_f32_e32 v9, v143, v2
	v_permlane32_swap_b32_e32 v74, v42
	v_permlane32_swap_b32_e32 v58, v10
	v_fmac_f32_e32 v3, v142, v2
	v_fmac_f32_e32 v9, v142, v8
	v_cvt_pk_bf16_f32 v2, v3, v9
	ds_write_b32 v171, v2 offset:4080
	v_fma_f32 v2, -v143, v9, v74
	v_fmac_f32_e32 v58, v143, v3
	v_permlane32_swap_b32_e32 v75, v43
	v_permlane32_swap_b32_e32 v59, v11
	v_fmac_f32_e32 v2, v142, v3
	v_fmac_f32_e32 v58, v142, v9
	v_cvt_pk_bf16_f32 v3, v2, v58
	ds_write_b32 v171, v3 offset:4352
	v_fma_f32 v3, -v143, v58, v75
	v_fmac_f32_e32 v59, v143, v2
	v_permlane32_swap_b32_e32 v76, v44
	v_permlane32_swap_b32_e32 v60, v12
	v_fmac_f32_e32 v3, v142, v2
	v_fmac_f32_e32 v59, v142, v58
	v_cvt_pk_bf16_f32 v2, v3, v59
	ds_write_b32 v171, v2 offset:4624
	v_fma_f32 v2, -v143, v59, v76
	v_fmac_f32_e32 v60, v143, v3
	v_permlane32_swap_b32_e32 v77, v45
	v_permlane32_swap_b32_e32 v61, v13
	v_fmac_f32_e32 v2, v142, v3
	v_fmac_f32_e32 v60, v142, v59
	v_cvt_pk_bf16_f32 v3, v2, v60
; #define LAS __attribute__((address_space(3)))
; __device__ __forceinline__ unsigned cvt_pk_bf16(float lo, float hi) { unsigned r; asm volatile("v_cvt_pk_bf16_f32 %0, %1, %2" : "=v"(r) : "v"(lo), "v"(hi)); return r; }
; #define LDS_WAIT() asm volatile("s_waitcnt lgkmcnt(0)" ::: "memory")
; template <int DIR> ...
;     ...
;     for (int s = 0; s < 4; ++s) { const int sb = DIR ? 3 - s : s; float BR[32], BI[32];
;         bu_block(ua[s], f, BR, BI);
; #pragma unroll
;         for (int tt = 0; tt < 32; ++tt) { const int t = DIR ? 31 - tt : tt; const float nsr = fmaf(ar, sr, fmaf(-ai, si, BR[t])), nsi = fmaf(ar, si, fmaf(ai, sr, BI[t])); sr = nsr; si = nsi;
;             *(LAS unsigned*)(sl + (t * 136 + 2 * lane) * 2) = cvt_pk_bf16(sr, si); }
;         LDS_WAIT();
; #pragma unroll
;         for (int rb = 0; rb < 2; ++rb)
; #pragma unroll
;             for (int ks = 0; ks < 4; ++ks) { const bf16x8 a = *(const LAS bf16x8*)(sl + ((16 * rb + (lane & 15)) * 136 + 32 * ks + 8 * (lane >> 4)) * 2);
;                 yacc[2 * sb + rb] = __builtin_amdgcn_mfma_f32_16x16x32_bf16(a, cb[ks], yacc[2 * sb + rb], 0, 0, 0); }
;         LDS_WAIT(); }
	ds_write_b32 v171, v3 offset:4896
	v_fma_f32 v3, -v143, v60, v77
	v_fmac_f32_e32 v61, v143, v2
	v_fmac_f32_e32 v3, v142, v2
	v_fmac_f32_e32 v61, v142, v60
	v_cvt_pk_bf16_f32 v2, v3, v61
	ds_write_b32 v171, v2 offset:5168
	v_fma_f32 v2, -v143, v61, v42
	v_fmac_f32_e32 v10, v143, v3
	v_fmac_f32_e32 v2, v142, v3
	v_fmac_f32_e32 v10, v142, v61
	v_cvt_pk_bf16_f32 v3, v2, v10
	ds_write_b32 v171, v3 offset:5440
	v_fma_f32 v3, -v143, v10, v43
	v_fmac_f32_e32 v11, v143, v2
	v_fmac_f32_e32 v3, v142, v2
	v_fmac_f32_e32 v11, v142, v10
	v_cvt_pk_bf16_f32 v2, v3, v11
	ds_write_b32 v171, v2 offset:5712
	v_fma_f32 v2, -v143, v11, v44
	v_fmac_f32_e32 v12, v143, v3
	v_fmac_f32_e32 v2, v142, v3
	v_fmac_f32_e32 v12, v142, v11
	v_cvt_pk_bf16_f32 v3, v2, v12
	ds_write_b32 v171, v3 offset:5984
	v_fma_f32 v3, -v143, v12, v45
	v_fmac_f32_e32 v13, v143, v2
	v_permlane32_swap_b32_e32 v78, v46
	v_permlane32_swap_b32_e32 v62, v14
	v_fmac_f32_e32 v3, v142, v2
	v_fmac_f32_e32 v13, v142, v12
	v_cvt_pk_bf16_f32 v2, v3, v13
	ds_write_b32 v171, v2 offset:6256
	v_fma_f32 v2, -v143, v13, v78
	v_fmac_f32_e32 v62, v143, v3
	v_permlane32_swap_b32_e32 v79, v47
	v_permlane32_swap_b32_e32 v63, v15
	v_fmac_f32_e32 v2, v142, v3
	v_fmac_f32_e32 v62, v142, v13
	v_cvt_pk_bf16_f32 v3, v2, v62
	ds_write_b32 v171, v3 offset:6528
	v_fma_f32 v3, -v143, v62, v79
	v_fmac_f32_e32 v63, v143, v2
	v_permlane32_swap_b32_e32 v80, v48
	v_permlane32_swap_b32_e32 v64, v16
	v_fmac_f32_e32 v3, v142, v2
	v_fmac_f32_e32 v63, v142, v62
	v_cvt_pk_bf16_f32 v2, v3, v63
	ds_write_b32 v171, v2 offset:6800
	v_fma_f32 v2, -v143, v63, v80
	v_fmac_f32_e32 v64, v143, v3
	v_permlane32_swap_b32_e32 v81, v49
	v_permlane32_swap_b32_e32 v65, v17
	v_fmac_f32_e32 v2, v142, v3
	v_fmac_f32_e32 v64, v142, v63
	v_cvt_pk_bf16_f32 v3, v2, v64
	ds_write_b32 v171, v3 offset:7072
	v_fma_f32 v3, -v143, v64, v81
	v_fmac_f32_e32 v65, v143, v2
	v_fmac_f32_e32 v3, v142, v2
	v_fmac_f32_e32 v65, v142, v64
	v_cvt_pk_bf16_f32 v2, v3, v65
	ds_write_b32 v171, v2 offset:7344
	v_fma_f32 v2, -v143, v65, v46
	v_fmac_f32_e32 v14, v143, v3
	v_fmac_f32_e32 v2, v142, v3
	v_fmac_f32_e32 v14, v142, v65
	v_cvt_pk_bf16_f32 v3, v2, v14
	ds_write_b32 v171, v3 offset:7616
	v_fma_f32 v3, -v143, v14, v47
	v_fmac_f32_e32 v15, v143, v2
	v_fmac_f32_e32 v3, v142, v2
	v_fmac_f32_e32 v15, v142, v14
	v_cvt_pk_bf16_f32 v2, v3, v15
	ds_write_b32 v171, v2 offset:7888
	v_fma_f32 v2, -v143, v15, v48
	v_fmac_f32_e32 v16, v143, v3
	v_fmac_f32_e32 v2, v142, v3
	v_fmac_f32_e32 v16, v142, v15
	v_fma_f32 v10, -v143, v16, v49
	v_fmac_f32_e32 v17, v143, v2
	v_cvt_pk_bf16_f32 v3, v2, v16
	ds_write_b32 v171, v3 offset:8160
	v_fmac_f32_e32 v10, v142, v2
	v_fmac_f32_e32 v17, v142, v16
	v_cvt_pk_bf16_f32 v2, v10, v17
	ds_write_b32 v171, v2 offset:8432
	s_waitcnt lgkmcnt(0)
	ds_read_b128 v[2:5], v175
	ds_read_b128 v[6:9], v175 offset:64
	s_waitcnt lgkmcnt(1)
	v_mfma_f32_16x16x32_bf16 v[2:5], v[2:5], v[118:121], 0
	s_waitcnt lgkmcnt(0)
	v_mfma_f32_16x16x32_bf16 v[2:5], v[6:9], v[114:117], v[2:5]
	ds_read_b128 v[6:9], v175 offset:128
	s_waitcnt lgkmcnt(0)
	v_mfma_f32_16x16x32_bf16 v[2:5], v[6:9], v[110:113], v[2:5]
	ds_read_b128 v[6:9], v175 offset:192
	s_waitcnt lgkmcnt(0)
	v_mfma_f32_16x16x32_bf16 v[98:101], v[6:9], v[106:109], v[2:5]
	s_nop 4
	ds_read_b128 v[2:5], v175 offset:4352
	ds_read_b128 v[6:9], v175 offset:4416
	s_waitcnt lgkmcnt(1)
	v_mfma_f32_16x16x32_bf16 v[2:5], v[2:5], v[118:121], 0
	s_waitcnt lgkmcnt(0)
	v_mfma_f32_16x16x32_bf16 v[2:5], v[6:9], v[114:117], v[2:5]
	ds_read_b128 v[6:9], v175 offset:4480
	s_waitcnt lgkmcnt(0)
	v_mfma_f32_16x16x32_bf16 v[2:5], v[6:9], v[110:113], v[2:5]
	ds_read_b128 v[6:9], v175 offset:4544
	s_waitcnt lgkmcnt(0)
	s_waitcnt vmcnt(0)
	v_mfma_f32_32x32x16_bf16 v[66:81], v[138:141], v[122:125], 0
	v_mfma_f32_32x32x16_bf16 v[34:49], v[138:141], v[126:129], 0
	v_mfma_f32_32x32x16_bf16 v[50:65], v[138:141], v[130:133], 0
	s_nop 10
	v_permlane32_swap_b32_e32 v66, v34
	v_permlane32_swap_b32_e32 v67, v35
	v_permlane32_swap_b32_e32 v68, v36
	v_permlane32_swap_b32_e32 v69, v37
	v_mfma_f32_32x32x16_bf16 v[18:33], v[138:141], v[134:137], 0
	v_permlane32_swap_b32_e32 v70, v38
	v_permlane32_swap_b32_e32 v71, v39
	v_permlane32_swap_b32_e32 v72, v40
	v_permlane32_swap_b32_e32 v73, v41
	s_nop 7
	v_permlane32_swap_b32_e32 v50, v18
	s_waitcnt lgkmcnt(0)
; #define LAS __attribute__((address_space(3)))
; __device__ __forceinline__ unsigned cvt_pk_bf16(float lo, float hi) { unsigned r; asm volatile("v_cvt_pk_bf16_f32 %0, %1, %2" : "=v"(r) : "v"(lo), "v"(hi)); return r; }
; #define LDS_WAIT() asm volatile("s_waitcnt lgkmcnt(0)" ::: "memory")
; template <int DIR> ...
;     ...
;     for (int s = 0; s < 4; ++s) { const int sb = DIR ? 3 - s : s; float BR[32], BI[32];
;         bu_block(ua[s], f, BR, BI);
; #pragma unroll
;         for (int tt = 0; tt < 32; ++tt) { const int t = DIR ? 31 - tt : tt; const float nsr = fmaf(ar, sr, fmaf(-ai, si, BR[t])), nsi = fmaf(ar, si, fmaf(ai, sr, BI[t])); sr = nsr; si = nsi;
;             *(LAS unsigned*)(sl + (t * 136 + 2 * lane) * 2) = cvt_pk_bf16(sr, si); }
;         LDS_WAIT();
; #pragma unroll
;         for (int rb = 0; rb < 2; ++rb)
; #pragma unroll
;             for (int ks = 0; ks < 4; ++ks) { const bf16x8 a = *(const LAS bf16x8*)(sl + ((16 * rb + (lane & 15)) * 136 + 32 * ks + 8 * (lane >> 4)) * 2);
;                 yacc[2 * sb + rb] = __builtin_amdgcn_mfma_f32_16x16x32_bf16(a, cb[ks], yacc[2 * sb + rb], 0, 0, 0); }
;         LDS_WAIT(); }
	v_mfma_f32_16x16x32_bf16 v[102:105], v[6:9], v[106:109], v[2:5]
	v_fmac_f32_e32 v50, v143, v10
	v_permlane32_swap_b32_e32 v51, v19
	s_nop 0
	v_fma_f32 v2, -v143, v17, v66
	v_fmac_f32_e32 v2, v142, v10
	v_fmac_f32_e32 v50, v142, v17
	v_cvt_pk_bf16_f32 v3, v2, v50
	ds_write_b32 v171, v3
	v_fma_f32 v3, -v143, v50, v67
	v_fmac_f32_e32 v51, v143, v2
	v_permlane32_swap_b32_e32 v52, v20
	v_fmac_f32_e32 v3, v142, v2
	v_fmac_f32_e32 v51, v142, v50
	v_cvt_pk_bf16_f32 v2, v3, v51
	ds_write_b32 v171, v2 offset:272
	v_fma_f32 v2, -v143, v51, v68
	v_fmac_f32_e32 v52, v143, v3
	v_permlane32_swap_b32_e32 v53, v21
	v_fmac_f32_e32 v2, v142, v3
	v_fmac_f32_e32 v52, v142, v51
	v_cvt_pk_bf16_f32 v3, v2, v52
	ds_write_b32 v171, v3 offset:544
	v_fma_f32 v3, -v143, v52, v69
	v_fmac_f32_e32 v53, v143, v2
	v_fmac_f32_e32 v3, v142, v2
	v_fmac_f32_e32 v53, v142, v52
	v_cvt_pk_bf16_f32 v2, v3, v53
	ds_write_b32 v171, v2 offset:816
	v_fma_f32 v2, -v143, v53, v34
	v_fmac_f32_e32 v18, v143, v3
	v_fmac_f32_e32 v2, v142, v3
	v_fmac_f32_e32 v18, v142, v53
	v_cvt_pk_bf16_f32 v3, v2, v18
	ds_write_b32 v171, v3 offset:1088
	v_fma_f32 v3, -v143, v18, v35
	v_fmac_f32_e32 v19, v143, v2
	v_fmac_f32_e32 v3, v142, v2
	v_fmac_f32_e32 v19, v142, v18
	v_cvt_pk_bf16_f32 v2, v3, v19
	ds_write_b32 v171, v2 offset:1360
	v_fma_f32 v2, -v143, v19, v36
	v_fmac_f32_e32 v20, v143, v3
	v_fmac_f32_e32 v2, v142, v3
	v_fmac_f32_e32 v20, v142, v19
	v_cvt_pk_bf16_f32 v3, v2, v20
	ds_write_b32 v171, v3 offset:1632
	v_fma_f32 v3, -v143, v20, v37
	v_fmac_f32_e32 v21, v143, v2
	v_permlane32_swap_b32_e32 v54, v22
	v_fmac_f32_e32 v3, v142, v2
	v_fmac_f32_e32 v21, v142, v20
	v_cvt_pk_bf16_f32 v2, v3, v21
	ds_write_b32 v171, v2 offset:1904
	v_fma_f32 v2, -v143, v21, v70
	v_fmac_f32_e32 v54, v143, v3
	v_permlane32_swap_b32_e32 v55, v23
	v_fmac_f32_e32 v2, v142, v3
	v_fmac_f32_e32 v54, v142, v21
	v_cvt_pk_bf16_f32 v3, v2, v54
	ds_write_b32 v171, v3 offset:2176
	v_fma_f32 v3, -v143, v54, v71
	v_fmac_f32_e32 v55, v143, v2
	v_permlane32_swap_b32_e32 v56, v24
	v_fmac_f32_e32 v3, v142, v2
	v_fmac_f32_e32 v55, v142, v54
	v_cvt_pk_bf16_f32 v2, v3, v55
	ds_write_b32 v171, v2 offset:2448
	v_fma_f32 v2, -v143, v55, v72
	v_fmac_f32_e32 v56, v143, v3
	v_permlane32_swap_b32_e32 v57, v25
	v_fmac_f32_e32 v2, v142, v3
	v_fmac_f32_e32 v56, v142, v55
	v_cvt_pk_bf16_f32 v3, v2, v56
	ds_write_b32 v171, v3 offset:2720
	v_fma_f32 v3, -v143, v56, v73
	v_fmac_f32_e32 v57, v143, v2
	v_fmac_f32_e32 v3, v142, v2
	v_fmac_f32_e32 v57, v142, v56
	v_cvt_pk_bf16_f32 v2, v3, v57
	ds_write_b32 v171, v2 offset:2992
	v_fma_f32 v2, -v143, v57, v38
	v_fmac_f32_e32 v22, v143, v3
	v_fmac_f32_e32 v2, v142, v3
	v_fmac_f32_e32 v22, v142, v57
	v_cvt_pk_bf16_f32 v3, v2, v22
	ds_write_b32 v171, v3 offset:3264
	v_fma_f32 v3, -v143, v22, v39
	v_fmac_f32_e32 v23, v143, v2
	v_fmac_f32_e32 v3, v142, v2
	v_fmac_f32_e32 v23, v142, v22
	v_cvt_pk_bf16_f32 v2, v3, v23
	ds_write_b32 v171, v2 offset:3536
	v_fma_f32 v2, -v143, v23, v40
	v_fmac_f32_e32 v24, v143, v3
	v_fmac_f32_e32 v2, v142, v3
	v_fmac_f32_e32 v24, v142, v23
	v_cvt_pk_bf16_f32 v3, v2, v24
	ds_write_b32 v171, v3 offset:3808
	v_fma_f32 v3, -v143, v24, v41
	v_fmac_f32_e32 v25, v143, v2
	v_permlane32_swap_b32_e32 v74, v42
	v_permlane32_swap_b32_e32 v58, v26
	v_fmac_f32_e32 v3, v142, v2
	v_fmac_f32_e32 v25, v142, v24
	v_cvt_pk_bf16_f32 v2, v3, v25
	ds_write_b32 v171, v2 offset:4080
	v_fma_f32 v2, -v143, v25, v74
	v_fmac_f32_e32 v58, v143, v3
	v_permlane32_swap_b32_e32 v75, v43
	v_permlane32_swap_b32_e32 v59, v27
	v_fmac_f32_e32 v2, v142, v3
	v_fmac_f32_e32 v58, v142, v25
	v_cvt_pk_bf16_f32 v3, v2, v58
	ds_write_b32 v171, v3 offset:4352
	v_fma_f32 v3, -v143, v58, v75
	v_fmac_f32_e32 v59, v143, v2
	v_permlane32_swap_b32_e32 v76, v44
	v_permlane32_swap_b32_e32 v60, v28
	v_fmac_f32_e32 v3, v142, v2
	v_fmac_f32_e32 v59, v142, v58
	v_cvt_pk_bf16_f32 v2, v3, v59
	ds_write_b32 v171, v2 offset:4624
	v_fma_f32 v2, -v143, v59, v76
	v_fmac_f32_e32 v60, v143, v3
	v_permlane32_swap_b32_e32 v77, v45
	v_permlane32_swap_b32_e32 v61, v29
	v_fmac_f32_e32 v2, v142, v3
	v_fmac_f32_e32 v60, v142, v59
	v_cvt_pk_bf16_f32 v3, v2, v60
	ds_write_b32 v171, v3 offset:4896
	v_fma_f32 v3, -v143, v60, v77
	v_fmac_f32_e32 v61, v143, v2
	v_fmac_f32_e32 v3, v142, v2
	v_fmac_f32_e32 v61, v142, v60
	v_cvt_pk_bf16_f32 v2, v3, v61
	ds_write_b32 v171, v2 offset:5168
	v_fma_f32 v2, -v143, v61, v42
	v_fmac_f32_e32 v26, v143, v3
	v_fmac_f32_e32 v2, v142, v3
	v_fmac_f32_e32 v26, v142, v61
	v_cvt_pk_bf16_f32 v3, v2, v26
	ds_write_b32 v171, v3 offset:5440
	v_fma_f32 v3, -v143, v26, v43
	v_fmac_f32_e32 v27, v143, v2
	v_fmac_f32_e32 v3, v142, v2
	v_fmac_f32_e32 v27, v142, v26
	v_cvt_pk_bf16_f32 v2, v3, v27
	ds_write_b32 v171, v2 offset:5712
	v_fma_f32 v2, -v143, v27, v44
	v_fmac_f32_e32 v28, v143, v3
	v_fmac_f32_e32 v2, v142, v3
	v_fmac_f32_e32 v28, v142, v27
	v_cvt_pk_bf16_f32 v3, v2, v28
	ds_write_b32 v171, v3 offset:5984
	v_fma_f32 v3, -v143, v28, v45
	v_fmac_f32_e32 v29, v143, v2
	v_permlane32_swap_b32_e32 v78, v46
	v_permlane32_swap_b32_e32 v62, v30
	v_fmac_f32_e32 v3, v142, v2
	v_fmac_f32_e32 v29, v142, v28
	v_cvt_pk_bf16_f32 v2, v3, v29
	ds_write_b32 v171, v2 offset:6256
	v_fma_f32 v2, -v143, v29, v78
	v_fmac_f32_e32 v62, v143, v3
	v_permlane32_swap_b32_e32 v79, v47
	v_permlane32_swap_b32_e32 v63, v31
	v_fmac_f32_e32 v2, v142, v3
	v_fmac_f32_e32 v62, v142, v29
	v_cvt_pk_bf16_f32 v3, v2, v62
	ds_write_b32 v171, v3 offset:6528
	v_fma_f32 v3, -v143, v62, v79
	v_fmac_f32_e32 v63, v143, v2
	v_permlane32_swap_b32_e32 v80, v48
	v_permlane32_swap_b32_e32 v64, v32
	v_fmac_f32_e32 v3, v142, v2
	v_fmac_f32_e32 v63, v142, v62
	v_cvt_pk_bf16_f32 v2, v3, v63
	ds_write_b32 v171, v2 offset:6800
	v_fma_f32 v2, -v143, v63, v80
	v_fmac_f32_e32 v64, v143, v3
	v_permlane32_swap_b32_e32 v81, v49
	v_permlane32_swap_b32_e32 v65, v33
	v_fmac_f32_e32 v2, v142, v3
	v_fmac_f32_e32 v64, v142, v63
	v_cvt_pk_bf16_f32 v3, v2, v64
	ds_write_b32 v171, v3 offset:7072
	v_fma_f32 v3, -v143, v64, v81
	v_fmac_f32_e32 v65, v143, v2
	v_fmac_f32_e32 v3, v142, v2
	v_fmac_f32_e32 v65, v142, v64
	v_cvt_pk_bf16_f32 v2, v3, v65
	ds_write_b32 v171, v2 offset:7344
	v_fma_f32 v2, -v143, v65, v46
	v_fmac_f32_e32 v30, v143, v3
	v_fmac_f32_e32 v2, v142, v3
	v_fmac_f32_e32 v30, v142, v65
	v_cvt_pk_bf16_f32 v3, v2, v30
	ds_write_b32 v171, v3 offset:7616
	v_fma_f32 v3, -v143, v30, v47
	v_fmac_f32_e32 v31, v143, v2
	v_fmac_f32_e32 v3, v142, v2
	v_fmac_f32_e32 v31, v142, v30
	v_cvt_pk_bf16_f32 v2, v3, v31
	ds_write_b32 v171, v2 offset:7888
	v_fma_f32 v2, -v143, v31, v48
	v_fmac_f32_e32 v32, v143, v3
	v_fmac_f32_e32 v2, v142, v3
	v_fmac_f32_e32 v32, v142, v31
	v_cvt_pk_bf16_f32 v3, v2, v32
	ds_write_b32 v171, v3 offset:8160
	v_fma_f32 v3, -v143, v32, v49
	v_fmac_f32_e32 v33, v143, v2
	v_fmac_f32_e32 v3, v142, v2
	v_fmac_f32_e32 v33, v142, v32
	v_cvt_pk_bf16_f32 v2, v3, v33
	ds_write_b32 v171, v2 offset:8432
	s_waitcnt lgkmcnt(0)
; #define LAS __attribute__((address_space(3)))
; #define LDS_WAIT() asm volatile("s_waitcnt lgkmcnt(0)" ::: "memory")
; template <class T> __device__ __forceinline__ void est(T* p, T v) { if constexpr (MK_EPI_NT != 0) __builtin_nontemporal_store(v, p); else *p = v; }
; template <int DIR> ...
;     const int dg = DIR * 64 + g; const float ar = lamb_l[(dg * 64 + lane) * 2], ai = lamb_l[(dg * 64 + lane) * 2 + 1], tr = lamt_l[(dg * 64 + lane) * 2], ti = lamt_l[(dg * 64 + lane) * 2 + 1];
;     float sr = 0.f, si = 0.f;
;     { const float* e = est + ((((size_t)(DIR * 2 + b) * 64 + g) * 32) * 64 + lane) * 2; f32x2 ev[32];
; #pragma unroll
;       for (int m = 0; m < 32; ++m) ev[m] = *(const f32x2*)(e + (size_t)m * 128);
; #pragma unroll
;       for (int mm = 0; mm < 32; ++mm) { const int m = DIR ? 31 - mm : mm; const bool use = DIR ? (m > n) : (m < n);
;           const float nsr = fmaf(tr, sr, fmaf(-ti, si, ev[m].x)), nsi = fmaf(tr, si, fmaf(ti, sr, ev[m].y)); sr = use ? nsr : sr; si = use ? nsi : si; } }
;     ...
;         for (int rb = 0; rb < 2; ++rb)
; #pragma unroll
;             for (int ks = 0; ks < 4; ++ks) { const bf16x8 a = *(const LAS bf16x8*)(sl + ((16 * rb + (lane & 15)) * 136 + 32 * ks + 8 * (lane >> 4)) * 2);
;                 yacc[2 * sb + rb] = __builtin_amdgcn_mfma_f32_16x16x32_bf16(a, cb[ks], yacc[2 * sb + rb], 0, 0, 0); }
;         LDS_WAIT(); }
	ds_read_b128 v[2:5], v175
	ds_read_b128 v[6:9], v175 offset:64
	s_waitcnt lgkmcnt(1)
	v_mfma_f32_16x16x32_bf16 v[2:5], v[2:5], v[118:121], 0
	s_waitcnt lgkmcnt(0)
	v_mfma_f32_16x16x32_bf16 v[2:5], v[6:9], v[114:117], v[2:5]
	ds_read_b128 v[6:9], v175 offset:128
	s_waitcnt lgkmcnt(0)
	v_mfma_f32_16x16x32_bf16 v[2:5], v[6:9], v[110:113], v[2:5]
	ds_read_b128 v[6:9], v175 offset:192
	s_waitcnt lgkmcnt(0)
	v_mfma_f32_16x16x32_bf16 v[66:69], v[6:9], v[106:109], v[2:5]
	s_nop 4
	ds_read_b128 v[2:5], v175 offset:4352
	ds_read_b128 v[6:9], v175 offset:4416
	s_waitcnt lgkmcnt(1)
	v_mfma_f32_16x16x32_bf16 v[2:5], v[2:5], v[118:121], 0
	s_waitcnt lgkmcnt(0)
	v_mfma_f32_16x16x32_bf16 v[2:5], v[6:9], v[114:117], v[2:5]
	ds_read_b128 v[6:9], v175 offset:4480
	s_waitcnt lgkmcnt(0)
	v_mfma_f32_16x16x32_bf16 v[2:5], v[6:9], v[110:113], v[2:5]
	ds_read_b128 v[6:9], v175 offset:4544
	s_waitcnt lgkmcnt(0)
	s_waitcnt lgkmcnt(0)
	v_mfma_f32_16x16x32_bf16 v[70:73], v[6:9], v[106:109], v[2:5]
	s_nop 4
	v_lshl_or_b32 v2, s17, 9, v174
	global_load_dwordx2 v[168:169], v2, s[10:11]
	global_load_dwordx2 v[4:5], v2, s[8:9]
	v_mov_b32_e32 v3, s5
	v_or_b32_e32 v2, s4, v194
	v_lshl_add_u64 v[12:13], v[2:3], 3, s[76:77]
	v_add_co_u32_e64 v20, s[4:5], s38, v12
	global_load_dwordx2 v[2:3], v[12:13], off offset:512
	global_load_dwordx2 v[6:7], v[12:13], off offset:1024
	global_load_dwordx2 v[8:9], v[12:13], off offset:1536
	global_load_dwordx2 v[10:11], v[12:13], off offset:2048
	global_load_dwordx2 v[14:15], v[12:13], off offset:2560
	global_load_dwordx2 v[16:17], v[12:13], off offset:3072
	global_load_dwordx2 v[18:19], v[12:13], off offset:3584
	v_addc_co_u32_e64 v21, s[4:5], 0, v13, s[4:5]
	v_add_co_u32_e64 v22, s[4:5], s39, v12
	s_nop 1
	v_addc_co_u32_e64 v23, s[4:5], 0, v13, s[4:5]
	v_add_co_u32_e64 v12, s[4:5], s40, v12
	global_load_dwordx2 v[24:25], v[22:23], off offset:-4096
	global_load_dwordx2 v[26:27], v[20:21], off offset:512
	global_load_dwordx2 v[28:29], v[20:21], off offset:1024
	global_load_dwordx2 v[30:31], v[20:21], off offset:1536
	global_load_dwordx2 v[32:33], v[20:21], off offset:2048
	global_load_dwordx2 v[34:35], v[20:21], off offset:2560
	global_load_dwordx2 v[36:37], v[20:21], off offset:3072
	s_nop 0
	global_load_dwordx2 v[20:21], v[20:21], off offset:3584
	s_nop 0
	global_load_dwordx2 v[38:39], v[22:23], off
	global_load_dwordx2 v[40:41], v[22:23], off offset:512
	global_load_dwordx2 v[42:43], v[22:23], off offset:1024
	global_load_dwordx2 v[44:45], v[22:23], off offset:1536
	global_load_dwordx2 v[46:47], v[22:23], off offset:2048
	global_load_dwordx2 v[48:49], v[22:23], off offset:2560
	global_load_dwordx2 v[50:51], v[22:23], off offset:3072
	s_nop 0
	global_load_dwordx2 v[22:23], v[22:23], off offset:3584
	v_addc_co_u32_e64 v13, s[4:5], 0, v13, s[4:5]
	global_load_dwordx2 v[52:53], v[12:13], off
	global_load_dwordx2 v[54:55], v[12:13], off offset:512
	global_load_dwordx2 v[56:57], v[12:13], off offset:1024
	global_load_dwordx2 v[58:59], v[12:13], off offset:1536
	global_load_dwordx2 v[60:61], v[12:13], off offset:2048
	global_load_dwordx2 v[62:63], v[12:13], off offset:2560
	global_load_dwordx2 v[64:65], v[12:13], off offset:3072
	s_nop 0
	global_load_dwordx2 v[12:13], v[12:13], off offset:3584
	s_waitcnt vmcnt(0)
	v_fmamk_f32 v12, v5, 0x80000000, v12
	v_fmac_f32_e32 v13, 0, v5
	v_fmac_f32_e32 v12, 0, v4
	v_fmac_f32_e32 v13, 0, v4
	v_cndmask_b32_e64 v12, v12, 0, s[0:1]
	v_cndmask_b32_e64 v13, v13, 0, s[0:1]
	v_fma_f32 v64, -v5, v13, v64
	v_fmac_f32_e32 v65, v5, v12
	s_cselect_b64 s[0:1], -1, 0
	v_fmac_f32_e32 v64, v4, v12
	v_fmac_f32_e32 v65, v4, v13
	v_cndmask_b32_e64 v12, v12, v64, s[0:1]
	v_cndmask_b32_e64 v13, v13, v65, s[0:1]
	s_cmp_lt_u32 s3, 29
	v_fma_f32 v62, -v5, v13, v62
	v_fmac_f32_e32 v63, v5, v12
	s_cselect_b64 s[0:1], -1, 0
	v_fmac_f32_e32 v62, v4, v12
	v_fmac_f32_e32 v63, v4, v13
	v_cndmask_b32_e64 v12, v12, v62, s[0:1]
	v_cndmask_b32_e64 v13, v13, v63, s[0:1]
	s_cmp_lt_u32 s3, 28
	v_fma_f32 v60, -v5, v13, v60
	v_fmac_f32_e32 v61, v5, v12
	s_cselect_b64 s[0:1], -1, 0
	v_fmac_f32_e32 v60, v4, v12
	v_fmac_f32_e32 v61, v4, v13
	v_cndmask_b32_e64 v12, v12, v60, s[0:1]
	v_cndmask_b32_e64 v13, v13, v61, s[0:1]
	s_cmp_lt_u32 s3, 27
	v_fma_f32 v58, -v5, v13, v58
	v_fmac_f32_e32 v59, v5, v12
	s_cselect_b64 s[0:1], -1, 0
	v_fmac_f32_e32 v58, v4, v12
	v_fmac_f32_e32 v59, v4, v13
	v_cndmask_b32_e64 v12, v12, v58, s[0:1]
	v_cndmask_b32_e64 v13, v13, v59, s[0:1]
	s_cmp_lt_u32 s3, 26
	v_fma_f32 v56, -v5, v13, v56
	v_fmac_f32_e32 v57, v5, v12
	s_cselect_b64 s[0:1], -1, 0
	v_fmac_f32_e32 v56, v4, v12
	v_fmac_f32_e32 v57, v4, v13
	v_cndmask_b32_e64 v12, v12, v56, s[0:1]
	v_cndmask_b32_e64 v13, v13, v57, s[0:1]
	s_cmp_lt_u32 s3, 25
	v_fma_f32 v54, -v5, v13, v54
	v_fmac_f32_e32 v55, v5, v12
	s_cselect_b64 s[0:1], -1, 0
	v_fmac_f32_e32 v54, v4, v12
	v_fmac_f32_e32 v55, v4, v13
	v_cndmask_b32_e64 v12, v12, v54, s[0:1]
	v_cndmask_b32_e64 v13, v13, v55, s[0:1]
	s_cmp_lt_u32 s3, 24
	v_fma_f32 v52, -v5, v13, v52
	v_fmac_f32_e32 v53, v5, v12
	s_cselect_b64 s[0:1], -1, 0
	v_fmac_f32_e32 v52, v4, v12
	v_fmac_f32_e32 v53, v4, v13
	v_cndmask_b32_e64 v12, v12, v52, s[0:1]
	v_cndmask_b32_e64 v13, v13, v53, s[0:1]
	s_cmp_lt_u32 s3, 23
	v_fma_f32 v22, -v5, v13, v22
	v_fmac_f32_e32 v23, v5, v12
	s_cselect_b64 s[0:1], -1, 0
	v_fmac_f32_e32 v22, v4, v12
	v_fmac_f32_e32 v23, v4, v13
	v_cndmask_b32_e64 v12, v12, v22, s[0:1]
	v_cndmask_b32_e64 v13, v13, v23, s[0:1]
	s_cmp_lt_u32 s3, 22
	v_fma_f32 v22, -v5, v13, v50
	v_fmac_f32_e32 v51, v5, v12
	s_cselect_b64 s[0:1], -1, 0
	v_fmac_f32_e32 v22, v4, v12
	v_fmac_f32_e32 v51, v4, v13
	v_cndmask_b32_e64 v12, v12, v22, s[0:1]
; template <class T> __device__ __forceinline__ void est(T* p, T v) { if constexpr (MK_EPI_NT != 0) __builtin_nontemporal_store(v, p); else *p = v; }
; template <int DIR> ...
;     ...
;     { const float* e = est + ((((size_t)(DIR * 2 + b) * 64 + g) * 32) * 64 + lane) * 2; f32x2 ev[32];
; #pragma unroll
;       for (int m = 0; m < 32; ++m) ev[m] = *(const f32x2*)(e + (size_t)m * 128);
; #pragma unroll
;       for (int mm = 0; mm < 32; ++mm) { const int m = DIR ? 31 - mm : mm; const bool use = DIR ? (m > n) : (m < n);
;           const float nsr = fmaf(tr, sr, fmaf(-ti, si, ev[m].x)), nsi = fmaf(tr, si, fmaf(ti, sr, ev[m].y)); sr = use ? nsr : sr; si = use ? nsi : si; } }
;     const BuFrags f = load_bufrags(bbar_l + (size_t)dg * 2 * 64 * 16, lane);
;     bf16x8 cb[4];
; #pragma unroll
;     for (int ks = 0; ks < 4; ++ks) cb[ks] = *(const bf16x8*)(ctt_l + ((size_t)dg * 16 + (lane & 15)) * 128 + 32 * ks + 8 * (lane >> 4));
;     bf16x8 ua[4];
; #pragma unroll
;     for (int s = 0; s < 4; ++s) ua[s] = bu_load(proj, b * SEQ + n * 128 + (DIR ? 3 - s : s) * 32, g, lane);
	v_cndmask_b32_e64 v13, v13, v51, s[0:1]
	s_cmp_lt_u32 s3, 21
	v_fma_f32 v22, -v5, v13, v48
	v_fmac_f32_e32 v49, v5, v12
	s_cselect_b64 s[0:1], -1, 0
	v_fmac_f32_e32 v22, v4, v12
	v_fmac_f32_e32 v49, v4, v13
	v_cndmask_b32_e64 v12, v12, v22, s[0:1]
	v_cndmask_b32_e64 v13, v13, v49, s[0:1]
	s_cmp_lt_u32 s3, 20
	v_fma_f32 v22, -v5, v13, v46
	v_fmac_f32_e32 v47, v5, v12
	s_cselect_b64 s[0:1], -1, 0
	v_fmac_f32_e32 v22, v4, v12
	v_fmac_f32_e32 v47, v4, v13
	v_cndmask_b32_e64 v12, v12, v22, s[0:1]
	v_cndmask_b32_e64 v13, v13, v47, s[0:1]
	s_cmp_lt_u32 s3, 19
	v_fma_f32 v22, -v5, v13, v44
	v_fmac_f32_e32 v45, v5, v12
	s_cselect_b64 s[0:1], -1, 0
	v_fmac_f32_e32 v22, v4, v12
	v_fmac_f32_e32 v45, v4, v13
	v_cndmask_b32_e64 v12, v12, v22, s[0:1]
	v_cndmask_b32_e64 v13, v13, v45, s[0:1]
	s_cmp_lt_u32 s3, 18
	v_fma_f32 v22, -v5, v13, v42
	v_fmac_f32_e32 v43, v5, v12
	s_cselect_b64 s[0:1], -1, 0
	v_fmac_f32_e32 v22, v4, v12
	v_fmac_f32_e32 v43, v4, v13
	v_cndmask_b32_e64 v12, v12, v22, s[0:1]
	v_cndmask_b32_e64 v13, v13, v43, s[0:1]
	s_cmp_lt_u32 s3, 17
	v_fma_f32 v22, -v5, v13, v40
	v_fmac_f32_e32 v41, v5, v12
	s_cselect_b64 s[0:1], -1, 0
	v_fmac_f32_e32 v22, v4, v12
	v_fmac_f32_e32 v41, v4, v13
	v_cndmask_b32_e64 v12, v12, v22, s[0:1]
	v_cndmask_b32_e64 v13, v13, v41, s[0:1]
	s_cmp_lt_u32 s3, 16
	v_fma_f32 v22, -v5, v13, v38
	v_fmac_f32_e32 v39, v5, v12
	s_cselect_b64 s[0:1], -1, 0
	v_fmac_f32_e32 v22, v4, v12
	v_fmac_f32_e32 v39, v4, v13
	v_cndmask_b32_e64 v12, v12, v22, s[0:1]
	v_cndmask_b32_e64 v13, v13, v39, s[0:1]
	s_cmp_lt_u32 s3, 15
	v_fma_f32 v20, -v5, v13, v20
	v_fmac_f32_e32 v21, v5, v12
	s_cselect_b64 s[0:1], -1, 0
	v_fmac_f32_e32 v20, v4, v12
	v_fmac_f32_e32 v21, v4, v13
	v_cndmask_b32_e64 v12, v12, v20, s[0:1]
	v_cndmask_b32_e64 v13, v13, v21, s[0:1]
	s_cmp_lt_u32 s3, 14
	v_fma_f32 v20, -v5, v13, v36
	v_fmac_f32_e32 v37, v5, v12
	s_cselect_b64 s[0:1], -1, 0
	v_fmac_f32_e32 v20, v4, v12
	v_fmac_f32_e32 v37, v4, v13
	v_cndmask_b32_e64 v12, v12, v20, s[0:1]
	v_cndmask_b32_e64 v13, v13, v37, s[0:1]
	s_cmp_lt_u32 s3, 13
	v_fma_f32 v20, -v5, v13, v34
	v_fmac_f32_e32 v35, v5, v12
	s_cselect_b64 s[0:1], -1, 0
	v_fmac_f32_e32 v20, v4, v12
	v_fmac_f32_e32 v35, v4, v13
	v_cndmask_b32_e64 v12, v12, v20, s[0:1]
	v_cndmask_b32_e64 v13, v13, v35, s[0:1]
	s_cmp_lt_u32 s3, 12
	v_fma_f32 v20, -v5, v13, v32
	v_fmac_f32_e32 v33, v5, v12
	s_cselect_b64 s[0:1], -1, 0
	v_fmac_f32_e32 v20, v4, v12
	v_fmac_f32_e32 v33, v4, v13
	v_cndmask_b32_e64 v12, v12, v20, s[0:1]
	v_cndmask_b32_e64 v13, v13, v33, s[0:1]
	s_cmp_lt_u32 s3, 11
	v_fma_f32 v20, -v5, v13, v30
	v_fmac_f32_e32 v31, v5, v12
	s_cselect_b64 s[0:1], -1, 0
	v_fmac_f32_e32 v20, v4, v12
	v_fmac_f32_e32 v31, v4, v13
	v_cndmask_b32_e64 v12, v12, v20, s[0:1]
	v_cndmask_b32_e64 v13, v13, v31, s[0:1]
	s_cmp_lt_u32 s3, 10
	v_fma_f32 v20, -v5, v13, v28
	v_fmac_f32_e32 v29, v5, v12
	s_cselect_b64 s[0:1], -1, 0
	v_fmac_f32_e32 v20, v4, v12
	v_fmac_f32_e32 v29, v4, v13
	v_cndmask_b32_e64 v12, v12, v20, s[0:1]
	v_cndmask_b32_e64 v13, v13, v29, s[0:1]
	s_cmp_lt_u32 s3, 9
	v_fma_f32 v20, -v5, v13, v26
	v_fmac_f32_e32 v27, v5, v12
	s_cselect_b64 s[0:1], -1, 0
	v_fmac_f32_e32 v20, v4, v12
	v_fmac_f32_e32 v27, v4, v13
	v_cndmask_b32_e64 v12, v12, v20, s[0:1]
	v_cndmask_b32_e64 v13, v13, v27, s[0:1]
	s_cmp_lt_u32 s3, 8
	v_fma_f32 v20, -v5, v13, v24
	v_fmac_f32_e32 v25, v5, v12
	s_cselect_b64 s[0:1], -1, 0
	v_fmac_f32_e32 v20, v4, v12
	v_fmac_f32_e32 v25, v4, v13
	v_cndmask_b32_e64 v12, v12, v20, s[0:1]
	v_cndmask_b32_e64 v13, v13, v25, s[0:1]
	s_cmp_lt_u32 s3, 7
	v_fma_f32 v18, -v5, v13, v18
	v_fmac_f32_e32 v19, v5, v12
	s_cselect_b64 s[0:1], -1, 0
	v_fmac_f32_e32 v18, v4, v12
	v_fmac_f32_e32 v19, v4, v13
	v_cndmask_b32_e64 v12, v12, v18, s[0:1]
	v_cndmask_b32_e64 v13, v13, v19, s[0:1]
	s_cmp_lt_u32 s3, 6
	v_fma_f32 v16, -v5, v13, v16
	v_fmac_f32_e32 v17, v5, v12
	s_cselect_b64 s[0:1], -1, 0
	v_fmac_f32_e32 v16, v4, v12
	v_fmac_f32_e32 v17, v4, v13
	v_cndmask_b32_e64 v12, v12, v16, s[0:1]
	v_cndmask_b32_e64 v13, v13, v17, s[0:1]
	s_cmp_lt_u32 s3, 5
	v_fma_f32 v14, -v5, v13, v14
	v_fmac_f32_e32 v15, v5, v12
	s_cselect_b64 s[0:1], -1, 0
	v_fmac_f32_e32 v14, v4, v12
	v_fmac_f32_e32 v15, v4, v13
	v_cndmask_b32_e64 v12, v12, v14, s[0:1]
	v_cndmask_b32_e64 v13, v13, v15, s[0:1]
	s_cmp_lt_u32 s3, 4
	v_fma_f32 v10, -v5, v13, v10
	v_fmac_f32_e32 v11, v5, v12
	s_cselect_b64 s[0:1], -1, 0
	v_fmac_f32_e32 v10, v4, v12
	v_fmac_f32_e32 v11, v4, v13
	v_cndmask_b32_e64 v10, v12, v10, s[0:1]
	v_cndmask_b32_e64 v11, v13, v11, s[0:1]
	s_cmp_lt_u32 s3, 3
	v_fma_f32 v8, -v5, v11, v8
	v_fmac_f32_e32 v9, v5, v10
	s_cselect_b64 s[0:1], -1, 0
	v_fmac_f32_e32 v8, v4, v10
	v_fmac_f32_e32 v9, v4, v11
	v_cndmask_b32_e64 v8, v10, v8, s[0:1]
	v_cndmask_b32_e64 v9, v11, v9, s[0:1]
	s_cmp_lt_u32 s3, 2
	v_fma_f32 v6, -v5, v9, v6
	v_fmac_f32_e32 v7, v5, v8
	s_cselect_b64 s[0:1], -1, 0
	v_fmac_f32_e32 v6, v4, v8
	v_fmac_f32_e32 v7, v4, v9
	v_cndmask_b32_e64 v8, v8, v6, s[0:1]
	v_cndmask_b32_e64 v6, v9, v7, s[0:1]
	s_lshl_b32 s0, s17, 12
	v_fma_f32 v2, -v5, v6, v2
	s_add_u32 s4, s82, s0
	v_fmac_f32_e32 v2, v4, v8
	s_addc_u32 s5, s83, 0
	v_fmac_f32_e32 v3, v5, v8
	v_cndmask_b32_e32 v78, v8, v2, vcc
	v_lshl_add_u64 v[8:9], s[4:5], 0, v[158:159]
	v_lshl_add_u64 v[10:11], s[4:5], 0, v[162:163]
	v_lshl_add_u64 v[8:9], v[8:9], 0, v[160:161]
	v_lshl_add_u64 v[10:11], v[10:11], 0, v[160:161]
	global_load_dwordx4 v[134:137], v[8:9], off
	global_load_dwordx4 v[130:133], v[10:11], off
	global_load_dwordx4 v[122:125], v[8:9], off offset:2048
	v_lshl_add_u64 v[8:9], s[4:5], 0, v[164:165]
	v_or_b32_e32 v2, s16, v194
	s_mov_b32 s1, s13
	v_lshl_add_u64 v[8:9], v[8:9], 0, v[160:161]
	v_or_b32_e32 v2, 0x60, v2
	global_load_dwordx4 v[126:129], v[8:9], off
	v_lshl_add_u64 v[8:9], v[156:157], 0, s[0:1]
	v_fmac_f32_e32 v3, v4, v6
	v_mad_i64_i32 v[4:5], s[0:1], v2, s41, v[166:167]
	v_lshl_add_u64 v[4:5], v[4:5], 0, s[12:13]
	v_lshl_add_u64 v[4:5], v[4:5], 0, v[160:161]
	global_load_dwordx4 v[118:121], v[8:9], off
	global_load_dwordx4 v[114:117], v[8:9], off offset:64
	global_load_dwordx4 v[110:113], v[8:9], off offset:128
	global_load_dwordx4 v[106:109], v[8:9], off offset:192
	global_load_dwordx4 v[34:37], v[4:5], off offset:3072
	v_subrev_u32_e32 v4, 32, v2
	v_mad_i64_i32 v[4:5], s[0:1], v4, s41, v[166:167]
	v_lshl_add_u64 v[4:5], v[4:5], 0, s[12:13]
	v_lshl_add_u64 v[4:5], v[4:5], 0, v[160:161]
	v_subrev_u32_e32 v2, 64, v2
	global_load_dwordx4 v[74:77], v[4:5], off offset:3072
	v_mad_i64_i32 v[4:5], s[0:1], v2, s41, v[166:167]
	v_lshl_add_u64 v[4:5], v[4:5], 0, s[12:13]
	v_lshl_add_u64 v[4:5], v[4:5], 0, v[160:161]
	v_bitop3_b32 v2, s16, v176, v194 bitop3:0xc8
	global_load_dwordx4 v[150:153], v[4:5], off offset:3072
	v_mad_i64_i32 v[4:5], s[0:1], v2, s41, v[166:167]
	v_lshl_add_u64 v[4:5], v[4:5], 0, s[12:13]
	v_lshl_add_u64 v[4:5], v[4:5], 0, v[160:161]
	global_load_dwordx4 v[146:149], v[4:5], off offset:3072
	v_cndmask_b32_e32 v79, v6, v3, vcc
	s_waitcnt vmcnt(3)
; #define LAS __attribute__((address_space(3)))
; __device__ __forceinline__ unsigned cvt_pk_bf16(float lo, float hi) { unsigned r; asm volatile("v_cvt_pk_bf16_f32 %0, %1, %2" : "=v"(r) : "v"(lo), "v"(hi)); return r; }
; __device__ __forceinline__ void bu_block(const bf16x8 ua, const BuFrags& f, float (&BR)[32], float (&BI)[32]) {
;     const f32x16 z = {};
;     const f32x16 R0 = __builtin_amdgcn_mfma_f32_32x32x16_bf16(ua, f.r0, z, 0, 0, 0), R1 = __builtin_amdgcn_mfma_f32_32x32x16_bf16(ua, f.r1, z, 0, 0, 0);
;     const f32x16 I0 = __builtin_amdgcn_mfma_f32_32x32x16_bf16(ua, f.i0, z, 0, 0, 0), I1 = __builtin_amdgcn_mfma_f32_32x32x16_bf16(ua, f.i1, z, 0, 0, 0);
; #pragma unroll
;     for (int r = 0; r < 16; ++r) {
;         auto s = __builtin_amdgcn_permlane32_swap(__float_as_uint(R0[r]), __float_as_uint(R1[r]), false, false);
;         BR[8 * (r >> 2) + (r & 3)] = __uint_as_float(s[0]); BR[8 * (r >> 2) + 4 + (r & 3)] = __uint_as_float(s[1]);
;         auto q = __builtin_amdgcn_permlane32_swap(__float_as_uint(I0[r]), __float_as_uint(I1[r]), false, false);
;         BI[8 * (r >> 2) + (r & 3)] = __uint_as_float(q[0]); BI[8 * (r >> 2) + 4 + (r & 3)] = __uint_as_float(q[1]);
;     }
; }
; template <int DIR> ...
;     ...
;     for (int s = 0; s < 4; ++s) { const int sb = DIR ? 3 - s : s; float BR[32], BI[32];
;         bu_block(ua[s], f, BR, BI);
; #pragma unroll
;         for (int tt = 0; tt < 32; ++tt) { const int t = DIR ? 31 - tt : tt; const float nsr = fmaf(ar, sr, fmaf(-ai, si, BR[t])), nsi = fmaf(ar, si, fmaf(ai, sr, BI[t])); sr = nsr; si = nsi;
;             *(LAS unsigned*)(sl + (t * 136 + 2 * lane) * 2) = cvt_pk_bf16(sr, si); }
	v_mfma_f32_32x32x16_bf16 v[18:33], v[34:37], v[134:137], 0
	s_add_i32 s57, s57, s58
	s_cmpk_gt_i32 s57, 0xfff
	v_mfma_f32_32x32x16_bf16 v[50:65], v[34:37], v[130:133], 0
	v_mfma_f32_32x32x16_bf16 v[2:17], v[34:37], v[122:125], 0
	s_nop 10
	v_permlane32_swap_b32_e32 v33, v65
	v_fma_f32 v65, -v169, v79, v65
	v_permlane32_swap_b32_e32 v32, v64
	v_fmac_f32_e32 v65, v168, v78
	v_permlane32_swap_b32_e32 v31, v63
	v_mfma_f32_32x32x16_bf16 v[34:49], v[34:37], v[126:129], 0
	v_permlane32_swap_b32_e32 v30, v62
	v_permlane32_swap_b32_e32 v29, v61
	v_permlane32_swap_b32_e32 v28, v60
	v_permlane32_swap_b32_e32 v27, v59
	s_nop 7
	v_permlane32_swap_b32_e32 v17, v49
	v_fmac_f32_e32 v49, v169, v78
	v_permlane32_swap_b32_e32 v16, v48
	v_fmac_f32_e32 v49, v168, v79
	v_fma_f32 v64, -v169, v49, v64
	v_fmac_f32_e32 v48, v169, v65
	v_permlane32_swap_b32_e32 v15, v47
	v_cvt_pk_bf16_f32 v78, v65, v49
	ds_write_b32 v171, v78 offset:8432
	v_fmac_f32_e32 v64, v168, v65
	v_fmac_f32_e32 v48, v168, v49
	v_cvt_pk_bf16_f32 v49, v64, v48
	ds_write_b32 v171, v49 offset:8160
	v_fma_f32 v49, -v169, v48, v63
	v_fmac_f32_e32 v47, v169, v64
	v_permlane32_swap_b32_e32 v14, v46
	v_fmac_f32_e32 v49, v168, v64
	v_fmac_f32_e32 v47, v168, v48
	v_cvt_pk_bf16_f32 v48, v49, v47
	ds_write_b32 v171, v48 offset:7888
	v_fma_f32 v48, -v169, v47, v62
	v_fmac_f32_e32 v46, v169, v49
	v_fmac_f32_e32 v48, v168, v49
	v_fmac_f32_e32 v46, v168, v47
	v_fma_f32 v33, -v169, v46, v33
	v_fmac_f32_e32 v17, v169, v48
	v_fmac_f32_e32 v33, v168, v48
	v_fmac_f32_e32 v17, v168, v46
	v_fma_f32 v32, -v169, v17, v32
	v_fmac_f32_e32 v16, v169, v33
	v_cvt_pk_bf16_f32 v47, v48, v46
	ds_write_b32 v171, v47 offset:7616
	v_cvt_pk_bf16_f32 v46, v33, v17
	ds_write_b32 v171, v46 offset:7344
	v_fmac_f32_e32 v32, v168, v33
	v_fmac_f32_e32 v16, v168, v17
	v_cvt_pk_bf16_f32 v17, v32, v16
	ds_write_b32 v171, v17 offset:7072
	v_fma_f32 v17, -v169, v16, v31
	v_fmac_f32_e32 v15, v169, v32
	v_fmac_f32_e32 v17, v168, v32
	v_fmac_f32_e32 v15, v168, v16
	v_cvt_pk_bf16_f32 v16, v17, v15
	ds_write_b32 v171, v16 offset:6800
	v_fma_f32 v16, -v169, v15, v30
	v_fmac_f32_e32 v14, v169, v17
	v_permlane32_swap_b32_e32 v13, v45
	v_fmac_f32_e32 v16, v168, v17
	v_fmac_f32_e32 v14, v168, v15
	v_cvt_pk_bf16_f32 v15, v16, v14
	ds_write_b32 v171, v15 offset:6528
	v_fma_f32 v15, -v169, v14, v61
	v_fmac_f32_e32 v45, v169, v16
	v_permlane32_swap_b32_e32 v12, v44
	v_fmac_f32_e32 v15, v168, v16
	v_fmac_f32_e32 v45, v168, v14
	v_cvt_pk_bf16_f32 v14, v15, v45
	ds_write_b32 v171, v14 offset:6256
	v_fma_f32 v14, -v169, v45, v60
	v_fmac_f32_e32 v44, v169, v15
	v_permlane32_swap_b32_e32 v11, v43
	v_fmac_f32_e32 v14, v168, v15
	v_fmac_f32_e32 v44, v168, v45
	v_cvt_pk_bf16_f32 v15, v14, v44
	ds_write_b32 v171, v15 offset:5984
	v_fma_f32 v15, -v169, v44, v59
	v_fmac_f32_e32 v43, v169, v14
	v_permlane32_swap_b32_e32 v26, v58
	v_permlane32_swap_b32_e32 v10, v42
	v_fmac_f32_e32 v15, v168, v14
	v_fmac_f32_e32 v43, v168, v44
	v_cvt_pk_bf16_f32 v14, v15, v43
	ds_write_b32 v171, v14 offset:5712
	v_fma_f32 v14, -v169, v43, v58
	v_fmac_f32_e32 v42, v169, v15
	v_fmac_f32_e32 v14, v168, v15
	v_fmac_f32_e32 v42, v168, v43
	v_cvt_pk_bf16_f32 v15, v14, v42
	ds_write_b32 v171, v15 offset:5440
	v_fma_f32 v15, -v169, v42, v29
	v_fmac_f32_e32 v13, v169, v14
	v_fmac_f32_e32 v15, v168, v14
	v_fmac_f32_e32 v13, v168, v42
	v_cvt_pk_bf16_f32 v14, v15, v13
	ds_write_b32 v171, v14 offset:5168
	v_fma_f32 v14, -v169, v13, v28
	v_fmac_f32_e32 v12, v169, v15
	v_fmac_f32_e32 v14, v168, v15
	v_fmac_f32_e32 v12, v168, v13
	v_cvt_pk_bf16_f32 v13, v14, v12
	ds_write_b32 v171, v13 offset:4896
	v_fma_f32 v13, -v169, v12, v27
	v_fmac_f32_e32 v11, v169, v14
	v_fmac_f32_e32 v13, v168, v14
	v_fmac_f32_e32 v11, v168, v12
	v_cvt_pk_bf16_f32 v12, v13, v11
	ds_write_b32 v171, v12 offset:4624
	v_fma_f32 v12, -v169, v11, v26
	v_fmac_f32_e32 v10, v169, v13
	v_permlane32_swap_b32_e32 v25, v57
	v_permlane32_swap_b32_e32 v9, v41
	v_fmac_f32_e32 v12, v168, v13
	v_fmac_f32_e32 v10, v168, v11
	v_cvt_pk_bf16_f32 v11, v12, v10
	ds_write_b32 v171, v11 offset:4352
	v_fma_f32 v11, -v169, v10, v57
	v_fmac_f32_e32 v41, v169, v12
	v_permlane32_swap_b32_e32 v24, v56
	v_permlane32_swap_b32_e32 v8, v40
	v_fmac_f32_e32 v11, v168, v12
	v_fmac_f32_e32 v41, v168, v10
	v_cvt_pk_bf16_f32 v10, v11, v41
	ds_write_b32 v171, v10 offset:4080
	v_fma_f32 v10, -v169, v41, v56
	v_fmac_f32_e32 v40, v169, v11
	v_permlane32_swap_b32_e32 v23, v55
	v_permlane32_swap_b32_e32 v7, v39
	v_fmac_f32_e32 v10, v168, v11
	v_fmac_f32_e32 v40, v168, v41
	v_cvt_pk_bf16_f32 v11, v10, v40
	ds_write_b32 v171, v11 offset:3808
	v_fma_f32 v11, -v169, v40, v55
	v_fmac_f32_e32 v39, v169, v10
	v_permlane32_swap_b32_e32 v22, v54
	v_permlane32_swap_b32_e32 v6, v38
	v_fmac_f32_e32 v11, v168, v10
	v_fmac_f32_e32 v39, v168, v40
	v_cvt_pk_bf16_f32 v10, v11, v39
	ds_write_b32 v171, v10 offset:3536
	v_fma_f32 v10, -v169, v39, v54
	v_fmac_f32_e32 v38, v169, v11
	v_fmac_f32_e32 v10, v168, v11
	v_fmac_f32_e32 v38, v168, v39
	v_cvt_pk_bf16_f32 v11, v10, v38
	ds_write_b32 v171, v11 offset:3264
	v_fma_f32 v11, -v169, v38, v25
	v_fmac_f32_e32 v9, v169, v10
	v_fmac_f32_e32 v11, v168, v10
	v_fmac_f32_e32 v9, v168, v38
	v_cvt_pk_bf16_f32 v10, v11, v9
	ds_write_b32 v171, v10 offset:2992
	v_fma_f32 v10, -v169, v9, v24
	v_fmac_f32_e32 v8, v169, v11
	v_fmac_f32_e32 v10, v168, v11
	v_fmac_f32_e32 v8, v168, v9
	v_cvt_pk_bf16_f32 v9, v10, v8
	ds_write_b32 v171, v9 offset:2720
	v_fma_f32 v9, -v169, v8, v23
	v_fmac_f32_e32 v7, v169, v10
	v_fmac_f32_e32 v9, v168, v10
	v_fmac_f32_e32 v7, v168, v8
	v_cvt_pk_bf16_f32 v8, v9, v7
	ds_write_b32 v171, v8 offset:2448
	v_fma_f32 v8, -v169, v7, v22
; #define LAS __attribute__((address_space(3)))
; __device__ __forceinline__ unsigned cvt_pk_bf16(float lo, float hi) { unsigned r; asm volatile("v_cvt_pk_bf16_f32 %0, %1, %2" : "=v"(r) : "v"(lo), "v"(hi)); return r; }
; #define LDS_WAIT() asm volatile("s_waitcnt lgkmcnt(0)" ::: "memory")
; __device__ __forceinline__ void bu_block(const bf16x8 ua, const BuFrags& f, float (&BR)[32], float (&BI)[32]) {
;     const f32x16 z = {};
;     const f32x16 R0 = __builtin_amdgcn_mfma_f32_32x32x16_bf16(ua, f.r0, z, 0, 0, 0), R1 = __builtin_amdgcn_mfma_f32_32x32x16_bf16(ua, f.r1, z, 0, 0, 0);
;     const f32x16 I0 = __builtin_amdgcn_mfma_f32_32x32x16_bf16(ua, f.i0, z, 0, 0, 0), I1 = __builtin_amdgcn_mfma_f32_32x32x16_bf16(ua, f.i1, z, 0, 0, 0);
; #pragma unroll
;     for (int r = 0; r < 16; ++r) {
;         auto s = __builtin_amdgcn_permlane32_swap(__float_as_uint(R0[r]), __float_as_uint(R1[r]), false, false);
;         BR[8 * (r >> 2) + (r & 3)] = __uint_as_float(s[0]); BR[8 * (r >> 2) + 4 + (r & 3)] = __uint_as_float(s[1]);
;         auto q = __builtin_amdgcn_permlane32_swap(__float_as_uint(I0[r]), __float_as_uint(I1[r]), false, false);
;         BI[8 * (r >> 2) + (r & 3)] = __uint_as_float(q[0]); BI[8 * (r >> 2) + 4 + (r & 3)] = __uint_as_float(q[1]);
;     }
; }
; template <int DIR> ...
;     ...
;     for (int s = 0; s < 4; ++s) { const int sb = DIR ? 3 - s : s; float BR[32], BI[32];
;         bu_block(ua[s], f, BR, BI);
; #pragma unroll
;         for (int tt = 0; tt < 32; ++tt) { const int t = DIR ? 31 - tt : tt; const float nsr = fmaf(ar, sr, fmaf(-ai, si, BR[t])), nsi = fmaf(ar, si, fmaf(ai, sr, BI[t])); sr = nsr; si = nsi;
;             *(LAS unsigned*)(sl + (t * 136 + 2 * lane) * 2) = cvt_pk_bf16(sr, si); }
;         LDS_WAIT();
; #pragma unroll
;         for (int rb = 0; rb < 2; ++rb)
; #pragma unroll
;             for (int ks = 0; ks < 4; ++ks) { const bf16x8 a = *(const LAS bf16x8*)(sl + ((16 * rb + (lane & 15)) * 136 + 32 * ks + 8 * (lane >> 4)) * 2);
;                 yacc[2 * sb + rb] = __builtin_amdgcn_mfma_f32_16x16x32_bf16(a, cb[ks], yacc[2 * sb + rb], 0, 0, 0); }
;         LDS_WAIT(); }
	v_fmac_f32_e32 v6, v169, v9
	v_permlane32_swap_b32_e32 v21, v53
	v_permlane32_swap_b32_e32 v5, v37
	v_fmac_f32_e32 v8, v168, v9
	v_fmac_f32_e32 v6, v168, v7
	v_cvt_pk_bf16_f32 v7, v8, v6
	ds_write_b32 v171, v7 offset:2176
	v_fma_f32 v7, -v169, v6, v53
	v_fmac_f32_e32 v37, v169, v8
	v_permlane32_swap_b32_e32 v20, v52
	v_permlane32_swap_b32_e32 v4, v36
	v_fmac_f32_e32 v7, v168, v8
	v_fmac_f32_e32 v37, v168, v6
	v_cvt_pk_bf16_f32 v6, v7, v37
	ds_write_b32 v171, v6 offset:1904
	v_fma_f32 v6, -v169, v37, v52
	v_fmac_f32_e32 v36, v169, v7
	v_permlane32_swap_b32_e32 v19, v51
	v_permlane32_swap_b32_e32 v3, v35
	v_fmac_f32_e32 v6, v168, v7
	v_fmac_f32_e32 v36, v168, v37
	v_cvt_pk_bf16_f32 v7, v6, v36
	ds_write_b32 v171, v7 offset:1632
	v_fma_f32 v7, -v169, v36, v51
	v_fmac_f32_e32 v35, v169, v6
	v_permlane32_swap_b32_e32 v18, v50
	v_permlane32_swap_b32_e32 v2, v34
	v_fmac_f32_e32 v7, v168, v6
	v_fmac_f32_e32 v35, v168, v36
	v_cvt_pk_bf16_f32 v6, v7, v35
	ds_write_b32 v171, v6 offset:1360
	v_fma_f32 v6, -v169, v35, v50
	v_fmac_f32_e32 v34, v169, v7
	v_fmac_f32_e32 v6, v168, v7
	v_fmac_f32_e32 v34, v168, v35
	v_cvt_pk_bf16_f32 v7, v6, v34
	ds_write_b32 v171, v7 offset:1088
	v_fma_f32 v7, -v169, v34, v21
	v_fmac_f32_e32 v5, v169, v6
	v_fmac_f32_e32 v7, v168, v6
	v_fmac_f32_e32 v5, v168, v34
	v_cvt_pk_bf16_f32 v6, v7, v5
	ds_write_b32 v171, v6 offset:816
	v_fma_f32 v6, -v169, v5, v20
	v_fmac_f32_e32 v4, v169, v7
	v_fmac_f32_e32 v6, v168, v7
	v_fmac_f32_e32 v4, v168, v5
	v_cvt_pk_bf16_f32 v5, v6, v4
	ds_write_b32 v171, v5 offset:544
	v_fma_f32 v5, -v169, v4, v19
	v_fmac_f32_e32 v3, v169, v6
	v_fmac_f32_e32 v5, v168, v6
	v_fmac_f32_e32 v3, v168, v4
	v_fma_f32 v12, -v169, v3, v18
	v_fmac_f32_e32 v2, v169, v5
	v_cvt_pk_bf16_f32 v4, v5, v3
	ds_write_b32 v171, v4 offset:272
	v_fmac_f32_e32 v12, v168, v5
	v_fmac_f32_e32 v2, v168, v3
	v_cvt_pk_bf16_f32 v3, v12, v2
	ds_write_b32 v171, v3
	s_waitcnt lgkmcnt(0)
	ds_read_b128 v[4:7], v175
	ds_read_b128 v[8:11], v175 offset:64
	s_waitcnt lgkmcnt(1)
	v_mfma_f32_16x16x32_bf16 v[4:7], v[4:7], v[118:121], v[66:69]
	s_waitcnt lgkmcnt(0)
	v_mfma_f32_16x16x32_bf16 v[4:7], v[8:11], v[114:117], v[4:7]
	ds_read_b128 v[8:11], v175 offset:128
	s_waitcnt lgkmcnt(0)
	v_mfma_f32_16x16x32_bf16 v[4:7], v[8:11], v[110:113], v[4:7]
	ds_read_b128 v[8:11], v175 offset:192
	s_waitcnt lgkmcnt(0)
	v_mfma_f32_16x16x32_bf16 v[142:145], v[8:11], v[106:109], v[4:7]
	s_nop 4
	ds_read_b128 v[4:7], v175 offset:4352
	ds_read_b128 v[8:11], v175 offset:4416
	s_waitcnt lgkmcnt(1)
	v_mfma_f32_16x16x32_bf16 v[4:7], v[4:7], v[118:121], v[70:73]
	s_waitcnt vmcnt(2)
	v_mfma_f32_32x32x16_bf16 v[34:49], v[74:77], v[134:137], 0
	v_mfma_f32_32x32x16_bf16 v[50:65], v[74:77], v[130:133], 0
	v_mfma_f32_32x32x16_bf16 v[18:33], v[74:77], v[122:125], 0
	s_nop 10
	v_permlane32_swap_b32_e32 v49, v65
	v_fma_f32 v3, -v169, v2, v65
	v_permlane32_swap_b32_e32 v48, v64
	v_fmac_f32_e32 v3, v168, v12
	v_permlane32_swap_b32_e32 v47, v63
	v_mfma_f32_32x32x16_bf16 v[66:81], v[74:77], v[126:129], 0
	v_permlane32_swap_b32_e32 v46, v62
	v_permlane32_swap_b32_e32 v45, v61
	v_permlane32_swap_b32_e32 v44, v60
	v_permlane32_swap_b32_e32 v43, v59
	s_waitcnt lgkmcnt(0)
	v_mfma_f32_16x16x32_bf16 v[4:7], v[8:11], v[114:117], v[4:7]
	ds_read_b128 v[8:11], v175 offset:4480
	s_nop 4
	v_permlane32_swap_b32_e32 v33, v81
	v_fmac_f32_e32 v81, v169, v12
	s_waitcnt lgkmcnt(0)
	v_mfma_f32_16x16x32_bf16 v[4:7], v[8:11], v[110:113], v[4:7]
	ds_read_b128 v[8:11], v175 offset:4544
	s_waitcnt lgkmcnt(0)
	v_permlane32_swap_b32_e32 v32, v80
	v_fmac_f32_e32 v81, v168, v2
	v_cvt_pk_bf16_f32 v2, v3, v81
	ds_write_b32 v171, v2 offset:8432
	v_fma_f32 v2, -v169, v81, v64
	v_fmac_f32_e32 v80, v169, v3
	v_permlane32_swap_b32_e32 v31, v79
	v_fmac_f32_e32 v2, v168, v3
	v_fmac_f32_e32 v80, v168, v81
	v_cvt_pk_bf16_f32 v3, v2, v80
	ds_write_b32 v171, v3 offset:8160
	v_fma_f32 v3, -v169, v80, v63
	v_fmac_f32_e32 v79, v169, v2
	v_permlane32_swap_b32_e32 v30, v78
	v_fmac_f32_e32 v3, v168, v2
	v_fmac_f32_e32 v79, v168, v80
	v_cvt_pk_bf16_f32 v2, v3, v79
	ds_write_b32 v171, v2 offset:7888
	v_fma_f32 v2, -v169, v79, v62
	v_fmac_f32_e32 v78, v169, v3
	v_fmac_f32_e32 v2, v168, v3
	v_fmac_f32_e32 v78, v168, v79
	v_cvt_pk_bf16_f32 v3, v2, v78
	ds_write_b32 v171, v3 offset:7616
	v_fma_f32 v3, -v169, v78, v49
	v_fmac_f32_e32 v33, v169, v2
	v_fmac_f32_e32 v3, v168, v2
	v_fmac_f32_e32 v33, v168, v78
	v_cvt_pk_bf16_f32 v2, v3, v33
	ds_write_b32 v171, v2 offset:7344
	v_fma_f32 v2, -v169, v33, v48
	v_fmac_f32_e32 v32, v169, v3
	v_fmac_f32_e32 v2, v168, v3
	v_fmac_f32_e32 v32, v168, v33
	v_cvt_pk_bf16_f32 v3, v2, v32
	ds_write_b32 v171, v3 offset:7072
	v_fma_f32 v3, -v169, v32, v47
	v_fmac_f32_e32 v31, v169, v2
	v_fmac_f32_e32 v3, v168, v2
	v_fmac_f32_e32 v31, v168, v32
	v_cvt_pk_bf16_f32 v2, v3, v31
	ds_write_b32 v171, v2 offset:6800
	v_fma_f32 v2, -v169, v31, v46
	v_fmac_f32_e32 v30, v169, v3
	v_permlane32_swap_b32_e32 v29, v77
	v_fmac_f32_e32 v2, v168, v3
	v_fmac_f32_e32 v30, v168, v31
	v_cvt_pk_bf16_f32 v3, v2, v30
	ds_write_b32 v171, v3 offset:6528
	v_fma_f32 v3, -v169, v30, v61
	v_fmac_f32_e32 v77, v169, v2
	v_permlane32_swap_b32_e32 v28, v76
	v_fmac_f32_e32 v3, v168, v2
	v_fmac_f32_e32 v77, v168, v30
	v_cvt_pk_bf16_f32 v2, v3, v77
	ds_write_b32 v171, v2 offset:6256
	v_fma_f32 v2, -v169, v77, v60
	v_fmac_f32_e32 v76, v169, v3
	v_permlane32_swap_b32_e32 v27, v75
	v_fmac_f32_e32 v2, v168, v3
	v_fmac_f32_e32 v76, v168, v77
	v_cvt_pk_bf16_f32 v3, v2, v76
	ds_write_b32 v171, v3 offset:5984
	v_fma_f32 v3, -v169, v76, v59
	v_fmac_f32_e32 v75, v169, v2
	v_permlane32_swap_b32_e32 v42, v58
	v_permlane32_swap_b32_e32 v26, v74
; #define LAS __attribute__((address_space(3)))
; __device__ __forceinline__ unsigned cvt_pk_bf16(float lo, float hi) { unsigned r; asm volatile("v_cvt_pk_bf16_f32 %0, %1, %2" : "=v"(r) : "v"(lo), "v"(hi)); return r; }
; #define LDS_WAIT() asm volatile("s_waitcnt lgkmcnt(0)" ::: "memory")
; __device__ __forceinline__ void bu_block(const bf16x8 ua, const BuFrags& f, float (&BR)[32], float (&BI)[32]) {
;     const f32x16 z = {};
;     const f32x16 R0 = __builtin_amdgcn_mfma_f32_32x32x16_bf16(ua, f.r0, z, 0, 0, 0), R1 = __builtin_amdgcn_mfma_f32_32x32x16_bf16(ua, f.r1, z, 0, 0, 0);
;     const f32x16 I0 = __builtin_amdgcn_mfma_f32_32x32x16_bf16(ua, f.i0, z, 0, 0, 0), I1 = __builtin_amdgcn_mfma_f32_32x32x16_bf16(ua, f.i1, z, 0, 0, 0);
; #pragma unroll
;     for (int r = 0; r < 16; ++r) {
;         auto s = __builtin_amdgcn_permlane32_swap(__float_as_uint(R0[r]), __float_as_uint(R1[r]), false, false);
;         BR[8 * (r >> 2) + (r & 3)] = __uint_as_float(s[0]); BR[8 * (r >> 2) + 4 + (r & 3)] = __uint_as_float(s[1]);
;         auto q = __builtin_amdgcn_permlane32_swap(__float_as_uint(I0[r]), __float_as_uint(I1[r]), false, false);
;         BI[8 * (r >> 2) + (r & 3)] = __uint_as_float(q[0]); BI[8 * (r >> 2) + 4 + (r & 3)] = __uint_as_float(q[1]);
;     }
; }
; template <int DIR> ...
;     ...
;     for (int s = 0; s < 4; ++s) { const int sb = DIR ? 3 - s : s; float BR[32], BI[32];
;         bu_block(ua[s], f, BR, BI);
; #pragma unroll
;         for (int tt = 0; tt < 32; ++tt) { const int t = DIR ? 31 - tt : tt; const float nsr = fmaf(ar, sr, fmaf(-ai, si, BR[t])), nsi = fmaf(ar, si, fmaf(ai, sr, BI[t])); sr = nsr; si = nsi;
;             *(LAS unsigned*)(sl + (t * 136 + 2 * lane) * 2) = cvt_pk_bf16(sr, si); }
;         LDS_WAIT();
; #pragma unroll
;         for (int rb = 0; rb < 2; ++rb)
; #pragma unroll
;             for (int ks = 0; ks < 4; ++ks) { const bf16x8 a = *(const LAS bf16x8*)(sl + ((16 * rb + (lane & 15)) * 136 + 32 * ks + 8 * (lane >> 4)) * 2);
;                 yacc[2 * sb + rb] = __builtin_amdgcn_mfma_f32_16x16x32_bf16(a, cb[ks], yacc[2 * sb + rb], 0, 0, 0); }
;         LDS_WAIT(); }
	v_fmac_f32_e32 v3, v168, v2
	v_fmac_f32_e32 v75, v168, v76
	v_cvt_pk_bf16_f32 v2, v3, v75
	ds_write_b32 v171, v2 offset:5712
	v_fma_f32 v2, -v169, v75, v58
	v_fmac_f32_e32 v74, v169, v3
	v_fmac_f32_e32 v2, v168, v3
	v_fmac_f32_e32 v74, v168, v75
	v_cvt_pk_bf16_f32 v3, v2, v74
	ds_write_b32 v171, v3 offset:5440
	v_fma_f32 v3, -v169, v74, v45
	v_fmac_f32_e32 v29, v169, v2
	v_fmac_f32_e32 v3, v168, v2
	v_fmac_f32_e32 v29, v168, v74
	v_cvt_pk_bf16_f32 v2, v3, v29
	ds_write_b32 v171, v2 offset:5168
	v_fma_f32 v2, -v169, v29, v44
	v_fmac_f32_e32 v28, v169, v3
	v_fmac_f32_e32 v2, v168, v3
	v_fmac_f32_e32 v28, v168, v29
	v_cvt_pk_bf16_f32 v3, v2, v28
	ds_write_b32 v171, v3 offset:4896
	v_fma_f32 v3, -v169, v28, v43
	v_fmac_f32_e32 v27, v169, v2
	v_fmac_f32_e32 v3, v168, v2
	v_fmac_f32_e32 v27, v168, v28
	v_cvt_pk_bf16_f32 v2, v3, v27
	ds_write_b32 v171, v2 offset:4624
	v_fma_f32 v2, -v169, v27, v42
	v_fmac_f32_e32 v26, v169, v3
	v_permlane32_swap_b32_e32 v41, v57
	v_permlane32_swap_b32_e32 v25, v73
	v_fmac_f32_e32 v2, v168, v3
	v_fmac_f32_e32 v26, v168, v27
	v_cvt_pk_bf16_f32 v3, v2, v26
	ds_write_b32 v171, v3 offset:4352
	v_fma_f32 v3, -v169, v26, v57
	v_fmac_f32_e32 v73, v169, v2
	v_permlane32_swap_b32_e32 v40, v56
	v_permlane32_swap_b32_e32 v24, v72
	v_fmac_f32_e32 v3, v168, v2
	v_fmac_f32_e32 v73, v168, v26
	v_cvt_pk_bf16_f32 v2, v3, v73
	ds_write_b32 v171, v2 offset:4080
	v_fma_f32 v2, -v169, v73, v56
	v_fmac_f32_e32 v72, v169, v3
	v_permlane32_swap_b32_e32 v39, v55
	v_permlane32_swap_b32_e32 v23, v71
	v_fmac_f32_e32 v2, v168, v3
	v_fmac_f32_e32 v72, v168, v73
	v_cvt_pk_bf16_f32 v3, v2, v72
	ds_write_b32 v171, v3 offset:3808
	v_fma_f32 v3, -v169, v72, v55
	v_fmac_f32_e32 v71, v169, v2
	v_permlane32_swap_b32_e32 v38, v54
	v_permlane32_swap_b32_e32 v22, v70
	v_fmac_f32_e32 v3, v168, v2
	v_fmac_f32_e32 v71, v168, v72
	v_cvt_pk_bf16_f32 v2, v3, v71
	ds_write_b32 v171, v2 offset:3536
	v_fma_f32 v2, -v169, v71, v54
	v_fmac_f32_e32 v70, v169, v3
	v_fmac_f32_e32 v2, v168, v3
	v_fmac_f32_e32 v70, v168, v71
	v_cvt_pk_bf16_f32 v3, v2, v70
	ds_write_b32 v171, v3 offset:3264
	v_fma_f32 v3, -v169, v70, v41
	v_fmac_f32_e32 v25, v169, v2
	v_fmac_f32_e32 v3, v168, v2
	v_fmac_f32_e32 v25, v168, v70
	v_cvt_pk_bf16_f32 v2, v3, v25
	ds_write_b32 v171, v2 offset:2992
	v_fma_f32 v2, -v169, v25, v40
	v_fmac_f32_e32 v24, v169, v3
	v_fmac_f32_e32 v2, v168, v3
	v_fmac_f32_e32 v24, v168, v25
	v_cvt_pk_bf16_f32 v3, v2, v24
	ds_write_b32 v171, v3 offset:2720
	v_fma_f32 v3, -v169, v24, v39
	v_fmac_f32_e32 v23, v169, v2
	v_fmac_f32_e32 v3, v168, v2
	v_fmac_f32_e32 v23, v168, v24
	v_cvt_pk_bf16_f32 v2, v3, v23
	ds_write_b32 v171, v2 offset:2448
	v_fma_f32 v2, -v169, v23, v38
	v_fmac_f32_e32 v22, v169, v3
	v_permlane32_swap_b32_e32 v37, v53
	v_permlane32_swap_b32_e32 v21, v69
	v_fmac_f32_e32 v2, v168, v3
	v_fmac_f32_e32 v22, v168, v23
	v_cvt_pk_bf16_f32 v3, v2, v22
	ds_write_b32 v171, v3 offset:2176
	v_fma_f32 v3, -v169, v22, v53
	v_fmac_f32_e32 v69, v169, v2
	v_permlane32_swap_b32_e32 v36, v52
	v_permlane32_swap_b32_e32 v20, v68
	v_fmac_f32_e32 v3, v168, v2
	v_fmac_f32_e32 v69, v168, v22
	v_cvt_pk_bf16_f32 v2, v3, v69
	ds_write_b32 v171, v2 offset:1904
	v_fma_f32 v2, -v169, v69, v52
	v_fmac_f32_e32 v68, v169, v3
	v_permlane32_swap_b32_e32 v35, v51
	v_permlane32_swap_b32_e32 v19, v67
	v_fmac_f32_e32 v2, v168, v3
	v_fmac_f32_e32 v68, v168, v69
	v_cvt_pk_bf16_f32 v3, v2, v68
	ds_write_b32 v171, v3 offset:1632
	v_fma_f32 v3, -v169, v68, v51
	v_fmac_f32_e32 v67, v169, v2
	v_permlane32_swap_b32_e32 v34, v50
	v_permlane32_swap_b32_e32 v18, v66
	v_fmac_f32_e32 v3, v168, v2
	v_fmac_f32_e32 v67, v168, v68
	v_cvt_pk_bf16_f32 v2, v3, v67
	ds_write_b32 v171, v2 offset:1360
	v_fma_f32 v2, -v169, v67, v50
	v_fmac_f32_e32 v66, v169, v3
	v_fmac_f32_e32 v2, v168, v3
	v_fmac_f32_e32 v66, v168, v67
	v_cvt_pk_bf16_f32 v3, v2, v66
	ds_write_b32 v171, v3 offset:1088
	v_fma_f32 v3, -v169, v66, v37
	v_fmac_f32_e32 v21, v169, v2
	v_fmac_f32_e32 v3, v168, v2
	v_fmac_f32_e32 v21, v168, v66
	v_cvt_pk_bf16_f32 v2, v3, v21
	ds_write_b32 v171, v2 offset:816
	v_fma_f32 v2, -v169, v21, v36
	v_fmac_f32_e32 v20, v169, v3
	v_fmac_f32_e32 v2, v168, v3
	v_fmac_f32_e32 v20, v168, v21
	v_cvt_pk_bf16_f32 v3, v2, v20
	ds_write_b32 v171, v3 offset:544
	v_fma_f32 v3, -v169, v20, v35
	v_fmac_f32_e32 v19, v169, v2
	v_fmac_f32_e32 v3, v168, v2
	v_fmac_f32_e32 v19, v168, v20
	v_cvt_pk_bf16_f32 v2, v3, v19
	v_fma_f32 v76, -v169, v19, v34
	v_fmac_f32_e32 v18, v169, v3
	ds_write_b32 v171, v2 offset:272
	v_fmac_f32_e32 v76, v168, v3
	v_fmac_f32_e32 v18, v168, v19
	v_cvt_pk_bf16_f32 v2, v76, v18
	ds_write_b32 v171, v2
	s_waitcnt lgkmcnt(0)
	s_waitcnt lgkmcnt(14)
	v_mfma_f32_16x16x32_bf16 v[138:141], v[8:11], v[106:109], v[4:7]
	s_nop 2
	ds_read_b128 v[2:5], v175
	ds_read_b128 v[6:9], v175 offset:64
	s_waitcnt lgkmcnt(1)
	v_mfma_f32_16x16x32_bf16 v[2:5], v[2:5], v[118:121], v[98:101]
	s_waitcnt lgkmcnt(0)
	v_mfma_f32_16x16x32_bf16 v[2:5], v[6:9], v[114:117], v[2:5]
	ds_read_b128 v[6:9], v175 offset:128
	s_waitcnt lgkmcnt(0)
	v_mfma_f32_16x16x32_bf16 v[2:5], v[6:9], v[110:113], v[2:5]
	ds_read_b128 v[6:9], v175 offset:192
	s_waitcnt lgkmcnt(0)
	v_mfma_f32_16x16x32_bf16 v[72:75], v[6:9], v[106:109], v[2:5]
	s_nop 4
	ds_read_b128 v[2:5], v175 offset:4352
	ds_read_b128 v[6:9], v175 offset:4416
	s_waitcnt lgkmcnt(1)
	v_mfma_f32_16x16x32_bf16 v[2:5], v[2:5], v[118:121], v[102:105]
	s_waitcnt lgkmcnt(0)
	v_mfma_f32_16x16x32_bf16 v[2:5], v[6:9], v[114:117], v[2:5]
	ds_read_b128 v[6:9], v175 offset:4480
	s_waitcnt lgkmcnt(0)
	v_mfma_f32_16x16x32_bf16 v[2:5], v[6:9], v[110:113], v[2:5]
	ds_read_b128 v[6:9], v175 offset:4544
	s_waitcnt lgkmcnt(0)
; #define LAS __attribute__((address_space(3)))
; __device__ __forceinline__ unsigned cvt_pk_bf16(float lo, float hi) { unsigned r; asm volatile("v_cvt_pk_bf16_f32 %0, %1, %2" : "=v"(r) : "v"(lo), "v"(hi)); return r; }
; #define LDS_WAIT() asm volatile("s_waitcnt lgkmcnt(0)" ::: "memory")
; __device__ __forceinline__ void bu_block(const bf16x8 ua, const BuFrags& f, float (&BR)[32], float (&BI)[32]) {
;     const f32x16 z = {};
;     const f32x16 R0 = __builtin_amdgcn_mfma_f32_32x32x16_bf16(ua, f.r0, z, 0, 0, 0), R1 = __builtin_amdgcn_mfma_f32_32x32x16_bf16(ua, f.r1, z, 0, 0, 0);
;     const f32x16 I0 = __builtin_amdgcn_mfma_f32_32x32x16_bf16(ua, f.i0, z, 0, 0, 0), I1 = __builtin_amdgcn_mfma_f32_32x32x16_bf16(ua, f.i1, z, 0, 0, 0);
; #pragma unroll
;     for (int r = 0; r < 16; ++r) {
;         auto s = __builtin_amdgcn_permlane32_swap(__float_as_uint(R0[r]), __float_as_uint(R1[r]), false, false);
;         BR[8 * (r >> 2) + (r & 3)] = __uint_as_float(s[0]); BR[8 * (r >> 2) + 4 + (r & 3)] = __uint_as_float(s[1]);
;         auto q = __builtin_amdgcn_permlane32_swap(__float_as_uint(I0[r]), __float_as_uint(I1[r]), false, false);
;         BI[8 * (r >> 2) + (r & 3)] = __uint_as_float(q[0]); BI[8 * (r >> 2) + 4 + (r & 3)] = __uint_as_float(q[1]);
;     }
; }
; template <int DIR> ...
;     ...
;     for (int s = 0; s < 4; ++s) { const int sb = DIR ? 3 - s : s; float BR[32], BI[32];
;         bu_block(ua[s], f, BR, BI);
; #pragma unroll
;         for (int tt = 0; tt < 32; ++tt) { const int t = DIR ? 31 - tt : tt; const float nsr = fmaf(ar, sr, fmaf(-ai, si, BR[t])), nsi = fmaf(ar, si, fmaf(ai, sr, BI[t])); sr = nsr; si = nsi;
;             *(LAS unsigned*)(sl + (t * 136 + 2 * lane) * 2) = cvt_pk_bf16(sr, si); }
;         LDS_WAIT();
; #pragma unroll
;         for (int rb = 0; rb < 2; ++rb)
; #pragma unroll
;             for (int ks = 0; ks < 4; ++ks) { const bf16x8 a = *(const LAS bf16x8*)(sl + ((16 * rb + (lane & 15)) * 136 + 32 * ks + 8 * (lane >> 4)) * 2);
;                 yacc[2 * sb + rb] = __builtin_amdgcn_mfma_f32_16x16x32_bf16(a, cb[ks], yacc[2 * sb + rb], 0, 0, 0); }
;         LDS_WAIT(); }
	s_waitcnt lgkmcnt(0)
	v_mfma_f32_16x16x32_bf16 v[68:71], v[6:9], v[106:109], v[2:5]
	s_waitcnt vmcnt(1)
	v_mfma_f32_32x32x16_bf16 v[20:35], v[150:153], v[134:137], 0
	v_mfma_f32_32x32x16_bf16 v[52:67], v[150:153], v[130:133], 0
	v_mfma_f32_32x32x16_bf16 v[2:17], v[150:153], v[122:125], 0
	s_nop 10
	v_permlane32_swap_b32_e32 v35, v67
	v_fma_f32 v19, -v169, v18, v67
	v_permlane32_swap_b32_e32 v34, v66
	v_fmac_f32_e32 v19, v168, v76
	v_permlane32_swap_b32_e32 v33, v65
	v_mfma_f32_32x32x16_bf16 v[36:51], v[150:153], v[126:129], 0
	v_permlane32_swap_b32_e32 v32, v64
	v_permlane32_swap_b32_e32 v31, v63
	v_permlane32_swap_b32_e32 v30, v62
	v_permlane32_swap_b32_e32 v29, v61
	s_nop 7
	v_permlane32_swap_b32_e32 v17, v51
	v_fmac_f32_e32 v51, v169, v76
	v_permlane32_swap_b32_e32 v16, v50
	v_fmac_f32_e32 v51, v168, v18
	v_cvt_pk_bf16_f32 v18, v19, v51
	ds_write_b32 v171, v18 offset:8432
	v_fma_f32 v18, -v169, v51, v66
	v_fmac_f32_e32 v50, v169, v19
	v_permlane32_swap_b32_e32 v15, v49
	v_fmac_f32_e32 v18, v168, v19
	v_fmac_f32_e32 v50, v168, v51
	v_cvt_pk_bf16_f32 v19, v18, v50
	ds_write_b32 v171, v19 offset:8160
	v_fma_f32 v19, -v169, v50, v65
	v_fmac_f32_e32 v49, v169, v18
	v_permlane32_swap_b32_e32 v14, v48
	v_fmac_f32_e32 v19, v168, v18
	v_fmac_f32_e32 v49, v168, v50
	v_cvt_pk_bf16_f32 v18, v19, v49
	ds_write_b32 v171, v18 offset:7888
	v_fma_f32 v18, -v169, v49, v64
	v_fmac_f32_e32 v48, v169, v19
	v_fmac_f32_e32 v18, v168, v19
	v_fmac_f32_e32 v48, v168, v49
	v_cvt_pk_bf16_f32 v19, v18, v48
	ds_write_b32 v171, v19 offset:7616
	v_fma_f32 v19, -v169, v48, v35
	v_fmac_f32_e32 v17, v169, v18
	v_fmac_f32_e32 v19, v168, v18
	v_fmac_f32_e32 v17, v168, v48
	v_cvt_pk_bf16_f32 v18, v19, v17
	ds_write_b32 v171, v18 offset:7344
	v_fma_f32 v18, -v169, v17, v34
	v_fmac_f32_e32 v16, v169, v19
	v_fmac_f32_e32 v18, v168, v19
	v_fmac_f32_e32 v16, v168, v17
	v_cvt_pk_bf16_f32 v17, v18, v16
	ds_write_b32 v171, v17 offset:7072
	v_fma_f32 v17, -v169, v16, v33
	v_fmac_f32_e32 v15, v169, v18
	v_fmac_f32_e32 v17, v168, v18
	v_fmac_f32_e32 v15, v168, v16
	v_cvt_pk_bf16_f32 v16, v17, v15
	ds_write_b32 v171, v16 offset:6800
	v_fma_f32 v16, -v169, v15, v32
	v_fmac_f32_e32 v14, v169, v17
	v_permlane32_swap_b32_e32 v13, v47
	v_fmac_f32_e32 v16, v168, v17
	v_fmac_f32_e32 v14, v168, v15
	v_cvt_pk_bf16_f32 v15, v16, v14
	ds_write_b32 v171, v15 offset:6528
	v_fma_f32 v15, -v169, v14, v63
	v_fmac_f32_e32 v47, v169, v16
	v_permlane32_swap_b32_e32 v12, v46
	v_fmac_f32_e32 v15, v168, v16
	v_fmac_f32_e32 v47, v168, v14
	v_cvt_pk_bf16_f32 v14, v15, v47
	ds_write_b32 v171, v14 offset:6256
	v_fma_f32 v14, -v169, v47, v62
	v_fmac_f32_e32 v46, v169, v15
	v_permlane32_swap_b32_e32 v11, v45
	v_fmac_f32_e32 v14, v168, v15
	v_fmac_f32_e32 v46, v168, v47
	v_cvt_pk_bf16_f32 v15, v14, v46
	ds_write_b32 v171, v15 offset:5984
	v_fma_f32 v15, -v169, v46, v61
	v_fmac_f32_e32 v45, v169, v14
	v_permlane32_swap_b32_e32 v28, v60
	v_permlane32_swap_b32_e32 v10, v44
	v_fmac_f32_e32 v15, v168, v14
	v_fmac_f32_e32 v45, v168, v46
	v_cvt_pk_bf16_f32 v14, v15, v45
	ds_write_b32 v171, v14 offset:5712
	v_fma_f32 v14, -v169, v45, v60
	v_fmac_f32_e32 v44, v169, v15
	v_fmac_f32_e32 v14, v168, v15
	v_fmac_f32_e32 v44, v168, v45
	v_cvt_pk_bf16_f32 v15, v14, v44
	ds_write_b32 v171, v15 offset:5440
	v_fma_f32 v15, -v169, v44, v31
	v_fmac_f32_e32 v13, v169, v14
	v_fmac_f32_e32 v15, v168, v14
	v_fmac_f32_e32 v13, v168, v44
	v_cvt_pk_bf16_f32 v14, v15, v13
	ds_write_b32 v171, v14 offset:5168
	v_fma_f32 v14, -v169, v13, v30
	v_fmac_f32_e32 v12, v169, v15
	v_fmac_f32_e32 v14, v168, v15
	v_fmac_f32_e32 v12, v168, v13
	v_cvt_pk_bf16_f32 v13, v14, v12
	ds_write_b32 v171, v13 offset:4896
	v_fma_f32 v13, -v169, v12, v29
	v_fmac_f32_e32 v11, v169, v14
	v_fmac_f32_e32 v13, v168, v14
	v_fmac_f32_e32 v11, v168, v12
	v_cvt_pk_bf16_f32 v12, v13, v11
	ds_write_b32 v171, v12 offset:4624
	v_fma_f32 v12, -v169, v11, v28
	v_fmac_f32_e32 v10, v169, v13
	v_permlane32_swap_b32_e32 v27, v59
	v_permlane32_swap_b32_e32 v9, v43
	v_fmac_f32_e32 v12, v168, v13
	v_fmac_f32_e32 v10, v168, v11
	v_cvt_pk_bf16_f32 v11, v12, v10
	ds_write_b32 v171, v11 offset:4352
	v_fma_f32 v11, -v169, v10, v59
	v_fmac_f32_e32 v43, v169, v12
	v_permlane32_swap_b32_e32 v26, v58
	v_permlane32_swap_b32_e32 v8, v42
	v_fmac_f32_e32 v11, v168, v12
	v_fmac_f32_e32 v43, v168, v10
	v_cvt_pk_bf16_f32 v10, v11, v43
	ds_write_b32 v171, v10 offset:4080
	v_fma_f32 v10, -v169, v43, v58
	v_fmac_f32_e32 v42, v169, v11
	v_permlane32_swap_b32_e32 v25, v57
	v_permlane32_swap_b32_e32 v7, v41
	v_fmac_f32_e32 v10, v168, v11
	v_fmac_f32_e32 v42, v168, v43
	v_cvt_pk_bf16_f32 v11, v10, v42
	ds_write_b32 v171, v11 offset:3808
	v_fma_f32 v11, -v169, v42, v57
	v_fmac_f32_e32 v41, v169, v10
	v_permlane32_swap_b32_e32 v24, v56
	v_permlane32_swap_b32_e32 v6, v40
	v_fmac_f32_e32 v11, v168, v10
	v_fmac_f32_e32 v41, v168, v42
	v_cvt_pk_bf16_f32 v10, v11, v41
	ds_write_b32 v171, v10 offset:3536
	v_fma_f32 v10, -v169, v41, v56
	v_fmac_f32_e32 v40, v169, v11
	v_fmac_f32_e32 v10, v168, v11
	v_fmac_f32_e32 v40, v168, v41
	v_cvt_pk_bf16_f32 v11, v10, v40
	ds_write_b32 v171, v11 offset:3264
	v_fma_f32 v11, -v169, v40, v27
	v_fmac_f32_e32 v9, v169, v10
	v_fmac_f32_e32 v11, v168, v10
	v_fmac_f32_e32 v9, v168, v40
	v_cvt_pk_bf16_f32 v10, v11, v9
	ds_write_b32 v171, v10 offset:2992
	v_fma_f32 v10, -v169, v9, v26
	v_fmac_f32_e32 v8, v169, v11
	v_fmac_f32_e32 v10, v168, v11
	v_fmac_f32_e32 v8, v168, v9
	v_cvt_pk_bf16_f32 v9, v10, v8
	ds_write_b32 v171, v9 offset:2720
	v_fma_f32 v9, -v169, v8, v25
	v_fmac_f32_e32 v7, v169, v10
	v_fmac_f32_e32 v9, v168, v10
	v_fmac_f32_e32 v7, v168, v8
	v_cvt_pk_bf16_f32 v8, v9, v7
; #define LAS __attribute__((address_space(3)))
; __device__ __forceinline__ unsigned cvt_pk_bf16(float lo, float hi) { unsigned r; asm volatile("v_cvt_pk_bf16_f32 %0, %1, %2" : "=v"(r) : "v"(lo), "v"(hi)); return r; }
; #define LDS_WAIT() asm volatile("s_waitcnt lgkmcnt(0)" ::: "memory")
; __device__ __forceinline__ void bu_block(const bf16x8 ua, const BuFrags& f, float (&BR)[32], float (&BI)[32]) {
;     const f32x16 z = {};
;     const f32x16 R0 = __builtin_amdgcn_mfma_f32_32x32x16_bf16(ua, f.r0, z, 0, 0, 0), R1 = __builtin_amdgcn_mfma_f32_32x32x16_bf16(ua, f.r1, z, 0, 0, 0);
;     const f32x16 I0 = __builtin_amdgcn_mfma_f32_32x32x16_bf16(ua, f.i0, z, 0, 0, 0), I1 = __builtin_amdgcn_mfma_f32_32x32x16_bf16(ua, f.i1, z, 0, 0, 0);
; #pragma unroll
;     for (int r = 0; r < 16; ++r) {
;         auto s = __builtin_amdgcn_permlane32_swap(__float_as_uint(R0[r]), __float_as_uint(R1[r]), false, false);
;         BR[8 * (r >> 2) + (r & 3)] = __uint_as_float(s[0]); BR[8 * (r >> 2) + 4 + (r & 3)] = __uint_as_float(s[1]);
;         auto q = __builtin_amdgcn_permlane32_swap(__float_as_uint(I0[r]), __float_as_uint(I1[r]), false, false);
;         BI[8 * (r >> 2) + (r & 3)] = __uint_as_float(q[0]); BI[8 * (r >> 2) + 4 + (r & 3)] = __uint_as_float(q[1]);
;     }
; }
; template <int DIR> ...
;     ...
;     for (int s = 0; s < 4; ++s) { const int sb = DIR ? 3 - s : s; float BR[32], BI[32];
;         bu_block(ua[s], f, BR, BI);
; #pragma unroll
;         for (int tt = 0; tt < 32; ++tt) { const int t = DIR ? 31 - tt : tt; const float nsr = fmaf(ar, sr, fmaf(-ai, si, BR[t])), nsi = fmaf(ar, si, fmaf(ai, sr, BI[t])); sr = nsr; si = nsi;
;             *(LAS unsigned*)(sl + (t * 136 + 2 * lane) * 2) = cvt_pk_bf16(sr, si); }
;         LDS_WAIT();
; #pragma unroll
;         for (int rb = 0; rb < 2; ++rb)
; #pragma unroll
;             for (int ks = 0; ks < 4; ++ks) { const bf16x8 a = *(const LAS bf16x8*)(sl + ((16 * rb + (lane & 15)) * 136 + 32 * ks + 8 * (lane >> 4)) * 2);
;                 yacc[2 * sb + rb] = __builtin_amdgcn_mfma_f32_16x16x32_bf16(a, cb[ks], yacc[2 * sb + rb], 0, 0, 0); }
;         LDS_WAIT(); }
	ds_write_b32 v171, v8 offset:2448
	v_fma_f32 v8, -v169, v7, v24
	v_fmac_f32_e32 v6, v169, v9
	v_permlane32_swap_b32_e32 v23, v55
	v_permlane32_swap_b32_e32 v5, v39
	v_fmac_f32_e32 v8, v168, v9
	v_fmac_f32_e32 v6, v168, v7
	v_cvt_pk_bf16_f32 v7, v8, v6
	ds_write_b32 v171, v7 offset:2176
	v_fma_f32 v7, -v169, v6, v55
	v_fmac_f32_e32 v39, v169, v8
	v_permlane32_swap_b32_e32 v22, v54
	v_permlane32_swap_b32_e32 v4, v38
	v_fmac_f32_e32 v7, v168, v8
	v_fmac_f32_e32 v39, v168, v6
	v_cvt_pk_bf16_f32 v6, v7, v39
	ds_write_b32 v171, v6 offset:1904
	v_fma_f32 v6, -v169, v39, v54
	v_fmac_f32_e32 v38, v169, v7
	v_permlane32_swap_b32_e32 v21, v53
	v_permlane32_swap_b32_e32 v3, v37
	v_fmac_f32_e32 v6, v168, v7
	v_fmac_f32_e32 v38, v168, v39
	v_cvt_pk_bf16_f32 v7, v6, v38
	ds_write_b32 v171, v7 offset:1632
	v_fma_f32 v7, -v169, v38, v53
	v_fmac_f32_e32 v37, v169, v6
	v_permlane32_swap_b32_e32 v20, v52
	v_permlane32_swap_b32_e32 v2, v36
	v_fmac_f32_e32 v7, v168, v6
	v_fmac_f32_e32 v37, v168, v38
	v_cvt_pk_bf16_f32 v6, v7, v37
	ds_write_b32 v171, v6 offset:1360
	v_fma_f32 v6, -v169, v37, v52
	v_fmac_f32_e32 v36, v169, v7
	v_fmac_f32_e32 v6, v168, v7
	v_fmac_f32_e32 v36, v168, v37
	v_cvt_pk_bf16_f32 v7, v6, v36
	ds_write_b32 v171, v7 offset:1088
	v_fma_f32 v7, -v169, v36, v23
	v_fmac_f32_e32 v5, v169, v6
	v_fmac_f32_e32 v7, v168, v6
	v_fmac_f32_e32 v5, v168, v36
	v_cvt_pk_bf16_f32 v6, v7, v5
	ds_write_b32 v171, v6 offset:816
	v_fma_f32 v6, -v169, v5, v22
	v_fmac_f32_e32 v4, v169, v7
	v_fmac_f32_e32 v6, v168, v7
	v_fmac_f32_e32 v4, v168, v5
	v_cvt_pk_bf16_f32 v5, v6, v4
	ds_write_b32 v171, v5 offset:544
	v_fma_f32 v5, -v169, v4, v21
	v_fmac_f32_e32 v3, v169, v6
	v_fmac_f32_e32 v5, v168, v6
	v_fmac_f32_e32 v3, v168, v4
	v_fma_f32 v80, -v169, v3, v20
	v_fmac_f32_e32 v2, v169, v5
	v_cvt_pk_bf16_f32 v4, v5, v3
	ds_write_b32 v171, v4 offset:272
	v_fmac_f32_e32 v80, v168, v5
	v_fmac_f32_e32 v2, v168, v3
	v_cvt_pk_bf16_f32 v3, v80, v2
	ds_write_b32 v171, v3
	s_waitcnt lgkmcnt(0)
	ds_read_b128 v[4:7], v175
	ds_read_b128 v[8:11], v175 offset:64
	s_waitcnt lgkmcnt(1)
	v_mfma_f32_16x16x32_bf16 v[4:7], v[4:7], v[118:121], v[90:93]
	s_waitcnt lgkmcnt(0)
	v_mfma_f32_16x16x32_bf16 v[4:7], v[8:11], v[114:117], v[4:7]
	ds_read_b128 v[8:11], v175 offset:128
	s_waitcnt lgkmcnt(0)
	v_mfma_f32_16x16x32_bf16 v[4:7], v[8:11], v[110:113], v[4:7]
	ds_read_b128 v[8:11], v175 offset:192
	s_waitcnt lgkmcnt(0)
	v_mfma_f32_16x16x32_bf16 v[90:93], v[8:11], v[106:109], v[4:7]
	s_nop 4
	ds_read_b128 v[4:7], v175 offset:4352
	ds_read_b128 v[8:11], v175 offset:4416
	s_waitcnt lgkmcnt(1)
	v_mfma_f32_16x16x32_bf16 v[4:7], v[4:7], v[118:121], v[94:97]
	s_waitcnt lgkmcnt(0)
	v_mfma_f32_16x16x32_bf16 v[4:7], v[8:11], v[114:117], v[4:7]
	ds_read_b128 v[8:11], v175 offset:4480
	s_waitcnt lgkmcnt(0)
	v_mfma_f32_16x16x32_bf16 v[4:7], v[8:11], v[110:113], v[4:7]
	ds_read_b128 v[8:11], v175 offset:4544
	s_waitcnt lgkmcnt(0)
	s_waitcnt lgkmcnt(0)
	v_mfma_f32_16x16x32_bf16 v[76:79], v[8:11], v[106:109], v[4:7]
	s_waitcnt vmcnt(0)
	v_mfma_f32_32x32x16_bf16 v[4:19], v[146:149], v[134:137], 0
	v_mfma_f32_32x32x16_bf16 v[52:67], v[146:149], v[130:133], 0
	v_mfma_f32_32x32x16_bf16 v[20:35], v[146:149], v[122:125], 0
	s_nop 10
	v_permlane32_swap_b32_e32 v19, v67
	v_fma_f32 v3, -v169, v2, v67
	v_permlane32_swap_b32_e32 v18, v66
	v_fmac_f32_e32 v3, v168, v80
	v_permlane32_swap_b32_e32 v17, v65
	v_mfma_f32_32x32x16_bf16 v[36:51], v[146:149], v[126:129], 0
	v_permlane32_swap_b32_e32 v16, v64
	v_permlane32_swap_b32_e32 v15, v63
	v_permlane32_swap_b32_e32 v14, v62
	v_permlane32_swap_b32_e32 v13, v61
	s_nop 7
	v_permlane32_swap_b32_e32 v35, v51
	v_fmac_f32_e32 v51, v169, v80
	v_permlane32_swap_b32_e32 v34, v50
	v_fmac_f32_e32 v51, v168, v2
	v_cvt_pk_bf16_f32 v2, v3, v51
	ds_write_b32 v171, v2 offset:8432
	v_fma_f32 v2, -v169, v51, v66
	v_fmac_f32_e32 v50, v169, v3
	v_permlane32_swap_b32_e32 v33, v49
	v_fmac_f32_e32 v2, v168, v3
	v_fmac_f32_e32 v50, v168, v51
	v_cvt_pk_bf16_f32 v3, v2, v50
	ds_write_b32 v171, v3 offset:8160
	v_fma_f32 v3, -v169, v50, v65
	v_fmac_f32_e32 v49, v169, v2
	v_permlane32_swap_b32_e32 v32, v48
	v_fmac_f32_e32 v3, v168, v2
	v_fmac_f32_e32 v49, v168, v50
	v_cvt_pk_bf16_f32 v2, v3, v49
	ds_write_b32 v171, v2 offset:7888
	v_fma_f32 v2, -v169, v49, v64
	v_fmac_f32_e32 v48, v169, v3
	v_fmac_f32_e32 v2, v168, v3
	v_fmac_f32_e32 v48, v168, v49
	v_cvt_pk_bf16_f32 v3, v2, v48
	ds_write_b32 v171, v3 offset:7616
	v_fma_f32 v3, -v169, v48, v19
	v_fmac_f32_e32 v35, v169, v2
	v_fmac_f32_e32 v3, v168, v2
	v_fmac_f32_e32 v35, v168, v48
	v_cvt_pk_bf16_f32 v2, v3, v35
	ds_write_b32 v171, v2 offset:7344
	v_fma_f32 v2, -v169, v35, v18
	v_fmac_f32_e32 v34, v169, v3
	v_fmac_f32_e32 v2, v168, v3
	v_fmac_f32_e32 v34, v168, v35
	v_cvt_pk_bf16_f32 v3, v2, v34
	ds_write_b32 v171, v3 offset:7072
	v_fma_f32 v3, -v169, v34, v17
	v_fmac_f32_e32 v33, v169, v2
	v_fmac_f32_e32 v3, v168, v2
	v_fmac_f32_e32 v33, v168, v34
	v_cvt_pk_bf16_f32 v2, v3, v33
	ds_write_b32 v171, v2 offset:6800
	v_fma_f32 v2, -v169, v33, v16
	v_fmac_f32_e32 v32, v169, v3
	v_permlane32_swap_b32_e32 v31, v47
	v_fmac_f32_e32 v2, v168, v3
	v_fmac_f32_e32 v32, v168, v33
	v_cvt_pk_bf16_f32 v3, v2, v32
	ds_write_b32 v171, v3 offset:6528
	v_fma_f32 v3, -v169, v32, v63
	v_fmac_f32_e32 v47, v169, v2
	v_permlane32_swap_b32_e32 v30, v46
	v_fmac_f32_e32 v3, v168, v2
	v_fmac_f32_e32 v47, v168, v32
	v_cvt_pk_bf16_f32 v2, v3, v47
	ds_write_b32 v171, v2 offset:6256
	v_fma_f32 v2, -v169, v47, v62
	v_fmac_f32_e32 v46, v169, v3
	v_permlane32_swap_b32_e32 v29, v45
	v_fmac_f32_e32 v2, v168, v3
	v_fmac_f32_e32 v46, v168, v47
	v_cvt_pk_bf16_f32 v3, v2, v46
; #define LAS __attribute__((address_space(3)))
; __device__ __forceinline__ unsigned cvt_pk_bf16(float lo, float hi) { unsigned r; asm volatile("v_cvt_pk_bf16_f32 %0, %1, %2" : "=v"(r) : "v"(lo), "v"(hi)); return r; }
; #define LDS_WAIT() asm volatile("s_waitcnt lgkmcnt(0)" ::: "memory")
; __device__ __forceinline__ void bu_block(const bf16x8 ua, const BuFrags& f, float (&BR)[32], float (&BI)[32]) {
;     const f32x16 z = {};
;     const f32x16 R0 = __builtin_amdgcn_mfma_f32_32x32x16_bf16(ua, f.r0, z, 0, 0, 0), R1 = __builtin_amdgcn_mfma_f32_32x32x16_bf16(ua, f.r1, z, 0, 0, 0);
;     const f32x16 I0 = __builtin_amdgcn_mfma_f32_32x32x16_bf16(ua, f.i0, z, 0, 0, 0), I1 = __builtin_amdgcn_mfma_f32_32x32x16_bf16(ua, f.i1, z, 0, 0, 0);
; #pragma unroll
;     for (int r = 0; r < 16; ++r) {
;         auto s = __builtin_amdgcn_permlane32_swap(__float_as_uint(R0[r]), __float_as_uint(R1[r]), false, false);
;         BR[8 * (r >> 2) + (r & 3)] = __uint_as_float(s[0]); BR[8 * (r >> 2) + 4 + (r & 3)] = __uint_as_float(s[1]);
;         auto q = __builtin_amdgcn_permlane32_swap(__float_as_uint(I0[r]), __float_as_uint(I1[r]), false, false);
;         BI[8 * (r >> 2) + (r & 3)] = __uint_as_float(q[0]); BI[8 * (r >> 2) + 4 + (r & 3)] = __uint_as_float(q[1]);
;     }
; }
; template <int DIR> ...
;     ...
;     for (int s = 0; s < 4; ++s) { const int sb = DIR ? 3 - s : s; float BR[32], BI[32];
;         bu_block(ua[s], f, BR, BI);
; #pragma unroll
;         for (int tt = 0; tt < 32; ++tt) { const int t = DIR ? 31 - tt : tt; const float nsr = fmaf(ar, sr, fmaf(-ai, si, BR[t])), nsi = fmaf(ar, si, fmaf(ai, sr, BI[t])); sr = nsr; si = nsi;
;             *(LAS unsigned*)(sl + (t * 136 + 2 * lane) * 2) = cvt_pk_bf16(sr, si); }
;         LDS_WAIT();
; #pragma unroll
;         for (int rb = 0; rb < 2; ++rb)
; #pragma unroll
;             for (int ks = 0; ks < 4; ++ks) { const bf16x8 a = *(const LAS bf16x8*)(sl + ((16 * rb + (lane & 15)) * 136 + 32 * ks + 8 * (lane >> 4)) * 2);
;                 yacc[2 * sb + rb] = __builtin_amdgcn_mfma_f32_16x16x32_bf16(a, cb[ks], yacc[2 * sb + rb], 0, 0, 0); }
;         LDS_WAIT(); }
	ds_write_b32 v171, v3 offset:5984
	v_fma_f32 v3, -v169, v46, v61
	v_fmac_f32_e32 v45, v169, v2
	v_permlane32_swap_b32_e32 v12, v60
	v_permlane32_swap_b32_e32 v28, v44
	v_fmac_f32_e32 v3, v168, v2
	v_fmac_f32_e32 v45, v168, v46
	v_cvt_pk_bf16_f32 v2, v3, v45
	ds_write_b32 v171, v2 offset:5712
	v_fma_f32 v2, -v169, v45, v60
	v_fmac_f32_e32 v44, v169, v3
	v_fmac_f32_e32 v2, v168, v3
	v_fmac_f32_e32 v44, v168, v45
	v_cvt_pk_bf16_f32 v3, v2, v44
	ds_write_b32 v171, v3 offset:5440
	v_fma_f32 v3, -v169, v44, v15
	v_fmac_f32_e32 v31, v169, v2
	v_fmac_f32_e32 v3, v168, v2
	v_fmac_f32_e32 v31, v168, v44
	v_cvt_pk_bf16_f32 v2, v3, v31
	ds_write_b32 v171, v2 offset:5168
	v_fma_f32 v2, -v169, v31, v14
	v_fmac_f32_e32 v30, v169, v3
	v_fmac_f32_e32 v2, v168, v3
	v_fmac_f32_e32 v30, v168, v31
	v_cvt_pk_bf16_f32 v3, v2, v30
	ds_write_b32 v171, v3 offset:4896
	v_fma_f32 v3, -v169, v30, v13
	v_fmac_f32_e32 v29, v169, v2
	v_fmac_f32_e32 v3, v168, v2
	v_fmac_f32_e32 v29, v168, v30
	v_cvt_pk_bf16_f32 v2, v3, v29
	ds_write_b32 v171, v2 offset:4624
	v_fma_f32 v2, -v169, v29, v12
	v_fmac_f32_e32 v28, v169, v3
	v_permlane32_swap_b32_e32 v11, v59
	v_permlane32_swap_b32_e32 v27, v43
	v_fmac_f32_e32 v2, v168, v3
	v_fmac_f32_e32 v28, v168, v29
	v_cvt_pk_bf16_f32 v3, v2, v28
	ds_write_b32 v171, v3 offset:4352
	v_fma_f32 v3, -v169, v28, v59
	v_fmac_f32_e32 v43, v169, v2
	v_permlane32_swap_b32_e32 v10, v58
	v_permlane32_swap_b32_e32 v26, v42
	v_fmac_f32_e32 v3, v168, v2
	v_fmac_f32_e32 v43, v168, v28
	v_cvt_pk_bf16_f32 v2, v3, v43
	ds_write_b32 v171, v2 offset:4080
	v_fma_f32 v2, -v169, v43, v58
	v_fmac_f32_e32 v42, v169, v3
	v_permlane32_swap_b32_e32 v9, v57
	v_permlane32_swap_b32_e32 v25, v41
	v_fmac_f32_e32 v2, v168, v3
	v_fmac_f32_e32 v42, v168, v43
	v_cvt_pk_bf16_f32 v3, v2, v42
	ds_write_b32 v171, v3 offset:3808
	v_fma_f32 v3, -v169, v42, v57
	v_fmac_f32_e32 v41, v169, v2
	v_permlane32_swap_b32_e32 v8, v56
	v_permlane32_swap_b32_e32 v24, v40
	v_fmac_f32_e32 v3, v168, v2
	v_fmac_f32_e32 v41, v168, v42
	v_cvt_pk_bf16_f32 v2, v3, v41
	ds_write_b32 v171, v2 offset:3536
	v_fma_f32 v2, -v169, v41, v56
	v_fmac_f32_e32 v40, v169, v3
	v_fmac_f32_e32 v2, v168, v3
	v_fmac_f32_e32 v40, v168, v41
	v_cvt_pk_bf16_f32 v3, v2, v40
	ds_write_b32 v171, v3 offset:3264
	v_fma_f32 v3, -v169, v40, v11
	v_fmac_f32_e32 v27, v169, v2
	v_fmac_f32_e32 v3, v168, v2
	v_fmac_f32_e32 v27, v168, v40
	v_cvt_pk_bf16_f32 v2, v3, v27
	ds_write_b32 v171, v2 offset:2992
	v_fma_f32 v2, -v169, v27, v10
	v_fmac_f32_e32 v26, v169, v3
	v_fmac_f32_e32 v2, v168, v3
	v_fmac_f32_e32 v26, v168, v27
	v_cvt_pk_bf16_f32 v3, v2, v26
	ds_write_b32 v171, v3 offset:2720
	v_fma_f32 v3, -v169, v26, v9
	v_fmac_f32_e32 v25, v169, v2
	v_fmac_f32_e32 v3, v168, v2
	v_fmac_f32_e32 v25, v168, v26
	v_cvt_pk_bf16_f32 v2, v3, v25
	ds_write_b32 v171, v2 offset:2448
	v_fma_f32 v2, -v169, v25, v8
	v_fmac_f32_e32 v24, v169, v3
	v_permlane32_swap_b32_e32 v7, v55
	v_permlane32_swap_b32_e32 v23, v39
	v_fmac_f32_e32 v2, v168, v3
	v_fmac_f32_e32 v24, v168, v25
	v_cvt_pk_bf16_f32 v3, v2, v24
	ds_write_b32 v171, v3 offset:2176
	v_fma_f32 v3, -v169, v24, v55
	v_fmac_f32_e32 v39, v169, v2
	v_permlane32_swap_b32_e32 v6, v54
	v_permlane32_swap_b32_e32 v22, v38
	v_fmac_f32_e32 v3, v168, v2
	v_fmac_f32_e32 v39, v168, v24
	v_cvt_pk_bf16_f32 v2, v3, v39
	ds_write_b32 v171, v2 offset:1904
	v_fma_f32 v2, -v169, v39, v54
	v_fmac_f32_e32 v38, v169, v3
	v_permlane32_swap_b32_e32 v5, v53
	v_permlane32_swap_b32_e32 v21, v37
	v_fmac_f32_e32 v2, v168, v3
	v_fmac_f32_e32 v38, v168, v39
	v_cvt_pk_bf16_f32 v3, v2, v38
	ds_write_b32 v171, v3 offset:1632
	v_fma_f32 v3, -v169, v38, v53
	v_fmac_f32_e32 v37, v169, v2
	v_permlane32_swap_b32_e32 v4, v52
	v_permlane32_swap_b32_e32 v20, v36
	v_fmac_f32_e32 v3, v168, v2
	v_fmac_f32_e32 v37, v168, v38
	v_cvt_pk_bf16_f32 v2, v3, v37
	ds_write_b32 v171, v2 offset:1360
	v_fma_f32 v2, -v169, v37, v52
	v_fmac_f32_e32 v36, v169, v3
	v_fmac_f32_e32 v2, v168, v3
	v_fmac_f32_e32 v36, v168, v37
	v_cvt_pk_bf16_f32 v3, v2, v36
	ds_write_b32 v171, v3 offset:1088
	v_fma_f32 v3, -v169, v36, v7
	v_fmac_f32_e32 v23, v169, v2
	v_fmac_f32_e32 v3, v168, v2
	v_fmac_f32_e32 v23, v168, v36
	v_cvt_pk_bf16_f32 v2, v3, v23
	ds_write_b32 v171, v2 offset:816
	v_fma_f32 v2, -v169, v23, v6
	v_fmac_f32_e32 v22, v169, v3
	v_fmac_f32_e32 v2, v168, v3
	v_fmac_f32_e32 v22, v168, v23
	v_cvt_pk_bf16_f32 v3, v2, v22
	ds_write_b32 v171, v3 offset:544
	v_fma_f32 v3, -v169, v22, v5
	v_fmac_f32_e32 v21, v169, v2
	v_fmac_f32_e32 v3, v168, v2
	v_fmac_f32_e32 v21, v168, v22
	v_cvt_pk_bf16_f32 v2, v3, v21
	ds_write_b32 v171, v2 offset:272
	v_fma_f32 v2, -v169, v21, v4
	v_fmac_f32_e32 v2, v168, v3
	v_fmac_f32_e32 v20, v169, v3
	v_fmac_f32_e32 v20, v168, v21
	v_cvt_pk_bf16_f32 v2, v2, v20
	ds_write_b32 v171, v2
	s_waitcnt lgkmcnt(0)
	ds_read_b128 v[2:5], v175
	ds_read_b128 v[6:9], v175 offset:64
	s_waitcnt lgkmcnt(1)
	v_mfma_f32_16x16x32_bf16 v[2:5], v[2:5], v[118:121], v[86:89]
	ds_read_b128 v[10:13], v175 offset:4416
	s_waitcnt lgkmcnt(1)
	v_mfma_f32_16x16x32_bf16 v[2:5], v[6:9], v[114:117], v[2:5]
	ds_read_b128 v[6:9], v175 offset:128
	s_waitcnt lgkmcnt(0)
	v_mfma_f32_16x16x32_bf16 v[2:5], v[6:9], v[110:113], v[2:5]
	ds_read_b128 v[6:9], v175 offset:192
	s_waitcnt lgkmcnt(0)
	v_mfma_f32_16x16x32_bf16 v[6:9], v[6:9], v[106:109], v[2:5]
	s_nop 4
	ds_read_b128 v[2:5], v175 offset:4352
	s_waitcnt lgkmcnt(0)
	v_mfma_f32_16x16x32_bf16 v[2:5], v[2:5], v[118:121], v[82:85]
	v_mfma_f32_16x16x32_bf16 v[2:5], v[10:13], v[114:117], v[2:5]
	ds_read_b128 v[10:13], v175 offset:4480
	s_waitcnt lgkmcnt(0)
	v_mfma_f32_16x16x32_bf16 v[2:5], v[10:13], v[110:113], v[2:5]
	ds_read_b128 v[10:13], v175 offset:4544
	s_waitcnt lgkmcnt(0)
; __device__ __forceinline__ float bf2f(bf16_t b) { return __uint_as_float((unsigned)b << 16); }
; __device__ __forceinline__ bf16_t f2bf(float f) { return (bf16_t)(cvt_pk_bf16(f, 0.f) & 0xffffu); }
; __device__ __forceinline__ float gelu_t(float x) { const float u = 0.7978845608028654f * (x + 0.044715f * x * x * x); return x * sigm(2.f * u); }
; __device__ __forceinline__ void ssm_pass2_item(const bf16_t* __restrict__ proj, const float* lamb_l, const float* lamt_l, const bf16_t* bbar_l, const bf16_t* ctt_l, const float* est, const float* __restrict__ dskip, ...
;     ...
;     const int c = lane & 15, ch = g * 16 + c; const float dk = dskip[ch];
; #pragma unroll
;     for (int blk = 0; blk < 8; ++blk)
; #pragma unroll
;         for (int r = 0; r < 4; ++r) { const int tok = b * SEQ + n * 128 + 16 * blk + 4 * (lane >> 4) + r;
;             const float y = yacc[blk][r] + dk * bf2f(proj[(size_t)tok * NIN + C_U + ch]); ssmy[(size_t)tok * 1024 + ch] = f2bf(gelu_t(y)); }
	s_waitcnt lgkmcnt(0)
	v_mfma_f32_16x16x32_bf16 v[2:5], v[10:13], v[106:109], v[2:5]
	v_lshl_or_b32 v10, s59, 4, v172
	v_or_b32_e32 v12, s16, v173
	v_and_b32_e32 v248, 3, v0
	v_sub_u32_e32 v249, v10, v248
	v_add_u32_e32 v12, v12, v248
	v_lshlrev_b32_e32 v13, 2, v249
	global_load_dwordx4 v[82:85], v13, s[14:15]
	v_lshlrev_b32_e32 v250, 1, v249
	v_mov_b32_e32 v251, 0
	v_mad_i64_i32 v[252:253], s[0:1], v12, s41, v[166:167]
	v_ashrrev_i32_e32 v13, 31, v12
	v_lshl_add_u64 v[252:253], v[252:253], 0, v[250:251]
	v_lshlrev_b64 v[14:15], 11, v[12:13]
	v_lshl_add_u64 v[254:255], s[28:29], 0, v[250:251]
	s_mov_b32 s101, 0
	v_lshl_add_u64 v[254:255], v[254:255], 0, v[14:15]
	global_load_dwordx2 v[106:107], v[252:253], off offset:3072
	s_mov_b32 s100, 0x54000
	v_lshl_add_u64 v[14:15], v[252:253], 0, s[100:101]
	global_load_dwordx2 v[108:109], v[14:15], off offset:3072
	s_mov_b32 s100, 0xa8000
	v_lshl_add_u64 v[14:15], v[252:253], 0, s[100:101]
	global_load_dwordx2 v[110:111], v[14:15], off offset:3072
	s_mov_b32 s100, 0xfc000
	v_lshl_add_u64 v[14:15], v[252:253], 0, s[100:101]
	global_load_dwordx2 v[112:113], v[14:15], off offset:3072
	s_mov_b32 s100, 0x150000
	v_lshl_add_u64 v[14:15], v[252:253], 0, s[100:101]
	global_load_dwordx2 v[114:115], v[14:15], off offset:3072
	s_mov_b32 s100, 0x1a4000
	v_lshl_add_u64 v[14:15], v[252:253], 0, s[100:101]
	global_load_dwordx2 v[116:117], v[14:15], off offset:3072
	s_mov_b32 s100, 0x1f8000
	v_lshl_add_u64 v[14:15], v[252:253], 0, s[100:101]
	global_load_dwordx2 v[118:119], v[14:15], off offset:3072
	s_mov_b32 s100, 0x24c000
	v_lshl_add_u64 v[14:15], v[252:253], 0, s[100:101]
	global_load_dwordx2 v[120:121], v[14:15], off offset:3072
	s_mov_b32 vcc_lo, 0xaaaaaaaa
	s_mov_b32 vcc_hi, 0xaaaaaaaa
	s_nop 1
	v_mov_b32_e32 v86, v7
	v_mov_b32_e32 v87, v9
	v_mov_b32_e32 v88, v3
	v_mov_b32_e32 v89, v5
	v_cndmask_b32_dpp v7, v6, v7, vcc quad_perm:[1,0,3,2] row_mask:0xf bank_mask:0xf
	v_cndmask_b32_dpp v9, v8, v9, vcc quad_perm:[1,0,3,2] row_mask:0xf bank_mask:0xf
	v_cndmask_b32_dpp v3, v2, v3, vcc quad_perm:[1,0,3,2] row_mask:0xf bank_mask:0xf
	v_cndmask_b32_dpp v5, v4, v5, vcc quad_perm:[1,0,3,2] row_mask:0xf bank_mask:0xf
	s_mov_b32 vcc_lo, 0x55555555
	s_mov_b32 vcc_hi, 0x55555555
	s_nop 1
	v_cndmask_b32_dpp v6, v86, v6, vcc quad_perm:[1,0,3,2] row_mask:0xf bank_mask:0xf
	v_cndmask_b32_dpp v8, v87, v8, vcc quad_perm:[1,0,3,2] row_mask:0xf bank_mask:0xf
	v_cndmask_b32_dpp v2, v88, v2, vcc quad_perm:[1,0,3,2] row_mask:0xf bank_mask:0xf
	v_cndmask_b32_dpp v4, v89, v4, vcc quad_perm:[1,0,3,2] row_mask:0xf bank_mask:0xf
	s_mov_b32 vcc_lo, 0xcccccccc
	s_mov_b32 vcc_hi, 0xcccccccc
	s_nop 1
	v_mov_b32_e32 v86, v8
	v_mov_b32_e32 v87, v9
	v_mov_b32_e32 v88, v4
	v_mov_b32_e32 v89, v5
	v_cndmask_b32_dpp v8, v6, v8, vcc quad_perm:[2,3,0,1] row_mask:0xf bank_mask:0xf
	v_cndmask_b32_dpp v9, v7, v9, vcc quad_perm:[2,3,0,1] row_mask:0xf bank_mask:0xf
	v_cndmask_b32_dpp v4, v2, v4, vcc quad_perm:[2,3,0,1] row_mask:0xf bank_mask:0xf
	v_cndmask_b32_dpp v5, v3, v5, vcc quad_perm:[2,3,0,1] row_mask:0xf bank_mask:0xf
	s_mov_b32 vcc_lo, 0x33333333
	s_mov_b32 vcc_hi, 0x33333333
	s_nop 1
	v_cndmask_b32_dpp v6, v86, v6, vcc quad_perm:[2,3,0,1] row_mask:0xf bank_mask:0xf
	v_cndmask_b32_dpp v7, v87, v7, vcc quad_perm:[2,3,0,1] row_mask:0xf bank_mask:0xf
	v_cndmask_b32_dpp v2, v88, v2, vcc quad_perm:[2,3,0,1] row_mask:0xf bank_mask:0xf
	v_cndmask_b32_dpp v3, v89, v3, vcc quad_perm:[2,3,0,1] row_mask:0xf bank_mask:0xf
	s_mov_b32 vcc_lo, 0xaaaaaaaa
	s_mov_b32 vcc_hi, 0xaaaaaaaa
	s_nop 1
	v_mov_b32_e32 v86, v91
	v_mov_b32_e32 v87, v93
	v_mov_b32_e32 v88, v77
	v_mov_b32_e32 v89, v79
	v_cndmask_b32_dpp v91, v90, v91, vcc quad_perm:[1,0,3,2] row_mask:0xf bank_mask:0xf
	v_cndmask_b32_dpp v93, v92, v93, vcc quad_perm:[1,0,3,2] row_mask:0xf bank_mask:0xf
	v_cndmask_b32_dpp v77, v76, v77, vcc quad_perm:[1,0,3,2] row_mask:0xf bank_mask:0xf
	v_cndmask_b32_dpp v79, v78, v79, vcc quad_perm:[1,0,3,2] row_mask:0xf bank_mask:0xf
	s_mov_b32 vcc_lo, 0x55555555
	s_mov_b32 vcc_hi, 0x55555555
	s_nop 1
	v_cndmask_b32_dpp v90, v86, v90, vcc quad_perm:[1,0,3,2] row_mask:0xf bank_mask:0xf
	v_cndmask_b32_dpp v92, v87, v92, vcc quad_perm:[1,0,3,2] row_mask:0xf bank_mask:0xf
	v_cndmask_b32_dpp v76, v88, v76, vcc quad_perm:[1,0,3,2] row_mask:0xf bank_mask:0xf
	v_cndmask_b32_dpp v78, v89, v78, vcc quad_perm:[1,0,3,2] row_mask:0xf bank_mask:0xf
	s_mov_b32 vcc_lo, 0xcccccccc
	s_mov_b32 vcc_hi, 0xcccccccc
	s_nop 1
	v_mov_b32_e32 v86, v92
	v_mov_b32_e32 v87, v93
	v_mov_b32_e32 v88, v78
	v_mov_b32_e32 v89, v79
	v_cndmask_b32_dpp v92, v90, v92, vcc quad_perm:[2,3,0,1] row_mask:0xf bank_mask:0xf
	v_cndmask_b32_dpp v93, v91, v93, vcc quad_perm:[2,3,0,1] row_mask:0xf bank_mask:0xf
	v_cndmask_b32_dpp v78, v76, v78, vcc quad_perm:[2,3,0,1] row_mask:0xf bank_mask:0xf
	v_cndmask_b32_dpp v79, v77, v79, vcc quad_perm:[2,3,0,1] row_mask:0xf bank_mask:0xf
	s_mov_b32 vcc_lo, 0x33333333
	s_mov_b32 vcc_hi, 0x33333333
	s_nop 1
	v_cndmask_b32_dpp v90, v86, v90, vcc quad_perm:[2,3,0,1] row_mask:0xf bank_mask:0xf
	v_cndmask_b32_dpp v91, v87, v91, vcc quad_perm:[2,3,0,1] row_mask:0xf bank_mask:0xf
	v_cndmask_b32_dpp v76, v88, v76, vcc quad_perm:[2,3,0,1] row_mask:0xf bank_mask:0xf
	v_cndmask_b32_dpp v77, v89, v77, vcc quad_perm:[2,3,0,1] row_mask:0xf bank_mask:0xf
	s_mov_b32 vcc_lo, 0xaaaaaaaa
	s_mov_b32 vcc_hi, 0xaaaaaaaa
	s_nop 1
	v_mov_b32_e32 v86, v73
	v_mov_b32_e32 v87, v75
	v_mov_b32_e32 v88, v69
	v_mov_b32_e32 v89, v71
	v_cndmask_b32_dpp v73, v72, v73, vcc quad_perm:[1,0,3,2] row_mask:0xf bank_mask:0xf
	v_cndmask_b32_dpp v75, v74, v75, vcc quad_perm:[1,0,3,2] row_mask:0xf bank_mask:0xf
; __device__ __forceinline__ float bf2f(bf16_t b) { return __uint_as_float((unsigned)b << 16); }
; __device__ __forceinline__ bf16_t f2bf(float f) { return (bf16_t)(cvt_pk_bf16(f, 0.f) & 0xffffu); }
; __device__ __forceinline__ float gelu_t(float x) { const float u = 0.7978845608028654f * (x + 0.044715f * x * x * x); return x * sigm(2.f * u); }
; __device__ __forceinline__ float sigm(float x) { return __builtin_amdgcn_rcpf(1.f + __builtin_amdgcn_exp2f(-1.4426950408889634f * x)); }
; __device__ __forceinline__ void ssm_pass2_item(const bf16_t* __restrict__ proj, const float* lamb_l, const float* lamt_l, const bf16_t* bbar_l, const bf16_t* ctt_l, const float* est, const float* __restrict__ dskip, ...
;     ...
;     const int c = lane & 15, ch = g * 16 + c; const float dk = dskip[ch];
; #pragma unroll
;     for (int blk = 0; blk < 8; ++blk)
; #pragma unroll
;         for (int r = 0; r < 4; ++r) { const int tok = b * SEQ + n * 128 + 16 * blk + 4 * (lane >> 4) + r;
;             const float y = yacc[blk][r] + dk * bf2f(proj[(size_t)tok * NIN + C_U + ch]); ssmy[(size_t)tok * 1024 + ch] = f2bf(gelu_t(y)); }
	v_cndmask_b32_dpp v69, v68, v69, vcc quad_perm:[1,0,3,2] row_mask:0xf bank_mask:0xf
	v_cndmask_b32_dpp v71, v70, v71, vcc quad_perm:[1,0,3,2] row_mask:0xf bank_mask:0xf
	s_mov_b32 vcc_lo, 0x55555555
	s_mov_b32 vcc_hi, 0x55555555
	s_nop 1
	v_cndmask_b32_dpp v72, v86, v72, vcc quad_perm:[1,0,3,2] row_mask:0xf bank_mask:0xf
	v_cndmask_b32_dpp v74, v87, v74, vcc quad_perm:[1,0,3,2] row_mask:0xf bank_mask:0xf
	v_cndmask_b32_dpp v68, v88, v68, vcc quad_perm:[1,0,3,2] row_mask:0xf bank_mask:0xf
	v_cndmask_b32_dpp v70, v89, v70, vcc quad_perm:[1,0,3,2] row_mask:0xf bank_mask:0xf
	s_mov_b32 vcc_lo, 0xcccccccc
	s_mov_b32 vcc_hi, 0xcccccccc
	s_nop 1
	v_mov_b32_e32 v86, v74
	v_mov_b32_e32 v87, v75
	v_mov_b32_e32 v88, v70
	v_mov_b32_e32 v89, v71
	v_cndmask_b32_dpp v74, v72, v74, vcc quad_perm:[2,3,0,1] row_mask:0xf bank_mask:0xf
	v_cndmask_b32_dpp v75, v73, v75, vcc quad_perm:[2,3,0,1] row_mask:0xf bank_mask:0xf
	v_cndmask_b32_dpp v70, v68, v70, vcc quad_perm:[2,3,0,1] row_mask:0xf bank_mask:0xf
	v_cndmask_b32_dpp v71, v69, v71, vcc quad_perm:[2,3,0,1] row_mask:0xf bank_mask:0xf
	s_mov_b32 vcc_lo, 0x33333333
	s_mov_b32 vcc_hi, 0x33333333
	s_nop 1
	v_cndmask_b32_dpp v72, v86, v72, vcc quad_perm:[2,3,0,1] row_mask:0xf bank_mask:0xf
	v_cndmask_b32_dpp v73, v87, v73, vcc quad_perm:[2,3,0,1] row_mask:0xf bank_mask:0xf
	v_cndmask_b32_dpp v68, v88, v68, vcc quad_perm:[2,3,0,1] row_mask:0xf bank_mask:0xf
	v_cndmask_b32_dpp v69, v89, v69, vcc quad_perm:[2,3,0,1] row_mask:0xf bank_mask:0xf
	s_mov_b32 vcc_lo, 0xaaaaaaaa
	s_mov_b32 vcc_hi, 0xaaaaaaaa
	s_nop 1
	v_mov_b32_e32 v86, v143
	v_mov_b32_e32 v87, v145
	v_mov_b32_e32 v88, v139
	v_mov_b32_e32 v89, v141
	v_cndmask_b32_dpp v143, v142, v143, vcc quad_perm:[1,0,3,2] row_mask:0xf bank_mask:0xf
	v_cndmask_b32_dpp v145, v144, v145, vcc quad_perm:[1,0,3,2] row_mask:0xf bank_mask:0xf
	v_cndmask_b32_dpp v139, v138, v139, vcc quad_perm:[1,0,3,2] row_mask:0xf bank_mask:0xf
	v_cndmask_b32_dpp v141, v140, v141, vcc quad_perm:[1,0,3,2] row_mask:0xf bank_mask:0xf
	s_mov_b32 vcc_lo, 0x55555555
	s_mov_b32 vcc_hi, 0x55555555
	s_nop 1
	v_cndmask_b32_dpp v142, v86, v142, vcc quad_perm:[1,0,3,2] row_mask:0xf bank_mask:0xf
	v_cndmask_b32_dpp v144, v87, v144, vcc quad_perm:[1,0,3,2] row_mask:0xf bank_mask:0xf
	v_cndmask_b32_dpp v138, v88, v138, vcc quad_perm:[1,0,3,2] row_mask:0xf bank_mask:0xf
	v_cndmask_b32_dpp v140, v89, v140, vcc quad_perm:[1,0,3,2] row_mask:0xf bank_mask:0xf
	s_mov_b32 vcc_lo, 0xcccccccc
	s_mov_b32 vcc_hi, 0xcccccccc
	s_nop 1
	v_mov_b32_e32 v86, v144
	v_mov_b32_e32 v87, v145
	v_mov_b32_e32 v88, v140
	v_mov_b32_e32 v89, v141
	v_cndmask_b32_dpp v144, v142, v144, vcc quad_perm:[2,3,0,1] row_mask:0xf bank_mask:0xf
	v_cndmask_b32_dpp v145, v143, v145, vcc quad_perm:[2,3,0,1] row_mask:0xf bank_mask:0xf
	v_cndmask_b32_dpp v140, v138, v140, vcc quad_perm:[2,3,0,1] row_mask:0xf bank_mask:0xf
	v_cndmask_b32_dpp v141, v139, v141, vcc quad_perm:[2,3,0,1] row_mask:0xf bank_mask:0xf
	s_mov_b32 vcc_lo, 0x33333333
	s_mov_b32 vcc_hi, 0x33333333
	s_nop 1
	v_cndmask_b32_dpp v142, v86, v142, vcc quad_perm:[2,3,0,1] row_mask:0xf bank_mask:0xf
	v_cndmask_b32_dpp v143, v87, v143, vcc quad_perm:[2,3,0,1] row_mask:0xf bank_mask:0xf
	v_cndmask_b32_dpp v138, v88, v138, vcc quad_perm:[2,3,0,1] row_mask:0xf bank_mask:0xf
	v_cndmask_b32_dpp v139, v89, v139, vcc quad_perm:[2,3,0,1] row_mask:0xf bank_mask:0xf
	s_waitcnt vmcnt(0)
	v_lshlrev_b32_e32 v86, 16, v106
	v_and_b32_e32 v87, 0xffff0000, v106
	v_lshlrev_b32_e32 v88, 16, v107
	v_and_b32_e32 v89, 0xffff0000, v107
	v_fma_f32 v6, v82, v86, v6
	v_fma_f32 v7, v83, v87, v7
	v_fma_f32 v8, v84, v88, v8
	v_fma_f32 v9, v85, v89, v9
	v_mul_f32_e32 v86, 0x3d372713, v6
	v_mul_f32_e32 v87, 0x3d372713, v7
	v_mul_f32_e32 v88, 0x3d372713, v8
	v_mul_f32_e32 v89, 0x3d372713, v9
	v_mul_f32_e32 v86, v6, v86
	v_mul_f32_e32 v87, v7, v87
	v_mul_f32_e32 v88, v8, v88
	v_mul_f32_e32 v89, v9, v89
	v_fma_f32 v86, v6, v86, v6
	v_fma_f32 v87, v7, v87, v7
	v_fma_f32 v88, v8, v88, v8
	v_fma_f32 v89, v9, v89, v9
	v_mul_f32_e32 v86, 0x3f4c422a, v86
	v_mul_f32_e32 v87, 0x3f4c422a, v87
	v_mul_f32_e32 v88, 0x3f4c422a, v88
	v_mul_f32_e32 v89, 0x3f4c422a, v89
	v_add_f32_e32 v86, v86, v86
	v_add_f32_e32 v87, v87, v87
	v_add_f32_e32 v88, v88, v88
	v_add_f32_e32 v89, v89, v89
	v_mul_f32_e32 v86, 0xbfb8aa3b, v86
	v_mul_f32_e32 v87, 0xbfb8aa3b, v87
	v_mul_f32_e32 v88, 0xbfb8aa3b, v88
	v_mul_f32_e32 v89, 0xbfb8aa3b, v89
	v_exp_f32_e32 v86, v86
	v_exp_f32_e32 v87, v87
	v_exp_f32_e32 v88, v88
	v_exp_f32_e32 v89, v89
	v_add_f32_e32 v86, 1.0, v86
	v_add_f32_e32 v87, 1.0, v87
	v_add_f32_e32 v88, 1.0, v88
	v_add_f32_e32 v89, 1.0, v89
	v_rcp_f32_e32 v86, v86
	v_rcp_f32_e32 v87, v87
	v_rcp_f32_e32 v88, v88
	v_rcp_f32_e32 v89, v89
	v_mul_f32_e32 v6, v6, v86
	v_mul_f32_e32 v7, v7, v87
	v_mul_f32_e32 v8, v8, v88
	v_mul_f32_e32 v9, v9, v89
	v_cvt_pk_bf16_f32 v6, v6, v7
	v_cvt_pk_bf16_f32 v7, v8, v9
	global_store_dwordx2 v[254:255], v[6:7], off
	v_lshlrev_b32_e32 v86, 16, v108
	v_and_b32_e32 v87, 0xffff0000, v108
	v_lshlrev_b32_e32 v88, 16, v109
	v_and_b32_e32 v89, 0xffff0000, v109
	v_fma_f32 v2, v82, v86, v2
	v_fma_f32 v3, v83, v87, v3
	v_fma_f32 v4, v84, v88, v4
	v_fma_f32 v5, v85, v89, v5
	v_mul_f32_e32 v86, 0x3d372713, v2
	v_mul_f32_e32 v87, 0x3d372713, v3
	v_mul_f32_e32 v88, 0x3d372713, v4
	v_mul_f32_e32 v89, 0x3d372713, v5
	v_mul_f32_e32 v86, v2, v86
	v_mul_f32_e32 v87, v3, v87
	v_mul_f32_e32 v88, v4, v88
	v_mul_f32_e32 v89, v5, v89
	v_fma_f32 v86, v2, v86, v2
	v_fma_f32 v87, v3, v87, v3
	v_fma_f32 v88, v4, v88, v4
	v_fma_f32 v89, v5, v89, v5
	v_mul_f32_e32 v86, 0x3f4c422a, v86
	v_mul_f32_e32 v87, 0x3f4c422a, v87
	v_mul_f32_e32 v88, 0x3f4c422a, v88
; __device__ __forceinline__ float bf2f(bf16_t b) { return __uint_as_float((unsigned)b << 16); }
; __device__ __forceinline__ bf16_t f2bf(float f) { return (bf16_t)(cvt_pk_bf16(f, 0.f) & 0xffffu); }
; __device__ __forceinline__ float gelu_t(float x) { const float u = 0.7978845608028654f * (x + 0.044715f * x * x * x); return x * sigm(2.f * u); }
; __device__ __forceinline__ float sigm(float x) { return __builtin_amdgcn_rcpf(1.f + __builtin_amdgcn_exp2f(-1.4426950408889634f * x)); }
; __device__ __forceinline__ void ssm_pass2_item(const bf16_t* __restrict__ proj, const float* lamb_l, const float* lamt_l, const bf16_t* bbar_l, const bf16_t* ctt_l, const float* est, const float* __restrict__ dskip, ...
;     ...
;     const int c = lane & 15, ch = g * 16 + c; const float dk = dskip[ch];
; #pragma unroll
;     for (int blk = 0; blk < 8; ++blk)
; #pragma unroll
;         for (int r = 0; r < 4; ++r) { const int tok = b * SEQ + n * 128 + 16 * blk + 4 * (lane >> 4) + r;
;             const float y = yacc[blk][r] + dk * bf2f(proj[(size_t)tok * NIN + C_U + ch]); ssmy[(size_t)tok * 1024 + ch] = f2bf(gelu_t(y)); }
	v_mul_f32_e32 v89, 0x3f4c422a, v89
	v_add_f32_e32 v86, v86, v86
	v_add_f32_e32 v87, v87, v87
	v_add_f32_e32 v88, v88, v88
	v_add_f32_e32 v89, v89, v89
	v_mul_f32_e32 v86, 0xbfb8aa3b, v86
	v_mul_f32_e32 v87, 0xbfb8aa3b, v87
	v_mul_f32_e32 v88, 0xbfb8aa3b, v88
	v_mul_f32_e32 v89, 0xbfb8aa3b, v89
	v_exp_f32_e32 v86, v86
	v_exp_f32_e32 v87, v87
	v_exp_f32_e32 v88, v88
	v_exp_f32_e32 v89, v89
	v_add_f32_e32 v86, 1.0, v86
	v_add_f32_e32 v87, 1.0, v87
	v_add_f32_e32 v88, 1.0, v88
	v_add_f32_e32 v89, 1.0, v89
	v_rcp_f32_e32 v86, v86
	v_rcp_f32_e32 v87, v87
	v_rcp_f32_e32 v88, v88
	v_rcp_f32_e32 v89, v89
	v_mul_f32_e32 v2, v2, v86
	v_mul_f32_e32 v3, v3, v87
	v_mul_f32_e32 v4, v4, v88
	v_mul_f32_e32 v5, v5, v89
	v_cvt_pk_bf16_f32 v2, v2, v3
	v_cvt_pk_bf16_f32 v3, v4, v5
	s_mov_b32 s100, 0x8000
	v_lshl_add_u64 v[14:15], v[254:255], 0, s[100:101]
	global_store_dwordx2 v[14:15], v[2:3], off
	v_lshlrev_b32_e32 v86, 16, v110
	v_and_b32_e32 v87, 0xffff0000, v110
	v_lshlrev_b32_e32 v88, 16, v111
	v_and_b32_e32 v89, 0xffff0000, v111
	v_fma_f32 v90, v82, v86, v90
	v_fma_f32 v91, v83, v87, v91
	v_fma_f32 v92, v84, v88, v92
	v_fma_f32 v93, v85, v89, v93
	v_mul_f32_e32 v86, 0x3d372713, v90
	v_mul_f32_e32 v87, 0x3d372713, v91
	v_mul_f32_e32 v88, 0x3d372713, v92
	v_mul_f32_e32 v89, 0x3d372713, v93
	v_mul_f32_e32 v86, v90, v86
	v_mul_f32_e32 v87, v91, v87
	v_mul_f32_e32 v88, v92, v88
	v_mul_f32_e32 v89, v93, v89
	v_fma_f32 v86, v90, v86, v90
	v_fma_f32 v87, v91, v87, v91
	v_fma_f32 v88, v92, v88, v92
	v_fma_f32 v89, v93, v89, v93
	v_mul_f32_e32 v86, 0x3f4c422a, v86
	v_mul_f32_e32 v87, 0x3f4c422a, v87
	v_mul_f32_e32 v88, 0x3f4c422a, v88
	v_mul_f32_e32 v89, 0x3f4c422a, v89
	v_add_f32_e32 v86, v86, v86
	v_add_f32_e32 v87, v87, v87
	v_add_f32_e32 v88, v88, v88
	v_add_f32_e32 v89, v89, v89
	v_mul_f32_e32 v86, 0xbfb8aa3b, v86
	v_mul_f32_e32 v87, 0xbfb8aa3b, v87
	v_mul_f32_e32 v88, 0xbfb8aa3b, v88
	v_mul_f32_e32 v89, 0xbfb8aa3b, v89
	v_exp_f32_e32 v86, v86
	v_exp_f32_e32 v87, v87
	v_exp_f32_e32 v88, v88
	v_exp_f32_e32 v89, v89
	v_add_f32_e32 v86, 1.0, v86
	v_add_f32_e32 v87, 1.0, v87
	v_add_f32_e32 v88, 1.0, v88
	v_add_f32_e32 v89, 1.0, v89
	v_rcp_f32_e32 v86, v86
	v_rcp_f32_e32 v87, v87
	v_rcp_f32_e32 v88, v88
	v_rcp_f32_e32 v89, v89
	v_mul_f32_e32 v90, v90, v86
	v_mul_f32_e32 v91, v91, v87
	v_mul_f32_e32 v92, v92, v88
	v_mul_f32_e32 v93, v93, v89
	v_cvt_pk_bf16_f32 v90, v90, v91
	v_cvt_pk_bf16_f32 v91, v92, v93
	s_mov_b32 s100, 0x10000
	v_lshl_add_u64 v[14:15], v[254:255], 0, s[100:101]
	global_store_dwordx2 v[14:15], v[90:91], off
	v_lshlrev_b32_e32 v86, 16, v112
	v_and_b32_e32 v87, 0xffff0000, v112
	v_lshlrev_b32_e32 v88, 16, v113
	v_and_b32_e32 v89, 0xffff0000, v113
	v_fma_f32 v76, v82, v86, v76
	v_fma_f32 v77, v83, v87, v77
	v_fma_f32 v78, v84, v88, v78
	v_fma_f32 v79, v85, v89, v79
	v_mul_f32_e32 v86, 0x3d372713, v76
	v_mul_f32_e32 v87, 0x3d372713, v77
	v_mul_f32_e32 v88, 0x3d372713, v78
	v_mul_f32_e32 v89, 0x3d372713, v79
	v_mul_f32_e32 v86, v76, v86
	v_mul_f32_e32 v87, v77, v87
	v_mul_f32_e32 v88, v78, v88
	v_mul_f32_e32 v89, v79, v89
	v_fma_f32 v86, v76, v86, v76
	v_fma_f32 v87, v77, v87, v77
	v_fma_f32 v88, v78, v88, v78
	v_fma_f32 v89, v79, v89, v79
	v_mul_f32_e32 v86, 0x3f4c422a, v86
	v_mul_f32_e32 v87, 0x3f4c422a, v87
	v_mul_f32_e32 v88, 0x3f4c422a, v88
	v_mul_f32_e32 v89, 0x3f4c422a, v89
	v_add_f32_e32 v86, v86, v86
	v_add_f32_e32 v87, v87, v87
	v_add_f32_e32 v88, v88, v88
	v_add_f32_e32 v89, v89, v89
	v_mul_f32_e32 v86, 0xbfb8aa3b, v86
	v_mul_f32_e32 v87, 0xbfb8aa3b, v87
	v_mul_f32_e32 v88, 0xbfb8aa3b, v88
	v_mul_f32_e32 v89, 0xbfb8aa3b, v89
	v_exp_f32_e32 v86, v86
	v_exp_f32_e32 v87, v87
	v_exp_f32_e32 v88, v88
	v_exp_f32_e32 v89, v89
	v_add_f32_e32 v86, 1.0, v86
	v_add_f32_e32 v87, 1.0, v87
	v_add_f32_e32 v88, 1.0, v88
	v_add_f32_e32 v89, 1.0, v89
	v_rcp_f32_e32 v86, v86
	v_rcp_f32_e32 v87, v87
	v_rcp_f32_e32 v88, v88
	v_rcp_f32_e32 v89, v89
	v_mul_f32_e32 v76, v76, v86
	v_mul_f32_e32 v77, v77, v87
	v_mul_f32_e32 v78, v78, v88
	v_mul_f32_e32 v79, v79, v89
	v_cvt_pk_bf16_f32 v76, v76, v77
	v_cvt_pk_bf16_f32 v77, v78, v79
	s_mov_b32 s100, 0x18000
	v_lshl_add_u64 v[14:15], v[254:255], 0, s[100:101]
	global_store_dwordx2 v[14:15], v[76:77], off
	v_lshlrev_b32_e32 v86, 16, v114
	v_and_b32_e32 v87, 0xffff0000, v114
	v_lshlrev_b32_e32 v88, 16, v115
	v_and_b32_e32 v89, 0xffff0000, v115
	v_fma_f32 v72, v82, v86, v72
	v_fma_f32 v73, v83, v87, v73
	v_fma_f32 v74, v84, v88, v74
	v_fma_f32 v75, v85, v89, v75
	v_mul_f32_e32 v86, 0x3d372713, v72
	v_mul_f32_e32 v87, 0x3d372713, v73
	v_mul_f32_e32 v88, 0x3d372713, v74
	v_mul_f32_e32 v89, 0x3d372713, v75
	v_mul_f32_e32 v86, v72, v86
	v_mul_f32_e32 v87, v73, v87
	v_mul_f32_e32 v88, v74, v88
	v_mul_f32_e32 v89, v75, v89
	v_fma_f32 v86, v72, v86, v72
	v_fma_f32 v87, v73, v87, v73
	v_fma_f32 v88, v74, v88, v74
	v_fma_f32 v89, v75, v89, v75
	v_mul_f32_e32 v86, 0x3f4c422a, v86
	v_mul_f32_e32 v87, 0x3f4c422a, v87
	v_mul_f32_e32 v88, 0x3f4c422a, v88
	v_mul_f32_e32 v89, 0x3f4c422a, v89
	v_add_f32_e32 v86, v86, v86
	v_add_f32_e32 v87, v87, v87
	v_add_f32_e32 v88, v88, v88
	v_add_f32_e32 v89, v89, v89
	v_mul_f32_e32 v86, 0xbfb8aa3b, v86
	v_mul_f32_e32 v87, 0xbfb8aa3b, v87
	v_mul_f32_e32 v88, 0xbfb8aa3b, v88
	v_mul_f32_e32 v89, 0xbfb8aa3b, v89
	v_exp_f32_e32 v86, v86
	v_exp_f32_e32 v87, v87
	v_exp_f32_e32 v88, v88
	v_exp_f32_e32 v89, v89
	v_add_f32_e32 v86, 1.0, v86
	v_add_f32_e32 v87, 1.0, v87
	v_add_f32_e32 v88, 1.0, v88
	v_add_f32_e32 v89, 1.0, v89
; __device__ __forceinline__ float bf2f(bf16_t b) { return __uint_as_float((unsigned)b << 16); }
; __device__ __forceinline__ bf16_t f2bf(float f) { return (bf16_t)(cvt_pk_bf16(f, 0.f) & 0xffffu); }
; __device__ __forceinline__ float gelu_t(float x) { const float u = 0.7978845608028654f * (x + 0.044715f * x * x * x); return x * sigm(2.f * u); }
; __device__ __forceinline__ float sigm(float x) { return __builtin_amdgcn_rcpf(1.f + __builtin_amdgcn_exp2f(-1.4426950408889634f * x)); }
; __device__ __forceinline__ void ssm_pass2_item(const bf16_t* __restrict__ proj, const float* lamb_l, const float* lamt_l, const bf16_t* bbar_l, const bf16_t* ctt_l, const float* est, const float* __restrict__ dskip, ...
;     ...
;     const int c = lane & 15, ch = g * 16 + c; const float dk = dskip[ch];
; #pragma unroll
;     for (int blk = 0; blk < 8; ++blk)
; #pragma unroll
;         for (int r = 0; r < 4; ++r) { const int tok = b * SEQ + n * 128 + 16 * blk + 4 * (lane >> 4) + r;
;             const float y = yacc[blk][r] + dk * bf2f(proj[(size_t)tok * NIN + C_U + ch]); ssmy[(size_t)tok * 1024 + ch] = f2bf(gelu_t(y)); }
	v_rcp_f32_e32 v86, v86
	v_rcp_f32_e32 v87, v87
	v_rcp_f32_e32 v88, v88
	v_rcp_f32_e32 v89, v89
	v_mul_f32_e32 v72, v72, v86
	v_mul_f32_e32 v73, v73, v87
	v_mul_f32_e32 v74, v74, v88
	v_mul_f32_e32 v75, v75, v89
	v_cvt_pk_bf16_f32 v72, v72, v73
	v_cvt_pk_bf16_f32 v73, v74, v75
	s_mov_b32 s100, 0x20000
	v_lshl_add_u64 v[14:15], v[254:255], 0, s[100:101]
	global_store_dwordx2 v[14:15], v[72:73], off
	v_lshlrev_b32_e32 v86, 16, v116
	v_and_b32_e32 v87, 0xffff0000, v116
	v_lshlrev_b32_e32 v88, 16, v117
	v_and_b32_e32 v89, 0xffff0000, v117
	v_fma_f32 v68, v82, v86, v68
	v_fma_f32 v69, v83, v87, v69
	v_fma_f32 v70, v84, v88, v70
	v_fma_f32 v71, v85, v89, v71
	v_mul_f32_e32 v86, 0x3d372713, v68
	v_mul_f32_e32 v87, 0x3d372713, v69
	v_mul_f32_e32 v88, 0x3d372713, v70
	v_mul_f32_e32 v89, 0x3d372713, v71
	v_mul_f32_e32 v86, v68, v86
	v_mul_f32_e32 v87, v69, v87
	v_mul_f32_e32 v88, v70, v88
	v_mul_f32_e32 v89, v71, v89
	v_fma_f32 v86, v68, v86, v68
	v_fma_f32 v87, v69, v87, v69
	v_fma_f32 v88, v70, v88, v70
	v_fma_f32 v89, v71, v89, v71
	v_mul_f32_e32 v86, 0x3f4c422a, v86
	v_mul_f32_e32 v87, 0x3f4c422a, v87
	v_mul_f32_e32 v88, 0x3f4c422a, v88
	v_mul_f32_e32 v89, 0x3f4c422a, v89
	v_add_f32_e32 v86, v86, v86
	v_add_f32_e32 v87, v87, v87
	v_add_f32_e32 v88, v88, v88
	v_add_f32_e32 v89, v89, v89
	v_mul_f32_e32 v86, 0xbfb8aa3b, v86
	v_mul_f32_e32 v87, 0xbfb8aa3b, v87
	v_mul_f32_e32 v88, 0xbfb8aa3b, v88
	v_mul_f32_e32 v89, 0xbfb8aa3b, v89
	v_exp_f32_e32 v86, v86
	v_exp_f32_e32 v87, v87
	v_exp_f32_e32 v88, v88
	v_exp_f32_e32 v89, v89
	v_add_f32_e32 v86, 1.0, v86
	v_add_f32_e32 v87, 1.0, v87
	v_add_f32_e32 v88, 1.0, v88
	v_add_f32_e32 v89, 1.0, v89
	v_rcp_f32_e32 v86, v86
	v_rcp_f32_e32 v87, v87
	v_rcp_f32_e32 v88, v88
	v_rcp_f32_e32 v89, v89
	v_mul_f32_e32 v68, v68, v86
	v_mul_f32_e32 v69, v69, v87
	v_mul_f32_e32 v70, v70, v88
	v_mul_f32_e32 v71, v71, v89
	v_cvt_pk_bf16_f32 v68, v68, v69
	v_cvt_pk_bf16_f32 v69, v70, v71
	s_mov_b32 s100, 0x28000
	v_lshl_add_u64 v[14:15], v[254:255], 0, s[100:101]
	global_store_dwordx2 v[14:15], v[68:69], off
	v_lshlrev_b32_e32 v86, 16, v118
	v_and_b32_e32 v87, 0xffff0000, v118
	v_lshlrev_b32_e32 v88, 16, v119
	v_and_b32_e32 v89, 0xffff0000, v119
	v_fma_f32 v142, v82, v86, v142
	v_fma_f32 v143, v83, v87, v143
	v_fma_f32 v144, v84, v88, v144
	v_fma_f32 v145, v85, v89, v145
	v_mul_f32_e32 v86, 0x3d372713, v142
	v_mul_f32_e32 v87, 0x3d372713, v143
	v_mul_f32_e32 v88, 0x3d372713, v144
	v_mul_f32_e32 v89, 0x3d372713, v145
	v_mul_f32_e32 v86, v142, v86
	v_mul_f32_e32 v87, v143, v87
	v_mul_f32_e32 v88, v144, v88
	v_mul_f32_e32 v89, v145, v89
	v_fma_f32 v86, v142, v86, v142
	v_fma_f32 v87, v143, v87, v143
	v_fma_f32 v88, v144, v88, v144
	v_fma_f32 v89, v145, v89, v145
	v_mul_f32_e32 v86, 0x3f4c422a, v86
	v_mul_f32_e32 v87, 0x3f4c422a, v87
	v_mul_f32_e32 v88, 0x3f4c422a, v88
	v_mul_f32_e32 v89, 0x3f4c422a, v89
	v_add_f32_e32 v86, v86, v86
	v_add_f32_e32 v87, v87, v87
	v_add_f32_e32 v88, v88, v88
	v_add_f32_e32 v89, v89, v89
	v_mul_f32_e32 v86, 0xbfb8aa3b, v86
	v_mul_f32_e32 v87, 0xbfb8aa3b, v87
	v_mul_f32_e32 v88, 0xbfb8aa3b, v88
	v_mul_f32_e32 v89, 0xbfb8aa3b, v89
	v_exp_f32_e32 v86, v86
	v_exp_f32_e32 v87, v87
	v_exp_f32_e32 v88, v88
	v_exp_f32_e32 v89, v89
	v_add_f32_e32 v86, 1.0, v86
	v_add_f32_e32 v87, 1.0, v87
	v_add_f32_e32 v88, 1.0, v88
	v_add_f32_e32 v89, 1.0, v89
	v_rcp_f32_e32 v86, v86
	v_rcp_f32_e32 v87, v87
	v_rcp_f32_e32 v88, v88
	v_rcp_f32_e32 v89, v89
	v_mul_f32_e32 v142, v142, v86
	v_mul_f32_e32 v143, v143, v87
	v_mul_f32_e32 v144, v144, v88
	v_mul_f32_e32 v145, v145, v89
	v_cvt_pk_bf16_f32 v142, v142, v143
	v_cvt_pk_bf16_f32 v143, v144, v145
	s_mov_b32 s100, 0x30000
	v_lshl_add_u64 v[14:15], v[254:255], 0, s[100:101]
	global_store_dwordx2 v[14:15], v[142:143], off
	v_lshlrev_b32_e32 v86, 16, v120
	v_and_b32_e32 v87, 0xffff0000, v120
	v_lshlrev_b32_e32 v88, 16, v121
	v_and_b32_e32 v89, 0xffff0000, v121
	v_fma_f32 v138, v82, v86, v138
	v_fma_f32 v139, v83, v87, v139
	v_fma_f32 v140, v84, v88, v140
	v_fma_f32 v141, v85, v89, v141
	v_mul_f32_e32 v86, 0x3d372713, v138
	v_mul_f32_e32 v87, 0x3d372713, v139
	v_mul_f32_e32 v88, 0x3d372713, v140
	v_mul_f32_e32 v89, 0x3d372713, v141
	v_mul_f32_e32 v86, v138, v86
	v_mul_f32_e32 v87, v139, v87
	v_mul_f32_e32 v88, v140, v88
	v_mul_f32_e32 v89, v141, v89
	v_fma_f32 v86, v138, v86, v138
	v_fma_f32 v87, v139, v87, v139
	v_fma_f32 v88, v140, v88, v140
	v_fma_f32 v89, v141, v89, v141
	v_mul_f32_e32 v86, 0x3f4c422a, v86
	v_mul_f32_e32 v87, 0x3f4c422a, v87
	v_mul_f32_e32 v88, 0x3f4c422a, v88
	v_mul_f32_e32 v89, 0x3f4c422a, v89
	v_add_f32_e32 v86, v86, v86
	v_add_f32_e32 v87, v87, v87
	v_add_f32_e32 v88, v88, v88
	v_add_f32_e32 v89, v89, v89
	v_mul_f32_e32 v86, 0xbfb8aa3b, v86
	v_mul_f32_e32 v87, 0xbfb8aa3b, v87
	v_mul_f32_e32 v88, 0xbfb8aa3b, v88
	v_mul_f32_e32 v89, 0xbfb8aa3b, v89
	v_exp_f32_e32 v86, v86
	v_exp_f32_e32 v87, v87
	v_exp_f32_e32 v88, v88
	v_exp_f32_e32 v89, v89
	v_add_f32_e32 v86, 1.0, v86
	v_add_f32_e32 v87, 1.0, v87
	v_add_f32_e32 v88, 1.0, v88
	v_add_f32_e32 v89, 1.0, v89
	v_rcp_f32_e32 v86, v86
	v_rcp_f32_e32 v87, v87
	v_rcp_f32_e32 v88, v88
	v_rcp_f32_e32 v89, v89
	v_mul_f32_e32 v138, v138, v86
	v_mul_f32_e32 v139, v139, v87
	v_mul_f32_e32 v140, v140, v88
	v_mul_f32_e32 v141, v141, v89
	v_cvt_pk_bf16_f32 v138, v138, v139
	v_cvt_pk_bf16_f32 v139, v140, v141
	s_mov_b32 s100, 0x38000
	v_lshl_add_u64 v[14:15], v[254:255], 0, s[100:101]
	global_store_dwordx2 v[14:15], v[138:139], off
	s_cbranch_scc0 .LBB0_1626
